# removed the redundant m0 save and restore around every LDS-DMA load (m0 has no other user); plus unscaled fp8 MFMA form
# speedup vs baseline: 1.0054x; 1.0054x over previous
.LBB0_111:
	s_andn2_b64 vcc, exec, s[6:7]
	s_cbranch_vccnz .LBB0_177
	s_waitcnt lgkmcnt(0)
	s_add_u32 s0, s4, 0x80000
	s_addc_u32 s1, s5, 0
	v_and_b32_e32 v4, 63, v2
	s_cmp_lt_u32 s26, 64
	v_mov_b32_e32 v3, v0
	s_cselect_b64 s[12:13], -1, 0
	s_cmp_gt_u32 s26, 63
	v_lshlrev_b32_e32 v210, 4, v4
	s_cbranch_scc1 .LBB0_114
	s_ashr_i32 s9, s8, 31
	s_lshl_b64 s[2:3], s[8:9], 10
	s_add_u32 s2, s0, s2
	s_addc_u32 s3, s1, s3
	s_add_i32 s6, 0, 0x24cc0
	s_mov_b32 m0, s6
	s_nop 0
	global_load_lds_dwordx4 v210, s[2:3] offset:0
.LBB0_114:
	v_lshlrev_b32_e32 v4, 4, v3
	s_movk_i32 s2, 0x70
	v_bitop3_b32 v4, v4, s2, v3 bitop3:0x48
	v_lshlrev_b32_e32 v3, 8, v3
	v_lshl_or_b32 v4, s8, 19, v4
	v_and_b32_e32 v3, 0xfffff800, v3
	v_add_u32_e32 v211, v4, v3
	v_lshrrev_b32_e32 v3, 4, v2
	v_ashrrev_i32_e32 v5, 3, v2
	v_xor_b32_e32 v4, v3, v2
	v_lshlrev_b32_e32 v6, 1, v5
	v_lshrrev_b32_e32 v7, 2, v5
	v_lshlrev_b32_e32 v4, 4, v4
	v_and_b32_e32 v6, 24, v6
	v_and_b32_e32 v7, 4, v7
	v_and_b32_e32 v5, 0x1fffe3, v5
	s_add_u32 s3, s4, 0x1600000
	v_and_b32_e32 v4, 0x70, v4
	v_or3_b32 v5, v5, v7, v6
	s_addc_u32 s33, s5, 0
	v_lshl_or_b32 v215, v5, 11, v4
	v_mov_b32_e32 v5, 0x2000
	s_add_u32 s14, s4, 0xdc00000
	v_lshl_add_u32 v5, v2, 4, v5
	s_addc_u32 s15, s5, 0
	v_ashrrev_i32_e32 v5, 7, v5
	s_lshl_b32 s7, s22, 10
	s_ashr_i32 s53, s52, 31
	s_ashr_i32 s6, s26, 8
	v_lshlrev_b32_e32 v6, 1, v5
	v_lshrrev_b32_e32 v7, 2, v5
	s_add_i32 s56, s7, 0
	s_lshl_b64 s[10:11], s[52:53], 19
	v_and_b32_e32 v6, 24, v6
	v_and_b32_e32 v7, 4, v7
	v_and_b32_e32 v5, 0x1fffe3, v5
	s_add_u32 s10, s3, s10
	v_or3_b32 v5, v5, v7, v6
	s_addc_u32 s11, s33, s11
	s_add_i32 s57, s56, 0x10000
	s_mov_b32 m0, s57
	s_nop 0
	global_load_lds_dwordx4 v215, s[10:11] offset:0
	s_add_i32 s58, s56, 0x12000
	v_lshl_or_b32 v216, v5, 11, v4
	s_mov_b32 m0, s58
	s_nop 0
	global_load_lds_dwordx4 v216, s[10:11] offset:0
	s_add_u32 s16, s10, 0x40000
	s_addc_u32 s17, s11, 0
	s_add_i32 s59, s56, 0x14000
	s_mov_b32 m0, s59
	s_nop 0
	global_load_lds_dwordx4 v215, s[16:17] offset:0
	s_add_i32 s60, s56, 0x16000
	s_mov_b32 m0, s60
	s_nop 0
	global_load_lds_dwordx4 v216, s[16:17] offset:0
	v_add_u32_e32 v213, 0x20000, v211
	s_mov_b32 m0, s56
	s_nop 0
	global_load_lds_dwordx4 v211, s[14:15] offset:0
	s_add_i32 s61, s56, 0x2000
	s_mov_b32 m0, s61
	s_nop 0
	global_load_lds_dwordx4 v213, s[14:15] offset:0
	v_add_u32_e32 v212, 0x40000, v211
	s_add_i32 s62, s56, 0x4000
	s_mov_b32 m0, s62
	s_nop 0
	global_load_lds_dwordx4 v212, s[14:15] offset:0
	v_add_u32_e32 v214, 0x60000, v211
	s_add_i32 s63, s56, 0x6000
	s_mov_b32 m0, s63
	s_nop 0
	global_load_lds_dwordx4 v214, s[14:15] offset:0
	s_cmp_eq_u32 s6, 1
	s_mov_b32 s49, 0
	s_cselect_b64 s[16:17], -1, 0
	s_cmp_lg_u32 s6, 1
	s_cbranch_scc1 .LBB0_116
	s_barrier
.LBB0_116:
	s_add_u32 s18, s4, 0x15c00000
	s_addc_u32 s19, s5, 0
	s_add_u32 s20, s4, 0x1200000
	s_addc_u32 s21, s5, 0
	s_lshl_b32 s4, s22, 5
	v_and_b32_e32 v4, 15, v2
	s_and_b32 s4, s4, 0x60
	v_lshlrev_b32_e32 v5, 7, v4
	v_or_b32_e32 v4, s4, v4
	s_add_u32 s4, s10, 0x80
	v_lshl_or_b32 v5, s6, 13, v5
	s_waitcnt vmcnt(2)
	s_barrier
	s_addc_u32 s5, s11, 0
	s_add_i32 s64, s56, 0x18000
	s_mov_b32 m0, s64
	s_nop 0
	global_load_lds_dwordx4 v215, s[4:5] offset:0
	s_add_i32 s65, s56, 0x1a000
	s_mov_b32 m0, s65
	s_nop 0
	global_load_lds_dwordx4 v216, s[4:5] offset:0
	s_add_u32 s22, s14, 0x80
	s_addc_u32 s23, s15, 0
	s_add_i32 s66, s56, 0x8000
	s_mov_b32 m0, s66
	s_nop 0
	global_load_lds_dwordx4 v211, s[22:23] offset:0
	s_add_i32 s67, s56, 0xa000
	s_mov_b32 m0, s67
	s_nop 0
	global_load_lds_dwordx4 v213, s[22:23] offset:0
	s_add_u32 s4, s10, 0x40080
	s_addc_u32 s5, s11, 0
	s_add_i32 s68, s56, 0x1c000
	s_add_i32 s69, s56, 0x1e000
	s_add_i32 s70, s56, 0xc000
	v_bfe_u32 v6, v2, 4, 2
	v_bfe_u32 v2, v2, 1, 3
	s_add_u32 s24, s14, 0x780
	v_bitop3_b32 v3, v3, v2, 3 bitop3:0x6c
	v_bitop3_b32 v2, v6, v2, 4 bitop3:0x36
	s_mov_b32 m0, s68
	s_nop 0
	global_load_lds_dwordx4 v215, s[4:5] offset:0
	s_addc_u32 s25, s15, 0
	v_lshlrev_b32_e32 v3, 4, v3
	v_lshlrev_b32_e32 v2, 4, v2
	v_lshlrev_b32_e32 v4, 7, v4
	s_mov_b32 m0, s69
	s_nop 0
	global_load_lds_dwordx4 v216, s[4:5] offset:0
	s_cmpk_lt_u32 s26, 0x100
	v_or_b32_e32 v217, v4, v3
	v_or_b32_e32 v218, v4, v2
	s_waitcnt vmcnt(6)
	s_cselect_b64 s[26:27], -1, 0
	s_add_i32 s4, 0, 0x10000
	v_or_b32_e32 v7, v3, v5
	v_or_b32_e32 v5, v2, v5
	v_add_u32_e32 v219, s4, v217
	v_add_u32_e32 v220, s4, v218
	s_add_i32 s4, 0, 0x14000
	s_add_i32 s71, s56, 0xe000
	s_ashr_i32 s72, s88, 31
	s_ashr_i32 s73, s82, 31
	v_add_u32_e32 v221, s4, v217
	v_add_u32_e32 v222, s4, v218
	v_add_u32_e32 v223, 0, v7
	v_add_u32_e32 v224, 0, v5
	s_mov_b64 s[28:29], 0x2000
	s_mov_b64 s[30:31], 0x2400
	s_mov_b64 s[34:35], 0x2800
	s_mov_b64 s[36:37], 0x2c00
	s_mov_b64 s[38:39], 0x80000
	s_mov_b32 s74, 0x80000
	s_mov_b64 s[40:41], 0x90000
	s_mov_b32 s75, 0x90000
	s_mov_b64 s[42:43], 0xa0000
	s_mov_b32 s76, 0xa0000
	s_mov_b64 s[44:45], 0xb0000
	v_mbcnt_hi_u32_b32 v225, -1, v1
	s_barrier
	s_branch .LBB0_119

.LBB0_126:
	.p2align 3
	s_nop 0
	ds_read_b128 v[130:133], v219
	ds_read_b128 v[134:137], v219 offset:2048
	ds_read_b128 v[138:141], v220
	ds_read_b128 v[142:145], v220 offset:2048
	ds_read_b128 v[146:149], v221
	ds_read_b128 v[150:153], v221 offset:2048
	ds_read_b128 v[154:157], v222
	ds_read_b128 v[158:161], v222 offset:2048
	ds_read_b128 v[162:165], v223
	ds_read_b128 v[166:169], v223 offset:2048
	ds_read_b128 v[170:173], v224
	ds_read_b128 v[174:177], v224 offset:2048
	ds_read_b128 v[178:181], v223 offset:4096
	ds_read_b128 v[182:185], v223 offset:6144
	ds_read_b128 v[186:189], v224 offset:4096
	ds_read_b128 v[190:193], v224 offset:6144
	s_add_u32 s47, s14, s4
	s_addc_u32 s50, s15, s5
	s_add_u32 s54, s47, 0x80
	s_addc_u32 s55, s50, 0
	s_mov_b32 m0, s70
	s_nop 0
	global_load_lds_dwordx4 v212, s[54:55] offset:0
	s_nop 0
	s_mov_b32 m0, s71
	s_nop 0
	global_load_lds_dwordx4 v214, s[54:55] offset:0
	s_waitcnt vmcnt(8)
	s_waitcnt lgkmcnt(0)
	s_barrier
	s_setprio 1
	s_waitcnt lgkmcnt(7)
	v_mfma_f32_16x16x32_bf16 v[126:129], v[130:133], v[162:165], v[126:129]
	v_mfma_f32_16x16x32_bf16 v[122:125], v[134:137], v[162:165], v[122:125]
	s_waitcnt lgkmcnt(6)
	v_mfma_f32_16x16x32_bf16 v[118:121], v[130:133], v[166:169], v[118:121]
	v_mfma_f32_16x16x32_bf16 v[114:117], v[134:137], v[166:169], v[114:117]
	s_waitcnt lgkmcnt(3)
	v_mfma_f32_16x16x32_bf16 v[110:113], v[130:133], v[178:181], v[110:113]
	v_mfma_f32_16x16x32_bf16 v[106:109], v[134:137], v[178:181], v[106:109]
	s_waitcnt lgkmcnt(2)
	v_mfma_f32_16x16x32_bf16 v[102:105], v[130:133], v[182:185], v[102:105]
	v_mfma_f32_16x16x32_bf16 v[98:101], v[134:137], v[182:185], v[98:101]
	v_mfma_f32_16x16x32_bf16 v[126:129], v[138:141], v[170:173], v[126:129]
	v_mfma_f32_16x16x32_bf16 v[122:125], v[142:145], v[170:173], v[122:125]
	v_mfma_f32_16x16x32_bf16 v[118:121], v[138:141], v[174:177], v[118:121]
	v_mfma_f32_16x16x32_bf16 v[114:117], v[142:145], v[174:177], v[114:117]
	s_waitcnt lgkmcnt(1)
	v_mfma_f32_16x16x32_bf16 v[110:113], v[138:141], v[186:189], v[110:113]
	v_mfma_f32_16x16x32_bf16 v[106:109], v[142:145], v[186:189], v[106:109]
	s_waitcnt lgkmcnt(0)
	v_mfma_f32_16x16x32_bf16 v[102:105], v[138:141], v[190:193], v[102:105]
	v_mfma_f32_16x16x32_bf16 v[98:101], v[142:145], v[190:193], v[98:101]
	s_setprio 0
	s_setprio 1
	v_mfma_f32_16x16x32_bf16 v[94:97], v[146:149], v[162:165], v[94:97]
	v_mfma_f32_16x16x32_bf16 v[90:93], v[150:153], v[162:165], v[90:93]
	v_mfma_f32_16x16x32_bf16 v[86:89], v[146:149], v[166:169], v[86:89]
	v_mfma_f32_16x16x32_bf16 v[82:85], v[150:153], v[166:169], v[82:85]
	v_mfma_f32_16x16x32_bf16 v[78:81], v[146:149], v[178:181], v[78:81]
	v_mfma_f32_16x16x32_bf16 v[74:77], v[150:153], v[178:181], v[74:77]
	v_mfma_f32_16x16x32_bf16 v[70:73], v[146:149], v[182:185], v[70:73]
	v_mfma_f32_16x16x32_bf16 v[66:69], v[150:153], v[182:185], v[66:69]
	v_mfma_f32_16x16x32_bf16 v[94:97], v[154:157], v[170:173], v[94:97]
	v_mfma_f32_16x16x32_bf16 v[90:93], v[158:161], v[170:173], v[90:93]
	v_mfma_f32_16x16x32_bf16 v[86:89], v[154:157], v[174:177], v[86:89]
	v_mfma_f32_16x16x32_bf16 v[82:85], v[158:161], v[174:177], v[82:85]
	v_mfma_f32_16x16x32_bf16 v[78:81], v[154:157], v[186:189], v[78:81]
	v_mfma_f32_16x16x32_bf16 v[74:77], v[158:161], v[186:189], v[74:77]
	v_mfma_f32_16x16x32_bf16 v[70:73], v[154:157], v[190:193], v[70:73]
	v_mfma_f32_16x16x32_bf16 v[66:69], v[158:161], v[190:193], v[66:69]
	s_setprio 0
	s_barrier
	s_add_u32 s51, s10, s4
	s_addc_u32 s53, s11, s5
	ds_read_b128 v[162:165], v223 offset:16384
	ds_read_b128 v[166:169], v223 offset:18432
	ds_read_b128 v[170:173], v224 offset:16384
	ds_read_b128 v[174:177], v224 offset:18432
	ds_read_b128 v[178:181], v223 offset:20480
	ds_read_b128 v[182:185], v223 offset:22528
	ds_read_b128 v[186:189], v224 offset:20480
	ds_read_b128 v[190:193], v224 offset:22528
	s_add_u32 s54, s51, 0x100
	s_addc_u32 s55, s53, 0
	s_mov_b32 m0, s57
	s_nop 0
	global_load_lds_dwordx4 v215, s[54:55] offset:0
	s_nop 0
	s_mov_b32 m0, s58
	s_nop 0
	global_load_lds_dwordx4 v216, s[54:55] offset:0
	s_add_u32 s54, s51, 0x40100
	s_addc_u32 s55, s53, 0
	s_mov_b32 m0, s59
	s_nop 0
	global_load_lds_dwordx4 v215, s[54:55] offset:0
	s_nop 0
	s_mov_b32 m0, s60
	s_nop 0
	global_load_lds_dwordx4 v216, s[54:55] offset:0
	s_add_u32 s54, s47, 0x100
	s_addc_u32 s55, s50, 0
	s_mov_b32 m0, s56
	s_nop 0
	global_load_lds_dwordx4 v211, s[54:55] offset:0
	s_nop 0
	s_mov_b32 m0, s61
	s_nop 0
	global_load_lds_dwordx4 v213, s[54:55] offset:0
	s_waitcnt vmcnt(8)
	s_waitcnt lgkmcnt(0)
	s_barrier
	s_setprio 1
	s_waitcnt lgkmcnt(7)
	v_mfma_f32_16x16x32_bf16 v[62:65], v[130:133], v[162:165], v[62:65]
	v_mfma_f32_16x16x32_bf16 v[58:61], v[134:137], v[162:165], v[58:61]
	s_waitcnt lgkmcnt(6)
	v_mfma_f32_16x16x32_bf16 v[54:57], v[130:133], v[166:169], v[54:57]
	v_mfma_f32_16x16x32_bf16 v[50:53], v[134:137], v[166:169], v[50:53]
	s_waitcnt lgkmcnt(3)
	v_mfma_f32_16x16x32_bf16 v[46:49], v[130:133], v[178:181], v[46:49]
	v_mfma_f32_16x16x32_bf16 v[42:45], v[134:137], v[178:181], v[42:45]
	s_waitcnt lgkmcnt(2)
	v_mfma_f32_16x16x32_bf16 v[38:41], v[130:133], v[182:185], v[38:41]
	v_mfma_f32_16x16x32_bf16 v[34:37], v[134:137], v[182:185], v[34:37]
	v_mfma_f32_16x16x32_bf16 v[62:65], v[138:141], v[170:173], v[62:65]
	v_mfma_f32_16x16x32_bf16 v[58:61], v[142:145], v[170:173], v[58:61]
	v_mfma_f32_16x16x32_bf16 v[54:57], v[138:141], v[174:177], v[54:57]
	v_mfma_f32_16x16x32_bf16 v[50:53], v[142:145], v[174:177], v[50:53]
	s_waitcnt lgkmcnt(1)
	v_mfma_f32_16x16x32_bf16 v[46:49], v[138:141], v[186:189], v[46:49]
	v_mfma_f32_16x16x32_bf16 v[42:45], v[142:145], v[186:189], v[42:45]
	s_waitcnt lgkmcnt(0)
	v_mfma_f32_16x16x32_bf16 v[38:41], v[138:141], v[190:193], v[38:41]
	v_mfma_f32_16x16x32_bf16 v[34:37], v[142:145], v[190:193], v[34:37]
	s_setprio 0
	s_setprio 1
	v_mfma_f32_16x16x32_bf16 v[30:33], v[146:149], v[162:165], v[30:33]
	v_mfma_f32_16x16x32_bf16 v[26:29], v[150:153], v[162:165], v[26:29]
	v_mfma_f32_16x16x32_bf16 v[22:25], v[146:149], v[166:169], v[22:25]
	v_mfma_f32_16x16x32_bf16 v[18:21], v[150:153], v[166:169], v[18:21]
	v_mfma_f32_16x16x32_bf16 v[14:17], v[146:149], v[178:181], v[14:17]
	v_mfma_f32_16x16x32_bf16 v[10:13], v[150:153], v[178:181], v[10:13]
	v_mfma_f32_16x16x32_bf16 v[6:9], v[146:149], v[182:185], v[6:9]
	v_mfma_f32_16x16x32_bf16 v[2:5], v[150:153], v[182:185], v[2:5]
	v_mfma_f32_16x16x32_bf16 v[30:33], v[154:157], v[170:173], v[30:33]
	v_mfma_f32_16x16x32_bf16 v[26:29], v[158:161], v[170:173], v[26:29]
	v_mfma_f32_16x16x32_bf16 v[22:25], v[154:157], v[174:177], v[22:25]
	v_mfma_f32_16x16x32_bf16 v[18:21], v[158:161], v[174:177], v[18:21]
	v_mfma_f32_16x16x32_bf16 v[14:17], v[154:157], v[186:189], v[14:17]
	v_mfma_f32_16x16x32_bf16 v[10:13], v[158:161], v[186:189], v[10:13]
	v_mfma_f32_16x16x32_bf16 v[6:9], v[154:157], v[190:193], v[6:9]
	v_mfma_f32_16x16x32_bf16 v[2:5], v[158:161], v[190:193], v[2:5]
	s_setprio 0
	s_barrier
	s_add_i32 s78, 0, 0x18000
	v_add_u32_e32 v162, s78, v217
	v_add_u32_e32 v163, s78, v218
	s_add_i32 s78, 0, 0x1c000
	v_add_u32_e32 v164, s78, v217
	ds_read_b128 v[130:133], v162
	ds_read_b128 v[134:137], v162 offset:2048
	ds_read_b128 v[138:141], v163
	ds_read_b128 v[142:145], v163 offset:2048
	v_add_u32_e32 v165, s78, v218
	ds_read_b128 v[146:149], v164
	ds_read_b128 v[150:153], v164 offset:2048
	ds_read_b128 v[154:157], v165
	ds_read_b128 v[158:161], v165 offset:2048
	ds_read_b128 v[166:169], v223 offset:32768
	ds_read_b128 v[170:173], v223 offset:34816
	ds_read_b128 v[174:177], v224 offset:32768
	ds_read_b128 v[178:181], v224 offset:34816
	ds_read_b128 v[182:185], v223 offset:36864
	ds_read_b128 v[186:189], v223 offset:38912
	ds_read_b128 v[190:193], v224 offset:36864
	ds_read_b128 v[198:201], v224 offset:38912
	s_mov_b32 m0, s62
	s_nop 0
	global_load_lds_dwordx4 v212, s[54:55] offset:0
	s_nop 0
	s_mov_b32 m0, s63
	s_nop 0
	global_load_lds_dwordx4 v214, s[54:55] offset:0
	s_waitcnt vmcnt(8)
	s_waitcnt lgkmcnt(0)
	s_barrier
	s_setprio 1
	s_waitcnt lgkmcnt(7)
	v_mfma_f32_16x16x32_bf16 v[126:129], v[130:133], v[166:169], v[126:129]
	v_mfma_f32_16x16x32_bf16 v[122:125], v[134:137], v[166:169], v[122:125]
	s_waitcnt lgkmcnt(6)
	v_mfma_f32_16x16x32_bf16 v[118:121], v[130:133], v[170:173], v[118:121]
	v_mfma_f32_16x16x32_bf16 v[114:117], v[134:137], v[170:173], v[114:117]
	s_waitcnt lgkmcnt(3)
	v_mfma_f32_16x16x32_bf16 v[110:113], v[130:133], v[182:185], v[110:113]
	v_mfma_f32_16x16x32_bf16 v[106:109], v[134:137], v[182:185], v[106:109]
	s_waitcnt lgkmcnt(2)
	v_mfma_f32_16x16x32_bf16 v[102:105], v[130:133], v[186:189], v[102:105]
	v_mfma_f32_16x16x32_bf16 v[98:101], v[134:137], v[186:189], v[98:101]
	v_mfma_f32_16x16x32_bf16 v[126:129], v[138:141], v[174:177], v[126:129]
	v_mfma_f32_16x16x32_bf16 v[122:125], v[142:145], v[174:177], v[122:125]
	v_mfma_f32_16x16x32_bf16 v[118:121], v[138:141], v[178:181], v[118:121]
	v_mfma_f32_16x16x32_bf16 v[114:117], v[142:145], v[178:181], v[114:117]
	s_waitcnt lgkmcnt(1)
	v_mfma_f32_16x16x32_bf16 v[110:113], v[138:141], v[190:193], v[110:113]
	v_mfma_f32_16x16x32_bf16 v[106:109], v[142:145], v[190:193], v[106:109]
	s_waitcnt lgkmcnt(0)
	v_mfma_f32_16x16x32_bf16 v[102:105], v[138:141], v[198:201], v[102:105]
	v_mfma_f32_16x16x32_bf16 v[98:101], v[142:145], v[198:201], v[98:101]
	s_setprio 0
	s_setprio 1
	v_mfma_f32_16x16x32_bf16 v[94:97], v[146:149], v[166:169], v[94:97]
	v_mfma_f32_16x16x32_bf16 v[90:93], v[150:153], v[166:169], v[90:93]
	v_mfma_f32_16x16x32_bf16 v[86:89], v[146:149], v[170:173], v[86:89]
	v_mfma_f32_16x16x32_bf16 v[82:85], v[150:153], v[170:173], v[82:85]
	v_mfma_f32_16x16x32_bf16 v[78:81], v[146:149], v[182:185], v[78:81]
	v_mfma_f32_16x16x32_bf16 v[74:77], v[150:153], v[182:185], v[74:77]
	v_mfma_f32_16x16x32_bf16 v[70:73], v[146:149], v[186:189], v[70:73]
	v_mfma_f32_16x16x32_bf16 v[66:69], v[150:153], v[186:189], v[66:69]
	v_mfma_f32_16x16x32_bf16 v[94:97], v[154:157], v[174:177], v[94:97]
	v_mfma_f32_16x16x32_bf16 v[90:93], v[158:161], v[174:177], v[90:93]
	v_mfma_f32_16x16x32_bf16 v[86:89], v[154:157], v[178:181], v[86:89]
	v_mfma_f32_16x16x32_bf16 v[82:85], v[158:161], v[178:181], v[82:85]
	v_mfma_f32_16x16x32_bf16 v[78:81], v[154:157], v[190:193], v[78:81]
	v_mfma_f32_16x16x32_bf16 v[74:77], v[158:161], v[190:193], v[74:77]
	v_mfma_f32_16x16x32_bf16 v[70:73], v[154:157], v[198:201], v[70:73]
	v_mfma_f32_16x16x32_bf16 v[66:69], v[158:161], v[198:201], v[66:69]
	s_setprio 0
	s_barrier
	ds_read_b128 v[166:169], v223 offset:49152
	ds_read_b128 v[170:173], v223 offset:51200
	ds_read_b128 v[174:177], v224 offset:49152
	ds_read_b128 v[178:181], v224 offset:51200
	ds_read_b128 v[182:185], v223 offset:53248
	ds_read_b128 v[186:189], v223 offset:55296
	ds_read_b128 v[190:193], v224 offset:53248
	ds_read_b128 v[198:201], v224 offset:55296
	s_add_u32 s54, s51, 0x180
	s_addc_u32 s55, s53, 0
	s_mov_b32 m0, s64
	s_nop 0
	global_load_lds_dwordx4 v215, s[54:55] offset:0
	s_nop 0
	s_mov_b32 m0, s65
	s_nop 0
	global_load_lds_dwordx4 v216, s[54:55] offset:0
	s_add_u32 s54, s51, 0x40180
	s_addc_u32 s55, s53, 0
	s_mov_b32 m0, s68
	s_nop 0
	global_load_lds_dwordx4 v215, s[54:55] offset:0
	s_nop 0
	s_mov_b32 m0, s69
	s_nop 0
	global_load_lds_dwordx4 v216, s[54:55] offset:0
	s_add_u32 s54, s47, 0x180
	s_addc_u32 s55, s50, 0
	s_mov_b32 m0, s66
	s_nop 0
	global_load_lds_dwordx4 v211, s[54:55] offset:0
	s_nop 0
	s_mov_b32 m0, s67
	s_nop 0
	global_load_lds_dwordx4 v213, s[54:55] offset:0
	s_waitcnt vmcnt(8)
	s_waitcnt lgkmcnt(0)
	s_barrier
	s_setprio 1
	s_waitcnt lgkmcnt(7)
	v_mfma_f32_16x16x32_bf16 v[62:65], v[130:133], v[166:169], v[62:65]
	v_mfma_f32_16x16x32_bf16 v[58:61], v[134:137], v[166:169], v[58:61]
	s_waitcnt lgkmcnt(6)
	v_mfma_f32_16x16x32_bf16 v[54:57], v[130:133], v[170:173], v[54:57]
	v_mfma_f32_16x16x32_bf16 v[50:53], v[134:137], v[170:173], v[50:53]
	s_waitcnt lgkmcnt(3)
	v_mfma_f32_16x16x32_bf16 v[46:49], v[130:133], v[182:185], v[46:49]
	v_mfma_f32_16x16x32_bf16 v[42:45], v[134:137], v[182:185], v[42:45]
	s_waitcnt lgkmcnt(2)
	v_mfma_f32_16x16x32_bf16 v[38:41], v[130:133], v[186:189], v[38:41]
	v_mfma_f32_16x16x32_bf16 v[34:37], v[134:137], v[186:189], v[34:37]
	v_mfma_f32_16x16x32_bf16 v[62:65], v[138:141], v[174:177], v[62:65]
	v_mfma_f32_16x16x32_bf16 v[58:61], v[142:145], v[174:177], v[58:61]
	v_mfma_f32_16x16x32_bf16 v[54:57], v[138:141], v[178:181], v[54:57]
	v_mfma_f32_16x16x32_bf16 v[50:53], v[142:145], v[178:181], v[50:53]
	s_waitcnt lgkmcnt(1)
	v_mfma_f32_16x16x32_bf16 v[46:49], v[138:141], v[190:193], v[46:49]
	v_mfma_f32_16x16x32_bf16 v[42:45], v[142:145], v[190:193], v[42:45]
	s_waitcnt lgkmcnt(0)
	v_mfma_f32_16x16x32_bf16 v[38:41], v[138:141], v[198:201], v[38:41]
	v_mfma_f32_16x16x32_bf16 v[34:37], v[142:145], v[198:201], v[34:37]
	s_setprio 0
	s_setprio 1
	v_mfma_f32_16x16x32_bf16 v[30:33], v[146:149], v[166:169], v[30:33]
	v_mfma_f32_16x16x32_bf16 v[26:29], v[150:153], v[166:169], v[26:29]
	v_mfma_f32_16x16x32_bf16 v[22:25], v[146:149], v[170:173], v[22:25]
	v_mfma_f32_16x16x32_bf16 v[18:21], v[150:153], v[170:173], v[18:21]
	v_mfma_f32_16x16x32_bf16 v[14:17], v[146:149], v[182:185], v[14:17]
	v_mfma_f32_16x16x32_bf16 v[10:13], v[150:153], v[182:185], v[10:13]
	v_mfma_f32_16x16x32_bf16 v[6:9], v[146:149], v[186:189], v[6:9]
	v_mfma_f32_16x16x32_bf16 v[2:5], v[150:153], v[186:189], v[2:5]
	v_mfma_f32_16x16x32_bf16 v[30:33], v[154:157], v[174:177], v[30:33]
	v_mfma_f32_16x16x32_bf16 v[26:29], v[158:161], v[174:177], v[26:29]
	v_mfma_f32_16x16x32_bf16 v[22:25], v[154:157], v[178:181], v[22:25]
	v_mfma_f32_16x16x32_bf16 v[18:21], v[158:161], v[178:181], v[18:21]
	v_mfma_f32_16x16x32_bf16 v[14:17], v[154:157], v[190:193], v[14:17]
	v_mfma_f32_16x16x32_bf16 v[10:13], v[158:161], v[190:193], v[10:13]
	v_mfma_f32_16x16x32_bf16 v[6:9], v[154:157], v[198:201], v[6:9]
	v_mfma_f32_16x16x32_bf16 v[2:5], v[158:161], v[198:201], v[2:5]
	s_setprio 0
	s_barrier
	s_add_i32 s9, s9, 2
	s_add_u32 s4, s4, 0x100
	s_addc_u32 s5, s5, 0
	s_cmp_lt_u32 s9, 12
	s_cbranch_scc1 .LBB0_126
	ds_read_b128 v[146:149], v219
	ds_read_b128 v[150:153], v219 offset:2048
	ds_read_b128 v[158:161], v220
	ds_read_b128 v[154:157], v220 offset:2048
	ds_read_b128 v[130:133], v221
	ds_read_b128 v[134:137], v221 offset:2048
	ds_read_b128 v[142:145], v222
	ds_read_b128 v[138:141], v222 offset:2048
	ds_read_b128 v[166:169], v223
	ds_read_b128 v[170:173], v223 offset:2048
	ds_read_b128 v[174:177], v224
	ds_read_b128 v[178:181], v224 offset:2048
	ds_read_b128 v[182:185], v223 offset:4096
	ds_read_b128 v[186:189], v223 offset:6144
	ds_read_b128 v[190:193], v224 offset:4096
	ds_read_b128 v[198:201], v224 offset:6144
	s_mov_b32 m0, s70
	s_nop 0
	global_load_lds_dwordx4 v212, s[24:25] offset:0
	s_nop 0
	s_mov_b32 m0, s71
	s_nop 0
	global_load_lds_dwordx4 v214, s[24:25] offset:0
	s_waitcnt vmcnt(8)
	s_waitcnt lgkmcnt(0)
	s_barrier
	s_setprio 1
	s_waitcnt lgkmcnt(7)
	v_mfma_f32_16x16x32_bf16 v[126:129], v[146:149], v[166:169], v[126:129]
	v_mfma_f32_16x16x32_bf16 v[122:125], v[150:153], v[166:169], v[122:125]
	s_waitcnt lgkmcnt(6)
	v_mfma_f32_16x16x32_bf16 v[118:121], v[146:149], v[170:173], v[118:121]
	v_mfma_f32_16x16x32_bf16 v[114:117], v[150:153], v[170:173], v[114:117]
	s_waitcnt lgkmcnt(3)
	v_mfma_f32_16x16x32_bf16 v[110:113], v[146:149], v[182:185], v[110:113]
	v_mfma_f32_16x16x32_bf16 v[106:109], v[150:153], v[182:185], v[106:109]
	s_waitcnt lgkmcnt(2)
	v_mfma_f32_16x16x32_bf16 v[102:105], v[146:149], v[186:189], v[102:105]
	v_mfma_f32_16x16x32_bf16 v[98:101], v[150:153], v[186:189], v[98:101]
	v_mfma_f32_16x16x32_bf16 v[126:129], v[158:161], v[174:177], v[126:129]
	v_mfma_f32_16x16x32_bf16 v[122:125], v[154:157], v[174:177], v[122:125]
	v_mfma_f32_16x16x32_bf16 v[118:121], v[158:161], v[178:181], v[118:121]
	v_mfma_f32_16x16x32_bf16 v[114:117], v[154:157], v[178:181], v[114:117]
	s_waitcnt lgkmcnt(1)
	v_mfma_f32_16x16x32_bf16 v[110:113], v[158:161], v[190:193], v[110:113]
	v_mfma_f32_16x16x32_bf16 v[106:109], v[154:157], v[190:193], v[106:109]
	s_waitcnt lgkmcnt(0)
	v_mfma_f32_16x16x32_bf16 v[102:105], v[158:161], v[198:201], v[102:105]
	v_mfma_f32_16x16x32_bf16 v[98:101], v[154:157], v[198:201], v[98:101]
	s_setprio 0
	s_setprio 1
	v_mfma_f32_16x16x32_bf16 v[94:97], v[130:133], v[166:169], v[94:97]
	v_mfma_f32_16x16x32_bf16 v[90:93], v[134:137], v[166:169], v[90:93]
	v_mfma_f32_16x16x32_bf16 v[86:89], v[130:133], v[170:173], v[86:89]
	v_mfma_f32_16x16x32_bf16 v[82:85], v[134:137], v[170:173], v[82:85]
	v_mfma_f32_16x16x32_bf16 v[78:81], v[130:133], v[182:185], v[78:81]
	v_mfma_f32_16x16x32_bf16 v[74:77], v[134:137], v[182:185], v[74:77]
	v_mfma_f32_16x16x32_bf16 v[70:73], v[130:133], v[186:189], v[70:73]
	v_mfma_f32_16x16x32_bf16 v[66:69], v[134:137], v[186:189], v[66:69]
	v_mfma_f32_16x16x32_bf16 v[94:97], v[142:145], v[174:177], v[94:97]
	v_mfma_f32_16x16x32_bf16 v[90:93], v[138:141], v[174:177], v[90:93]
	v_mfma_f32_16x16x32_bf16 v[86:89], v[142:145], v[178:181], v[86:89]
	v_mfma_f32_16x16x32_bf16 v[82:85], v[138:141], v[178:181], v[82:85]
	v_mfma_f32_16x16x32_bf16 v[78:81], v[142:145], v[190:193], v[78:81]
	v_mfma_f32_16x16x32_bf16 v[74:77], v[138:141], v[190:193], v[74:77]
	v_mfma_f32_16x16x32_bf16 v[70:73], v[142:145], v[198:201], v[70:73]
	v_mfma_f32_16x16x32_bf16 v[66:69], v[138:141], v[198:201], v[66:69]
	s_setprio 0
	s_barrier
	v_cndmask_b32_e64 v166, 0, 1, s[6:7]
	v_cmp_ne_u32_e64 s[4:5], 1, v166
	s_andn2_b64 vcc, exec, s[6:7]
	s_cbranch_vccnz .LBB0_129
	v_mov_b32_e32 v166, v0
	s_nop 0
	v_lshlrev_b32_e32 v167, 4, v166
	v_bitop3_b32 v167, v167, s2, v166 bitop3:0x48
	v_lshlrev_b32_e32 v166, 8, v166
	v_lshl_or_b32 v167, s48, 19, v167
	v_and_b32_e32 v166, 0xfffff800, v166
	v_add_u32_e32 v211, v167, v166
	v_add_u32_e32 v212, 0x40000, v211
	v_add_u32_e32 v213, 0x20000, v211
	v_add_u32_e32 v214, 0x60000, v211
.LBB0_129:
	s_ashr_i32 s47, s46, 31
	s_lshl_b64 s[50:51], s[46:47], 19
	s_add_u32 s50, s3, s50
	s_addc_u32 s51, s33, s51
	s_and_b64 s[6:7], s[6:7], exec
	ds_read_b128 v[166:169], v223 offset:16384
	ds_read_b128 v[170:173], v223 offset:18432
	ds_read_b128 v[174:177], v224 offset:16384
	ds_read_b128 v[178:181], v224 offset:18432
	ds_read_b128 v[182:185], v223 offset:20480
	ds_read_b128 v[186:189], v223 offset:22528
	ds_read_b128 v[190:193], v224 offset:20480
	ds_read_b128 v[198:201], v224 offset:22528
	s_cselect_b32 s7, s51, s11
	s_cselect_b32 s6, s50, s10
	s_mov_b32 m0, s57
	s_nop 0
	global_load_lds_dwordx4 v215, s[6:7] offset:0
	s_add_u32 s10, s6, 0x40000
	s_mov_b32 m0, s58
	s_nop 0
	global_load_lds_dwordx4 v216, s[6:7] offset:0
	s_addc_u32 s11, s7, 0
	s_mov_b32 m0, s59
	s_nop 0
	global_load_lds_dwordx4 v215, s[10:11] offset:0
	s_nop 0
	s_mov_b32 m0, s60
	s_nop 0
	global_load_lds_dwordx4 v216, s[10:11] offset:0
	s_nop 0
	s_mov_b32 m0, s56
	s_nop 0
	global_load_lds_dwordx4 v211, s[14:15] offset:0
	s_nop 0
	s_mov_b32 m0, s61
	s_nop 0
	global_load_lds_dwordx4 v213, s[14:15] offset:0
	s_waitcnt vmcnt(8)
	s_waitcnt lgkmcnt(0)
	s_barrier
	s_setprio 1
	s_waitcnt lgkmcnt(6)
	v_mfma_f32_16x16x32_bf16 v[54:57], v[146:149], v[170:173], v[54:57]
	v_mfma_f32_16x16x32_bf16 v[50:53], v[150:153], v[170:173], v[50:53]
	v_mfma_f32_16x16x32_bf16 v[62:65], v[146:149], v[166:169], v[62:65]
	v_mfma_f32_16x16x32_bf16 v[58:61], v[150:153], v[166:169], v[58:61]
	s_waitcnt lgkmcnt(4)
	v_mfma_f32_16x16x32_bf16 v[54:57], v[158:161], v[178:181], v[54:57]
	v_mfma_f32_16x16x32_bf16 v[50:53], v[154:157], v[178:181], v[50:53]
	s_waitcnt lgkmcnt(3)
	v_mfma_f32_16x16x32_bf16 v[46:49], v[146:149], v[182:185], v[46:49]
	v_mfma_f32_16x16x32_bf16 v[42:45], v[150:153], v[182:185], v[42:45]
	s_waitcnt lgkmcnt(2)
	v_mfma_f32_16x16x32_bf16 v[38:41], v[146:149], v[186:189], v[38:41]
	v_mfma_f32_16x16x32_bf16 v[34:37], v[150:153], v[186:189], v[34:37]
	v_mfma_f32_16x16x32_bf16 v[62:65], v[158:161], v[174:177], v[62:65]
	v_mfma_f32_16x16x32_bf16 v[58:61], v[154:157], v[174:177], v[58:61]
	s_waitcnt lgkmcnt(1)
	v_mfma_f32_16x16x32_bf16 v[46:49], v[158:161], v[190:193], v[46:49]
	v_mfma_f32_16x16x32_bf16 v[42:45], v[154:157], v[190:193], v[42:45]
	s_waitcnt lgkmcnt(0)
	v_mfma_f32_16x16x32_bf16 v[202:205], v[158:161], v[198:201], v[38:41]
	v_mfma_f32_16x16x32_bf16 v[34:37], v[154:157], v[198:201], v[34:37]
	s_setprio 0
	s_setprio 1
	v_mfma_f32_16x16x32_bf16 v[22:25], v[130:133], v[170:173], v[22:25]
	v_mfma_f32_16x16x32_bf16 v[18:21], v[134:137], v[170:173], v[18:21]
	v_mfma_f32_16x16x32_bf16 v[6:9], v[130:133], v[186:189], v[6:9]
	v_mfma_f32_16x16x32_bf16 v[30:33], v[130:133], v[166:169], v[30:33]
	v_mfma_f32_16x16x32_bf16 v[26:29], v[134:137], v[166:169], v[26:29]
	v_mfma_f32_16x16x32_bf16 v[22:25], v[142:145], v[178:181], v[22:25]
	v_mfma_f32_16x16x32_bf16 v[18:21], v[138:141], v[178:181], v[18:21]
	v_mfma_f32_16x16x32_bf16 v[14:17], v[130:133], v[182:185], v[14:17]
	v_mfma_f32_16x16x32_bf16 v[10:13], v[134:137], v[182:185], v[10:13]
	v_mfma_f32_16x16x32_bf16 v[6:9], v[142:145], v[198:201], v[6:9]
	v_mfma_f32_16x16x32_bf16 v[2:5], v[134:137], v[186:189], v[2:5]
	v_mfma_f32_16x16x32_bf16 v[206:209], v[142:145], v[174:177], v[30:33]
	v_mfma_f32_16x16x32_bf16 v[26:29], v[138:141], v[174:177], v[26:29]
	v_mfma_f32_16x16x32_bf16 v[226:229], v[142:145], v[190:193], v[14:17]
	v_mfma_f32_16x16x32_bf16 v[230:233], v[138:141], v[190:193], v[10:13]
	v_mfma_f32_16x16x32_bf16 v[198:201], v[138:141], v[198:201], v[2:5]
	s_setprio 0
	s_barrier
	s_nop 0
	ds_read_b128 v[2:5], v162
	ds_read_b128 v[10:13], v162 offset:2048
	ds_read_b128 v[14:17], v163
	ds_read_b128 v[234:237], v163 offset:2048
	ds_read_b128 v[238:241], v164
	ds_read_b128 v[242:245], v164 offset:2048
	ds_read_b128 v[246:249], v165
	ds_read_b128 v[250:253], v165 offset:2048
	ds_read_b128 v[30:33], v223 offset:32768
	ds_read_b128 v[38:41], v223 offset:34816
	ds_read_b128 v[130:133], v224 offset:32768
	ds_read_b128 v[134:137], v224 offset:34816
	ds_read_b128 v[146:149], v223 offset:36864
	ds_read_b128 v[194:197], v223 offset:38912
	ds_read_b128 v[138:141], v224 offset:36864
	ds_read_b128 v[142:145], v224 offset:38912
	s_mov_b32 m0, s62
	s_nop 0
	global_load_lds_dwordx4 v212, s[14:15] offset:0
	s_nop 0
	s_mov_b32 m0, s63
	s_nop 0
	global_load_lds_dwordx4 v214, s[14:15] offset:0
	s_waitcnt vmcnt(8)
	s_waitcnt lgkmcnt(0)
	s_barrier
	s_setprio 1
	s_waitcnt lgkmcnt(7)
	v_mfma_f32_16x16x32_bf16 v[126:129], v[2:5], v[30:33], v[126:129]
	v_mfma_f32_16x16x32_bf16 v[122:125], v[10:13], v[30:33], v[122:125]
	s_waitcnt lgkmcnt(6)
	v_mfma_f32_16x16x32_bf16 v[118:121], v[2:5], v[38:41], v[118:121]
	v_mfma_f32_16x16x32_bf16 v[114:117], v[10:13], v[38:41], v[114:117]
	s_waitcnt lgkmcnt(3)
	v_mfma_f32_16x16x32_bf16 v[110:113], v[2:5], v[146:149], v[110:113]
	v_mfma_f32_16x16x32_bf16 v[106:109], v[10:13], v[146:149], v[106:109]
	s_waitcnt lgkmcnt(2)
	v_mfma_f32_16x16x32_bf16 v[102:105], v[2:5], v[194:197], v[102:105]
	v_mfma_f32_16x16x32_bf16 v[98:101], v[10:13], v[194:197], v[98:101]
	v_mfma_f32_16x16x32_bf16 v[190:193], v[14:17], v[130:133], v[126:129]
	v_mfma_f32_16x16x32_bf16 v[186:189], v[234:237], v[130:133], v[122:125]
	v_mfma_f32_16x16x32_bf16 v[174:177], v[14:17], v[134:137], v[118:121]
	v_mfma_f32_16x16x32_bf16 v[170:173], v[234:237], v[134:137], v[114:117]
	s_waitcnt lgkmcnt(1)
	v_mfma_f32_16x16x32_bf16 v[158:161], v[14:17], v[138:141], v[110:113]
	v_mfma_f32_16x16x32_bf16 v[154:157], v[234:237], v[138:141], v[106:109]
	s_waitcnt lgkmcnt(0)
	v_mfma_f32_16x16x32_bf16 v[102:105], v[14:17], v[142:145], v[102:105]
	v_mfma_f32_16x16x32_bf16 v[98:101], v[234:237], v[142:145], v[98:101]
	s_setprio 0
	s_setprio 1
	v_mfma_f32_16x16x32_bf16 v[94:97], v[238:241], v[30:33], v[94:97]
	v_mfma_f32_16x16x32_bf16 v[30:33], v[242:245], v[30:33], v[90:93]
	v_mfma_f32_16x16x32_bf16 v[178:181], v[250:253], v[130:133], v[30:33]
	v_mfma_f32_16x16x32_bf16 v[30:33], v[238:241], v[38:41], v[86:89]
	v_mfma_f32_16x16x32_bf16 v[166:169], v[246:249], v[134:137], v[30:33]
	v_mfma_f32_16x16x32_bf16 v[30:33], v[242:245], v[38:41], v[82:85]
	v_mfma_f32_16x16x32_bf16 v[162:165], v[250:253], v[134:137], v[30:33]
	v_mfma_f32_16x16x32_bf16 v[30:33], v[238:241], v[146:149], v[78:81]
	v_mfma_f32_16x16x32_bf16 v[150:153], v[246:249], v[138:141], v[30:33]
	v_mfma_f32_16x16x32_bf16 v[30:33], v[242:245], v[146:149], v[74:77]
	v_mfma_f32_16x16x32_bf16 v[146:149], v[250:253], v[138:141], v[30:33]
	v_mfma_f32_16x16x32_bf16 v[30:33], v[238:241], v[194:197], v[70:73]
	v_mfma_f32_16x16x32_bf16 v[134:137], v[246:249], v[142:145], v[30:33]
	v_mfma_f32_16x16x32_bf16 v[30:33], v[242:245], v[194:197], v[66:69]
	v_mfma_f32_16x16x32_bf16 v[182:185], v[246:249], v[130:133], v[94:97]
	v_mfma_f32_16x16x32_bf16 v[130:133], v[250:253], v[142:145], v[30:33]
	s_setprio 0
	s_barrier
	ds_read_b128 v[66:69], v223 offset:49152
	ds_read_b128 v[70:73], v223 offset:51200
	ds_read_b128 v[82:85], v224 offset:49152
	ds_read_b128 v[86:89], v224 offset:51200
	ds_read_b128 v[94:97], v223 offset:53248
	ds_read_b128 v[114:117], v223 offset:55296
	ds_read_b128 v[118:121], v224 offset:53248
	ds_read_b128 v[122:125], v224 offset:55296
	s_add_u32 s10, s6, 0x80
	s_addc_u32 s11, s7, 0
	s_mov_b32 m0, s64
	s_nop 0
	global_load_lds_dwordx4 v215, s[10:11] offset:0
	s_add_u32 s6, s6, 0x40080
	s_mov_b32 m0, s65
	s_nop 0
	global_load_lds_dwordx4 v216, s[10:11] offset:0
	s_addc_u32 s7, s7, 0
	s_mov_b32 m0, s68
	s_nop 0
	global_load_lds_dwordx4 v215, s[6:7] offset:0
	s_nop 0
	s_mov_b32 m0, s69
	s_nop 0
	global_load_lds_dwordx4 v216, s[6:7] offset:0
	s_mov_b32 m0, s66
	s_nop 0
	global_load_lds_dwordx4 v211, s[22:23] offset:0
	s_nop 0
	s_mov_b32 m0, s67
	s_nop 0
	global_load_lds_dwordx4 v213, s[22:23] offset:0
	s_waitcnt vmcnt(8)
	s_waitcnt lgkmcnt(0)
	s_barrier
	s_setprio 1
	s_waitcnt lgkmcnt(7)
	v_mfma_f32_16x16x32_bf16 v[30:33], v[2:5], v[66:69], v[62:65]
	s_waitcnt lgkmcnt(5)
	v_mfma_f32_16x16x32_bf16 v[106:109], v[14:17], v[82:85], v[30:33]
	v_mfma_f32_16x16x32_bf16 v[30:33], v[10:13], v[66:69], v[58:61]
	v_mfma_f32_16x16x32_bf16 v[110:113], v[234:237], v[82:85], v[30:33]
	v_mfma_f32_16x16x32_bf16 v[30:33], v[2:5], v[70:73], v[54:57]
	s_waitcnt lgkmcnt(4)
	v_mfma_f32_16x16x32_bf16 v[78:81], v[14:17], v[86:89], v[30:33]
	v_mfma_f32_16x16x32_bf16 v[30:33], v[10:13], v[70:73], v[50:53]
	v_mfma_f32_16x16x32_bf16 v[74:77], v[234:237], v[86:89], v[30:33]
	s_waitcnt lgkmcnt(3)
	v_mfma_f32_16x16x32_bf16 v[30:33], v[2:5], v[94:97], v[46:49]
	s_waitcnt lgkmcnt(2)
	v_mfma_f32_16x16x32_bf16 v[2:5], v[2:5], v[114:117], v[202:205]
	s_waitcnt lgkmcnt(1)
	v_mfma_f32_16x16x32_bf16 v[38:41], v[14:17], v[118:121], v[30:33]
	v_mfma_f32_16x16x32_bf16 v[30:33], v[10:13], v[94:97], v[42:45]
	s_waitcnt lgkmcnt(0)
	v_mfma_f32_16x16x32_bf16 v[14:17], v[14:17], v[122:125], v[2:5]
	v_mfma_f32_16x16x32_bf16 v[2:5], v[10:13], v[114:117], v[34:37]
	v_mfma_f32_16x16x32_bf16 v[30:33], v[234:237], v[118:121], v[30:33]
	v_mfma_f32_16x16x32_bf16 v[10:13], v[234:237], v[122:125], v[2:5]
	s_setprio 0
	s_setprio 1
	v_mfma_f32_16x16x32_bf16 v[2:5], v[238:241], v[66:69], v[206:209]
	v_mfma_f32_16x16x32_bf16 v[90:93], v[246:249], v[82:85], v[2:5]
	v_mfma_f32_16x16x32_bf16 v[2:5], v[242:245], v[66:69], v[26:29]
	v_mfma_f32_16x16x32_bf16 v[82:85], v[250:253], v[82:85], v[2:5]
	v_mfma_f32_16x16x32_bf16 v[2:5], v[238:241], v[70:73], v[22:25]
	v_mfma_f32_16x16x32_bf16 v[54:57], v[246:249], v[86:89], v[2:5]
	v_mfma_f32_16x16x32_bf16 v[2:5], v[242:245], v[70:73], v[18:21]
	v_mfma_f32_16x16x32_bf16 v[50:53], v[250:253], v[86:89], v[2:5]
	v_mfma_f32_16x16x32_bf16 v[2:5], v[238:241], v[94:97], v[226:229]
	v_mfma_f32_16x16x32_bf16 v[22:25], v[246:249], v[118:121], v[2:5]
	v_mfma_f32_16x16x32_bf16 v[2:5], v[242:245], v[94:97], v[230:233]
	v_mfma_f32_16x16x32_bf16 v[18:21], v[250:253], v[118:121], v[2:5]
	v_mfma_f32_16x16x32_bf16 v[2:5], v[238:241], v[114:117], v[6:9]
	v_mfma_f32_16x16x32_bf16 v[6:9], v[242:245], v[114:117], v[198:201]
	v_mfma_f32_16x16x32_bf16 v[2:5], v[246:249], v[122:125], v[2:5]
	v_mfma_f32_16x16x32_bf16 v[6:9], v[250:253], v[122:125], v[6:9]
	s_setprio 0
	s_barrier
	s_andn2_b64 vcc, exec, s[26:27]
	s_cbranch_vccnz .LBB0_131
	s_barrier

.LBB0_171:
	v_mov_b32_e32 v19, v18
	s_waitcnt lgkmcnt(2)
	v_mov_b32_e32 v20, v18
	s_waitcnt lgkmcnt(0)
	v_mov_b32_e32 v21, v18
	v_pk_mul_f32 v[22:23], v[8:9], v[20:21]
	v_pk_mul_f32 v[8:9], v[6:7], v[18:19]
	v_pk_mul_f32 v[20:21], v[4:5], v[20:21]
	v_pk_mul_f32 v[6:7], v[2:3], v[18:19]
	v_cvt_pk_bf16_f32 v2, v14, v15
	v_cvt_pk_bf16_f32 v3, v16, v17
	v_cvt_pk_bf16_f32 v4, v10, v11
	v_add_co_u32_e32 v10, vcc, 0xb0000, v30
	v_cvt_pk_bf16_f32 v5, v12, v13
	v_lshl_add_u64 v[18:19], v[30:31], 0, s[44:45]
	s_nop 0
	v_addc_co_u32_e32 v11, vcc, 0, v31, vcc
	s_and_b64 vcc, exec, s[4:5]
	s_mov_b64 s[4:5], -1
	v_cvt_pk_bf16_f32 v6, v6, v7
	v_cvt_pk_bf16_f32 v7, v20, v21
	v_cvt_pk_bf16_f32 v8, v8, v9
	v_cvt_pk_bf16_f32 v9, v22, v23
	global_store_dwordx4 v[10:11], v[2:5], off
	global_store_dwordx4 v[18:19], v[6:9], off offset:64
	s_cbranch_vccnz .LBB0_118
	s_andn2_b64 vcc, exec, s[12:13]
	s_cbranch_vccnz .LBB0_174
	s_ashr_i32 s49, s48, 31
	s_lshl_b64 s[4:5], s[48:49], 10
	s_add_u32 s4, s0, s4
	s_addc_u32 s5, s1, s5
	s_lshl_b32 s6, s77, 10
	s_and_b32 s6, s6, 0x400
	s_add_i32 s6, s6, 0
	s_add_i32 s6, s6, 0x24cc0
	s_mov_b32 m0, s6
	s_nop 0
	global_load_lds_dwordx4 v210, s[4:5] offset:0

.LBB0_230:
	s_load_dwordx2 s[0:1], s[12:13], 0x40
	v_writelane_b32 v254, s82, 6
	v_writelane_b32 v254, s80, 7
	s_add_u32 s9, s40, 0x25c00000
	s_waitcnt lgkmcnt(0)
	v_add_f32_e32 v6, v4, v5
	v_writelane_b32 v254, s81, 8
	v_writelane_b32 v254, s0, 9
	s_mov_b32 s2, 0x3fb8aa3b
	v_mul_f32_e32 v4, 0x3fb8aa3b, v6
	v_writelane_b32 v254, s1, 10
	v_writelane_b32 v254, s40, 11
	s_addc_u32 s10, s41, 0
	s_ashr_i32 s0, s3, 4
	s_ashr_i32 s1, s0, 31
	s_lshl_b32 s6, s3, 8
	s_lshl_b64 s[4:5], s[0:1], 11
	s_and_b32 s68, s6, 0x300
	s_or_b32 s4, s4, s68
	s_lshl_b64 s[6:7], s[4:5], 12
	s_add_u32 s6, s42, s6
	s_addc_u32 s7, s43, s7
	s_lshl_b32 s8, s3, 6
	s_and_b32 s8, s8, 0x300
	s_add_u32 s6, s6, s8
	s_addc_u32 s7, s7, 0
	s_add_u32 s12, s6, 0x80
	v_writelane_b32 v254, s41, 12
	s_addc_u32 s13, s7, 0
	v_writelane_b32 v254, s12, 13
	s_lshl_b64 s[0:1], s[0:1], 23
	s_add_u32 s0, s42, s0
	v_writelane_b32 v254, s13, 14
	v_writelane_b32 v254, s42, 15
	s_addc_u32 s1, s43, s1
	s_add_u32 s0, s0, s8
	s_addc_u32 s1, s1, 0
	s_add_u32 s90, s0, 0x480
	s_addc_u32 s91, s1, 0
	s_add_u32 s92, s0, 0x800
	s_addc_u32 s93, s1, 0
	s_lshl_b64 s[0:1], s[4:5], 11
	v_fma_f32 v5, v6, s2, -v4
	v_rndne_f32_e32 v7, v4
	v_writelane_b32 v254, s43, 16
	s_add_u32 s0, s9, s0
	v_fmac_f32_e32 v5, 0x32a5705f, v6
	v_sub_f32_e32 v4, v4, v7
	v_writelane_b32 v254, s9, 17
	s_addc_u32 s1, s10, s1
	v_mov_b32_e32 v9, v0
	v_add_f32_e32 v4, v4, v5
	v_writelane_b32 v254, s10, 18
	s_add_u32 s10, s0, s8
	v_exp_f32_e32 v8, v4
	v_readfirstlane_b32 s0, v9
	s_addc_u32 s11, s1, 0
	s_ashr_i32 s0, s0, 6
	v_and_b32_e32 v4, 31, v9
	v_lshl_or_b32 v4, s0, 5, v4
	v_ashrrev_i32_e32 v5, 31, v4
	v_lshlrev_b64 v[4:5], 12, v[4:5]
	v_lshrrev_b32_e32 v10, 1, v9
	v_lshl_add_u64 v[4:5], s[6:7], 0, v[4:5]
	v_and_b32_e32 v118, 16, v10
	v_mov_b32_e32 v119, 0
	v_lshl_add_u64 v[4:5], v[4:5], 0, v[118:119]
	global_load_dwordx4 v[110:113], v[4:5], off offset:128
	global_load_dwordx4 v[106:109], v[4:5], off offset:160
	global_load_dwordx4 v[102:105], v[4:5], off offset:192
	global_load_dwordx4 v[98:101], v[4:5], off offset:224
	v_cvt_i32_f32_e32 v7, v7
	v_add_f32_e32 v2, v2, v3
	v_mul_f32_e32 v3, 0x3fb8aa3b, v2
	v_fma_f32 v5, v2, s2, -v3
	v_ldexp_f32 v4, v8, v7
	v_rndne_f32_e32 v7, v3
	v_fmac_f32_e32 v5, 0x32a5705f, v2
	v_sub_f32_e32 v3, v3, v7
	v_add_f32_e32 v3, v3, v5
	v_exp_f32_e32 v3, v3
	v_cvt_i32_f32_e32 v5, v7
	s_mov_b32 s1, 0xc2ce8ed0
	v_cmp_ngt_f32_e32 vcc, s1, v6
	s_mov_b32 s4, 0x42b17218
	v_mov_b32_e32 v7, 0x7f800000
	v_cndmask_b32_e32 v4, 0, v4, vcc
	v_cmp_nlt_f32_e32 vcc, s4, v6
	v_ldexp_f32 v3, v3, v5
	v_and_b32_e32 v6, 8, v10
	v_cndmask_b32_e32 v4, v7, v4, vcc
	v_cmp_ngt_f32_e32 vcc, s1, v2
	s_mov_b32 s1, 0xffff0
	s_lshl_b32 s0, s0, 10
	v_cndmask_b32_e32 v3, 0, v3, vcc
	v_cmp_nlt_f32_e32 vcc, s4, v2
	s_cmp_lg_u32 0, -1
	s_movk_i32 s2, 0x70
	v_cndmask_b32_e32 v2, v7, v3, vcc
	v_sub_f32_e32 v2, v4, v2
	v_add_f32_e32 v157, 0x3e4ccccd, v2
	v_lshlrev_b32_e32 v2, 3, v9
	v_and_b32_e32 v3, 0x60, v9
	v_and_or_b32 v2, v2, 24, v3
	v_add_u32_e32 v3, 0x200, v9
	v_ashrrev_i32_e32 v4, 4, v3
	v_bfe_u32 v5, v3, 2, 2
	v_and_or_b32 v5, v4, s1, v5
	v_lshrrev_b32_e32 v3, 1, v3
	v_lshrrev_b32_e32 v4, 1, v4
	v_and_b32_e32 v3, 8, v3
	v_and_b32_e32 v4, 4, v4
	v_or3_b32 v3, v5, v3, v4
	v_ashrrev_i32_e32 v4, 4, v9
	v_bfe_u32 v5, v9, 2, 2
	v_and_or_b32 v5, v4, s1, v5
	v_lshrrev_b32_e32 v4, 1, v4
	v_and_b32_e32 v4, 4, v4
	v_or3_b32 v4, v5, v6, v4
	v_lshlrev_b32_e32 v2, 1, v2
	s_cselect_b32 s1, 0, 0
	v_lshl_or_b32 v3, v3, 12, v2
	v_lshl_or_b32 v2, v4, 12, v2
	v_lshlrev_b32_e32 v4, 9, v9
	v_lshlrev_b32_e32 v5, 4, v9
	s_add_i32 s0, s0, s1
	v_and_b32_e32 v4, 0xfffff000, v4
	v_xor_b32_e32 v5, v5, v9
	s_add_i32 s1, s0, 0x10000
	v_and_or_b32 v4, v5, s2, v4
	s_mov_b32 m0, s1
	s_nop 0
	global_load_lds_dwordx4 v4, s[90:91] offset:0
	s_mov_b32 m0, s0
	s_nop 0
	global_load_lds_dwordx4 v2, s[92:93] offset:0
	s_addk_i32 s0, 0x2000
	s_mov_b32 m0, s0
	s_nop 0
	global_load_lds_dwordx4 v3, s[92:93] offset:0
	s_waitcnt vmcnt(0)
	v_writelane_b32 v254, s86, 19
	s_mov_b32 s8, 0
	s_mov_b32 s97, 1
	v_writelane_b32 v254, s87, 20
	s_mov_b32 s33, 0x41000000
	v_mov_b32_e32 v158, 0x3727c5ac
	v_mov_b32_e32 v159, 0x260
	v_mov_b32_e32 v160, 0xff800000
	v_mov_b32_e32 v161, 0xf149f2ca
	s_movk_i32 s2, 0x7fff
	s_mov_b32 s84, 0x3e38aa3b
	v_writelane_b32 v254, s94, 21
	s_barrier
	s_nop 0
	v_writelane_b32 v254, s95, 22
	s_branch .LBB0_232

.LBB0_235:
	v_mov_b32_e32 v39, v0
	s_movk_i32 s7, 0x70
	v_readfirstlane_b32 s1, v39
	s_ashr_i32 s76, s1, 6
	v_bfe_u32 v164, v39, 5, 1
	v_and_b32_e32 v165, 31, v39
	s_lshl_b32 s96, s76, 5
	v_lshlrev_b32_e32 v138, 2, v164
	s_add_i32 s77, s96, s68
	v_sub_u32_e32 v2, v165, v138
	v_add_u32_e32 v167, s77, v2
	v_lshlrev_b32_e32 v2, 9, v39
	v_lshlrev_b32_e32 v3, 4, v39
	v_and_b32_e32 v2, 0xfffff000, v2
	v_xor_b32_e32 v3, v3, v39
	v_and_or_b32 v168, v3, s7, v2
	v_ashrrev_i32_e32 v2, 4, v39
	v_bfe_u32 v3, v39, 2, 2
	s_mov_b32 s0, 0xffff0
	v_and_or_b32 v3, v2, s0, v3
	v_lshrrev_b32_e32 v4, 1, v39
	v_lshrrev_b32_e32 v2, 1, v2
	v_and_b32_e32 v4, 8, v4
	v_and_b32_e32 v2, 4, v2
	v_or3_b32 v2, v3, v4, v2
	v_and_b32_e32 v3, 0x60, v39
	v_lshlrev_b32_e32 v162, 3, v39
	s_lshl_b32 s86, s76, 10
	v_and_or_b32 v3, v162, 24, v3
	v_lshlrev_b32_e32 v3, 1, v3
	s_add_u32 s4, s90, 0x40000
	v_lshl_or_b32 v169, v2, 12, v3
	v_add_u32_e32 v2, 0x200, v39
	s_addc_u32 s5, s91, 0
	v_ashrrev_i32_e32 v4, 4, v2
	v_bfe_u32 v5, v2, 2, 2
	s_cmp_lg_u32 0, -1
	v_and_or_b32 v5, v4, s0, v5
	s_cselect_b32 s0, 0, 0
	s_add_i32 s0, s0, s86
	v_lshrrev_b32_e32 v2, 1, v2
	v_lshrrev_b32_e32 v4, 1, v4
	s_add_i32 s81, s0, 0x12000
	v_and_b32_e32 v2, 8, v2
	v_and_b32_e32 v4, 4, v4
	s_mov_b32 m0, s81
	s_nop 0
	global_load_lds_dwordx4 v168, s[4:5] offset:0
	s_add_u32 s4, s92, 0x40000
	v_or3_b32 v2, v5, v2, v4
	s_addc_u32 s5, s93, 0
	s_add_i32 s74, s0, 0x4000
	s_mov_b32 m0, s74
	s_nop 0
	global_load_lds_dwordx4 v169, s[4:5] offset:0
	v_lshl_or_b32 v170, v2, 12, v3
	s_addk_i32 s0, 0x6000
	s_mov_b32 m0, s0
	s_nop 0
	global_load_lds_dwordx4 v170, s[4:5] offset:0
	v_lshlrev_b32_e32 v35, 7, v165
	v_lshlrev_b32_e32 v118, 4, v164
	s_add_i32 s4, 0, 0x10000
	v_add_u32_e32 v48, s4, v35
	v_bitop3_b32 v37, v118, v162, s7 bitop3:0x78
	v_add_u32_e32 v171, v48, v37
	ds_read_b128 v[2:5], v171
	ds_read_b128 v[6:9], v171 offset:4096
	s_waitcnt vmcnt(3) lgkmcnt(1)
	v_mfma_f32_32x32x16_bf16 v[18:33], v[2:5], v[110:113], 0
	v_and_b32_e32 v34, 0x70, v162
	v_bitop3_b32 v38, v118, v34, 32 bitop3:0x36
	v_add_u32_e32 v172, v48, v38
	ds_read_b128 v[40:43], v172
	ds_read_b128 v[44:47], v172 offset:4096
	v_bitop3_b32 v36, v118, v34, 64 bitop3:0x36
	v_add_u32_e32 v173, v48, v36
	s_movk_i32 s4, 0x60
	s_waitcnt lgkmcnt(2)
	v_mfma_f32_32x32x16_bf16 v[2:17], v[6:9], v[110:113], 0
	v_bitop3_b32 v34, v118, v34, s4 bitop3:0x36
	v_add_u32_e32 v174, v48, v34
	s_movk_i32 s69, 0x70
	s_cmp_gt_i32 s77, 62
	v_writelane_b32 v254, s12, 33
	s_waitcnt vmcnt(2) lgkmcnt(1)
	v_mfma_f32_32x32x16_bf16 v[18:33], v[40:43], v[106:109], v[18:33]
	s_waitcnt lgkmcnt(0)
	v_mfma_f32_32x32x16_bf16 v[2:17], v[44:47], v[106:109], v[2:17]
	ds_read_b128 v[40:43], v173
	ds_read_b128 v[44:47], v173 offset:4096
	s_waitcnt vmcnt(1) lgkmcnt(1)
	v_mfma_f32_32x32x16_bf16 v[18:33], v[40:43], v[102:105], v[18:33]
	s_waitcnt lgkmcnt(0)
	v_mfma_f32_32x32x16_bf16 v[2:17], v[44:47], v[102:105], v[2:17]
	ds_read_b128 v[40:43], v174
	ds_read_b128 v[44:47], v174 offset:4096
	s_waitcnt vmcnt(0) lgkmcnt(1)
	v_mfma_f32_32x32x16_bf16 v[18:33], v[40:43], v[98:101], v[18:33]
	s_waitcnt lgkmcnt(0)
	v_mfma_f32_32x32x16_bf16 v[2:17], v[44:47], v[98:101], v[2:17]
	s_cbranch_scc1 .LBB0_237
	v_cmp_gt_i32_e64 s[64:65], 26, v167
	v_cmp_gt_i32_e64 s[66:67], 27, v167
	v_cmp_gt_i32_e64 s[62:63], 25, v167
	s_and_b64 s[64:65], s[66:67], s[64:65]
	v_cmp_gt_i32_e64 s[60:61], 24, v167
	s_and_b64 s[62:63], s[64:65], s[62:63]
	v_cmp_gt_i32_e64 s[58:59], 19, v167
	s_and_b64 s[60:61], s[62:63], s[60:61]
	v_cmp_gt_i32_e64 s[56:57], 18, v167
	s_and_b64 s[58:59], s[60:61], s[58:59]
	v_cmp_gt_i32_e64 s[54:55], 17, v167
	s_and_b64 s[56:57], s[58:59], s[56:57]
	v_cmp_gt_i32_e64 s[52:53], 16, v167
	s_and_b64 s[54:55], s[56:57], s[54:55]
	v_cmp_gt_i32_e64 s[50:51], 11, v167
	s_and_b64 s[52:53], s[54:55], s[52:53]
	v_cmp_gt_i32_e64 s[48:49], 10, v167
	s_and_b64 s[50:51], s[52:53], s[50:51]
	v_cmp_gt_i32_e64 s[44:45], 9, v167
	s_and_b64 s[48:49], s[50:51], s[48:49]
	v_cmp_gt_i32_e64 s[42:43], 8, v167
	s_and_b64 s[44:45], s[48:49], s[44:45]
	v_cmp_gt_i32_e64 s[40:41], 3, v167
	s_and_b64 s[42:43], s[44:45], s[42:43]
	v_cmp_gt_i32_e64 s[38:39], 2, v167
	s_and_b64 s[40:41], s[42:43], s[40:41]
	v_cmp_gt_i32_e64 s[36:37], 1, v167
	s_and_b64 s[38:39], s[40:41], s[38:39]
	v_cmp_gt_i32_e64 s[34:35], 0, v167
	s_and_b64 s[36:37], s[38:39], s[36:37]
	s_and_b64 s[34:35], s[36:37], s[34:35]
	v_cmp_gt_i32_e64 s[30:31], 58, v167
	v_cndmask_b32_e64 v18, v18, v160, s[34:35]
	v_cmp_gt_i32_e64 s[34:35], 59, v167
	v_cmp_gt_i32_e64 s[28:29], 57, v167
	s_and_b64 s[30:31], s[34:35], s[30:31]
	v_cmp_gt_i32_e64 s[26:27], 56, v167
	s_and_b64 s[28:29], s[30:31], s[28:29]
	v_cmp_gt_i32_e64 s[24:25], 51, v167
	s_and_b64 s[26:27], s[28:29], s[26:27]
	v_cmp_gt_i32_e64 s[22:23], 50, v167
	s_and_b64 s[24:25], s[26:27], s[24:25]
	v_cmp_gt_i32_e64 s[20:21], 49, v167
	s_and_b64 s[22:23], s[24:25], s[22:23]
	v_cmp_gt_i32_e64 s[18:19], 48, v167
	s_and_b64 s[20:21], s[22:23], s[20:21]
	v_cmp_gt_i32_e64 s[16:17], 43, v167
	s_and_b64 s[18:19], s[20:21], s[18:19]
	v_cmp_gt_i32_e64 s[14:15], 42, v167
	s_and_b64 s[16:17], s[18:19], s[16:17]
	v_cmp_gt_i32_e64 s[12:13], 41, v167
	s_and_b64 s[14:15], s[16:17], s[14:15]
	v_cmp_gt_i32_e64 s[10:11], 40, v167
	s_and_b64 s[12:13], s[14:15], s[12:13]
	v_cmp_gt_i32_e64 s[8:9], 35, v167
	s_and_b64 s[10:11], s[12:13], s[10:11]
	v_cmp_gt_i32_e64 s[6:7], 34, v167
	s_and_b64 s[8:9], s[10:11], s[8:9]
	v_cmp_gt_i32_e64 s[4:5], 33, v167
	s_and_b64 s[6:7], s[8:9], s[6:7]
	v_cmp_gt_i32_e32 vcc, 32, v167
	s_and_b64 s[4:5], s[6:7], s[4:5]
	s_and_b64 vcc, s[4:5], vcc
	v_cndmask_b32_e64 v33, v33, v160, s[66:67]
	v_cndmask_b32_e64 v32, v32, v160, s[64:65]
	v_cndmask_b32_e64 v31, v31, v160, s[62:63]
	v_cndmask_b32_e64 v30, v30, v160, s[60:61]
	v_cndmask_b32_e64 v29, v29, v160, s[58:59]
	v_cndmask_b32_e64 v28, v28, v160, s[56:57]
	v_cndmask_b32_e64 v27, v27, v160, s[54:55]
	v_cndmask_b32_e64 v26, v26, v160, s[52:53]
	v_cndmask_b32_e64 v25, v25, v160, s[50:51]
	v_cndmask_b32_e64 v24, v24, v160, s[48:49]
	v_cndmask_b32_e64 v23, v23, v160, s[44:45]
	v_cndmask_b32_e64 v22, v22, v160, s[42:43]
	v_cndmask_b32_e64 v21, v21, v160, s[40:41]
	v_cndmask_b32_e64 v20, v20, v160, s[38:39]
	v_cndmask_b32_e64 v19, v19, v160, s[36:37]
	v_cndmask_b32_e64 v17, v17, v160, s[34:35]
	v_cndmask_b32_e64 v16, v16, v160, s[30:31]
	v_cndmask_b32_e64 v15, v15, v160, s[28:29]
	v_cndmask_b32_e64 v14, v14, v160, s[26:27]
	v_cndmask_b32_e64 v13, v13, v160, s[24:25]
	v_cndmask_b32_e64 v12, v12, v160, s[22:23]
	v_cndmask_b32_e64 v11, v11, v160, s[20:21]
	v_cndmask_b32_e64 v10, v10, v160, s[18:19]
	v_cndmask_b32_e64 v9, v9, v160, s[16:17]
	v_cndmask_b32_e64 v8, v8, v160, s[14:15]
	v_cndmask_b32_e64 v7, v7, v160, s[12:13]
	v_cndmask_b32_e64 v6, v6, v160, s[10:11]
	v_cndmask_b32_e64 v5, v5, v160, s[8:9]
	v_cndmask_b32_e64 v4, v4, v160, s[6:7]
	v_cndmask_b32_e64 v3, v3, v160, s[4:5]
	v_cndmask_b32_e32 v2, v2, v160, vcc
.LBB0_237:
	v_and_b32_e32 v163, 63, v39
	v_lshlrev_b32_e32 v40, 4, v163
	v_lshlrev_b32_e32 v39, 3, v163
	v_and_b32_e32 v40, 0xc0, v40
	v_lshlrev_b32_e32 v41, 1, v163
	s_cmp_lg_u32 0, -1
	v_and_or_b32 v40, v39, 24, v40
	v_and_b32_e32 v41, 32, v41
	v_and_b32_e32 v39, 0x100, v39
	s_cselect_b32 s4, 0, 0
	v_or3_b32 v39, v40, v41, v39
	v_add_u32_e32 v166, s4, v39
	v_max_f32_e32 v39, v19, v19
	v_max_f32_e32 v40, v18, v18
	v_max_f32_e32 v39, v40, v39
	v_max3_f32 v39, v39, v20, v21
	v_max3_f32 v39, v39, v22, v23
	v_max3_f32 v39, v39, v24, v25
	v_max3_f32 v39, v39, v26, v27
	v_max3_f32 v39, v39, v28, v29
	v_max3_f32 v39, v39, v30, v31
	v_max3_f32 v39, v39, v32, v33
	v_max3_f32 v39, v39, v2, v3
	v_max3_f32 v39, v39, v4, v5
	v_max3_f32 v39, v39, v6, v7
	v_max3_f32 v39, v39, v8, v9
	v_max3_f32 v39, v39, v10, v11
	v_max3_f32 v39, v39, v12, v13
	v_max3_f32 v39, v39, v14, v15
	v_max3_f32 v39, v39, v16, v17
	v_mov_b32_e32 v40, v39
	s_nop 1
	v_permlane32_swap_b32_e32 v39, v40
	v_max_f32_e32 v40, v40, v40
	v_max_f32_e32 v39, v39, v39
	v_max_f32_e32 v39, v39, v40
	v_add_f32_e32 v40, 0x7149f2ca, v39
	s_add_i32 s83, s4, s86
	v_mul_f32_e32 v40, 0x3e000000, v40
	s_add_i32 s85, s83, 0x10000
	v_cmp_ge_f32_e32 vcc, s33, v40
	s_cmp_eq_u64 vcc, exec
	v_max_f32_e32 v39, 0xf149f2ca, v39
	v_sub_f32_e32 v40, 0xf149f2ca, v39
	s_cselect_b64 s[4:5], -1, 0
	v_mul_f32_e32 v40, 0x3e38aa3b, v40
	v_cndmask_b32_e64 v116, v39, v161, s[4:5]
	v_exp_f32_e32 v179, v40
	v_mul_f32_e32 v40, 0xbe38aa3b, v116
	v_pk_fma_f32 v[32:33], v[32:33], s[84:85], v[40:41] op_sel_hi:[1,0,0]
	v_pk_fma_f32 v[30:31], v[30:31], s[84:85], v[40:41] op_sel_hi:[1,0,0]
	v_pk_fma_f32 v[28:29], v[28:29], s[84:85], v[40:41] op_sel_hi:[1,0,0]
	v_pk_fma_f32 v[26:27], v[26:27], s[84:85], v[40:41] op_sel_hi:[1,0,0]
	v_pk_fma_f32 v[24:25], v[24:25], s[84:85], v[40:41] op_sel_hi:[1,0,0]
	v_pk_fma_f32 v[22:23], v[22:23], s[84:85], v[40:41] op_sel_hi:[1,0,0]
	v_pk_fma_f32 v[20:21], v[20:21], s[84:85], v[40:41] op_sel_hi:[1,0,0]
	v_pk_fma_f32 v[18:19], v[18:19], s[84:85], v[40:41] op_sel_hi:[1,0,0]
	v_exp_f32_e32 v58, v20
	v_exp_f32_e32 v56, v18
	v_exp_f32_e32 v57, v19
	v_exp_f32_e32 v59, v21
	v_exp_f32_e32 v60, v22
	v_exp_f32_e32 v61, v23
	v_exp_f32_e32 v62, v24
	v_exp_f32_e32 v63, v25
	v_exp_f32_e32 v26, v26
	v_exp_f32_e32 v27, v27
	v_exp_f32_e32 v28, v28
	v_exp_f32_e32 v29, v29
	v_exp_f32_e32 v30, v30
	v_exp_f32_e32 v31, v31
	v_exp_f32_e32 v32, v32
	v_exp_f32_e32 v33, v33
	s_waitcnt vmcnt(0)
	v_pk_fma_f32 v[42:43], v[16:17], s[84:85], v[40:41] op_sel_hi:[1,0,0]
	v_pk_fma_f32 v[44:45], v[14:15], s[84:85], v[40:41] op_sel_hi:[1,0,0]
	v_pk_fma_f32 v[46:47], v[12:13], s[84:85], v[40:41] op_sel_hi:[1,0,0]
	v_pk_fma_f32 v[48:49], v[10:11], s[84:85], v[40:41] op_sel_hi:[1,0,0]
	v_pk_fma_f32 v[50:51], v[8:9], s[84:85], v[40:41] op_sel_hi:[1,0,0]
	v_pk_fma_f32 v[52:53], v[6:7], s[84:85], v[40:41] op_sel_hi:[1,0,0]
	v_pk_fma_f32 v[54:55], v[4:5], s[84:85], v[40:41] op_sel_hi:[1,0,0]
	v_pk_fma_f32 v[40:41], v[2:3], s[84:85], v[40:41] op_sel_hi:[1,0,0]
	s_barrier
	s_add_u32 s6, s90, 0x80000
	s_addc_u32 s7, s91, 0
	s_mov_b32 m0, s85
	s_nop 0
	global_load_lds_dwordx4 v168, s[6:7] offset:0
	s_add_u32 s6, s92, 0x80000
	s_addc_u32 s7, s93, 0
	s_add_i32 s82, s83, 0x8000
	s_mov_b32 m0, s82
	s_nop 0
	global_load_lds_dwordx4 v169, s[6:7] offset:0
	s_add_i32 s83, s83, 0xa000
	s_mov_b32 m0, s83
	s_nop 0
	global_load_lds_dwordx4 v170, s[6:7] offset:0
	s_add_i32 s6, 0, 0x12000
	v_add_u32_e32 v10, s6, v35
	v_add_u32_e32 v175, v10, v37
	ds_read_b128 v[2:5], v175
	ds_read_b128 v[6:9], v175 offset:4096
	v_add_u32_e32 v176, v10, v38
	v_add_u32_e32 v177, v10, v36
	v_add_u32_e32 v178, v10, v34
	s_waitcnt lgkmcnt(1)
	v_mfma_f32_32x32x16_bf16 v[66:81], v[2:5], v[110:113], 0
	ds_read_b128 v[2:5], v176
	ds_read_b128 v[10:13], v176 offset:4096
	ds_read_b128 v[14:17], v177
	ds_read_b128 v[18:21], v177 offset:4096
	v_exp_f32_e32 v34, v40
	v_exp_f32_e32 v35, v41
	v_exp_f32_e32 v36, v54
	v_exp_f32_e32 v37, v55
	v_exp_f32_e32 v38, v52
	v_exp_f32_e32 v39, v53
	s_waitcnt lgkmcnt(4)
	v_mfma_f32_32x32x16_bf16 v[82:97], v[6:9], v[110:113], 0
	ds_read_b128 v[6:9], v178
	ds_read_b128 v[22:25], v178 offset:4096
	v_exp_f32_e32 v40, v50
	v_exp_f32_e32 v41, v51
	v_exp_f32_e32 v48, v48
	v_exp_f32_e32 v49, v49
	v_exp_f32_e32 v46, v46
	v_exp_f32_e32 v47, v47
	s_waitcnt lgkmcnt(5)
	v_mfma_f32_32x32x16_bf16 v[66:81], v[2:5], v[106:109], v[66:81]
	v_add_f32_e64 v4, v58, v36
	v_add_f32_e64 v5, v59, v37
	v_add_f32_e64 v52, v60, v38
	v_add_f32_e64 v53, v61, v39
	v_add_f32_e64 v2, v28, v46
	v_add_f32_e64 v3, v29, v47
	v_pk_add_f32 v[2:3], v[4:5], v[2:3]
	s_waitcnt lgkmcnt(4)
	v_mfma_f32_32x32x16_bf16 v[82:97], v[10:13], v[106:109], v[82:97]
	v_exp_f32_e32 v10, v44
	v_exp_f32_e32 v12, v42
	v_exp_f32_e32 v13, v43
	v_exp_f32_e32 v11, v45
	v_pk_add_f32 v[44:45], v[56:57], v[34:35]
	v_pk_add_f32 v[42:43], v[32:33], v[12:13]
	s_waitcnt lgkmcnt(3)
	v_mfma_f32_32x32x16_bf16 v[66:81], v[14:17], v[102:105], v[66:81]
	v_add_f32_e64 v14, v62, v40
	v_add_f32_e64 v15, v63, v41
	v_add_f32_e64 v16, v26, v48
	v_add_f32_e64 v17, v27, v49
	v_add_f32_e64 v50, v30, v10
	v_add_f32_e64 v51, v31, v11
	v_pk_add_f32 v[16:17], v[44:45], v[16:17]
	v_pk_add_f32 v[50:51], v[52:53], v[50:51]
	v_pk_add_f32 v[14:15], v[14:15], v[42:43]
	v_pk_add_f32 v[4:5], v[16:17], v[50:51]
	s_waitcnt lgkmcnt(2)
	v_mfma_f32_32x32x16_bf16 v[82:97], v[18:21], v[102:105], v[82:97]
	v_add_f32_e64 v2, v2, v14
	v_add_f32_e64 v3, v3, v15
	v_add_f32_e64 v2, v4, v2
	v_add_f32_e64 v3, v5, v3
	v_add_f32_e64 v114, v2, v3
	v_add_f32_e64 v115, v3, v2
	v_cvt_pk_bf16_f32 v2, v56, v57
	v_cvt_pk_bf16_f32 v3, v58, v59
	s_waitcnt lgkmcnt(1)
	v_mfma_f32_32x32x16_bf16 v[66:81], v[6:9], v[98:101], v[66:81]
	v_mov_b32_e32 v115, v114
	v_cvt_pk_bf16_f32 v4, v60, v61
	v_cvt_pk_bf16_f32 v5, v62, v63
	s_nop 1
	v_permlane32_swap_b32_e32 v114, v115
	v_permlane32_swap_b32_e32 v2, v4
	s_waitcnt lgkmcnt(0)
	v_mfma_f32_32x32x16_bf16 v[82:97], v[22:25], v[98:101], v[82:97]
	v_permlane32_swap_b32_e32 v3, v5
	v_cvt_pk_bf16_f32 v120, v26, v27
	v_cvt_pk_bf16_f32 v121, v28, v29
	v_cvt_pk_bf16_f32 v122, v30, v31
	v_cvt_pk_bf16_f32 v123, v32, v33
	v_cvt_pk_bf16_f32 v124, v34, v35
	v_cvt_pk_bf16_f32 v125, v36, v37
	v_cvt_pk_bf16_f32 v126, v38, v39
	v_cvt_pk_bf16_f32 v127, v40, v41
	v_cvt_pk_bf16_f32 v128, v48, v49
	v_cvt_pk_bf16_f32 v129, v46, v47
	v_cvt_pk_bf16_f32 v130, v10, v11
	v_cvt_pk_bf16_f32 v131, v12, v13
	s_nop 0
	v_permlane32_swap_b32_e32 v120, v122
	v_permlane32_swap_b32_e32 v121, v123
	v_permlane32_swap_b32_e32 v124, v126
	v_permlane32_swap_b32_e32 v125, v127
	v_permlane32_swap_b32_e32 v128, v130
	v_permlane32_swap_b32_e32 v129, v131
	ds_read_b64_tr_b16 v[6:7], v166 offset:0
	ds_read_b64_tr_b16 v[8:9], v166 offset:0x800
	ds_read_b64_tr_b16 v[10:11], v166 offset:0x1000
	ds_read_b64_tr_b16 v[12:13], v166 offset:0x1800
	ds_read_b64_tr_b16 v[14:15], v166 offset:0x2000
	ds_read_b64_tr_b16 v[16:17], v166 offset:0x2800
	ds_read_b64_tr_b16 v[34:35], v166 offset:0x3000
	ds_read_b64_tr_b16 v[36:37], v166 offset:0x3800
	ds_read_b64_tr_b16 v[38:39], v166 offset:0x200
	ds_read_b64_tr_b16 v[40:41], v166 offset:0xa00
	ds_read_b64_tr_b16 v[50:51], v166 offset:0x1200
	ds_read_b64_tr_b16 v[52:53], v166 offset:0x1a00
	ds_read_b64_tr_b16 v[54:55], v166 offset:0x2200
	ds_read_b64_tr_b16 v[56:57], v166 offset:0x2a00
	ds_read_b64_tr_b16 v[58:59], v166 offset:0x3200
	ds_read_b64_tr_b16 v[60:61], v166 offset:0x3a00
	s_waitcnt lgkmcnt(8)
	s_nop 0
	v_mfma_f32_32x32x16_bf16 v[18:33], v[2:5], v[6:9], 0
	v_mfma_f32_32x32x16_bf16 v[18:33], v[120:123], v[10:13], v[18:33]
	v_mfma_f32_32x32x16_bf16 v[18:33], v[124:127], v[14:17], v[18:33]
	v_mfma_f32_32x32x16_bf16 v[18:33], v[128:131], v[34:37], v[18:33]
	ds_read_b64_tr_b16 v[6:7], v166 offset:0x400
	ds_read_b64_tr_b16 v[8:9], v166 offset:0xc00
	ds_read_b64_tr_b16 v[10:11], v166 offset:0x1400
	ds_read_b64_tr_b16 v[12:13], v166 offset:0x1c00
	ds_read_b64_tr_b16 v[14:15], v166 offset:0x2400
	ds_read_b64_tr_b16 v[16:17], v166 offset:0x2c00
	ds_read_b64_tr_b16 v[132:133], v166 offset:0x3400
	ds_read_b64_tr_b16 v[134:135], v166 offset:0x3c00
	s_waitcnt lgkmcnt(8)
	v_mfma_f32_32x32x16_bf16 v[34:49], v[2:5], v[38:41], 0
	v_mfma_f32_32x32x16_bf16 v[34:49], v[120:123], v[50:53], v[34:49]
	v_mfma_f32_32x32x16_bf16 v[34:49], v[124:127], v[54:57], v[34:49]
	v_mfma_f32_32x32x16_bf16 v[34:49], v[128:131], v[58:61], v[34:49]
	ds_read_b64_tr_b16 v[140:141], v166 offset:0x600
	ds_read_b64_tr_b16 v[142:143], v166 offset:0xe00
	ds_read_b64_tr_b16 v[144:145], v166 offset:0x1600
	ds_read_b64_tr_b16 v[146:147], v166 offset:0x1e00
	ds_read_b64_tr_b16 v[148:149], v166 offset:0x2600
	ds_read_b64_tr_b16 v[150:151], v166 offset:0x2e00
	ds_read_b64_tr_b16 v[152:153], v166 offset:0x3600
	ds_read_b64_tr_b16 v[154:155], v166 offset:0x3e00
	s_waitcnt lgkmcnt(8)
	v_mfma_f32_32x32x16_bf16 v[50:65], v[2:5], v[6:9], 0
	v_mfma_f32_32x32x16_bf16 v[50:65], v[120:123], v[10:13], v[50:65]
	v_mfma_f32_32x32x16_bf16 v[50:65], v[124:127], v[14:17], v[50:65]
	v_mfma_f32_32x32x16_bf16 v[50:65], v[128:131], v[132:135], v[50:65]
	s_waitcnt lgkmcnt(0)
	v_mfma_f32_32x32x16_bf16 v[2:17], v[2:5], v[140:143], 0
	s_cmpk_gt_i32 s77, 0x7e
	v_mfma_f32_32x32x16_bf16 v[2:17], v[120:123], v[144:147], v[2:17]
	v_mfma_f32_32x32x16_bf16 v[2:17], v[124:127], v[148:151], v[2:17]
	v_mfma_f32_32x32x16_bf16 v[2:17], v[128:131], v[152:155], v[2:17]
	s_cbranch_scc1 .LBB0_239
	s_movk_i32 s60, 0x5a
	s_movk_i32 s62, 0x5b
	v_cmp_gt_i32_e64 s[60:61], s60, v167
	v_cmp_gt_i32_e64 s[62:63], s62, v167
	s_and_b64 s[60:61], s[62:63], s[60:61]
	s_movk_i32 s28, 0x58
	v_cndmask_b32_e64 v81, v81, v160, s[62:63]
	s_movk_i32 s62, 0x59
	v_cmp_gt_i32_e64 s[62:63], s62, v167
	s_movk_i32 s26, 0x53
	v_cmp_gt_i32_e64 s[58:59], s28, v167
	v_cndmask_b32_e64 v80, v80, v160, s[60:61]
	s_and_b64 s[60:61], s[60:61], s[62:63]
	s_movk_i32 s24, 0x52
	v_cmp_gt_i32_e64 s[56:57], s26, v167
	s_and_b64 s[58:59], s[60:61], s[58:59]
	s_movk_i32 s22, 0x51
	v_cmp_gt_i32_e64 s[54:55], s24, v167
	s_and_b64 s[56:57], s[58:59], s[56:57]
	s_movk_i32 s20, 0x50
	v_cmp_gt_i32_e64 s[52:53], s22, v167
	s_and_b64 s[54:55], s[56:57], s[54:55]
	s_movk_i32 s18, 0x4b
	v_cmp_gt_i32_e64 s[50:51], s20, v167
	s_and_b64 s[52:53], s[54:55], s[52:53]
	s_movk_i32 s16, 0x4a
	v_cmp_gt_i32_e64 s[48:49], s18, v167
	s_and_b64 s[50:51], s[52:53], s[50:51]
	s_movk_i32 s14, 0x49
	v_cmp_gt_i32_e64 s[44:45], s16, v167
	s_and_b64 s[48:49], s[50:51], s[48:49]
	s_movk_i32 s12, 0x48
	v_cmp_gt_i32_e64 s[42:43], s14, v167
	s_and_b64 s[44:45], s[48:49], s[44:45]
	s_movk_i32 s10, 0x43
	v_cmp_gt_i32_e64 s[40:41], s12, v167
	s_and_b64 s[42:43], s[44:45], s[42:43]
	s_movk_i32 s6, 0x60
	s_movk_i32 s8, 0x42
	v_cmp_gt_i32_e64 s[38:39], s10, v167
	s_and_b64 s[40:41], s[42:43], s[40:41]
	v_cmp_gt_i32_e32 vcc, s6, v167
	s_movk_i32 s6, 0x41
	v_cmp_gt_i32_e64 s[36:37], s8, v167
	s_and_b64 s[38:39], s[40:41], s[38:39]
	v_cmp_gt_i32_e64 s[34:35], s6, v167
	s_and_b64 s[36:37], s[38:39], s[36:37]
	v_cmp_gt_i32_e64 s[30:31], 64, v167
	s_and_b64 s[34:35], s[36:37], s[34:35]
	s_and_b64 s[30:31], s[34:35], s[30:31]
	v_cndmask_b32_e64 v79, v79, v160, s[60:61]
	s_movk_i32 s60, 0x7a
	v_cndmask_b32_e64 v66, v66, v160, s[30:31]
	s_movk_i32 s30, 0x7b
	s_movk_i32 s62, 0x79
	v_cmp_gt_i32_e64 s[60:61], s60, v167
	v_cmp_gt_i32_e64 s[30:31], s30, v167
	s_movk_i32 s28, 0x78
	v_cmp_gt_i32_e64 s[62:63], s62, v167
	v_cndmask_b32_e64 v97, v97, v160, s[30:31]
	s_and_b64 s[30:31], s[30:31], s[60:61]
	s_movk_i32 s26, 0x73
	v_cmp_gt_i32_e64 s[28:29], s28, v167
	v_cndmask_b32_e64 v96, v96, v160, s[30:31]
	s_and_b64 s[30:31], s[30:31], s[62:63]
	s_movk_i32 s24, 0x72
	v_cmp_gt_i32_e64 s[26:27], s26, v167
	s_and_b64 s[28:29], s[30:31], s[28:29]
	s_movk_i32 s22, 0x71
	v_cmp_gt_i32_e64 s[24:25], s24, v167
	s_and_b64 s[26:27], s[28:29], s[26:27]
	v_cmp_gt_i32_e64 s[22:23], s22, v167
	s_and_b64 s[24:25], s[26:27], s[24:25]
	s_movk_i32 s18, 0x6b
	v_cmp_gt_i32_e64 s[20:21], s69, v167
	s_and_b64 s[22:23], s[24:25], s[22:23]
	s_movk_i32 s16, 0x6a
	v_cmp_gt_i32_e64 s[18:19], s18, v167
	s_and_b64 s[20:21], s[22:23], s[20:21]
	s_movk_i32 s14, 0x69
	v_cmp_gt_i32_e64 s[16:17], s16, v167
	s_and_b64 s[18:19], s[20:21], s[18:19]
	s_movk_i32 s12, 0x68
	v_cmp_gt_i32_e64 s[14:15], s14, v167
	s_and_b64 s[16:17], s[18:19], s[16:17]
	s_movk_i32 s10, 0x63
	v_cmp_gt_i32_e64 s[12:13], s12, v167
	s_and_b64 s[14:15], s[16:17], s[14:15]
	s_movk_i32 s8, 0x62
	v_cmp_gt_i32_e64 s[10:11], s10, v167
	s_and_b64 s[12:13], s[14:15], s[12:13]
	s_movk_i32 s6, 0x61
	v_cmp_gt_i32_e64 s[8:9], s8, v167
	s_and_b64 s[10:11], s[12:13], s[10:11]
	v_cmp_gt_i32_e64 s[6:7], s6, v167
	s_and_b64 s[8:9], s[10:11], s[8:9]
	s_and_b64 s[6:7], s[8:9], s[6:7]
	s_and_b64 vcc, s[6:7], vcc
	v_cndmask_b32_e64 v78, v78, v160, s[58:59]
	v_cndmask_b32_e64 v77, v77, v160, s[56:57]
	v_cndmask_b32_e64 v76, v76, v160, s[54:55]
	v_cndmask_b32_e64 v75, v75, v160, s[52:53]
	v_cndmask_b32_e64 v74, v74, v160, s[50:51]
	v_cndmask_b32_e64 v73, v73, v160, s[48:49]
	v_cndmask_b32_e64 v72, v72, v160, s[44:45]
	v_cndmask_b32_e64 v71, v71, v160, s[42:43]
	v_cndmask_b32_e64 v70, v70, v160, s[40:41]
	v_cndmask_b32_e64 v69, v69, v160, s[38:39]
	v_cndmask_b32_e64 v68, v68, v160, s[36:37]
	v_cndmask_b32_e64 v67, v67, v160, s[34:35]
	v_cndmask_b32_e64 v95, v95, v160, s[30:31]
	v_cndmask_b32_e64 v94, v94, v160, s[28:29]
	v_cndmask_b32_e64 v93, v93, v160, s[26:27]
	v_cndmask_b32_e64 v92, v92, v160, s[24:25]
	v_cndmask_b32_e64 v91, v91, v160, s[22:23]
	v_cndmask_b32_e64 v90, v90, v160, s[20:21]
	v_cndmask_b32_e64 v89, v89, v160, s[18:19]
	v_cndmask_b32_e64 v88, v88, v160, s[16:17]
	v_cndmask_b32_e64 v87, v87, v160, s[14:15]
	v_cndmask_b32_e64 v86, v86, v160, s[12:13]
	v_cndmask_b32_e64 v85, v85, v160, s[10:11]
	v_cndmask_b32_e64 v84, v84, v160, s[8:9]
	v_cndmask_b32_e64 v83, v83, v160, s[6:7]
	v_cndmask_b32_e32 v82, v82, v160, vcc

.LBB0_243:
	v_cndmask_b32_e64 v120, v117, v116, s[6:7]
	s_waitcnt vmcnt(0)
	v_mul_f32_e32 v116, 0xbe38aa3b, v120
	v_pk_fma_f32 v[80:81], v[80:81], s[84:85], v[116:117] op_sel_hi:[1,0,0]
	v_pk_fma_f32 v[78:79], v[78:79], s[84:85], v[116:117] op_sel_hi:[1,0,0]
	v_pk_fma_f32 v[76:77], v[76:77], s[84:85], v[116:117] op_sel_hi:[1,0,0]
	v_pk_fma_f32 v[74:75], v[74:75], s[84:85], v[116:117] op_sel_hi:[1,0,0]
	v_pk_fma_f32 v[72:73], v[72:73], s[84:85], v[116:117] op_sel_hi:[1,0,0]
	v_pk_fma_f32 v[70:71], v[70:71], s[84:85], v[116:117] op_sel_hi:[1,0,0]
	v_pk_fma_f32 v[68:69], v[68:69], s[84:85], v[116:117] op_sel_hi:[1,0,0]
	v_pk_fma_f32 v[66:67], v[66:67], s[84:85], v[116:117] op_sel_hi:[1,0,0]
	v_pk_fma_f32 v[148:149], v[96:97], s[84:85], v[116:117] op_sel_hi:[1,0,0]
	v_pk_fma_f32 v[150:151], v[94:95], s[84:85], v[116:117] op_sel_hi:[1,0,0]
	v_pk_fma_f32 v[152:153], v[92:93], s[84:85], v[116:117] op_sel_hi:[1,0,0]
	v_pk_fma_f32 v[154:155], v[90:91], s[84:85], v[116:117] op_sel_hi:[1,0,0]
	v_pk_fma_f32 v[180:181], v[88:89], s[84:85], v[116:117] op_sel_hi:[1,0,0]
	v_pk_fma_f32 v[184:185], v[86:87], s[84:85], v[116:117] op_sel_hi:[1,0,0]
	v_pk_fma_f32 v[186:187], v[84:85], s[84:85], v[116:117] op_sel_hi:[1,0,0]
	v_pk_fma_f32 v[116:117], v[82:83], s[84:85], v[116:117] op_sel_hi:[1,0,0]
	v_exp_f32_e32 v196, v66
	v_exp_f32_e32 v197, v67
	v_exp_f32_e32 v198, v68
	v_exp_f32_e32 v199, v69
	v_exp_f32_e32 v200, v70
	v_exp_f32_e32 v201, v71
	v_exp_f32_e32 v202, v72
	v_exp_f32_e32 v203, v73
	v_exp_f32_e32 v204, v74
	v_exp_f32_e32 v205, v75
	v_exp_f32_e32 v206, v76
	v_exp_f32_e32 v207, v77
	v_exp_f32_e32 v208, v78
	v_exp_f32_e32 v209, v79
	v_exp_f32_e32 v210, v80
	v_exp_f32_e32 v211, v81
	s_barrier
	s_add_u32 s6, s90, 0xc0000
	s_addc_u32 s7, s91, 0
	s_mov_b32 m0, s81
	s_nop 0
	global_load_lds_dwordx4 v168, s[6:7] offset:0
	s_add_u32 s6, s92, 0xc0000
	s_addc_u32 s7, s93, 0
	s_cmp_lg_u32 0, -1
	s_cselect_b32 s1, 0, 0
	s_add_i32 s79, s1, s86
	s_add_i32 s78, s79, 0xc000
	s_mov_b32 m0, s78
	s_nop 0
	global_load_lds_dwordx4 v169, s[6:7] offset:0
	s_add_i32 s79, s79, 0xe000
	s_mov_b32 m0, s79
	s_nop 0
	global_load_lds_dwordx4 v170, s[6:7] offset:0
	ds_read_b128 v[66:69], v171
	ds_read_b128 v[70:73], v171 offset:4096
	ds_read_b128 v[122:125], v172
	ds_read_b128 v[126:129], v172 offset:4096
	ds_read_b128 v[130:133], v173
	ds_read_b128 v[134:137], v173 offset:4096
	ds_read_b128 v[140:143], v174
	ds_read_b128 v[144:147], v174 offset:4096
	s_waitcnt lgkmcnt(7)
	v_mfma_f32_32x32x16_bf16 v[82:97], v[66:69], v[110:113], 0
	v_exp_f32_e32 v212, v116
	v_exp_f32_e32 v213, v117
	v_exp_f32_e32 v186, v186
	v_exp_f32_e32 v187, v187
	v_exp_f32_e32 v184, v184
	v_exp_f32_e32 v185, v185
	v_exp_f32_e32 v180, v180
	s_waitcnt lgkmcnt(6)
	v_mfma_f32_32x32x16_bf16 v[66:81], v[70:73], v[110:113], 0
	v_exp_f32_e32 v181, v181
	v_exp_f32_e32 v154, v154
	v_exp_f32_e32 v155, v155
	v_exp_f32_e32 v152, v152
	v_exp_f32_e32 v153, v153
	v_exp_f32_e32 v150, v150
	v_exp_f32_e32 v151, v151
	s_waitcnt lgkmcnt(5)
	v_mfma_f32_32x32x16_bf16 v[82:97], v[122:125], v[106:109], v[82:97]
	v_exp_f32_e32 v148, v148
	v_exp_f32_e32 v149, v149
	v_pk_add_f32 v[116:117], v[206:207], v[152:153]
	v_pk_add_f32 v[122:123], v[198:199], v[186:187]
	v_pk_add_f32 v[214:215], v[196:197], v[212:213]
	v_pk_add_f32 v[124:125], v[210:211], v[148:149]
	v_pk_add_f32 v[216:217], v[208:209], v[150:151]
	s_waitcnt lgkmcnt(4)
	v_mfma_f32_32x32x16_bf16 v[66:81], v[126:129], v[106:109], v[66:81]
	v_add_f32_e64 v126, v202, v180
	v_add_f32_e64 v127, v203, v181
	v_add_f32_e64 v128, v204, v154
	v_add_f32_e64 v129, v205, v155
	v_add_f32_e64 v218, v200, v184
	v_add_f32_e64 v219, v201, v185
	v_pk_add_f32 v[128:129], v[214:215], v[128:129]
	v_pk_add_f32 v[216:217], v[218:219], v[216:217]
	v_pk_add_f32 v[124:125], v[126:127], v[124:125]
	v_pk_add_f32 v[116:117], v[122:123], v[116:117]
	s_waitcnt lgkmcnt(3)
	v_mfma_f32_32x32x16_bf16 v[82:97], v[130:133], v[102:105], v[82:97]
	v_add_f32_e64 v116, v116, v124
	v_add_f32_e64 v117, v117, v125
	v_add_f32_e64 v122, v128, v216
	v_add_f32_e64 v123, v129, v217
	v_add_f32_e64 v116, v122, v116
	v_add_f32_e64 v117, v123, v117
	v_cvt_pk_bf16_f32 v122, v196, v197
	v_cvt_pk_bf16_f32 v123, v198, v199
	v_cvt_pk_bf16_f32 v124, v200, v201
	s_waitcnt lgkmcnt(2)
	v_mfma_f32_32x32x16_bf16 v[66:81], v[134:137], v[102:105], v[66:81]
	v_pk_add_f32 v[116:117], v[116:117], v[116:117] op_sel:[0,1] op_sel_hi:[1,0]
	v_cvt_pk_bf16_f32 v125, v202, v203
	v_cvt_pk_bf16_f32 v126, v204, v205
	v_cvt_pk_bf16_f32 v127, v206, v207
	v_cvt_pk_bf16_f32 v128, v208, v209
	v_cvt_pk_bf16_f32 v129, v210, v211
	s_nop 0
	v_mov_b32_e32 v117, v116
	s_waitcnt lgkmcnt(1)
	v_mfma_f32_32x32x16_bf16 v[82:97], v[140:143], v[98:101], v[82:97]
	v_permlane32_swap_b32_e32 v116, v117
	v_cvt_pk_bf16_f32 v130, v212, v213
	v_cvt_pk_bf16_f32 v131, v186, v187
	v_cvt_pk_bf16_f32 v132, v184, v185
	v_cvt_pk_bf16_f32 v133, v180, v181
	v_cvt_pk_bf16_f32 v134, v154, v155
	s_waitcnt lgkmcnt(0)
	v_mfma_f32_32x32x16_bf16 v[66:81], v[144:147], v[98:101], v[66:81]
	v_cvt_pk_bf16_f32 v135, v152, v153
	v_cvt_pk_bf16_f32 v136, v150, v151
	v_cvt_pk_bf16_f32 v137, v148, v149
	v_permlane32_swap_b32_e32 v122, v124
	v_permlane32_swap_b32_e32 v123, v125
	v_permlane32_swap_b32_e32 v126, v128
	v_permlane32_swap_b32_e32 v127, v129
	v_permlane32_swap_b32_e32 v130, v132
	v_permlane32_swap_b32_e32 v131, v133
	v_permlane32_swap_b32_e32 v134, v136
	v_permlane32_swap_b32_e32 v135, v137
	ds_read_b64_tr_b16 v[140:141], v166 offset:0x4000
	ds_read_b64_tr_b16 v[142:143], v166 offset:0x4800
	ds_read_b64_tr_b16 v[144:145], v166 offset:0x5000
	ds_read_b64_tr_b16 v[146:147], v166 offset:0x5800
	ds_read_b64_tr_b16 v[148:149], v166 offset:0x6000
	ds_read_b64_tr_b16 v[150:151], v166 offset:0x6800
	ds_read_b64_tr_b16 v[152:153], v166 offset:0x7000
	ds_read_b64_tr_b16 v[154:155], v166 offset:0x7800
	ds_read_b64_tr_b16 v[184:185], v166 offset:0x4200
	ds_read_b64_tr_b16 v[186:187], v166 offset:0x4a00
	ds_read_b64_tr_b16 v[196:197], v166 offset:0x5200
	ds_read_b64_tr_b16 v[198:199], v166 offset:0x5a00
	ds_read_b64_tr_b16 v[200:201], v166 offset:0x6200
	ds_read_b64_tr_b16 v[202:203], v166 offset:0x6a00
	ds_read_b64_tr_b16 v[204:205], v166 offset:0x7200
	ds_read_b64_tr_b16 v[206:207], v166 offset:0x7a00
	s_waitcnt lgkmcnt(8)
	s_nop 0
	v_mfma_f32_32x32x16_bf16 v[18:33], v[122:125], v[140:143], v[18:33]
	v_mfma_f32_32x32x16_bf16 v[18:33], v[126:129], v[144:147], v[18:33]
	v_mfma_f32_32x32x16_bf16 v[18:33], v[130:133], v[148:151], v[18:33]
	v_mfma_f32_32x32x16_bf16 v[18:33], v[134:137], v[152:155], v[18:33]
	ds_read_b64_tr_b16 v[140:141], v166 offset:0x4400
	ds_read_b64_tr_b16 v[142:143], v166 offset:0x4c00
	ds_read_b64_tr_b16 v[144:145], v166 offset:0x5400
	ds_read_b64_tr_b16 v[146:147], v166 offset:0x5c00
	ds_read_b64_tr_b16 v[148:149], v166 offset:0x6400
	ds_read_b64_tr_b16 v[150:151], v166 offset:0x6c00
	ds_read_b64_tr_b16 v[152:153], v166 offset:0x7400
	ds_read_b64_tr_b16 v[154:155], v166 offset:0x7c00
	s_waitcnt lgkmcnt(8)
	v_mfma_f32_32x32x16_bf16 v[34:49], v[122:125], v[184:187], v[34:49]
	v_mfma_f32_32x32x16_bf16 v[34:49], v[126:129], v[196:199], v[34:49]
	v_mfma_f32_32x32x16_bf16 v[34:49], v[130:133], v[200:203], v[34:49]
	v_mfma_f32_32x32x16_bf16 v[34:49], v[134:137], v[204:207], v[34:49]
	ds_read_b64_tr_b16 v[184:185], v166 offset:0x4600
	ds_read_b64_tr_b16 v[186:187], v166 offset:0x4e00
	ds_read_b64_tr_b16 v[196:197], v166 offset:0x5600
	ds_read_b64_tr_b16 v[198:199], v166 offset:0x5e00
	ds_read_b64_tr_b16 v[200:201], v166 offset:0x6600
	ds_read_b64_tr_b16 v[202:203], v166 offset:0x6e00
	ds_read_b64_tr_b16 v[204:205], v166 offset:0x7600
	ds_read_b64_tr_b16 v[206:207], v166 offset:0x7e00
	s_waitcnt lgkmcnt(8)
	v_mfma_f32_32x32x16_bf16 v[50:65], v[122:125], v[140:143], v[50:65]
	v_mfma_f32_32x32x16_bf16 v[50:65], v[126:129], v[144:147], v[50:65]
	v_mfma_f32_32x32x16_bf16 v[50:65], v[130:133], v[148:151], v[50:65]
	v_mfma_f32_32x32x16_bf16 v[50:65], v[134:137], v[152:155], v[50:65]
	s_waitcnt lgkmcnt(0)
	v_mfma_f32_32x32x16_bf16 v[2:17], v[122:125], v[184:187], v[2:17]
	s_cmpk_gt_i32 s77, 0xbe
	v_mfma_f32_32x32x16_bf16 v[2:17], v[126:129], v[196:199], v[2:17]
	v_mfma_f32_32x32x16_bf16 v[2:17], v[130:133], v[200:203], v[2:17]
	v_mfma_f32_32x32x16_bf16 v[2:17], v[134:137], v[204:207], v[2:17]
	s_cbranch_scc1 .LBB0_245
	s_movk_i32 s1, 0x80
	v_cmp_gt_i32_e64 s[30:31], s1, v167
	s_movk_i32 s1, 0xa0
	v_cmp_gt_i32_e32 vcc, s1, v167
	s_movk_i32 s1, 0x81
	v_cmp_gt_i32_e64 s[34:35], s1, v167
	s_movk_i32 s1, 0xa1
	v_cmp_gt_i32_e64 s[6:7], s1, v167
	s_movk_i32 s1, 0x82
	v_cmp_gt_i32_e64 s[36:37], s1, v167
	s_movk_i32 s1, 0xa2
	v_cmp_gt_i32_e64 s[8:9], s1, v167
	s_movk_i32 s1, 0x83
	v_cmp_gt_i32_e64 s[38:39], s1, v167
	s_movk_i32 s1, 0xa3
	v_cmp_gt_i32_e64 s[10:11], s1, v167
	s_movk_i32 s1, 0x88
	v_cmp_gt_i32_e64 s[40:41], s1, v167
	s_movk_i32 s1, 0xa8
	v_cmp_gt_i32_e64 s[12:13], s1, v167
	s_movk_i32 s1, 0x89
	v_cmp_gt_i32_e64 s[42:43], s1, v167
	s_movk_i32 s1, 0xa9
	v_cmp_gt_i32_e64 s[14:15], s1, v167
	s_movk_i32 s1, 0x8a
	v_cmp_gt_i32_e64 s[44:45], s1, v167
	s_movk_i32 s1, 0xaa
	v_cmp_gt_i32_e64 s[16:17], s1, v167
	s_movk_i32 s1, 0x8b
	v_cmp_gt_i32_e64 s[48:49], s1, v167
	s_movk_i32 s1, 0xab
	v_cmp_gt_i32_e64 s[18:19], s1, v167
	s_movk_i32 s1, 0x90
	v_cmp_gt_i32_e64 s[50:51], s1, v167
	s_movk_i32 s1, 0xb0
	v_cmp_gt_i32_e64 s[20:21], s1, v167
	s_movk_i32 s1, 0x91
	v_cmp_gt_i32_e64 s[52:53], s1, v167
	s_movk_i32 s1, 0xb1
	v_cmp_gt_i32_e64 s[22:23], s1, v167
	s_movk_i32 s1, 0x92
	v_cmp_gt_i32_e64 s[54:55], s1, v167
	s_movk_i32 s1, 0xb2
	v_cmp_gt_i32_e64 s[24:25], s1, v167
	s_movk_i32 s1, 0x93
	v_cmp_gt_i32_e64 s[56:57], s1, v167
	s_movk_i32 s1, 0xb3
	v_cmp_gt_i32_e64 s[26:27], s1, v167
	s_movk_i32 s1, 0x98
	v_cmp_gt_i32_e64 s[58:59], s1, v167
	s_movk_i32 s1, 0xb8
	v_cmp_gt_i32_e64 s[28:29], s1, v167
	s_movk_i32 s1, 0x9a
	v_cmp_gt_i32_e64 s[60:61], s1, v167
	s_movk_i32 s1, 0x9b
	v_cmp_gt_i32_e64 s[62:63], s1, v167
	s_movk_i32 s1, 0x99
	s_and_b64 s[60:61], s[62:63], s[60:61]
	v_cndmask_b32_e64 v97, v97, v160, s[62:63]
	v_cmp_gt_i32_e64 s[62:63], s1, v167
	v_cndmask_b32_e64 v96, v96, v160, s[60:61]
	s_and_b64 s[60:61], s[60:61], s[62:63]
	s_and_b64 s[58:59], s[60:61], s[58:59]
	s_and_b64 s[56:57], s[58:59], s[56:57]
	s_and_b64 s[54:55], s[56:57], s[54:55]
	s_and_b64 s[52:53], s[54:55], s[52:53]
	s_and_b64 s[50:51], s[52:53], s[50:51]
	s_and_b64 s[48:49], s[50:51], s[48:49]
	s_and_b64 s[44:45], s[48:49], s[44:45]
	s_and_b64 s[42:43], s[44:45], s[42:43]
	s_and_b64 s[40:41], s[42:43], s[40:41]
	s_and_b64 s[38:39], s[40:41], s[38:39]
	s_movk_i32 s1, 0xb9
	s_and_b64 s[36:37], s[38:39], s[36:37]
	v_cmp_gt_i32_e64 s[62:63], s1, v167
	s_movk_i32 s1, 0xba
	s_and_b64 s[34:35], s[36:37], s[34:35]
	v_cndmask_b32_e64 v95, v95, v160, s[60:61]
	v_cmp_gt_i32_e64 s[60:61], s1, v167
	s_and_b64 s[30:31], s[34:35], s[30:31]
	s_movk_i32 s1, 0xbb
	v_cndmask_b32_e64 v82, v82, v160, s[30:31]
	v_cmp_gt_i32_e64 s[30:31], s1, v167
	v_cndmask_b32_e64 v94, v94, v160, s[58:59]
	v_cndmask_b32_e64 v93, v93, v160, s[56:57]
	v_cndmask_b32_e64 v81, v81, v160, s[30:31]
	s_and_b64 s[30:31], s[30:31], s[60:61]
	v_cndmask_b32_e64 v80, v80, v160, s[30:31]
	s_and_b64 s[30:31], s[30:31], s[62:63]
	s_and_b64 s[28:29], s[30:31], s[28:29]
	s_and_b64 s[26:27], s[28:29], s[26:27]
	s_and_b64 s[24:25], s[26:27], s[24:25]
	s_and_b64 s[22:23], s[24:25], s[22:23]
	s_and_b64 s[20:21], s[22:23], s[20:21]
	s_and_b64 s[18:19], s[20:21], s[18:19]
	s_and_b64 s[16:17], s[18:19], s[16:17]
	s_and_b64 s[14:15], s[16:17], s[14:15]
	s_and_b64 s[12:13], s[14:15], s[12:13]
	s_and_b64 s[10:11], s[12:13], s[10:11]
	s_and_b64 s[8:9], s[10:11], s[8:9]
	s_and_b64 s[6:7], s[8:9], s[6:7]
	s_and_b64 vcc, s[6:7], vcc
	v_cndmask_b32_e64 v92, v92, v160, s[54:55]
	v_cndmask_b32_e64 v91, v91, v160, s[52:53]
	v_cndmask_b32_e64 v90, v90, v160, s[50:51]
	v_cndmask_b32_e64 v89, v89, v160, s[48:49]
	v_cndmask_b32_e64 v88, v88, v160, s[44:45]
	v_cndmask_b32_e64 v87, v87, v160, s[42:43]
	v_cndmask_b32_e64 v86, v86, v160, s[40:41]
	v_cndmask_b32_e64 v85, v85, v160, s[38:39]
	v_cndmask_b32_e64 v84, v84, v160, s[36:37]
	v_cndmask_b32_e64 v83, v83, v160, s[34:35]
	v_cndmask_b32_e64 v79, v79, v160, s[30:31]
	v_cndmask_b32_e64 v78, v78, v160, s[28:29]
	v_cndmask_b32_e64 v77, v77, v160, s[26:27]
	v_cndmask_b32_e64 v76, v76, v160, s[24:25]
	v_cndmask_b32_e64 v75, v75, v160, s[22:23]
	v_cndmask_b32_e64 v74, v74, v160, s[20:21]
	v_cndmask_b32_e64 v73, v73, v160, s[18:19]
	v_cndmask_b32_e64 v72, v72, v160, s[16:17]
	v_cndmask_b32_e64 v71, v71, v160, s[14:15]
	v_cndmask_b32_e64 v70, v70, v160, s[12:13]
	v_cndmask_b32_e64 v69, v69, v160, s[10:11]
	v_cndmask_b32_e64 v68, v68, v160, s[8:9]
	v_cndmask_b32_e64 v67, v67, v160, s[6:7]
	v_cndmask_b32_e32 v66, v66, v160, vcc

.LBB0_251:
	.p2align 3
	s_nop 0
	s_add_u32 s72, s90, s70
	s_addc_u32 s73, s91, s71
	s_add_u32 s6, s72, 0x100000
	s_addc_u32 s7, s73, 0
	s_add_u32 s88, s92, s70
	s_addc_u32 s89, s93, s71
	s_mov_b32 m0, s85
	s_nop 0
	global_load_lds_dwordx4 v168, s[6:7] offset:0
	s_add_u32 s6, s88, 0x100000
	s_addc_u32 s7, s89, 0
	s_mov_b32 m0, s86
	s_nop 0
	global_load_lds_dwordx4 v169, s[6:7] offset:0
	s_nop 0
	s_mov_b32 m0, s87
	s_nop 0
	global_load_lds_dwordx4 v170, s[6:7] offset:0
	ds_read_b128 v[66:69], v175
	ds_read_b128 v[82:85], v175 offset:4096
	ds_read_b128 v[114:117], v176
	ds_read_b128 v[184:187], v176 offset:4096
	ds_read_b128 v[196:199], v177
	ds_read_b128 v[200:203], v177 offset:4096
	ds_read_b128 v[204:207], v178
	ds_read_b128 v[208:211], v178 offset:4096
	s_waitcnt lgkmcnt(7)
	v_mfma_f32_32x32x16_bf16 v[66:81], v[66:69], v[110:113], 0
	v_exp_f32_e32 v120, v154
	v_exp_f32_e32 v121, v155
	v_exp_f32_e32 v152, v152
	v_exp_f32_e32 v153, v153
	v_exp_f32_e32 v150, v150
	v_exp_f32_e32 v151, v151
	v_exp_f32_e32 v148, v148
	s_waitcnt lgkmcnt(6)
	v_mfma_f32_32x32x16_bf16 v[82:97], v[82:85], v[110:113], 0
	v_exp_f32_e32 v149, v149
	v_exp_f32_e32 v146, v146
	v_exp_f32_e32 v147, v147
	v_exp_f32_e32 v144, v144
	v_exp_f32_e32 v145, v145
	v_exp_f32_e32 v154, v140
	v_exp_f32_e32 v155, v141
	s_waitcnt lgkmcnt(5)
	v_mfma_f32_32x32x16_bf16 v[66:81], v[114:117], v[106:109], v[66:81]
	v_exp_f32_e32 v116, v142
	v_exp_f32_e32 v117, v143
	v_pk_add_f32 v[114:115], v[126:127], v[144:145]
	v_pk_add_f32 v[140:141], v[134:135], v[152:153]
	v_pk_add_f32 v[142:143], v[122:123], v[154:155]
	v_pk_add_f32 v[212:213], v[136:137], v[120:121]
	v_pk_add_f32 v[214:215], v[124:125], v[116:117]
	s_waitcnt lgkmcnt(4)
	v_mfma_f32_32x32x16_bf16 v[82:97], v[184:187], v[106:109], v[82:97]
	v_add_f32_e64 v184, v130, v148
	v_add_f32_e64 v185, v131, v149
	v_add_f32_e64 v186, v128, v146
	v_add_f32_e64 v187, v129, v147
	v_add_f32_e64 v216, v132, v150
	v_add_f32_e64 v217, v133, v151
	v_pk_add_f32 v[186:187], v[212:213], v[186:187]
	v_pk_add_f32 v[214:215], v[216:217], v[214:215]
	v_pk_add_f32 v[142:143], v[184:185], v[142:143]
	v_pk_add_f32 v[114:115], v[140:141], v[114:115]
	s_waitcnt lgkmcnt(3)
	v_mfma_f32_32x32x16_bf16 v[66:81], v[196:199], v[102:105], v[66:81]
	v_add_f32_e64 v114, v114, v142
	v_add_f32_e64 v115, v115, v143
	v_add_f32_e64 v140, v186, v214
	v_add_f32_e64 v141, v187, v215
	v_add_f32_e64 v114, v140, v114
	v_add_f32_e64 v115, v141, v115
	v_cvt_pk_bf16_f32 v140, v136, v137
	v_cvt_pk_bf16_f32 v141, v134, v135
	v_cvt_pk_bf16_f32 v142, v132, v133
	s_waitcnt lgkmcnt(2)
	v_mfma_f32_32x32x16_bf16 v[82:97], v[200:203], v[102:105], v[82:97]
	v_pk_add_f32 v[114:115], v[114:115], v[114:115] op_sel:[0,1] op_sel_hi:[1,0]
	v_cvt_pk_bf16_f32 v143, v130, v131
	v_cvt_pk_bf16_f32 v128, v128, v129
	v_cvt_pk_bf16_f32 v129, v126, v127
	v_cvt_pk_bf16_f32 v130, v124, v125
	v_cvt_pk_bf16_f32 v131, v122, v123
	s_nop 0
	v_mov_b32_e32 v115, v114
	s_waitcnt lgkmcnt(1)
	v_mfma_f32_32x32x16_bf16 v[66:81], v[204:207], v[98:101], v[66:81]
	v_permlane32_swap_b32_e32 v114, v115
	v_cvt_pk_bf16_f32 v120, v120, v121
	v_cvt_pk_bf16_f32 v121, v152, v153
	v_cvt_pk_bf16_f32 v122, v150, v151
	v_cvt_pk_bf16_f32 v123, v148, v149
	v_cvt_pk_bf16_f32 v124, v146, v147
	s_waitcnt lgkmcnt(0)
	v_mfma_f32_32x32x16_bf16 v[82:97], v[208:211], v[98:101], v[82:97]
	v_cvt_pk_bf16_f32 v125, v144, v145
	v_cvt_pk_bf16_f32 v126, v116, v117
	v_cvt_pk_bf16_f32 v127, v154, v155
	v_permlane32_swap_b32_e32 v140, v142
	v_permlane32_swap_b32_e32 v141, v143
	v_permlane32_swap_b32_e32 v128, v130
	v_permlane32_swap_b32_e32 v129, v131
	v_permlane32_swap_b32_e32 v120, v122
	v_permlane32_swap_b32_e32 v121, v123
	v_permlane32_swap_b32_e32 v124, v126
	v_permlane32_swap_b32_e32 v125, v127
	ds_read_b64_tr_b16 v[132:133], v166 offset:0x8000
	ds_read_b64_tr_b16 v[134:135], v166 offset:0x8800
	ds_read_b64_tr_b16 v[144:145], v166 offset:0x9000
	ds_read_b64_tr_b16 v[146:147], v166 offset:0x9800
	ds_read_b64_tr_b16 v[148:149], v166 offset:0xa000
	ds_read_b64_tr_b16 v[150:151], v166 offset:0xa800
	ds_read_b64_tr_b16 v[152:153], v166 offset:0xb000
	ds_read_b64_tr_b16 v[154:155], v166 offset:0xb800
	ds_read_b64_tr_b16 v[184:185], v166 offset:0x8200
	ds_read_b64_tr_b16 v[186:187], v166 offset:0x8a00
	ds_read_b64_tr_b16 v[196:197], v166 offset:0x9200
	ds_read_b64_tr_b16 v[198:199], v166 offset:0x9a00
	ds_read_b64_tr_b16 v[200:201], v166 offset:0xa200
	ds_read_b64_tr_b16 v[202:203], v166 offset:0xaa00
	ds_read_b64_tr_b16 v[204:205], v166 offset:0xb200
	ds_read_b64_tr_b16 v[206:207], v166 offset:0xba00
	s_waitcnt lgkmcnt(8)
	s_nop 0
	v_mfma_f32_32x32x16_bf16 v[18:33], v[140:143], v[132:135], v[18:33]
	v_mfma_f32_32x32x16_bf16 v[18:33], v[128:131], v[144:147], v[18:33]
	v_mfma_f32_32x32x16_bf16 v[18:33], v[120:123], v[148:151], v[18:33]
	v_mfma_f32_32x32x16_bf16 v[18:33], v[124:127], v[152:155], v[18:33]
	ds_read_b64_tr_b16 v[132:133], v166 offset:0x8400
	ds_read_b64_tr_b16 v[134:135], v166 offset:0x8c00
	ds_read_b64_tr_b16 v[144:145], v166 offset:0x9400
	ds_read_b64_tr_b16 v[146:147], v166 offset:0x9c00
	ds_read_b64_tr_b16 v[148:149], v166 offset:0xa400
	ds_read_b64_tr_b16 v[150:151], v166 offset:0xac00
	ds_read_b64_tr_b16 v[152:153], v166 offset:0xb400
	ds_read_b64_tr_b16 v[154:155], v166 offset:0xbc00
	s_waitcnt lgkmcnt(8)
	v_mfma_f32_32x32x16_bf16 v[34:49], v[140:143], v[184:187], v[34:49]
	v_mfma_f32_32x32x16_bf16 v[34:49], v[128:131], v[196:199], v[34:49]
	v_mfma_f32_32x32x16_bf16 v[34:49], v[120:123], v[200:203], v[34:49]
	v_mfma_f32_32x32x16_bf16 v[34:49], v[124:127], v[204:207], v[34:49]
	ds_read_b64_tr_b16 v[184:185], v166 offset:0x8600
	ds_read_b64_tr_b16 v[186:187], v166 offset:0x8e00
	ds_read_b64_tr_b16 v[196:197], v166 offset:0x9600
	ds_read_b64_tr_b16 v[198:199], v166 offset:0x9e00
	ds_read_b64_tr_b16 v[200:201], v166 offset:0xa600
	ds_read_b64_tr_b16 v[202:203], v166 offset:0xae00
	ds_read_b64_tr_b16 v[204:205], v166 offset:0xb600
	ds_read_b64_tr_b16 v[206:207], v166 offset:0xbe00
	s_waitcnt lgkmcnt(8)
	v_mfma_f32_32x32x16_bf16 v[50:65], v[140:143], v[132:135], v[50:65]
	v_mfma_f32_32x32x16_bf16 v[50:65], v[128:131], v[144:147], v[50:65]
	v_mfma_f32_32x32x16_bf16 v[50:65], v[120:123], v[148:151], v[50:65]
	v_mfma_f32_32x32x16_bf16 v[50:65], v[124:127], v[152:155], v[50:65]
	s_waitcnt lgkmcnt(0)
	v_mfma_f32_32x32x16_bf16 v[2:17], v[140:143], v[184:187], v[2:17]
	s_add_i32 s6, s95, 0xffffff40
	s_cmp_le_i32 s6, s77
	v_mfma_f32_32x32x16_bf16 v[2:17], v[128:131], v[196:199], v[2:17]
	v_mfma_f32_32x32x16_bf16 v[2:17], v[120:123], v[200:203], v[2:17]
	v_mfma_f32_32x32x16_bf16 v[2:17], v[124:127], v[204:207], v[2:17]
	s_cbranch_scc1 .LBB0_253
	v_cmp_gt_i32_e64 s[66:67], 26, v183
	v_cmp_gt_i32_e64 s[68:69], 27, v183
	v_cmp_gt_i32_e64 s[64:65], 25, v183
	s_and_b64 s[66:67], s[68:69], s[66:67]
	v_cmp_gt_i32_e64 s[62:63], 24, v183
	s_and_b64 s[64:65], s[66:67], s[64:65]
	v_cmp_gt_i32_e64 s[60:61], 19, v183
	s_and_b64 s[62:63], s[64:65], s[62:63]
	v_cmp_gt_i32_e64 s[58:59], 18, v183
	s_and_b64 s[60:61], s[62:63], s[60:61]
	v_cmp_gt_i32_e64 s[56:57], 17, v183
	s_and_b64 s[58:59], s[60:61], s[58:59]
	v_cmp_gt_i32_e64 s[54:55], 16, v183
	s_and_b64 s[56:57], s[58:59], s[56:57]
	v_cmp_gt_i32_e64 s[52:53], 11, v183
	s_and_b64 s[54:55], s[56:57], s[54:55]
	v_cmp_gt_i32_e64 s[50:51], 10, v183
	s_and_b64 s[52:53], s[54:55], s[52:53]
	v_cmp_gt_i32_e64 s[48:49], 9, v183
	s_and_b64 s[50:51], s[52:53], s[50:51]
	v_cmp_gt_i32_e64 s[44:45], 8, v183
	s_and_b64 s[48:49], s[50:51], s[48:49]
	v_cmp_gt_i32_e64 s[42:43], 3, v183
	s_and_b64 s[44:45], s[48:49], s[44:45]
	v_cmp_gt_i32_e64 s[40:41], 2, v183
	s_and_b64 s[42:43], s[44:45], s[42:43]
	v_cmp_gt_i32_e64 s[38:39], 1, v183
	s_and_b64 s[40:41], s[42:43], s[40:41]
	v_cmp_gt_i32_e64 s[36:37], 0, v183
	s_and_b64 s[38:39], s[40:41], s[38:39]
	s_and_b64 s[36:37], s[38:39], s[36:37]
	v_cmp_gt_i32_e64 s[34:35], 58, v183
	v_cndmask_b32_e64 v66, v66, v160, s[36:37]
	v_cmp_gt_i32_e64 s[36:37], 59, v183
	v_cmp_gt_i32_e64 s[30:31], 57, v183
	s_and_b64 s[34:35], s[36:37], s[34:35]
	v_cmp_gt_i32_e64 s[28:29], 56, v183
	s_and_b64 s[30:31], s[34:35], s[30:31]
	v_cmp_gt_i32_e64 s[26:27], 51, v183
	s_and_b64 s[28:29], s[30:31], s[28:29]
	v_cmp_gt_i32_e64 s[24:25], 50, v183
	s_and_b64 s[26:27], s[28:29], s[26:27]
	v_cmp_gt_i32_e64 s[22:23], 49, v183
	s_and_b64 s[24:25], s[26:27], s[24:25]
	v_cmp_gt_i32_e64 s[20:21], 48, v183
	s_and_b64 s[22:23], s[24:25], s[22:23]
	v_cmp_gt_i32_e64 s[18:19], 43, v183
	s_and_b64 s[20:21], s[22:23], s[20:21]
	v_cmp_gt_i32_e64 s[16:17], 42, v183
	s_and_b64 s[18:19], s[20:21], s[18:19]
	v_cmp_gt_i32_e64 s[14:15], 41, v183
	s_and_b64 s[16:17], s[18:19], s[16:17]
	v_cmp_gt_i32_e64 s[12:13], 40, v183
	s_and_b64 s[14:15], s[16:17], s[14:15]
	v_cmp_gt_i32_e64 s[10:11], 35, v183
	s_and_b64 s[12:13], s[14:15], s[12:13]
	v_cmp_gt_i32_e64 s[8:9], 34, v183
	s_and_b64 s[10:11], s[12:13], s[10:11]
	v_cmp_gt_i32_e64 s[6:7], 33, v183
	s_and_b64 s[8:9], s[10:11], s[8:9]
	v_cmp_gt_i32_e32 vcc, 32, v183
	s_and_b64 s[6:7], s[8:9], s[6:7]
	s_and_b64 vcc, s[6:7], vcc
	v_cndmask_b32_e64 v81, v81, v160, s[68:69]
	v_cndmask_b32_e64 v80, v80, v160, s[66:67]
	v_cndmask_b32_e64 v79, v79, v160, s[64:65]
	v_cndmask_b32_e64 v78, v78, v160, s[62:63]
	v_cndmask_b32_e64 v77, v77, v160, s[60:61]
	v_cndmask_b32_e64 v76, v76, v160, s[58:59]
	v_cndmask_b32_e64 v75, v75, v160, s[56:57]
	v_cndmask_b32_e64 v74, v74, v160, s[54:55]
	v_cndmask_b32_e64 v73, v73, v160, s[52:53]
	v_cndmask_b32_e64 v72, v72, v160, s[50:51]
	v_cndmask_b32_e64 v71, v71, v160, s[48:49]
	v_cndmask_b32_e64 v70, v70, v160, s[44:45]
	v_cndmask_b32_e64 v69, v69, v160, s[42:43]
	v_cndmask_b32_e64 v68, v68, v160, s[40:41]
	v_cndmask_b32_e64 v67, v67, v160, s[38:39]
	v_cndmask_b32_e64 v97, v97, v160, s[36:37]
	v_cndmask_b32_e64 v96, v96, v160, s[34:35]
	v_cndmask_b32_e64 v95, v95, v160, s[30:31]
	v_cndmask_b32_e64 v94, v94, v160, s[28:29]
	v_cndmask_b32_e64 v93, v93, v160, s[26:27]
	v_cndmask_b32_e64 v92, v92, v160, s[24:25]
	v_cndmask_b32_e64 v91, v91, v160, s[22:23]
	v_cndmask_b32_e64 v90, v90, v160, s[20:21]
	v_cndmask_b32_e64 v89, v89, v160, s[18:19]
	v_cndmask_b32_e64 v88, v88, v160, s[16:17]
	v_cndmask_b32_e64 v87, v87, v160, s[14:15]
	v_cndmask_b32_e64 v86, v86, v160, s[12:13]
	v_cndmask_b32_e64 v85, v85, v160, s[10:11]
	v_cndmask_b32_e64 v84, v84, v160, s[8:9]
	v_cndmask_b32_e64 v83, v83, v160, s[6:7]
	v_cndmask_b32_e32 v82, v82, v160, vcc

.LBB0_257:
	v_cndmask_b32_e64 v120, v116, v139, s[6:7]
	s_waitcnt vmcnt(0)
	v_mul_f32_e32 v116, 0xbe38aa3b, v120
	v_pk_fma_f32 v[80:81], v[80:81], s[84:85], v[116:117] op_sel_hi:[1,0,0]
	v_pk_fma_f32 v[78:79], v[78:79], s[84:85], v[116:117] op_sel_hi:[1,0,0]
	v_pk_fma_f32 v[76:77], v[76:77], s[84:85], v[116:117] op_sel_hi:[1,0,0]
	v_pk_fma_f32 v[74:75], v[74:75], s[84:85], v[116:117] op_sel_hi:[1,0,0]
	v_pk_fma_f32 v[72:73], v[72:73], s[84:85], v[116:117] op_sel_hi:[1,0,0]
	v_pk_fma_f32 v[70:71], v[70:71], s[84:85], v[116:117] op_sel_hi:[1,0,0]
	v_pk_fma_f32 v[68:69], v[68:69], s[84:85], v[116:117] op_sel_hi:[1,0,0]
	v_pk_fma_f32 v[66:67], v[66:67], s[84:85], v[116:117] op_sel_hi:[1,0,0]
	v_pk_fma_f32 v[154:155], v[88:89], s[84:85], v[116:117] op_sel_hi:[1,0,0]
	v_pk_fma_f32 v[186:187], v[86:87], s[84:85], v[116:117] op_sel_hi:[1,0,0]
	v_pk_fma_f32 v[86:87], v[84:85], s[84:85], v[116:117] op_sel_hi:[1,0,0]
	v_pk_fma_f32 v[88:89], v[82:83], s[84:85], v[116:117] op_sel_hi:[1,0,0]
	v_pk_fma_f32 v[146:147], v[96:97], s[84:85], v[116:117] op_sel_hi:[1,0,0]
	v_pk_fma_f32 v[148:149], v[94:95], s[84:85], v[116:117] op_sel_hi:[1,0,0]
	v_pk_fma_f32 v[150:151], v[92:93], s[84:85], v[116:117] op_sel_hi:[1,0,0]
	v_pk_fma_f32 v[152:153], v[90:91], s[84:85], v[116:117] op_sel_hi:[1,0,0]
	v_exp_f32_e32 v196, v66
	v_exp_f32_e32 v197, v67
	v_exp_f32_e32 v198, v68
	v_exp_f32_e32 v199, v69
	v_exp_f32_e32 v200, v70
	v_exp_f32_e32 v201, v71
	v_exp_f32_e32 v202, v72
	v_exp_f32_e32 v203, v73
	v_exp_f32_e32 v204, v74
	v_exp_f32_e32 v205, v75
	v_exp_f32_e32 v206, v76
	v_exp_f32_e32 v207, v77
	v_exp_f32_e32 v208, v78
	v_exp_f32_e32 v209, v79
	v_exp_f32_e32 v210, v80
	v_exp_f32_e32 v211, v81
	s_barrier
	s_add_u32 s6, s72, 0x140000
	s_addc_u32 s7, s73, 0
	s_mov_b32 m0, s81
	s_nop 0
	global_load_lds_dwordx4 v168, s[6:7] offset:0
	s_add_u32 s6, s88, 0x140000
	s_addc_u32 s7, s89, 0
	s_mov_b32 m0, s74
	s_nop 0
	global_load_lds_dwordx4 v169, s[6:7] offset:0
	s_nop 0
	s_mov_b32 m0, s0
	s_nop 0
	global_load_lds_dwordx4 v170, s[6:7] offset:0
	ds_read_b128 v[66:69], v171
	ds_read_b128 v[82:85], v171 offset:4096
	ds_read_b128 v[122:125], v172
	ds_read_b128 v[126:129], v172 offset:4096
	v_exp_f32_e32 v212, v88
	s_waitcnt lgkmcnt(3)
	v_mfma_f32_32x32x16_bf16 v[66:81], v[66:69], v[110:113], 0
	v_exp_f32_e32 v213, v89
	v_exp_f32_e32 v214, v86
	v_exp_f32_e32 v215, v87
	ds_read_b128 v[130:133], v173
	ds_read_b128 v[134:137], v173 offset:4096
	ds_read_b128 v[138:141], v174
	ds_read_b128 v[142:145], v174 offset:4096
	v_exp_f32_e32 v186, v186
	v_exp_f32_e32 v187, v187
	v_exp_f32_e32 v154, v154
	s_waitcnt lgkmcnt(6)
	v_mfma_f32_32x32x16_bf16 v[82:97], v[82:85], v[110:113], 0
	v_exp_f32_e32 v155, v155
	v_exp_f32_e32 v152, v152
	v_exp_f32_e32 v153, v153
	v_exp_f32_e32 v150, v150
	v_exp_f32_e32 v151, v151
	v_exp_f32_e32 v148, v148
	v_exp_f32_e32 v149, v149
	s_waitcnt lgkmcnt(5)
	v_mfma_f32_32x32x16_bf16 v[66:81], v[122:125], v[106:109], v[66:81]
	v_exp_f32_e32 v146, v146
	v_exp_f32_e32 v147, v147
	v_pk_add_f32 v[116:117], v[206:207], v[150:151]
	v_pk_add_f32 v[122:123], v[198:199], v[214:215]
	v_pk_add_f32 v[216:217], v[196:197], v[212:213]
	v_pk_add_f32 v[124:125], v[210:211], v[146:147]
	v_pk_add_f32 v[218:219], v[208:209], v[148:149]
	s_waitcnt lgkmcnt(4)
	v_mfma_f32_32x32x16_bf16 v[82:97], v[126:129], v[106:109], v[82:97]
	v_add_f32_e64 v126, v202, v154
	v_add_f32_e64 v127, v203, v155
	v_add_f32_e64 v128, v204, v152
	v_add_f32_e64 v129, v205, v153
	v_add_f32_e64 v220, v200, v186
	v_add_f32_e64 v221, v201, v187
	v_pk_add_f32 v[128:129], v[216:217], v[128:129]
	v_pk_add_f32 v[218:219], v[220:221], v[218:219]
	v_pk_add_f32 v[124:125], v[126:127], v[124:125]
	v_pk_add_f32 v[116:117], v[122:123], v[116:117]
	s_waitcnt lgkmcnt(3)
	v_mfma_f32_32x32x16_bf16 v[66:81], v[130:133], v[102:105], v[66:81]
	v_add_f32_e64 v116, v116, v124
	v_add_f32_e64 v117, v117, v125
	v_add_f32_e64 v122, v128, v218
	v_add_f32_e64 v123, v129, v219
	v_add_f32_e64 v116, v122, v116
	v_add_f32_e64 v117, v123, v117
	v_cvt_pk_bf16_f32 v122, v196, v197
	v_cvt_pk_bf16_f32 v123, v198, v199
	v_cvt_pk_bf16_f32 v124, v200, v201
	s_waitcnt lgkmcnt(2)
	v_mfma_f32_32x32x16_bf16 v[82:97], v[134:137], v[102:105], v[82:97]
	v_pk_add_f32 v[116:117], v[116:117], v[116:117] op_sel:[0,1] op_sel_hi:[1,0]
	v_cvt_pk_bf16_f32 v125, v202, v203
	v_cvt_pk_bf16_f32 v126, v204, v205
	v_cvt_pk_bf16_f32 v127, v206, v207
	v_cvt_pk_bf16_f32 v128, v208, v209
	v_cvt_pk_bf16_f32 v129, v210, v211
	s_nop 0
	v_mov_b32_e32 v117, v116
	s_waitcnt lgkmcnt(1)
	v_mfma_f32_32x32x16_bf16 v[66:81], v[138:141], v[98:101], v[66:81]
	v_permlane32_swap_b32_e32 v116, v117
	v_cvt_pk_bf16_f32 v130, v212, v213
	v_cvt_pk_bf16_f32 v131, v214, v215
	v_cvt_pk_bf16_f32 v132, v186, v187
	v_cvt_pk_bf16_f32 v133, v154, v155
	v_cvt_pk_bf16_f32 v134, v152, v153
	s_waitcnt lgkmcnt(0)
	v_mfma_f32_32x32x16_bf16 v[82:97], v[142:145], v[98:101], v[82:97]
	v_cvt_pk_bf16_f32 v135, v150, v151
	v_cvt_pk_bf16_f32 v136, v148, v149
	v_cvt_pk_bf16_f32 v137, v146, v147
	v_permlane32_swap_b32_e32 v122, v124
	v_permlane32_swap_b32_e32 v123, v125
	v_permlane32_swap_b32_e32 v126, v128
	v_permlane32_swap_b32_e32 v127, v129
	v_permlane32_swap_b32_e32 v130, v132
	v_permlane32_swap_b32_e32 v131, v133
	v_permlane32_swap_b32_e32 v134, v136
	v_permlane32_swap_b32_e32 v135, v137
	ds_read_b64_tr_b16 v[138:139], v166 offset:0xc000
	ds_read_b64_tr_b16 v[140:141], v166 offset:0xc800
	ds_read_b64_tr_b16 v[142:143], v166 offset:0xd000
	ds_read_b64_tr_b16 v[144:145], v166 offset:0xd800
	ds_read_b64_tr_b16 v[146:147], v166 offset:0xe000
	ds_read_b64_tr_b16 v[148:149], v166 offset:0xe800
	ds_read_b64_tr_b16 v[150:151], v166 offset:0xf000
	ds_read_b64_tr_b16 v[152:153], v166 offset:0xf800
	ds_read_b64_tr_b16 v[196:197], v166 offset:0xc200
	ds_read_b64_tr_b16 v[198:199], v166 offset:0xca00
	ds_read_b64_tr_b16 v[200:201], v166 offset:0xd200
	ds_read_b64_tr_b16 v[202:203], v166 offset:0xda00
	ds_read_b64_tr_b16 v[204:205], v166 offset:0xe200
	ds_read_b64_tr_b16 v[206:207], v166 offset:0xea00
	ds_read_b64_tr_b16 v[208:209], v166 offset:0xf200
	ds_read_b64_tr_b16 v[210:211], v166 offset:0xfa00
	s_waitcnt lgkmcnt(8)
	s_nop 0
	v_mfma_f32_32x32x16_bf16 v[18:33], v[122:125], v[138:141], v[18:33]
	v_mfma_f32_32x32x16_bf16 v[18:33], v[126:129], v[142:145], v[18:33]
	v_mfma_f32_32x32x16_bf16 v[18:33], v[130:133], v[146:149], v[18:33]
	v_mfma_f32_32x32x16_bf16 v[18:33], v[134:137], v[150:153], v[18:33]
	ds_read_b64_tr_b16 v[138:139], v166 offset:0xc400
	ds_read_b64_tr_b16 v[140:141], v166 offset:0xcc00
	ds_read_b64_tr_b16 v[142:143], v166 offset:0xd400
	ds_read_b64_tr_b16 v[144:145], v166 offset:0xdc00
	ds_read_b64_tr_b16 v[146:147], v166 offset:0xe400
	ds_read_b64_tr_b16 v[148:149], v166 offset:0xec00
	ds_read_b64_tr_b16 v[150:151], v166 offset:0xf400
	ds_read_b64_tr_b16 v[152:153], v166 offset:0xfc00
	s_waitcnt lgkmcnt(8)
	v_mfma_f32_32x32x16_bf16 v[34:49], v[122:125], v[196:199], v[34:49]
	v_mfma_f32_32x32x16_bf16 v[34:49], v[126:129], v[200:203], v[34:49]
	v_mfma_f32_32x32x16_bf16 v[34:49], v[130:133], v[204:207], v[34:49]
	v_mfma_f32_32x32x16_bf16 v[34:49], v[134:137], v[208:211], v[34:49]
	ds_read_b64_tr_b16 v[196:197], v166 offset:0xc600
	ds_read_b64_tr_b16 v[198:199], v166 offset:0xce00
	ds_read_b64_tr_b16 v[200:201], v166 offset:0xd600
	ds_read_b64_tr_b16 v[202:203], v166 offset:0xde00
	ds_read_b64_tr_b16 v[204:205], v166 offset:0xe600
	ds_read_b64_tr_b16 v[206:207], v166 offset:0xee00
	ds_read_b64_tr_b16 v[208:209], v166 offset:0xf600
	ds_read_b64_tr_b16 v[210:211], v166 offset:0xfe00
	s_waitcnt lgkmcnt(8)
	v_mfma_f32_32x32x16_bf16 v[50:65], v[122:125], v[138:141], v[50:65]
	v_mfma_f32_32x32x16_bf16 v[50:65], v[126:129], v[142:145], v[50:65]
	v_mfma_f32_32x32x16_bf16 v[50:65], v[130:133], v[146:149], v[50:65]
	v_mfma_f32_32x32x16_bf16 v[50:65], v[134:137], v[150:153], v[50:65]
	s_waitcnt lgkmcnt(0)
	v_mfma_f32_32x32x16_bf16 v[2:17], v[122:125], v[196:199], v[2:17]
	s_add_i32 s6, s95, 0xffffff80
	s_cmp_le_i32 s6, s77
	v_mfma_f32_32x32x16_bf16 v[2:17], v[126:129], v[200:203], v[2:17]
	v_mfma_f32_32x32x16_bf16 v[2:17], v[130:133], v[204:207], v[2:17]
	v_mfma_f32_32x32x16_bf16 v[2:17], v[134:137], v[208:211], v[2:17]
	s_cbranch_scc1 .LBB0_259
	v_subrev_u32_e32 v121, 64, v183
	v_cmp_gt_i32_e64 s[66:67], 26, v121
	v_cmp_gt_i32_e64 s[68:69], 27, v121
	v_cmp_gt_i32_e64 s[64:65], 25, v121
	s_and_b64 s[66:67], s[68:69], s[66:67]
	v_cmp_gt_i32_e64 s[62:63], 24, v121
	s_and_b64 s[64:65], s[66:67], s[64:65]
	v_cmp_gt_i32_e64 s[60:61], 19, v121
	s_and_b64 s[62:63], s[64:65], s[62:63]
	v_cmp_gt_i32_e64 s[58:59], 18, v121
	s_and_b64 s[60:61], s[62:63], s[60:61]
	v_cmp_gt_i32_e64 s[56:57], 17, v121
	s_and_b64 s[58:59], s[60:61], s[58:59]
	v_cmp_gt_i32_e64 s[54:55], 16, v121
	s_and_b64 s[56:57], s[58:59], s[56:57]
	v_cmp_gt_i32_e64 s[52:53], 11, v121
	s_and_b64 s[54:55], s[56:57], s[54:55]
	v_cmp_gt_i32_e64 s[50:51], 10, v121
	s_and_b64 s[52:53], s[54:55], s[52:53]
	v_cmp_gt_i32_e64 s[48:49], 9, v121
	s_and_b64 s[50:51], s[52:53], s[50:51]
	v_cmp_gt_i32_e64 s[44:45], 8, v121
	s_and_b64 s[48:49], s[50:51], s[48:49]
	v_cmp_gt_i32_e64 s[42:43], 3, v121
	s_and_b64 s[44:45], s[48:49], s[44:45]
	v_cmp_gt_i32_e64 s[40:41], 2, v121
	s_and_b64 s[42:43], s[44:45], s[42:43]
	v_cmp_gt_i32_e64 s[38:39], 1, v121
	s_and_b64 s[40:41], s[42:43], s[40:41]
	v_cmp_gt_i32_e64 s[36:37], 0, v121
	s_and_b64 s[38:39], s[40:41], s[38:39]
	s_and_b64 s[36:37], s[38:39], s[36:37]
	v_cmp_gt_i32_e64 s[34:35], 58, v121
	v_cndmask_b32_e64 v66, v66, v160, s[36:37]
	v_cmp_gt_i32_e64 s[36:37], 59, v121
	v_cmp_gt_i32_e64 s[30:31], 57, v121
	s_and_b64 s[34:35], s[36:37], s[34:35]
	v_cmp_gt_i32_e64 s[28:29], 56, v121
	s_and_b64 s[30:31], s[34:35], s[30:31]
	v_cmp_gt_i32_e64 s[26:27], 51, v121
	s_and_b64 s[28:29], s[30:31], s[28:29]
	v_cmp_gt_i32_e64 s[24:25], 50, v121
	s_and_b64 s[26:27], s[28:29], s[26:27]
	v_cmp_gt_i32_e64 s[22:23], 49, v121
	s_and_b64 s[24:25], s[26:27], s[24:25]
	v_cmp_gt_i32_e64 s[20:21], 48, v121
	s_and_b64 s[22:23], s[24:25], s[22:23]
	v_cmp_gt_i32_e64 s[18:19], 43, v121
	s_and_b64 s[20:21], s[22:23], s[20:21]
	v_cmp_gt_i32_e64 s[16:17], 42, v121
	s_and_b64 s[18:19], s[20:21], s[18:19]
	v_cmp_gt_i32_e64 s[14:15], 41, v121
	s_and_b64 s[16:17], s[18:19], s[16:17]
	v_cmp_gt_i32_e64 s[12:13], 40, v121
	s_and_b64 s[14:15], s[16:17], s[14:15]
	v_cmp_gt_i32_e64 s[10:11], 35, v121
	s_and_b64 s[12:13], s[14:15], s[12:13]
	v_cmp_gt_i32_e64 s[8:9], 34, v121
	s_and_b64 s[10:11], s[12:13], s[10:11]
	v_cmp_gt_i32_e64 s[6:7], 33, v121
	s_and_b64 s[8:9], s[10:11], s[8:9]
	v_cmp_gt_i32_e32 vcc, 32, v121
	s_and_b64 s[6:7], s[8:9], s[6:7]
	s_and_b64 vcc, s[6:7], vcc
	v_cndmask_b32_e64 v81, v81, v160, s[68:69]
	v_cndmask_b32_e64 v80, v80, v160, s[66:67]
	v_cndmask_b32_e64 v79, v79, v160, s[64:65]
	v_cndmask_b32_e64 v78, v78, v160, s[62:63]
	v_cndmask_b32_e64 v77, v77, v160, s[60:61]
	v_cndmask_b32_e64 v76, v76, v160, s[58:59]
	v_cndmask_b32_e64 v75, v75, v160, s[56:57]
	v_cndmask_b32_e64 v74, v74, v160, s[54:55]
	v_cndmask_b32_e64 v73, v73, v160, s[52:53]
	v_cndmask_b32_e64 v72, v72, v160, s[50:51]
	v_cndmask_b32_e64 v71, v71, v160, s[48:49]
	v_cndmask_b32_e64 v70, v70, v160, s[44:45]
	v_cndmask_b32_e64 v69, v69, v160, s[42:43]
	v_cndmask_b32_e64 v68, v68, v160, s[40:41]
	v_cndmask_b32_e64 v67, v67, v160, s[38:39]
	v_cndmask_b32_e64 v97, v97, v160, s[36:37]
	v_cndmask_b32_e64 v96, v96, v160, s[34:35]
	v_cndmask_b32_e64 v95, v95, v160, s[30:31]
	v_cndmask_b32_e64 v94, v94, v160, s[28:29]
	v_cndmask_b32_e64 v93, v93, v160, s[26:27]
	v_cndmask_b32_e64 v92, v92, v160, s[24:25]
	v_cndmask_b32_e64 v91, v91, v160, s[22:23]
	v_cndmask_b32_e64 v90, v90, v160, s[20:21]
	v_cndmask_b32_e64 v89, v89, v160, s[18:19]
	v_cndmask_b32_e64 v88, v88, v160, s[16:17]
	v_cndmask_b32_e64 v87, v87, v160, s[14:15]
	v_cndmask_b32_e64 v86, v86, v160, s[12:13]
	v_cndmask_b32_e64 v85, v85, v160, s[10:11]
	v_cndmask_b32_e64 v84, v84, v160, s[8:9]
	v_cndmask_b32_e64 v83, v83, v160, s[6:7]
	v_cndmask_b32_e32 v82, v82, v160, vcc

.LBB0_263:
	v_cndmask_b32_e64 v122, v121, v120, s[6:7]
	s_waitcnt vmcnt(0)
	v_mul_f32_e32 v120, 0xbe38aa3b, v122
	v_pk_fma_f32 v[80:81], v[80:81], s[84:85], v[120:121] op_sel_hi:[1,0,0]
	v_pk_fma_f32 v[78:79], v[78:79], s[84:85], v[120:121] op_sel_hi:[1,0,0]
	v_pk_fma_f32 v[76:77], v[76:77], s[84:85], v[120:121] op_sel_hi:[1,0,0]
	v_pk_fma_f32 v[74:75], v[74:75], s[84:85], v[120:121] op_sel_hi:[1,0,0]
	v_pk_fma_f32 v[72:73], v[72:73], s[84:85], v[120:121] op_sel_hi:[1,0,0]
	v_pk_fma_f32 v[70:71], v[70:71], s[84:85], v[120:121] op_sel_hi:[1,0,0]
	v_pk_fma_f32 v[68:69], v[68:69], s[84:85], v[120:121] op_sel_hi:[1,0,0]
	v_pk_fma_f32 v[66:67], v[66:67], s[84:85], v[120:121] op_sel_hi:[1,0,0]
	v_pk_fma_f32 v[186:187], v[88:89], s[84:85], v[120:121] op_sel_hi:[1,0,0]
	v_pk_fma_f32 v[196:197], v[86:87], s[84:85], v[120:121] op_sel_hi:[1,0,0]
	v_pk_fma_f32 v[86:87], v[84:85], s[84:85], v[120:121] op_sel_hi:[1,0,0]
	v_pk_fma_f32 v[88:89], v[82:83], s[84:85], v[120:121] op_sel_hi:[1,0,0]
	v_pk_fma_f32 v[148:149], v[96:97], s[84:85], v[120:121] op_sel_hi:[1,0,0]
	v_pk_fma_f32 v[150:151], v[94:95], s[84:85], v[120:121] op_sel_hi:[1,0,0]
	v_pk_fma_f32 v[152:153], v[92:93], s[84:85], v[120:121] op_sel_hi:[1,0,0]
	v_pk_fma_f32 v[154:155], v[90:91], s[84:85], v[120:121] op_sel_hi:[1,0,0]
	v_exp_f32_e32 v198, v66
	v_exp_f32_e32 v199, v67
	v_exp_f32_e32 v200, v68
	v_exp_f32_e32 v201, v69
	v_exp_f32_e32 v202, v70
	v_exp_f32_e32 v203, v71
	v_exp_f32_e32 v204, v72
	v_exp_f32_e32 v205, v73
	v_exp_f32_e32 v206, v74
	v_exp_f32_e32 v207, v75
	v_exp_f32_e32 v208, v76
	v_exp_f32_e32 v209, v77
	v_exp_f32_e32 v210, v78
	v_exp_f32_e32 v211, v79
	v_exp_f32_e32 v212, v80
	v_exp_f32_e32 v213, v81
	s_barrier
	s_add_u32 s6, s72, 0x180000
	s_addc_u32 s7, s73, 0
	s_mov_b32 m0, s85
	s_nop 0
	global_load_lds_dwordx4 v168, s[6:7] offset:0
	s_add_u32 s6, s88, 0x180000
	s_addc_u32 s7, s89, 0
	s_mov_b32 m0, s82
	s_nop 0
	global_load_lds_dwordx4 v169, s[6:7] offset:0
	s_nop 0
	s_mov_b32 m0, s83
	s_nop 0
	global_load_lds_dwordx4 v170, s[6:7] offset:0
	ds_read_b128 v[66:69], v175
	ds_read_b128 v[82:85], v175 offset:4096
	ds_read_b128 v[124:127], v176
	ds_read_b128 v[128:131], v176 offset:4096
	v_exp_f32_e32 v214, v88
	s_waitcnt lgkmcnt(3)
	v_mfma_f32_32x32x16_bf16 v[66:81], v[66:69], v[110:113], 0
	v_exp_f32_e32 v215, v89
	v_exp_f32_e32 v216, v86
	v_exp_f32_e32 v217, v87
	ds_read_b128 v[132:135], v177
	ds_read_b128 v[136:139], v177 offset:4096
	ds_read_b128 v[140:143], v178
	ds_read_b128 v[144:147], v178 offset:4096
	v_exp_f32_e32 v196, v196
	v_exp_f32_e32 v197, v197
	v_exp_f32_e32 v218, v186
	s_waitcnt lgkmcnt(6)
	v_mfma_f32_32x32x16_bf16 v[82:97], v[82:85], v[110:113], 0
	v_exp_f32_e32 v219, v187
	v_exp_f32_e32 v154, v154
	v_exp_f32_e32 v155, v155
	v_exp_f32_e32 v152, v152
	v_exp_f32_e32 v153, v153
	v_exp_f32_e32 v150, v150
	v_exp_f32_e32 v151, v151
	s_waitcnt lgkmcnt(5)
	v_mfma_f32_32x32x16_bf16 v[66:81], v[124:127], v[106:109], v[66:81]
	v_exp_f32_e32 v148, v148
	v_exp_f32_e32 v149, v149
	v_pk_add_f32 v[120:121], v[208:209], v[152:153]
	v_pk_add_f32 v[124:125], v[200:201], v[216:217]
	v_pk_add_f32 v[186:187], v[198:199], v[214:215]
	v_pk_add_f32 v[126:127], v[212:213], v[148:149]
	v_pk_add_f32 v[220:221], v[210:211], v[150:151]
	s_waitcnt lgkmcnt(4)
	v_mfma_f32_32x32x16_bf16 v[82:97], v[128:131], v[106:109], v[82:97]
	v_add_f32_e64 v128, v204, v218
	v_add_f32_e64 v129, v205, v219
	v_add_f32_e64 v130, v206, v154
	v_add_f32_e64 v131, v207, v155
	v_add_f32_e64 v222, v202, v196
	v_add_f32_e64 v223, v203, v197
	v_pk_add_f32 v[130:131], v[186:187], v[130:131]
	v_pk_add_f32 v[220:221], v[222:223], v[220:221]
	v_pk_add_f32 v[126:127], v[128:129], v[126:127]
	v_pk_add_f32 v[120:121], v[124:125], v[120:121]
	s_waitcnt lgkmcnt(3)
	v_mfma_f32_32x32x16_bf16 v[66:81], v[132:135], v[102:105], v[66:81]
	v_add_f32_e64 v120, v120, v126
	v_add_f32_e64 v121, v121, v127
	v_add_f32_e64 v124, v130, v220
	v_add_f32_e64 v125, v131, v221
	v_add_f32_e64 v120, v124, v120
	v_add_f32_e64 v121, v125, v121
	v_cvt_pk_bf16_f32 v124, v198, v199
	v_cvt_pk_bf16_f32 v125, v200, v201
	v_cvt_pk_bf16_f32 v126, v202, v203
	s_waitcnt lgkmcnt(2)
	v_mfma_f32_32x32x16_bf16 v[82:97], v[136:139], v[102:105], v[82:97]
	v_pk_add_f32 v[120:121], v[120:121], v[120:121] op_sel:[0,1] op_sel_hi:[1,0]
	v_cvt_pk_bf16_f32 v127, v204, v205
	v_cvt_pk_bf16_f32 v128, v206, v207
	v_cvt_pk_bf16_f32 v129, v208, v209
	v_cvt_pk_bf16_f32 v130, v210, v211
	v_cvt_pk_bf16_f32 v131, v212, v213
	s_nop 0
	v_mov_b32_e32 v186, v120
	s_waitcnt lgkmcnt(1)
	v_mfma_f32_32x32x16_bf16 v[66:81], v[140:143], v[98:101], v[66:81]
	v_permlane32_swap_b32_e32 v120, v186
	v_cvt_pk_bf16_f32 v132, v214, v215
	v_cvt_pk_bf16_f32 v133, v216, v217
	v_cvt_pk_bf16_f32 v134, v196, v197
	v_cvt_pk_bf16_f32 v135, v218, v219
	v_cvt_pk_bf16_f32 v136, v154, v155
	s_waitcnt lgkmcnt(0)
	v_mfma_f32_32x32x16_bf16 v[82:97], v[144:147], v[98:101], v[82:97]
	v_cvt_pk_bf16_f32 v137, v152, v153
	v_cvt_pk_bf16_f32 v138, v150, v151
	v_cvt_pk_bf16_f32 v139, v148, v149
	v_permlane32_swap_b32_e32 v124, v126
	v_permlane32_swap_b32_e32 v125, v127
	v_permlane32_swap_b32_e32 v128, v130
	v_permlane32_swap_b32_e32 v129, v131
	v_permlane32_swap_b32_e32 v132, v134
	v_permlane32_swap_b32_e32 v133, v135
	v_permlane32_swap_b32_e32 v136, v138
	v_permlane32_swap_b32_e32 v137, v139
	ds_read_b64_tr_b16 v[140:141], v166 offset:0
	ds_read_b64_tr_b16 v[142:143], v166 offset:0x800
	ds_read_b64_tr_b16 v[144:145], v166 offset:0x1000
	ds_read_b64_tr_b16 v[146:147], v166 offset:0x1800
	ds_read_b64_tr_b16 v[148:149], v166 offset:0x2000
	ds_read_b64_tr_b16 v[150:151], v166 offset:0x2800
	ds_read_b64_tr_b16 v[152:153], v166 offset:0x3000
	ds_read_b64_tr_b16 v[154:155], v166 offset:0x3800
	ds_read_b64_tr_b16 v[196:197], v166 offset:0x200
	ds_read_b64_tr_b16 v[198:199], v166 offset:0xa00
	ds_read_b64_tr_b16 v[200:201], v166 offset:0x1200
	ds_read_b64_tr_b16 v[202:203], v166 offset:0x1a00
	ds_read_b64_tr_b16 v[204:205], v166 offset:0x2200
	ds_read_b64_tr_b16 v[206:207], v166 offset:0x2a00
	ds_read_b64_tr_b16 v[208:209], v166 offset:0x3200
	ds_read_b64_tr_b16 v[210:211], v166 offset:0x3a00
	s_waitcnt lgkmcnt(8)
	s_nop 0
	v_mfma_f32_32x32x16_bf16 v[18:33], v[124:127], v[140:143], v[18:33]
	v_mfma_f32_32x32x16_bf16 v[18:33], v[128:131], v[144:147], v[18:33]
	v_mfma_f32_32x32x16_bf16 v[18:33], v[132:135], v[148:151], v[18:33]
	v_mfma_f32_32x32x16_bf16 v[18:33], v[136:139], v[152:155], v[18:33]
	ds_read_b64_tr_b16 v[140:141], v166 offset:0x400
	ds_read_b64_tr_b16 v[142:143], v166 offset:0xc00
	ds_read_b64_tr_b16 v[144:145], v166 offset:0x1400
	ds_read_b64_tr_b16 v[146:147], v166 offset:0x1c00
	ds_read_b64_tr_b16 v[148:149], v166 offset:0x2400
	ds_read_b64_tr_b16 v[150:151], v166 offset:0x2c00
	ds_read_b64_tr_b16 v[152:153], v166 offset:0x3400
	ds_read_b64_tr_b16 v[154:155], v166 offset:0x3c00
	s_waitcnt lgkmcnt(8)
	v_mfma_f32_32x32x16_bf16 v[34:49], v[124:127], v[196:199], v[34:49]
	v_mfma_f32_32x32x16_bf16 v[34:49], v[128:131], v[200:203], v[34:49]
	v_mfma_f32_32x32x16_bf16 v[34:49], v[132:135], v[204:207], v[34:49]
	v_mfma_f32_32x32x16_bf16 v[34:49], v[136:139], v[208:211], v[34:49]
	ds_read_b64_tr_b16 v[196:197], v166 offset:0x600
	ds_read_b64_tr_b16 v[198:199], v166 offset:0xe00
	ds_read_b64_tr_b16 v[200:201], v166 offset:0x1600
	ds_read_b64_tr_b16 v[202:203], v166 offset:0x1e00
	ds_read_b64_tr_b16 v[204:205], v166 offset:0x2600
	ds_read_b64_tr_b16 v[206:207], v166 offset:0x2e00
	ds_read_b64_tr_b16 v[208:209], v166 offset:0x3600
	ds_read_b64_tr_b16 v[210:211], v166 offset:0x3e00
	s_waitcnt lgkmcnt(8)
	v_mfma_f32_32x32x16_bf16 v[50:65], v[124:127], v[140:143], v[50:65]
	v_mfma_f32_32x32x16_bf16 v[50:65], v[128:131], v[144:147], v[50:65]
	v_mfma_f32_32x32x16_bf16 v[50:65], v[132:135], v[148:151], v[50:65]
	v_mfma_f32_32x32x16_bf16 v[50:65], v[136:139], v[152:155], v[50:65]
	s_waitcnt lgkmcnt(0)
	v_mfma_f32_32x32x16_bf16 v[2:17], v[124:127], v[196:199], v[2:17]
	s_sub_i32 s6, s95, 64
	s_cmp_le_i32 s6, s77
	v_mfma_f32_32x32x16_bf16 v[2:17], v[128:131], v[200:203], v[2:17]
	v_mfma_f32_32x32x16_bf16 v[2:17], v[132:135], v[204:207], v[2:17]
	v_mfma_f32_32x32x16_bf16 v[2:17], v[136:139], v[208:211], v[2:17]
	s_cbranch_scc1 .LBB0_265
	v_add_u32_e32 v121, 0xffffff80, v183
	v_cmp_gt_i32_e64 s[66:67], 26, v121
	v_cmp_gt_i32_e64 s[68:69], 27, v121
	v_cmp_gt_i32_e64 s[64:65], 25, v121
	s_and_b64 s[66:67], s[68:69], s[66:67]
	v_cmp_gt_i32_e64 s[62:63], 24, v121
	s_and_b64 s[64:65], s[66:67], s[64:65]
	v_cmp_gt_i32_e64 s[60:61], 19, v121
	s_and_b64 s[62:63], s[64:65], s[62:63]
	v_cmp_gt_i32_e64 s[58:59], 18, v121
	s_and_b64 s[60:61], s[62:63], s[60:61]
	v_cmp_gt_i32_e64 s[56:57], 17, v121
	s_and_b64 s[58:59], s[60:61], s[58:59]
	v_cmp_gt_i32_e64 s[54:55], 16, v121
	s_and_b64 s[56:57], s[58:59], s[56:57]
	v_cmp_gt_i32_e64 s[52:53], 11, v121
	s_and_b64 s[54:55], s[56:57], s[54:55]
	v_cmp_gt_i32_e64 s[50:51], 10, v121
	s_and_b64 s[52:53], s[54:55], s[52:53]
	v_cmp_gt_i32_e64 s[48:49], 9, v121
	s_and_b64 s[50:51], s[52:53], s[50:51]
	v_cmp_gt_i32_e64 s[44:45], 8, v121
	s_and_b64 s[48:49], s[50:51], s[48:49]
	v_cmp_gt_i32_e64 s[42:43], 3, v121
	s_and_b64 s[44:45], s[48:49], s[44:45]
	v_cmp_gt_i32_e64 s[40:41], 2, v121
	s_and_b64 s[42:43], s[44:45], s[42:43]
	v_cmp_gt_i32_e64 s[38:39], 1, v121
	s_and_b64 s[40:41], s[42:43], s[40:41]
	v_cmp_gt_i32_e64 s[36:37], 0, v121
	s_and_b64 s[38:39], s[40:41], s[38:39]
	s_and_b64 s[36:37], s[38:39], s[36:37]
	v_cmp_gt_i32_e64 s[34:35], 58, v121
	v_cndmask_b32_e64 v66, v66, v160, s[36:37]
	v_cmp_gt_i32_e64 s[36:37], 59, v121
	v_cmp_gt_i32_e64 s[30:31], 57, v121
	s_and_b64 s[34:35], s[36:37], s[34:35]
	v_cmp_gt_i32_e64 s[28:29], 56, v121
	s_and_b64 s[30:31], s[34:35], s[30:31]
	v_cmp_gt_i32_e64 s[26:27], 51, v121
	s_and_b64 s[28:29], s[30:31], s[28:29]
	v_cmp_gt_i32_e64 s[24:25], 50, v121
	s_and_b64 s[26:27], s[28:29], s[26:27]
	v_cmp_gt_i32_e64 s[22:23], 49, v121
	s_and_b64 s[24:25], s[26:27], s[24:25]
	v_cmp_gt_i32_e64 s[20:21], 48, v121
	s_and_b64 s[22:23], s[24:25], s[22:23]
	v_cmp_gt_i32_e64 s[18:19], 43, v121
	s_and_b64 s[20:21], s[22:23], s[20:21]
	v_cmp_gt_i32_e64 s[16:17], 42, v121
	s_and_b64 s[18:19], s[20:21], s[18:19]
	v_cmp_gt_i32_e64 s[14:15], 41, v121
	s_and_b64 s[16:17], s[18:19], s[16:17]
	v_cmp_gt_i32_e64 s[12:13], 40, v121
	s_and_b64 s[14:15], s[16:17], s[14:15]
	v_cmp_gt_i32_e64 s[10:11], 35, v121
	s_and_b64 s[12:13], s[14:15], s[12:13]
	v_cmp_gt_i32_e64 s[8:9], 34, v121
	s_and_b64 s[10:11], s[12:13], s[10:11]
	v_cmp_gt_i32_e64 s[6:7], 33, v121
	s_and_b64 s[8:9], s[10:11], s[8:9]
	v_cmp_gt_i32_e32 vcc, 32, v121
	s_and_b64 s[6:7], s[8:9], s[6:7]
	s_and_b64 vcc, s[6:7], vcc
	v_cndmask_b32_e64 v81, v81, v160, s[68:69]
	v_cndmask_b32_e64 v80, v80, v160, s[66:67]
	v_cndmask_b32_e64 v79, v79, v160, s[64:65]
	v_cndmask_b32_e64 v78, v78, v160, s[62:63]
	v_cndmask_b32_e64 v77, v77, v160, s[60:61]
	v_cndmask_b32_e64 v76, v76, v160, s[58:59]
	v_cndmask_b32_e64 v75, v75, v160, s[56:57]
	v_cndmask_b32_e64 v74, v74, v160, s[54:55]
	v_cndmask_b32_e64 v73, v73, v160, s[52:53]
	v_cndmask_b32_e64 v72, v72, v160, s[50:51]
	v_cndmask_b32_e64 v71, v71, v160, s[48:49]
	v_cndmask_b32_e64 v70, v70, v160, s[44:45]
	v_cndmask_b32_e64 v69, v69, v160, s[42:43]
	v_cndmask_b32_e64 v68, v68, v160, s[40:41]
	v_cndmask_b32_e64 v67, v67, v160, s[38:39]
	v_cndmask_b32_e64 v97, v97, v160, s[36:37]
	v_cndmask_b32_e64 v96, v96, v160, s[34:35]
	v_cndmask_b32_e64 v95, v95, v160, s[30:31]
	v_cndmask_b32_e64 v94, v94, v160, s[28:29]
	v_cndmask_b32_e64 v93, v93, v160, s[26:27]
	v_cndmask_b32_e64 v92, v92, v160, s[24:25]
	v_cndmask_b32_e64 v91, v91, v160, s[22:23]
	v_cndmask_b32_e64 v90, v90, v160, s[20:21]
	v_cndmask_b32_e64 v89, v89, v160, s[18:19]
	v_cndmask_b32_e64 v88, v88, v160, s[16:17]
	v_cndmask_b32_e64 v87, v87, v160, s[14:15]
	v_cndmask_b32_e64 v86, v86, v160, s[12:13]
	v_cndmask_b32_e64 v85, v85, v160, s[10:11]
	v_cndmask_b32_e64 v84, v84, v160, s[8:9]
	v_cndmask_b32_e64 v83, v83, v160, s[6:7]
	v_cndmask_b32_e32 v82, v82, v160, vcc

.LBB0_269:
	v_cndmask_b32_e64 v121, v121, v122, s[6:7]
	s_waitcnt vmcnt(0)
	v_mul_f32_e32 v122, 0xbe38aa3b, v121
	v_pk_fma_f32 v[80:81], v[80:81], s[84:85], v[122:123] op_sel_hi:[1,0,0]
	v_pk_fma_f32 v[78:79], v[78:79], s[84:85], v[122:123] op_sel_hi:[1,0,0]
	v_pk_fma_f32 v[76:77], v[76:77], s[84:85], v[122:123] op_sel_hi:[1,0,0]
	v_pk_fma_f32 v[74:75], v[74:75], s[84:85], v[122:123] op_sel_hi:[1,0,0]
	v_pk_fma_f32 v[72:73], v[72:73], s[84:85], v[122:123] op_sel_hi:[1,0,0]
	v_pk_fma_f32 v[70:71], v[70:71], s[84:85], v[122:123] op_sel_hi:[1,0,0]
	v_pk_fma_f32 v[68:69], v[68:69], s[84:85], v[122:123] op_sel_hi:[1,0,0]
	v_pk_fma_f32 v[66:67], v[66:67], s[84:85], v[122:123] op_sel_hi:[1,0,0]
	v_pk_fma_f32 v[138:139], v[96:97], s[84:85], v[122:123] op_sel_hi:[1,0,0]
	v_pk_fma_f32 v[148:149], v[94:95], s[84:85], v[122:123] op_sel_hi:[1,0,0]
	v_pk_fma_f32 v[150:151], v[92:93], s[84:85], v[122:123] op_sel_hi:[1,0,0]
	v_pk_fma_f32 v[152:153], v[90:91], s[84:85], v[122:123] op_sel_hi:[1,0,0]
	v_pk_fma_f32 v[154:155], v[88:89], s[84:85], v[122:123] op_sel_hi:[1,0,0]
	v_pk_fma_f32 v[196:197], v[86:87], s[84:85], v[122:123] op_sel_hi:[1,0,0]
	v_pk_fma_f32 v[198:199], v[84:85], s[84:85], v[122:123] op_sel_hi:[1,0,0]
	v_pk_fma_f32 v[200:201], v[82:83], s[84:85], v[122:123] op_sel_hi:[1,0,0]
	v_exp_f32_e32 v202, v66
	v_exp_f32_e32 v203, v67
	v_exp_f32_e32 v204, v68
	v_exp_f32_e32 v205, v69
	v_exp_f32_e32 v206, v70
	v_exp_f32_e32 v207, v71
	v_exp_f32_e32 v208, v72
	v_exp_f32_e32 v209, v73
	v_exp_f32_e32 v210, v74
	v_exp_f32_e32 v211, v75
	v_exp_f32_e32 v212, v76
	v_exp_f32_e32 v213, v77
	v_exp_f32_e32 v214, v78
	v_exp_f32_e32 v215, v79
	v_exp_f32_e32 v216, v80
	v_exp_f32_e32 v217, v81
	s_barrier
	s_add_u32 s6, s72, 0x1c0000
	s_addc_u32 s7, s73, 0
	s_mov_b32 m0, s81
	s_nop 0
	global_load_lds_dwordx4 v168, s[6:7] offset:0
	s_add_u32 s6, s88, 0x1c0000
	s_addc_u32 s7, s89, 0
	s_mov_b32 m0, s78
	s_nop 0
	global_load_lds_dwordx4 v169, s[6:7] offset:0
	s_nop 0
	s_mov_b32 m0, s79
	s_nop 0
	global_load_lds_dwordx4 v170, s[6:7] offset:0
	ds_read_b128 v[66:69], v171
	ds_read_b128 v[70:73], v171 offset:4096
	ds_read_b128 v[122:125], v172
	ds_read_b128 v[126:129], v172 offset:4096
	ds_read_b128 v[130:133], v173
	ds_read_b128 v[134:137], v173 offset:4096
	ds_read_b128 v[140:143], v174
	ds_read_b128 v[144:147], v174 offset:4096
	s_waitcnt lgkmcnt(7)
	v_mfma_f32_32x32x16_bf16 v[82:97], v[66:69], v[110:113], 0
	v_exp_f32_e32 v200, v200
	v_exp_f32_e32 v201, v201
	v_exp_f32_e32 v198, v198
	v_exp_f32_e32 v199, v199
	v_exp_f32_e32 v196, v196
	v_exp_f32_e32 v197, v197
	v_exp_f32_e32 v154, v154
	s_waitcnt lgkmcnt(6)
	v_mfma_f32_32x32x16_bf16 v[66:81], v[70:73], v[110:113], 0
	v_exp_f32_e32 v155, v155
	v_exp_f32_e32 v152, v152
	v_exp_f32_e32 v153, v153
	v_exp_f32_e32 v150, v150
	v_exp_f32_e32 v151, v151
	v_exp_f32_e32 v148, v148
	v_exp_f32_e32 v149, v149
	s_waitcnt lgkmcnt(5)
	v_mfma_f32_32x32x16_bf16 v[82:97], v[122:125], v[106:109], v[82:97]
	v_exp_f32_e32 v218, v138
	v_exp_f32_e32 v219, v139
	v_pk_add_f32 v[122:123], v[212:213], v[150:151]
	v_pk_add_f32 v[124:125], v[204:205], v[198:199]
	v_pk_add_f32 v[138:139], v[210:211], v[152:153]
	v_pk_add_f32 v[220:221], v[202:203], v[200:201]
	v_pk_add_f32 v[222:223], v[214:215], v[148:149]
	s_waitcnt lgkmcnt(4)
	v_mfma_f32_32x32x16_bf16 v[66:81], v[126:129], v[106:109], v[66:81]
	v_add_f32_e64 v126, v216, v218
	v_add_f32_e64 v127, v217, v219
	v_add_f32_e64 v128, v208, v154
	v_add_f32_e64 v129, v209, v155
	v_add_f32_e64 v224, v206, v196
	v_add_f32_e64 v225, v207, v197
	v_pk_add_f32 v[126:127], v[128:129], v[126:127]
	v_pk_add_f32 v[222:223], v[224:225], v[222:223]
	v_pk_add_f32 v[122:123], v[124:125], v[122:123]
	s_waitcnt lgkmcnt(3)
	v_mfma_f32_32x32x16_bf16 v[82:97], v[130:133], v[102:105], v[82:97]
	v_add_f32_e64 v130, v220, v138
	v_add_f32_e64 v131, v221, v139
	v_add_f32_e64 v122, v122, v126
	v_add_f32_e64 v123, v123, v127
	v_add_f32_e64 v124, v130, v222
	v_add_f32_e64 v125, v131, v223
	v_pk_add_f32 v[122:123], v[124:125], v[122:123]
	s_nop 0
	v_pk_add_f32 v[138:139], v[122:123], v[122:123] op_sel:[0,1] op_sel_hi:[1,0]
	s_waitcnt lgkmcnt(2)
	v_mfma_f32_32x32x16_bf16 v[66:81], v[134:137], v[102:105], v[66:81]
	v_mov_b32_e32 v195, v138
	s_nop 1
	v_permlane32_swap_b32_e32 v138, v195
	v_cvt_pk_bf16_f32 v122, v202, v203
	v_cvt_pk_bf16_f32 v123, v204, v205
	v_cvt_pk_bf16_f32 v124, v206, v207
	v_cvt_pk_bf16_f32 v125, v208, v209
	s_waitcnt lgkmcnt(1)
	v_mfma_f32_32x32x16_bf16 v[82:97], v[140:143], v[98:101], v[82:97]
	v_cvt_pk_bf16_f32 v126, v210, v211
	v_cvt_pk_bf16_f32 v127, v212, v213
	v_cvt_pk_bf16_f32 v128, v214, v215
	v_cvt_pk_bf16_f32 v129, v216, v217
	v_cvt_pk_bf16_f32 v130, v200, v201
	v_cvt_pk_bf16_f32 v131, v198, v199
	v_cvt_pk_bf16_f32 v132, v196, v197
	s_waitcnt lgkmcnt(0)
	v_mfma_f32_32x32x16_bf16 v[66:81], v[144:147], v[98:101], v[66:81]
	v_cvt_pk_bf16_f32 v133, v154, v155
	v_cvt_pk_bf16_f32 v134, v152, v153
	v_cvt_pk_bf16_f32 v135, v150, v151
	v_cvt_pk_bf16_f32 v136, v148, v149
	v_cvt_pk_bf16_f32 v137, v218, v219
	v_permlane32_swap_b32_e32 v122, v124
	v_permlane32_swap_b32_e32 v123, v125
	v_permlane32_swap_b32_e32 v126, v128
	v_permlane32_swap_b32_e32 v127, v129
	v_permlane32_swap_b32_e32 v130, v132
	v_permlane32_swap_b32_e32 v131, v133
	v_permlane32_swap_b32_e32 v134, v136
	v_permlane32_swap_b32_e32 v135, v137
	ds_read_b64_tr_b16 v[140:141], v166 offset:0x4000
	ds_read_b64_tr_b16 v[142:143], v166 offset:0x4800
	ds_read_b64_tr_b16 v[144:145], v166 offset:0x5000
	ds_read_b64_tr_b16 v[146:147], v166 offset:0x5800
	ds_read_b64_tr_b16 v[148:149], v166 offset:0x6000
	ds_read_b64_tr_b16 v[150:151], v166 offset:0x6800
	ds_read_b64_tr_b16 v[152:153], v166 offset:0x7000
	ds_read_b64_tr_b16 v[154:155], v166 offset:0x7800
	ds_read_b64_tr_b16 v[196:197], v166 offset:0x4200
	ds_read_b64_tr_b16 v[198:199], v166 offset:0x4a00
	ds_read_b64_tr_b16 v[200:201], v166 offset:0x5200
	ds_read_b64_tr_b16 v[202:203], v166 offset:0x5a00
	ds_read_b64_tr_b16 v[204:205], v166 offset:0x6200
	ds_read_b64_tr_b16 v[206:207], v166 offset:0x6a00
	ds_read_b64_tr_b16 v[208:209], v166 offset:0x7200
	ds_read_b64_tr_b16 v[210:211], v166 offset:0x7a00
	s_waitcnt lgkmcnt(8)
	s_nop 0
	v_mfma_f32_32x32x16_bf16 v[18:33], v[122:125], v[140:143], v[18:33]
	v_mfma_f32_32x32x16_bf16 v[18:33], v[126:129], v[144:147], v[18:33]
	v_mfma_f32_32x32x16_bf16 v[18:33], v[130:133], v[148:151], v[18:33]
	v_mfma_f32_32x32x16_bf16 v[18:33], v[134:137], v[152:155], v[18:33]
	ds_read_b64_tr_b16 v[140:141], v166 offset:0x4400
	ds_read_b64_tr_b16 v[142:143], v166 offset:0x4c00
	ds_read_b64_tr_b16 v[144:145], v166 offset:0x5400
	ds_read_b64_tr_b16 v[146:147], v166 offset:0x5c00
	ds_read_b64_tr_b16 v[148:149], v166 offset:0x6400
	ds_read_b64_tr_b16 v[150:151], v166 offset:0x6c00
	ds_read_b64_tr_b16 v[152:153], v166 offset:0x7400
	ds_read_b64_tr_b16 v[154:155], v166 offset:0x7c00
	s_waitcnt lgkmcnt(8)
	v_mfma_f32_32x32x16_bf16 v[34:49], v[122:125], v[196:199], v[34:49]
	v_mfma_f32_32x32x16_bf16 v[34:49], v[126:129], v[200:203], v[34:49]
	v_mfma_f32_32x32x16_bf16 v[34:49], v[130:133], v[204:207], v[34:49]
	v_mfma_f32_32x32x16_bf16 v[34:49], v[134:137], v[208:211], v[34:49]
	ds_read_b64_tr_b16 v[196:197], v166 offset:0x4600
	ds_read_b64_tr_b16 v[198:199], v166 offset:0x4e00
	ds_read_b64_tr_b16 v[200:201], v166 offset:0x5600
	ds_read_b64_tr_b16 v[202:203], v166 offset:0x5e00
	ds_read_b64_tr_b16 v[204:205], v166 offset:0x6600
	ds_read_b64_tr_b16 v[206:207], v166 offset:0x6e00
	ds_read_b64_tr_b16 v[208:209], v166 offset:0x7600
	ds_read_b64_tr_b16 v[210:211], v166 offset:0x7e00
	s_waitcnt lgkmcnt(8)
	v_mfma_f32_32x32x16_bf16 v[50:65], v[122:125], v[140:143], v[50:65]
	v_mfma_f32_32x32x16_bf16 v[50:65], v[126:129], v[144:147], v[50:65]
	v_mfma_f32_32x32x16_bf16 v[50:65], v[130:133], v[148:151], v[50:65]
	v_mfma_f32_32x32x16_bf16 v[50:65], v[134:137], v[152:155], v[50:65]
	s_waitcnt lgkmcnt(0)
	v_mfma_f32_32x32x16_bf16 v[2:17], v[122:125], v[196:199], v[2:17]
	s_cmp_le_i32 s95, s77
	v_mfma_f32_32x32x16_bf16 v[2:17], v[126:129], v[200:203], v[2:17]
	v_mfma_f32_32x32x16_bf16 v[2:17], v[130:133], v[204:207], v[2:17]
	v_mfma_f32_32x32x16_bf16 v[2:17], v[134:137], v[208:211], v[2:17]
	s_cbranch_scc1 .LBB0_271
	v_add_u32_e32 v122, 0xffffff40, v183
	v_cmp_gt_i32_e64 s[66:67], 26, v122
	v_cmp_gt_i32_e64 s[68:69], 27, v122
	v_cmp_gt_i32_e64 s[64:65], 25, v122
	s_and_b64 s[66:67], s[68:69], s[66:67]
	v_cmp_gt_i32_e64 s[62:63], 24, v122
	s_and_b64 s[64:65], s[66:67], s[64:65]
	v_cmp_gt_i32_e64 s[60:61], 19, v122
	s_and_b64 s[62:63], s[64:65], s[62:63]
	v_cmp_gt_i32_e64 s[58:59], 18, v122
	s_and_b64 s[60:61], s[62:63], s[60:61]
	v_cmp_gt_i32_e64 s[56:57], 17, v122
	s_and_b64 s[58:59], s[60:61], s[58:59]
	v_cmp_gt_i32_e64 s[54:55], 16, v122
	s_and_b64 s[56:57], s[58:59], s[56:57]
	v_cmp_gt_i32_e64 s[52:53], 11, v122
	s_and_b64 s[54:55], s[56:57], s[54:55]
	v_cmp_gt_i32_e64 s[50:51], 10, v122
	s_and_b64 s[52:53], s[54:55], s[52:53]
	v_cmp_gt_i32_e64 s[48:49], 9, v122
	s_and_b64 s[50:51], s[52:53], s[50:51]
	v_cmp_gt_i32_e64 s[44:45], 8, v122
	s_and_b64 s[48:49], s[50:51], s[48:49]
	v_cmp_gt_i32_e64 s[42:43], 3, v122
	s_and_b64 s[44:45], s[48:49], s[44:45]
	v_cmp_gt_i32_e64 s[40:41], 2, v122
	s_and_b64 s[42:43], s[44:45], s[42:43]
	v_cmp_gt_i32_e64 s[38:39], 1, v122
	s_and_b64 s[40:41], s[42:43], s[40:41]
	v_cmp_gt_i32_e64 s[36:37], 0, v122
	s_and_b64 s[38:39], s[40:41], s[38:39]
	s_and_b64 s[36:37], s[38:39], s[36:37]
	v_cmp_gt_i32_e64 s[34:35], 58, v122
	v_cndmask_b32_e64 v82, v82, v160, s[36:37]
	v_cmp_gt_i32_e64 s[36:37], 59, v122
	v_cmp_gt_i32_e64 s[30:31], 57, v122
	s_and_b64 s[34:35], s[36:37], s[34:35]
	v_cmp_gt_i32_e64 s[28:29], 56, v122
	s_and_b64 s[30:31], s[34:35], s[30:31]
	v_cmp_gt_i32_e64 s[26:27], 51, v122
	s_and_b64 s[28:29], s[30:31], s[28:29]
	v_cmp_gt_i32_e64 s[24:25], 50, v122
	s_and_b64 s[26:27], s[28:29], s[26:27]
	v_cmp_gt_i32_e64 s[22:23], 49, v122
	s_and_b64 s[24:25], s[26:27], s[24:25]
	v_cmp_gt_i32_e64 s[20:21], 48, v122
	s_and_b64 s[22:23], s[24:25], s[22:23]
	v_cmp_gt_i32_e64 s[18:19], 43, v122
	s_and_b64 s[20:21], s[22:23], s[20:21]
	v_cmp_gt_i32_e64 s[16:17], 42, v122
	s_and_b64 s[18:19], s[20:21], s[18:19]
	v_cmp_gt_i32_e64 s[14:15], 41, v122
	s_and_b64 s[16:17], s[18:19], s[16:17]
	v_cmp_gt_i32_e64 s[12:13], 40, v122
	s_and_b64 s[14:15], s[16:17], s[14:15]
	v_cmp_gt_i32_e64 s[10:11], 35, v122
	s_and_b64 s[12:13], s[14:15], s[12:13]
	v_cmp_gt_i32_e64 s[8:9], 34, v122
	s_and_b64 s[10:11], s[12:13], s[10:11]
	v_cmp_gt_i32_e64 s[6:7], 33, v122
	s_and_b64 s[8:9], s[10:11], s[8:9]
	v_cmp_gt_i32_e32 vcc, 32, v122
	s_and_b64 s[6:7], s[8:9], s[6:7]
	s_and_b64 vcc, s[6:7], vcc
	v_cndmask_b32_e64 v97, v97, v160, s[68:69]
	v_cndmask_b32_e64 v96, v96, v160, s[66:67]
	v_cndmask_b32_e64 v95, v95, v160, s[64:65]
	v_cndmask_b32_e64 v94, v94, v160, s[62:63]
	v_cndmask_b32_e64 v93, v93, v160, s[60:61]
	v_cndmask_b32_e64 v92, v92, v160, s[58:59]
	v_cndmask_b32_e64 v91, v91, v160, s[56:57]
	v_cndmask_b32_e64 v90, v90, v160, s[54:55]
	v_cndmask_b32_e64 v89, v89, v160, s[52:53]
	v_cndmask_b32_e64 v88, v88, v160, s[50:51]
	v_cndmask_b32_e64 v87, v87, v160, s[48:49]
	v_cndmask_b32_e64 v86, v86, v160, s[44:45]
	v_cndmask_b32_e64 v85, v85, v160, s[42:43]
	v_cndmask_b32_e64 v84, v84, v160, s[40:41]
	v_cndmask_b32_e64 v83, v83, v160, s[38:39]
	v_cndmask_b32_e64 v81, v81, v160, s[36:37]
	v_cndmask_b32_e64 v80, v80, v160, s[34:35]
	v_cndmask_b32_e64 v79, v79, v160, s[30:31]
	v_cndmask_b32_e64 v78, v78, v160, s[28:29]
	v_cndmask_b32_e64 v77, v77, v160, s[26:27]
	v_cndmask_b32_e64 v76, v76, v160, s[24:25]
	v_cndmask_b32_e64 v75, v75, v160, s[22:23]
	v_cndmask_b32_e64 v74, v74, v160, s[20:21]
	v_cndmask_b32_e64 v73, v73, v160, s[18:19]
	v_cndmask_b32_e64 v72, v72, v160, s[16:17]
	v_cndmask_b32_e64 v71, v71, v160, s[14:15]
	v_cndmask_b32_e64 v70, v70, v160, s[12:13]
	v_cndmask_b32_e64 v69, v69, v160, s[10:11]
	v_cndmask_b32_e64 v68, v68, v160, s[8:9]
	v_cndmask_b32_e64 v67, v67, v160, s[6:7]
	v_cndmask_b32_e32 v66, v66, v160, vcc

.LBB0_279:
	ds_read_b128 v[66:69], v175
	ds_read_b128 v[82:85], v175 offset:4096
	ds_read_b128 v[86:89], v176
	ds_read_b128 v[114:117], v176 offset:4096
	s_waitcnt lgkmcnt(0)
	v_mfma_f32_32x32x16_bf16 v[66:81], v[66:69], v[110:113], 0
	v_mfma_f32_32x32x16_bf16 v[66:81], v[86:89], v[106:109], v[66:81]
	ds_read_b128 v[86:89], v177
	ds_read_b128 v[172:175], v177 offset:4096
	s_waitcnt lgkmcnt(1)
	v_mfma_f32_32x32x16_bf16 v[66:81], v[86:89], v[102:105], v[66:81]
	ds_read_b128 v[86:89], v178
	ds_read_b128 v[182:185], v178 offset:4096
	s_waitcnt lgkmcnt(1)
	v_mfma_f32_32x32x16_bf16 v[66:81], v[86:89], v[98:101], v[66:81]
	v_readlane_b32 s4, v254, 28
	v_readlane_b32 s5, v254, 29
	s_mov_b32 m0, s85
	s_nop 0
	global_load_lds_dwordx4 v168, s[4:5] offset:0
	s_nop 0
	s_mov_b32 m0, s86
	s_nop 0
	global_load_lds_dwordx4 v169, s[46:47] offset:0
	s_nop 0
	s_mov_b32 m0, s87
	s_nop 0
	global_load_lds_dwordx4 v170, s[46:47] offset:0
	v_mfma_f32_32x32x16_bf16 v[82:97], v[82:85], v[110:113], 0
	v_readlane_b32 s4, v254, 13
	v_readlane_b32 s5, v254, 14
	v_mfma_f32_32x32x16_bf16 v[82:97], v[114:117], v[106:109], v[82:97]
	v_or_b32_e32 v106, s96, v165
	v_ashrrev_i32_e32 v107, 31, v106
	v_lshlrev_b64 v[106:107], 12, v[106:107]
	v_lshl_add_u64 v[106:107], s[4:5], 0, v[106:107]
	v_lshl_add_u64 v[114:115], v[106:107], 0, v[118:119]
	global_load_dwordx4 v[110:113], v[114:115], off
	global_load_dwordx4 v[106:109], v[114:115], off offset:32
	v_mfma_f32_32x32x16_bf16 v[82:97], v[172:175], v[102:105], v[82:97]
	global_load_dwordx4 v[102:105], v[114:115], off offset:64
	s_nop 0
	global_load_dwordx4 v[114:117], v[114:115], off offset:96
	s_waitcnt lgkmcnt(0)
	v_mfma_f32_32x32x16_bf16 v[82:97], v[182:185], v[98:101], v[82:97]
	v_exp_f32_e32 v100, v154
	v_exp_f32_e32 v101, v155
	v_exp_f32_e32 v152, v152
	v_exp_f32_e32 v153, v153
	v_exp_f32_e32 v150, v150
	v_exp_f32_e32 v151, v151
	v_exp_f32_e32 v148, v148
	v_exp_f32_e32 v149, v149
	v_exp_f32_e32 v146, v146
	v_exp_f32_e32 v147, v147
	v_exp_f32_e32 v144, v144
	v_exp_f32_e32 v145, v145
	v_exp_f32_e32 v154, v142
	v_exp_f32_e32 v168, v140
	v_exp_f32_e32 v169, v141
	v_exp_f32_e32 v155, v143
	v_pk_add_f32 v[98:99], v[126:127], v[144:145]
	v_pk_add_f32 v[140:141], v[134:135], v[152:153]
	v_pk_add_f32 v[142:143], v[122:123], v[168:169]
	v_pk_add_f32 v[170:171], v[130:131], v[148:149]
	v_pk_add_f32 v[172:173], v[128:129], v[146:147]
	v_pk_add_f32 v[174:175], v[136:137], v[100:101]
	v_pk_add_f32 v[176:177], v[124:125], v[154:155]
	v_pk_add_f32 v[182:183], v[132:133], v[150:151]
	v_pk_add_f32 v[172:173], v[174:175], v[172:173]
	v_pk_add_f32 v[176:177], v[182:183], v[176:177]
	v_pk_add_f32 v[142:143], v[170:171], v[142:143]
	v_pk_add_f32 v[98:99], v[140:141], v[98:99]
	v_pk_add_f32 v[140:141], v[172:173], v[176:177]
	v_pk_add_f32 v[98:99], v[98:99], v[142:143]
	s_nop 0
	v_pk_add_f32 v[98:99], v[140:141], v[98:99]
	v_cvt_pk_bf16_f32 v140, v136, v137
	v_cvt_pk_bf16_f32 v141, v134, v135
	v_cvt_pk_bf16_f32 v142, v132, v133
	v_cvt_pk_bf16_f32 v143, v130, v131
	v_cvt_pk_bf16_f32 v128, v128, v129
	s_nop 0
	v_pk_add_f32 v[98:99], v[98:99], v[98:99] op_sel:[0,1] op_sel_hi:[1,0]
	v_cvt_pk_bf16_f32 v129, v126, v127
	v_cvt_pk_bf16_f32 v130, v124, v125
	v_cvt_pk_bf16_f32 v131, v122, v123
	v_cvt_pk_bf16_f32 v122, v100, v101
	v_cvt_pk_bf16_f32 v123, v152, v153
	s_nop 0
	v_mov_b32_e32 v99, v98
	s_nop 1
	v_permlane32_swap_b32_e32 v98, v99
	v_cvt_pk_bf16_f32 v124, v150, v151
	v_cvt_pk_bf16_f32 v125, v148, v149
	v_cvt_pk_bf16_f32 v132, v146, v147
	v_cvt_pk_bf16_f32 v133, v144, v145
	v_cvt_pk_bf16_f32 v134, v154, v155
	v_cvt_pk_bf16_f32 v135, v168, v169
	v_permlane32_swap_b32_e32 v140, v142
	v_permlane32_swap_b32_e32 v141, v143
	v_permlane32_swap_b32_e32 v128, v130
	v_permlane32_swap_b32_e32 v129, v131
	v_permlane32_swap_b32_e32 v122, v124
	v_permlane32_swap_b32_e32 v123, v125
	v_permlane32_swap_b32_e32 v132, v134
	v_permlane32_swap_b32_e32 v133, v135
	ds_read_b64_tr_b16 v[144:145], v166 offset:0x8000
	ds_read_b64_tr_b16 v[146:147], v166 offset:0x8800
	ds_read_b64_tr_b16 v[148:149], v166 offset:0x9000
	ds_read_b64_tr_b16 v[150:151], v166 offset:0x9800
	ds_read_b64_tr_b16 v[152:153], v166 offset:0xa000
	ds_read_b64_tr_b16 v[154:155], v166 offset:0xa800
	ds_read_b64_tr_b16 v[168:169], v166 offset:0xb000
	ds_read_b64_tr_b16 v[170:171], v166 offset:0xb800
	ds_read_b64_tr_b16 v[172:173], v166 offset:0x8200
	ds_read_b64_tr_b16 v[174:175], v166 offset:0x8a00
	ds_read_b64_tr_b16 v[182:183], v166 offset:0x9200
	ds_read_b64_tr_b16 v[184:185], v166 offset:0x9a00
	ds_read_b64_tr_b16 v[196:197], v166 offset:0xa200
	ds_read_b64_tr_b16 v[198:199], v166 offset:0xaa00
	ds_read_b64_tr_b16 v[200:201], v166 offset:0xb200
	ds_read_b64_tr_b16 v[202:203], v166 offset:0xba00
	s_waitcnt lgkmcnt(8)
	s_nop 0
	v_mfma_f32_32x32x16_bf16 v[18:33], v[140:143], v[144:147], v[18:33]
	v_mfma_f32_32x32x16_bf16 v[18:33], v[128:131], v[148:151], v[18:33]
	v_mfma_f32_32x32x16_bf16 v[18:33], v[122:125], v[152:155], v[18:33]
	v_mfma_f32_32x32x16_bf16 v[18:33], v[132:135], v[168:171], v[18:33]
	ds_read_b64_tr_b16 v[144:145], v166 offset:0x8400
	ds_read_b64_tr_b16 v[146:147], v166 offset:0x8c00
	ds_read_b64_tr_b16 v[148:149], v166 offset:0x9400
	ds_read_b64_tr_b16 v[150:151], v166 offset:0x9c00
	ds_read_b64_tr_b16 v[152:153], v166 offset:0xa400
	ds_read_b64_tr_b16 v[154:155], v166 offset:0xac00
	ds_read_b64_tr_b16 v[168:169], v166 offset:0xb400
	ds_read_b64_tr_b16 v[170:171], v166 offset:0xbc00
	s_waitcnt lgkmcnt(8)
	v_mfma_f32_32x32x16_bf16 v[34:49], v[140:143], v[172:175], v[34:49]
	v_mfma_f32_32x32x16_bf16 v[34:49], v[128:131], v[182:185], v[34:49]
	v_mfma_f32_32x32x16_bf16 v[34:49], v[122:125], v[196:199], v[34:49]
	v_mfma_f32_32x32x16_bf16 v[34:49], v[132:135], v[200:203], v[34:49]
	ds_read_b64_tr_b16 v[172:173], v166 offset:0x8600
	ds_read_b64_tr_b16 v[174:175], v166 offset:0x8e00
	ds_read_b64_tr_b16 v[182:183], v166 offset:0x9600
	ds_read_b64_tr_b16 v[184:185], v166 offset:0x9e00
	ds_read_b64_tr_b16 v[196:197], v166 offset:0xa600
	ds_read_b64_tr_b16 v[198:199], v166 offset:0xae00
	ds_read_b64_tr_b16 v[200:201], v166 offset:0xb600
	ds_read_b64_tr_b16 v[202:203], v166 offset:0xbe00
	s_waitcnt lgkmcnt(8)
	v_mfma_f32_32x32x16_bf16 v[50:65], v[140:143], v[144:147], v[50:65]
	v_mfma_f32_32x32x16_bf16 v[50:65], v[128:131], v[148:151], v[50:65]
	v_mfma_f32_32x32x16_bf16 v[50:65], v[122:125], v[152:155], v[50:65]
	v_mfma_f32_32x32x16_bf16 v[50:65], v[132:135], v[168:171], v[50:65]
	s_waitcnt lgkmcnt(0)
	v_mfma_f32_32x32x16_bf16 v[2:17], v[140:143], v[172:175], v[2:17]
	s_and_b32 s0, s1, 0xffffffc0
	s_add_i32 s1, s0, -1
	s_cmp_gt_i32 s1, s77
	v_mfma_f32_32x32x16_bf16 v[2:17], v[128:131], v[182:185], v[2:17]
	v_mfma_f32_32x32x16_bf16 v[2:17], v[122:125], v[196:199], v[2:17]
	v_mfma_f32_32x32x16_bf16 v[2:17], v[132:135], v[200:203], v[2:17]
	s_cbranch_scc0 .LBB0_281
	v_subrev_u32_e32 v100, s0, v167
	s_movk_i32 s0, 0xffc0
	v_cmp_gt_i32_e64 s[30:31], s0, v100
	s_movk_i32 s0, 0xffe0
	v_cmp_gt_i32_e32 vcc, s0, v100
	s_movk_i32 s0, 0xffc1
	v_cmp_gt_i32_e64 s[36:37], s0, v100
	s_movk_i32 s0, 0xffe1
	v_cmp_gt_i32_e64 s[4:5], s0, v100
	s_movk_i32 s0, 0xffc2
	v_cmp_gt_i32_e64 s[38:39], s0, v100
	s_movk_i32 s0, 0xffe2
	v_cmp_gt_i32_e64 s[6:7], s0, v100
	s_movk_i32 s0, 0xffc3
	v_cmp_gt_i32_e64 s[40:41], s0, v100
	s_movk_i32 s0, 0xffe3
	v_cmp_gt_i32_e64 s[8:9], s0, v100
	s_movk_i32 s0, 0xffc8
	v_cmp_gt_i32_e64 s[42:43], s0, v100
	s_movk_i32 s0, 0xffe8
	v_cmp_gt_i32_e64 s[10:11], s0, v100
	s_movk_i32 s0, 0xffc9
	v_cmp_gt_i32_e64 s[44:45], s0, v100
	s_movk_i32 s0, 0xffe9
	v_cmp_gt_i32_e64 s[12:13], s0, v100
	s_movk_i32 s0, 0xffca
	v_cmp_gt_i32_e64 s[48:49], s0, v100
	s_movk_i32 s0, 0xffea
	v_cmp_gt_i32_e64 s[14:15], s0, v100
	s_movk_i32 s0, 0xffcb
	v_cmp_gt_i32_e64 s[50:51], s0, v100
	s_movk_i32 s0, 0xffeb
	v_cmp_gt_i32_e64 s[16:17], s0, v100
	s_movk_i32 s0, 0xffd0
	v_cmp_gt_i32_e64 s[52:53], s0, v100
	s_movk_i32 s0, 0xffd1
	v_cmp_gt_i32_e64 s[54:55], s0, v100
	s_movk_i32 s0, 0xffd2
	v_cmp_gt_i32_e64 s[56:57], s0, v100
	s_movk_i32 s0, 0xffd3
	v_cmp_gt_i32_e64 s[58:59], s0, v100
	s_movk_i32 s0, 0xffd8
	v_cmp_gt_i32_e64 s[60:61], s0, v100
	s_movk_i32 s0, 0xffd9
	v_cmp_gt_i32_e64 s[62:63], s0, v100
	s_movk_i32 s0, 0xffda
	v_cmp_gt_i32_e64 s[64:65], s0, v100
	s_movk_i32 s0, 0xffdb
	v_cmp_gt_i32_e64 s[66:67], s0, v100
	s_and_b64 s[64:65], s[66:67], s[64:65]
	s_and_b64 s[62:63], s[64:65], s[62:63]
	s_and_b64 s[60:61], s[62:63], s[60:61]
	s_and_b64 s[58:59], s[60:61], s[58:59]
	s_and_b64 s[56:57], s[58:59], s[56:57]
	s_and_b64 s[54:55], s[56:57], s[54:55]
	s_and_b64 s[52:53], s[54:55], s[52:53]
	s_and_b64 s[50:51], s[52:53], s[50:51]
	s_and_b64 s[48:49], s[50:51], s[48:49]
	s_and_b64 s[44:45], s[48:49], s[44:45]
	s_and_b64 s[42:43], s[44:45], s[42:43]
	s_and_b64 s[40:41], s[42:43], s[40:41]
	s_and_b64 s[38:39], s[40:41], s[38:39]
	s_and_b64 s[36:37], s[38:39], s[36:37]
	s_and_b64 s[30:31], s[36:37], s[30:31]
	v_cmp_gt_i32_e64 s[34:35], -6, v100
	v_cndmask_b32_e64 v66, v66, v160, s[30:31]
	v_cmp_gt_i32_e64 s[30:31], -5, v100
	v_cmp_gt_i32_e64 s[28:29], -7, v100
	v_cmp_gt_i32_e64 s[26:27], -8, v100
	v_cndmask_b32_e64 v97, v97, v160, s[30:31]
	s_and_b64 s[30:31], s[30:31], s[34:35]
	s_and_b64 s[28:29], s[30:31], s[28:29]
	v_cmp_gt_i32_e64 s[24:25], -13, v100
	s_and_b64 s[26:27], s[28:29], s[26:27]
	v_cmp_gt_i32_e64 s[22:23], -14, v100
	s_and_b64 s[24:25], s[26:27], s[24:25]
	v_cmp_gt_i32_e64 s[20:21], -15, v100
	s_and_b64 s[22:23], s[24:25], s[22:23]
	v_cmp_gt_i32_e64 s[18:19], -16, v100
	s_and_b64 s[20:21], s[22:23], s[20:21]
	s_and_b64 s[18:19], s[20:21], s[18:19]
	s_and_b64 s[16:17], s[18:19], s[16:17]
	s_and_b64 s[14:15], s[16:17], s[14:15]
	s_and_b64 s[12:13], s[14:15], s[12:13]
	s_and_b64 s[10:11], s[12:13], s[10:11]
	s_and_b64 s[8:9], s[10:11], s[8:9]
	s_and_b64 s[6:7], s[8:9], s[6:7]
	s_and_b64 s[4:5], s[6:7], s[4:5]
	s_and_b64 vcc, s[4:5], vcc
	v_cndmask_b32_e64 v81, v81, v160, s[66:67]
	v_cndmask_b32_e64 v80, v80, v160, s[64:65]
	v_cndmask_b32_e64 v79, v79, v160, s[62:63]
	v_cndmask_b32_e64 v78, v78, v160, s[60:61]
	v_cndmask_b32_e64 v77, v77, v160, s[58:59]
	v_cndmask_b32_e64 v76, v76, v160, s[56:57]
	v_cndmask_b32_e64 v75, v75, v160, s[54:55]
	v_cndmask_b32_e64 v74, v74, v160, s[52:53]
	v_cndmask_b32_e64 v73, v73, v160, s[50:51]
	v_cndmask_b32_e64 v72, v72, v160, s[48:49]
	v_cndmask_b32_e64 v71, v71, v160, s[44:45]
	v_cndmask_b32_e64 v70, v70, v160, s[42:43]
	v_cndmask_b32_e64 v69, v69, v160, s[40:41]
	v_cndmask_b32_e64 v68, v68, v160, s[38:39]
	v_cndmask_b32_e64 v67, v67, v160, s[36:37]
	v_cndmask_b32_e64 v96, v96, v160, s[30:31]
	v_cndmask_b32_e64 v95, v95, v160, s[28:29]
	v_cndmask_b32_e64 v94, v94, v160, s[26:27]
	v_cndmask_b32_e64 v93, v93, v160, s[24:25]
	v_cndmask_b32_e64 v92, v92, v160, s[22:23]
	v_cndmask_b32_e64 v91, v91, v160, s[20:21]
	v_cndmask_b32_e64 v90, v90, v160, s[18:19]
	v_cndmask_b32_e64 v89, v89, v160, s[16:17]
	v_cndmask_b32_e64 v88, v88, v160, s[14:15]
	v_cndmask_b32_e64 v87, v87, v160, s[12:13]
	v_cndmask_b32_e64 v86, v86, v160, s[10:11]
	v_cndmask_b32_e64 v85, v85, v160, s[8:9]
	v_cndmask_b32_e64 v84, v84, v160, s[6:7]
	v_cndmask_b32_e64 v83, v83, v160, s[4:5]
	v_cndmask_b32_e32 v82, v82, v160, vcc

.LBB0_356:
	s_waitcnt lgkmcnt(0)
	s_add_u32 s1, s4, 0x1a00000
	s_addc_u32 s2, s5, 0
	s_add_u32 s8, s4, 0x25c00000
	s_addc_u32 s9, s5, 0
	s_add_i32 s6, s10, s6
	s_ashr_i32 s10, s6, 31
	s_lshr_b32 s10, s10, 27
	s_lshl_b32 s11, s18, 10
	s_add_i32 s10, s6, s10
	v_lshrrev_b32_e32 v3, 4, v2
	v_ashrrev_i32_e32 v5, 3, v2
	s_add_i32 s38, s11, 0
	s_ashr_i32 s11, s10, 5
	s_and_b32 s10, s10, 0xffe0
	v_xor_b32_e32 v4, v3, v2
	v_lshlrev_b32_e32 v6, 1, v5
	v_lshrrev_b32_e32 v7, 2, v5
	s_sub_i32 s10, s6, s10
	v_lshlrev_b32_e32 v4, 4, v4
	v_and_b32_e32 v6, 24, v6
	v_and_b32_e32 v7, 4, v7
	v_and_b32_e32 v5, 0x1fffe3, v5
	s_bfe_i32 s6, s10, 0x80000
	v_and_b32_e32 v4, 0x70, v4
	v_or3_b32 v5, v5, v7, v6
	s_bfe_u32 s6, s6, 0x3000c
	v_lshl_or_b32 v195, v5, 11, v4
	v_mov_b32_e32 v5, 0x2000
	s_add_i32 s12, s10, s6
	v_lshl_add_u32 v5, v2, 4, v5
	s_bfe_i32 s6, s12, 0x80000
	s_and_b32 s12, s12, 0xf8
	v_ashrrev_i32_e32 v5, 7, v5
	s_sext_i32_i16 s6, s6
	s_sub_i32 s10, s10, s12
	s_ashr_i32 s7, s22, 8
	v_lshlrev_b32_e32 v6, 1, v5
	v_lshrrev_b32_e32 v7, 2, v5
	s_lshl_b32 s11, s11, 3
	s_lshr_b32 s6, s6, 3
	s_sext_i32_i8 s10, s10
	v_and_b32_e32 v6, 24, v6
	v_and_b32_e32 v7, 4, v7
	v_and_b32_e32 v5, 0x1fffe3, v5
	s_add_i32 s56, s11, s10
	s_bfe_i64 s[10:11], s[6:7], 0x100000
	v_or3_b32 v5, v5, v7, v6
	s_lshl_b64 s[10:11], s[10:11], 19
	v_lshl_or_b32 v196, v5, 11, v4
	v_mov_b32_e32 v4, v0
	s_add_u32 s34, s1, s10
	s_addc_u32 s35, s2, s11
	s_add_i32 s39, s38, 0x10000
	s_mov_b32 m0, s39
	s_nop 0
	global_load_lds_dwordx4 v195, s[34:35] offset:0
	s_add_i32 s40, s38, 0x12000
	s_movk_i32 s3, 0x70
	v_lshlrev_b32_e32 v5, 4, v4
	s_mov_b32 m0, s40
	s_nop 0
	global_load_lds_dwordx4 v196, s[34:35] offset:0
	s_add_u32 s12, s34, 0x40000
	v_bitop3_b32 v5, v5, s3, v4 bitop3:0x48
	v_lshlrev_b32_e32 v4, 8, v4
	s_addc_u32 s13, s35, 0
	s_add_i32 s41, s38, 0x14000
	s_mov_b32 m0, s41
	s_nop 0
	global_load_lds_dwordx4 v195, s[12:13] offset:0
	v_lshl_or_b32 v5, s56, 19, v5
	v_and_b32_e32 v4, 0xfffff800, v4
	s_add_i32 s42, s38, 0x16000
	s_mov_b32 m0, s42
	s_nop 0
	global_load_lds_dwordx4 v196, s[12:13] offset:0
	v_add_u32_e32 v197, v5, v4
	s_mov_b32 m0, s38
	s_nop 0
	global_load_lds_dwordx4 v197, s[8:9] offset:0
	v_add_u32_e32 v199, 0x20000, v197
	s_add_i32 s43, s38, 0x2000
	s_mov_b32 m0, s43
	s_nop 0
	global_load_lds_dwordx4 v199, s[8:9] offset:0
	v_add_u32_e32 v198, 0x40000, v197
	s_add_i32 s44, s38, 0x4000
	s_mov_b32 m0, s44
	s_nop 0
	global_load_lds_dwordx4 v198, s[8:9] offset:0
	v_add_u32_e32 v200, 0x60000, v197
	s_add_i32 s45, s38, 0x6000
	s_mov_b32 m0, s45
	s_nop 0
	global_load_lds_dwordx4 v200, s[8:9] offset:0
	s_cmp_eq_u32 s7, 1
	s_mov_b32 s33, 0
	s_mov_b64 s[10:11], 0x40000
	s_cselect_b64 s[12:13], -1, 0
	s_cmp_lg_u32 s7, 1
	s_cbranch_scc1 .LBB0_358
	s_barrier
.LBB0_358:
	s_add_u32 s14, s4, 0x36c00000
	s_addc_u32 s15, s5, 0
	s_add_u32 s16, s4, 0xdc00000
	s_addc_u32 s17, s5, 0
	s_lshl_b32 s4, s18, 5
	v_and_b32_e32 v4, 15, v2
	s_and_b32 s4, s4, 0x60
	v_lshlrev_b32_e32 v5, 7, v4
	v_or_b32_e32 v4, s4, v4
	s_add_u32 s4, s34, 0x80
	s_sext_i32_i8 s57, s6
	s_waitcnt vmcnt(2)
	s_barrier
	s_addc_u32 s5, s35, 0
	s_add_i32 s46, s38, 0x18000
	s_mov_b32 m0, s46
	s_nop 0
	global_load_lds_dwordx4 v195, s[4:5] offset:0
	s_add_i32 s47, s38, 0x1a000
	s_mov_b32 m0, s47
	s_nop 0
	global_load_lds_dwordx4 v196, s[4:5] offset:0
	s_add_u32 s18, s8, 0x80
	s_addc_u32 s19, s9, 0
	s_add_i32 s48, s38, 0x8000
	s_mov_b32 m0, s48
	s_nop 0
	global_load_lds_dwordx4 v197, s[18:19] offset:0
	s_add_i32 s49, s38, 0xa000
	s_mov_b32 m0, s49
	s_nop 0
	global_load_lds_dwordx4 v199, s[18:19] offset:0
	s_add_u32 s4, s34, 0x40080
	s_addc_u32 s5, s35, 0
	s_add_i32 s50, s38, 0x1c000
	s_add_i32 s51, s38, 0x1e000
	s_add_i32 s52, s38, 0xc000
	v_bfe_u32 v6, v2, 4, 2
	v_bfe_u32 v2, v2, 1, 3
	s_add_u32 s20, s8, 0x780
	v_bitop3_b32 v3, v3, v2, 3 bitop3:0x6c
	v_bitop3_b32 v2, v6, v2, 4 bitop3:0x36
	s_mov_b32 m0, s50
	s_nop 0
	global_load_lds_dwordx4 v195, s[4:5] offset:0
	s_addc_u32 s21, s9, 0
	v_lshlrev_b32_e32 v3, 4, v3
	v_lshlrev_b32_e32 v2, 4, v2
	v_lshlrev_b32_e32 v4, 7, v4
	s_mov_b32 m0, s51
	s_nop 0
	global_load_lds_dwordx4 v196, s[4:5] offset:0
	s_cmpk_lt_u32 s22, 0x100
	v_lshl_or_b32 v5, s7, 13, v5
	v_or_b32_e32 v201, v4, v3
	v_or_b32_e32 v202, v4, v2
	s_waitcnt vmcnt(6)
	s_cselect_b64 s[22:23], -1, 0
	s_add_i32 s4, 0, 0x10000
	v_or_b32_e32 v7, v3, v5
	v_or_b32_e32 v5, v2, v5
	v_add_u32_e32 v203, s4, v201
	v_add_u32_e32 v204, s4, v202
	s_add_i32 s4, 0, 0x14000
	s_add_i32 s53, s38, 0xe000
	s_ashr_i32 s54, s88, 31
	v_mov_b64_e32 v[170:171], 0x400
	v_mov_b64_e32 v[172:173], 0x3ff
	v_add_u32_e32 v205, s4, v201
	v_add_u32_e32 v206, s4, v202
	v_add_u32_e32 v207, 0, v7
	v_add_u32_e32 v208, 0, v5
	s_mov_b64 s[24:25], 0x48000
	s_mov_b64 s[26:27], 0x50000
	s_mov_b64 s[28:29], 0x58000
	s_barrier
	s_branch .LBB0_361

.LBB0_368:
	.p2align 3
	s_nop 0
	ds_read_b128 v[130:133], v203
	ds_read_b128 v[134:137], v203 offset:2048
	ds_read_b128 v[138:141], v204
	ds_read_b128 v[142:145], v204 offset:2048
	ds_read_b128 v[146:149], v205
	ds_read_b128 v[150:153], v205 offset:2048
	ds_read_b128 v[154:157], v206
	ds_read_b128 v[158:161], v206 offset:2048
	ds_read_b128 v[162:165], v207
	ds_read_b128 v[166:169], v207 offset:2048
	ds_read_b128 v[174:177], v208
	ds_read_b128 v[178:181], v208 offset:2048
	ds_read_b128 v[182:185], v207 offset:4096
	ds_read_b128 v[210:213], v207 offset:6144
	ds_read_b128 v[214:217], v208 offset:4096
	ds_read_b128 v[218:221], v208 offset:6144
	s_add_u32 s36, s8, s6
	s_addc_u32 s37, s9, s7
	s_add_u32 s58, s36, 0x80
	s_addc_u32 s59, s37, 0
	s_mov_b32 m0, s52
	s_nop 0
	global_load_lds_dwordx4 v198, s[58:59] offset:0
	s_nop 0
	s_mov_b32 m0, s53
	s_nop 0
	global_load_lds_dwordx4 v200, s[58:59] offset:0
	s_waitcnt vmcnt(8)
	s_waitcnt lgkmcnt(0)
	s_barrier
	s_setprio 1
	s_waitcnt lgkmcnt(7)
	v_mfma_f32_16x16x32_bf16 v[126:129], v[130:133], v[162:165], v[126:129]
	v_mfma_f32_16x16x32_bf16 v[122:125], v[134:137], v[162:165], v[122:125]
	s_waitcnt lgkmcnt(6)
	v_mfma_f32_16x16x32_bf16 v[118:121], v[130:133], v[166:169], v[118:121]
	v_mfma_f32_16x16x32_bf16 v[114:117], v[134:137], v[166:169], v[114:117]
	s_waitcnt lgkmcnt(3)
	v_mfma_f32_16x16x32_bf16 v[110:113], v[130:133], v[182:185], v[110:113]
	v_mfma_f32_16x16x32_bf16 v[106:109], v[134:137], v[182:185], v[106:109]
	s_waitcnt lgkmcnt(2)
	v_mfma_f32_16x16x32_bf16 v[102:105], v[130:133], v[210:213], v[102:105]
	v_mfma_f32_16x16x32_bf16 v[98:101], v[134:137], v[210:213], v[98:101]
	v_mfma_f32_16x16x32_bf16 v[126:129], v[138:141], v[174:177], v[126:129]
	v_mfma_f32_16x16x32_bf16 v[122:125], v[142:145], v[174:177], v[122:125]
	v_mfma_f32_16x16x32_bf16 v[118:121], v[138:141], v[178:181], v[118:121]
	v_mfma_f32_16x16x32_bf16 v[114:117], v[142:145], v[178:181], v[114:117]
	s_waitcnt lgkmcnt(1)
	v_mfma_f32_16x16x32_bf16 v[110:113], v[138:141], v[214:217], v[110:113]
	v_mfma_f32_16x16x32_bf16 v[106:109], v[142:145], v[214:217], v[106:109]
	s_waitcnt lgkmcnt(0)
	v_mfma_f32_16x16x32_bf16 v[102:105], v[138:141], v[218:221], v[102:105]
	v_mfma_f32_16x16x32_bf16 v[98:101], v[142:145], v[218:221], v[98:101]
	s_setprio 0
	s_setprio 1
	v_mfma_f32_16x16x32_bf16 v[94:97], v[146:149], v[162:165], v[94:97]
	v_mfma_f32_16x16x32_bf16 v[90:93], v[150:153], v[162:165], v[90:93]
	v_mfma_f32_16x16x32_bf16 v[86:89], v[146:149], v[166:169], v[86:89]
	v_mfma_f32_16x16x32_bf16 v[82:85], v[150:153], v[166:169], v[82:85]
	v_mfma_f32_16x16x32_bf16 v[78:81], v[146:149], v[182:185], v[78:81]
	v_mfma_f32_16x16x32_bf16 v[74:77], v[150:153], v[182:185], v[74:77]
	v_mfma_f32_16x16x32_bf16 v[70:73], v[146:149], v[210:213], v[70:73]
	v_mfma_f32_16x16x32_bf16 v[66:69], v[150:153], v[210:213], v[66:69]
	v_mfma_f32_16x16x32_bf16 v[94:97], v[154:157], v[174:177], v[94:97]
	v_mfma_f32_16x16x32_bf16 v[90:93], v[158:161], v[174:177], v[90:93]
	v_mfma_f32_16x16x32_bf16 v[86:89], v[154:157], v[178:181], v[86:89]
	v_mfma_f32_16x16x32_bf16 v[82:85], v[158:161], v[178:181], v[82:85]
	v_mfma_f32_16x16x32_bf16 v[78:81], v[154:157], v[214:217], v[78:81]
	v_mfma_f32_16x16x32_bf16 v[74:77], v[158:161], v[214:217], v[74:77]
	v_mfma_f32_16x16x32_bf16 v[70:73], v[154:157], v[218:221], v[70:73]
	v_mfma_f32_16x16x32_bf16 v[66:69], v[158:161], v[218:221], v[66:69]
	s_setprio 0
	s_barrier
	s_add_u32 s60, s34, s6
	s_addc_u32 s61, s35, s7
	ds_read_b128 v[162:165], v207 offset:16384
	ds_read_b128 v[166:169], v207 offset:18432
	ds_read_b128 v[174:177], v208 offset:16384
	ds_read_b128 v[178:181], v208 offset:18432
	ds_read_b128 v[182:185], v207 offset:20480
	ds_read_b128 v[210:213], v207 offset:22528
	ds_read_b128 v[214:217], v208 offset:20480
	ds_read_b128 v[218:221], v208 offset:22528
	s_add_u32 s58, s60, 0x100
	s_addc_u32 s59, s61, 0
	s_mov_b32 m0, s39
	s_nop 0
	global_load_lds_dwordx4 v195, s[58:59] offset:0
	s_nop 0
	s_mov_b32 m0, s40
	s_nop 0
	global_load_lds_dwordx4 v196, s[58:59] offset:0
	s_add_u32 s58, s60, 0x40100
	s_addc_u32 s59, s61, 0
	s_mov_b32 m0, s41
	s_nop 0
	global_load_lds_dwordx4 v195, s[58:59] offset:0
	s_nop 0
	s_mov_b32 m0, s42
	s_nop 0
	global_load_lds_dwordx4 v196, s[58:59] offset:0
	s_add_u32 s58, s36, 0x100
	s_addc_u32 s59, s37, 0
	s_mov_b32 m0, s38
	s_nop 0
	global_load_lds_dwordx4 v197, s[58:59] offset:0
	s_nop 0
	s_mov_b32 m0, s43
	s_nop 0
	global_load_lds_dwordx4 v199, s[58:59] offset:0
	s_waitcnt vmcnt(8)
	s_waitcnt lgkmcnt(0)
	s_barrier
	s_setprio 1
	s_waitcnt lgkmcnt(7)
	v_mfma_f32_16x16x32_bf16 v[62:65], v[130:133], v[162:165], v[62:65]
	v_mfma_f32_16x16x32_bf16 v[58:61], v[134:137], v[162:165], v[58:61]
	s_waitcnt lgkmcnt(6)
	v_mfma_f32_16x16x32_bf16 v[54:57], v[130:133], v[166:169], v[54:57]
	v_mfma_f32_16x16x32_bf16 v[50:53], v[134:137], v[166:169], v[50:53]
	s_waitcnt lgkmcnt(3)
	v_mfma_f32_16x16x32_bf16 v[46:49], v[130:133], v[182:185], v[46:49]
	v_mfma_f32_16x16x32_bf16 v[42:45], v[134:137], v[182:185], v[42:45]
	s_waitcnt lgkmcnt(2)
	v_mfma_f32_16x16x32_bf16 v[38:41], v[130:133], v[210:213], v[38:41]
	v_mfma_f32_16x16x32_bf16 v[34:37], v[134:137], v[210:213], v[34:37]
	v_mfma_f32_16x16x32_bf16 v[62:65], v[138:141], v[174:177], v[62:65]
	v_mfma_f32_16x16x32_bf16 v[58:61], v[142:145], v[174:177], v[58:61]
	v_mfma_f32_16x16x32_bf16 v[54:57], v[138:141], v[178:181], v[54:57]
	v_mfma_f32_16x16x32_bf16 v[50:53], v[142:145], v[178:181], v[50:53]
	s_waitcnt lgkmcnt(1)
	v_mfma_f32_16x16x32_bf16 v[46:49], v[138:141], v[214:217], v[46:49]
	v_mfma_f32_16x16x32_bf16 v[42:45], v[142:145], v[214:217], v[42:45]
	s_waitcnt lgkmcnt(0)
	v_mfma_f32_16x16x32_bf16 v[38:41], v[138:141], v[218:221], v[38:41]
	v_mfma_f32_16x16x32_bf16 v[34:37], v[142:145], v[218:221], v[34:37]
	s_setprio 0
	s_setprio 1
	v_mfma_f32_16x16x32_bf16 v[30:33], v[146:149], v[162:165], v[30:33]
	v_mfma_f32_16x16x32_bf16 v[26:29], v[150:153], v[162:165], v[26:29]
	v_mfma_f32_16x16x32_bf16 v[22:25], v[146:149], v[166:169], v[22:25]
	v_mfma_f32_16x16x32_bf16 v[18:21], v[150:153], v[166:169], v[18:21]
	v_mfma_f32_16x16x32_bf16 v[14:17], v[146:149], v[182:185], v[14:17]
	v_mfma_f32_16x16x32_bf16 v[10:13], v[150:153], v[182:185], v[10:13]
	v_mfma_f32_16x16x32_bf16 v[6:9], v[146:149], v[210:213], v[6:9]
	v_mfma_f32_16x16x32_bf16 v[2:5], v[150:153], v[210:213], v[2:5]
	v_mfma_f32_16x16x32_bf16 v[30:33], v[154:157], v[174:177], v[30:33]
	v_mfma_f32_16x16x32_bf16 v[26:29], v[158:161], v[174:177], v[26:29]
	v_mfma_f32_16x16x32_bf16 v[22:25], v[154:157], v[178:181], v[22:25]
	v_mfma_f32_16x16x32_bf16 v[18:21], v[158:161], v[178:181], v[18:21]
	v_mfma_f32_16x16x32_bf16 v[14:17], v[154:157], v[214:217], v[14:17]
	v_mfma_f32_16x16x32_bf16 v[10:13], v[158:161], v[214:217], v[10:13]
	v_mfma_f32_16x16x32_bf16 v[6:9], v[154:157], v[218:221], v[6:9]
	v_mfma_f32_16x16x32_bf16 v[2:5], v[158:161], v[218:221], v[2:5]
	s_setprio 0
	s_barrier
	s_add_i32 s62, 0, 0x18000
	v_add_u32_e32 v174, s62, v201
	v_add_u32_e32 v175, s62, v202
	s_add_i32 s62, 0, 0x1c000
	v_add_u32_e32 v176, s62, v201
	ds_read_b128 v[130:133], v174
	ds_read_b128 v[134:137], v174 offset:2048
	ds_read_b128 v[138:141], v175
	ds_read_b128 v[142:145], v175 offset:2048
	v_add_u32_e32 v177, s62, v202
	ds_read_b128 v[146:149], v176
	ds_read_b128 v[150:153], v176 offset:2048
	ds_read_b128 v[154:157], v177
	ds_read_b128 v[158:161], v177 offset:2048
	ds_read_b128 v[162:165], v207 offset:32768
	ds_read_b128 v[166:169], v207 offset:34816
	ds_read_b128 v[178:181], v208 offset:32768
	ds_read_b128 v[182:185], v208 offset:34816
	ds_read_b128 v[210:213], v207 offset:36864
	ds_read_b128 v[214:217], v207 offset:38912
	ds_read_b128 v[218:221], v208 offset:36864
	ds_read_b128 v[222:225], v208 offset:38912
	s_mov_b32 m0, s44
	s_nop 0
	global_load_lds_dwordx4 v198, s[58:59] offset:0
	s_nop 0
	s_mov_b32 m0, s45
	s_nop 0
	global_load_lds_dwordx4 v200, s[58:59] offset:0
	s_waitcnt vmcnt(8)
	s_waitcnt lgkmcnt(0)
	s_barrier
	s_setprio 1
	s_waitcnt lgkmcnt(7)
	v_mfma_f32_16x16x32_bf16 v[126:129], v[130:133], v[162:165], v[126:129]
	v_mfma_f32_16x16x32_bf16 v[122:125], v[134:137], v[162:165], v[122:125]
	s_waitcnt lgkmcnt(6)
	v_mfma_f32_16x16x32_bf16 v[118:121], v[130:133], v[166:169], v[118:121]
	v_mfma_f32_16x16x32_bf16 v[114:117], v[134:137], v[166:169], v[114:117]
	s_waitcnt lgkmcnt(3)
	v_mfma_f32_16x16x32_bf16 v[110:113], v[130:133], v[210:213], v[110:113]
	v_mfma_f32_16x16x32_bf16 v[106:109], v[134:137], v[210:213], v[106:109]
	s_waitcnt lgkmcnt(2)
	v_mfma_f32_16x16x32_bf16 v[102:105], v[130:133], v[214:217], v[102:105]
	v_mfma_f32_16x16x32_bf16 v[98:101], v[134:137], v[214:217], v[98:101]
	v_mfma_f32_16x16x32_bf16 v[126:129], v[138:141], v[178:181], v[126:129]
	v_mfma_f32_16x16x32_bf16 v[122:125], v[142:145], v[178:181], v[122:125]
	v_mfma_f32_16x16x32_bf16 v[118:121], v[138:141], v[182:185], v[118:121]
	v_mfma_f32_16x16x32_bf16 v[114:117], v[142:145], v[182:185], v[114:117]
	s_waitcnt lgkmcnt(1)
	v_mfma_f32_16x16x32_bf16 v[110:113], v[138:141], v[218:221], v[110:113]
	v_mfma_f32_16x16x32_bf16 v[106:109], v[142:145], v[218:221], v[106:109]
	s_waitcnt lgkmcnt(0)
	v_mfma_f32_16x16x32_bf16 v[102:105], v[138:141], v[222:225], v[102:105]
	v_mfma_f32_16x16x32_bf16 v[98:101], v[142:145], v[222:225], v[98:101]
	s_setprio 0
	s_setprio 1
	v_mfma_f32_16x16x32_bf16 v[94:97], v[146:149], v[162:165], v[94:97]
	v_mfma_f32_16x16x32_bf16 v[90:93], v[150:153], v[162:165], v[90:93]
	v_mfma_f32_16x16x32_bf16 v[86:89], v[146:149], v[166:169], v[86:89]
	v_mfma_f32_16x16x32_bf16 v[82:85], v[150:153], v[166:169], v[82:85]
	v_mfma_f32_16x16x32_bf16 v[78:81], v[146:149], v[210:213], v[78:81]
	v_mfma_f32_16x16x32_bf16 v[74:77], v[150:153], v[210:213], v[74:77]
	v_mfma_f32_16x16x32_bf16 v[70:73], v[146:149], v[214:217], v[70:73]
	v_mfma_f32_16x16x32_bf16 v[66:69], v[150:153], v[214:217], v[66:69]
	v_mfma_f32_16x16x32_bf16 v[94:97], v[154:157], v[178:181], v[94:97]
	v_mfma_f32_16x16x32_bf16 v[90:93], v[158:161], v[178:181], v[90:93]
	v_mfma_f32_16x16x32_bf16 v[86:89], v[154:157], v[182:185], v[86:89]
	v_mfma_f32_16x16x32_bf16 v[82:85], v[158:161], v[182:185], v[82:85]
	v_mfma_f32_16x16x32_bf16 v[78:81], v[154:157], v[218:221], v[78:81]
	v_mfma_f32_16x16x32_bf16 v[74:77], v[158:161], v[218:221], v[74:77]
	v_mfma_f32_16x16x32_bf16 v[70:73], v[154:157], v[222:225], v[70:73]
	v_mfma_f32_16x16x32_bf16 v[66:69], v[158:161], v[222:225], v[66:69]
	s_setprio 0
	s_barrier
	ds_read_b128 v[162:165], v207 offset:49152
	ds_read_b128 v[166:169], v207 offset:51200
	ds_read_b128 v[178:181], v208 offset:49152
	ds_read_b128 v[182:185], v208 offset:51200
	ds_read_b128 v[210:213], v207 offset:53248
	ds_read_b128 v[214:217], v207 offset:55296
	ds_read_b128 v[218:221], v208 offset:53248
	ds_read_b128 v[222:225], v208 offset:55296
	s_add_u32 s58, s60, 0x180
	s_addc_u32 s59, s61, 0
	s_mov_b32 m0, s46
	s_nop 0
	global_load_lds_dwordx4 v195, s[58:59] offset:0
	s_nop 0
	s_mov_b32 m0, s47
	s_nop 0
	global_load_lds_dwordx4 v196, s[58:59] offset:0
	s_add_u32 s58, s60, 0x40180
	s_addc_u32 s59, s61, 0
	s_mov_b32 m0, s50
	s_nop 0
	global_load_lds_dwordx4 v195, s[58:59] offset:0
	s_add_u32 s36, s36, 0x180
	s_mov_b32 m0, s51
	s_nop 0
	global_load_lds_dwordx4 v196, s[58:59] offset:0
	s_addc_u32 s37, s37, 0
	s_mov_b32 m0, s48
	s_nop 0
	global_load_lds_dwordx4 v197, s[36:37] offset:0
	s_nop 0
	s_mov_b32 m0, s49
	s_nop 0
	global_load_lds_dwordx4 v199, s[36:37] offset:0
	s_waitcnt vmcnt(8)
	s_waitcnt lgkmcnt(0)
	s_barrier
	s_setprio 1
	s_waitcnt lgkmcnt(7)
	v_mfma_f32_16x16x32_bf16 v[62:65], v[130:133], v[162:165], v[62:65]
	v_mfma_f32_16x16x32_bf16 v[58:61], v[134:137], v[162:165], v[58:61]
	s_waitcnt lgkmcnt(6)
	v_mfma_f32_16x16x32_bf16 v[54:57], v[130:133], v[166:169], v[54:57]
	v_mfma_f32_16x16x32_bf16 v[50:53], v[134:137], v[166:169], v[50:53]
	s_waitcnt lgkmcnt(3)
	v_mfma_f32_16x16x32_bf16 v[46:49], v[130:133], v[210:213], v[46:49]
	v_mfma_f32_16x16x32_bf16 v[42:45], v[134:137], v[210:213], v[42:45]
	s_waitcnt lgkmcnt(2)
	v_mfma_f32_16x16x32_bf16 v[38:41], v[130:133], v[214:217], v[38:41]
	v_mfma_f32_16x16x32_bf16 v[34:37], v[134:137], v[214:217], v[34:37]
	v_mfma_f32_16x16x32_bf16 v[62:65], v[138:141], v[178:181], v[62:65]
	v_mfma_f32_16x16x32_bf16 v[58:61], v[142:145], v[178:181], v[58:61]
	v_mfma_f32_16x16x32_bf16 v[54:57], v[138:141], v[182:185], v[54:57]
	v_mfma_f32_16x16x32_bf16 v[50:53], v[142:145], v[182:185], v[50:53]
	s_waitcnt lgkmcnt(1)
	v_mfma_f32_16x16x32_bf16 v[46:49], v[138:141], v[218:221], v[46:49]
	v_mfma_f32_16x16x32_bf16 v[42:45], v[142:145], v[218:221], v[42:45]
	s_waitcnt lgkmcnt(0)
	v_mfma_f32_16x16x32_bf16 v[38:41], v[138:141], v[222:225], v[38:41]
	v_mfma_f32_16x16x32_bf16 v[34:37], v[142:145], v[222:225], v[34:37]
	s_setprio 0
	s_setprio 1
	v_mfma_f32_16x16x32_bf16 v[30:33], v[146:149], v[162:165], v[30:33]
	v_mfma_f32_16x16x32_bf16 v[26:29], v[150:153], v[162:165], v[26:29]
	v_mfma_f32_16x16x32_bf16 v[22:25], v[146:149], v[166:169], v[22:25]
	v_mfma_f32_16x16x32_bf16 v[18:21], v[150:153], v[166:169], v[18:21]
	v_mfma_f32_16x16x32_bf16 v[14:17], v[146:149], v[210:213], v[14:17]
	v_mfma_f32_16x16x32_bf16 v[10:13], v[150:153], v[210:213], v[10:13]
	v_mfma_f32_16x16x32_bf16 v[6:9], v[146:149], v[214:217], v[6:9]
	v_mfma_f32_16x16x32_bf16 v[2:5], v[150:153], v[214:217], v[2:5]
	v_mfma_f32_16x16x32_bf16 v[30:33], v[154:157], v[178:181], v[30:33]
	v_mfma_f32_16x16x32_bf16 v[26:29], v[158:161], v[178:181], v[26:29]
	v_mfma_f32_16x16x32_bf16 v[22:25], v[154:157], v[182:185], v[22:25]
	v_mfma_f32_16x16x32_bf16 v[18:21], v[158:161], v[182:185], v[18:21]
	v_mfma_f32_16x16x32_bf16 v[14:17], v[154:157], v[218:221], v[14:17]
	v_mfma_f32_16x16x32_bf16 v[10:13], v[158:161], v[218:221], v[10:13]
	v_mfma_f32_16x16x32_bf16 v[6:9], v[154:157], v[222:225], v[6:9]
	v_mfma_f32_16x16x32_bf16 v[2:5], v[158:161], v[222:225], v[2:5]
	s_setprio 0
	s_barrier
	s_add_i32 s31, s31, 2
	s_add_u32 s6, s6, 0x100
	s_addc_u32 s7, s7, 0
	s_cmp_lt_u32 s31, 12
	s_cbranch_scc1 .LBB0_368
	ds_read_b128 v[154:157], v203
	ds_read_b128 v[158:161], v203 offset:2048
	ds_read_b128 v[166:169], v204
	ds_read_b128 v[162:165], v204 offset:2048
	ds_read_b128 v[138:141], v205
	ds_read_b128 v[142:145], v205 offset:2048
	ds_read_b128 v[150:153], v206
	ds_read_b128 v[146:149], v206 offset:2048
	ds_read_b128 v[134:137], v207
	ds_read_b128 v[178:181], v207 offset:2048
	ds_read_b128 v[182:185], v208
	ds_read_b128 v[210:213], v208 offset:2048
	ds_read_b128 v[214:217], v207 offset:4096
	ds_read_b128 v[218:221], v207 offset:6144
	ds_read_b128 v[222:225], v208 offset:4096
	ds_read_b128 v[226:229], v208 offset:6144
	s_mov_b32 m0, s52
	s_nop 0
	global_load_lds_dwordx4 v198, s[20:21] offset:0
	s_nop 0
	s_mov_b32 m0, s53
	s_nop 0
	global_load_lds_dwordx4 v200, s[20:21] offset:0
	s_waitcnt vmcnt(8)
	s_waitcnt lgkmcnt(0)
	s_barrier
	s_setprio 1
	s_waitcnt lgkmcnt(7)
	v_mfma_f32_16x16x32_bf16 v[126:129], v[154:157], v[134:137], v[126:129]
	v_mfma_f32_16x16x32_bf16 v[122:125], v[158:161], v[134:137], v[122:125]
	s_waitcnt lgkmcnt(6)
	v_mfma_f32_16x16x32_bf16 v[118:121], v[154:157], v[178:181], v[118:121]
	v_mfma_f32_16x16x32_bf16 v[114:117], v[158:161], v[178:181], v[114:117]
	s_waitcnt lgkmcnt(3)
	v_mfma_f32_16x16x32_bf16 v[110:113], v[154:157], v[214:217], v[110:113]
	v_mfma_f32_16x16x32_bf16 v[106:109], v[158:161], v[214:217], v[106:109]
	s_waitcnt lgkmcnt(2)
	v_mfma_f32_16x16x32_bf16 v[102:105], v[154:157], v[218:221], v[102:105]
	v_mfma_f32_16x16x32_bf16 v[98:101], v[158:161], v[218:221], v[98:101]
	v_mfma_f32_16x16x32_bf16 v[126:129], v[166:169], v[182:185], v[126:129]
	v_mfma_f32_16x16x32_bf16 v[122:125], v[162:165], v[182:185], v[122:125]
	v_mfma_f32_16x16x32_bf16 v[118:121], v[166:169], v[210:213], v[118:121]
	v_mfma_f32_16x16x32_bf16 v[114:117], v[162:165], v[210:213], v[114:117]
	s_waitcnt lgkmcnt(1)
	v_mfma_f32_16x16x32_bf16 v[110:113], v[166:169], v[222:225], v[110:113]
	v_mfma_f32_16x16x32_bf16 v[106:109], v[162:165], v[222:225], v[106:109]
	s_waitcnt lgkmcnt(0)
	v_mfma_f32_16x16x32_bf16 v[102:105], v[166:169], v[226:229], v[102:105]
	v_mfma_f32_16x16x32_bf16 v[98:101], v[162:165], v[226:229], v[98:101]
	s_setprio 0
	s_setprio 1
	v_mfma_f32_16x16x32_bf16 v[94:97], v[138:141], v[134:137], v[94:97]
	v_mfma_f32_16x16x32_bf16 v[90:93], v[142:145], v[134:137], v[90:93]
	v_mfma_f32_16x16x32_bf16 v[86:89], v[138:141], v[178:181], v[86:89]
	v_mfma_f32_16x16x32_bf16 v[82:85], v[142:145], v[178:181], v[82:85]
	v_mfma_f32_16x16x32_bf16 v[78:81], v[138:141], v[214:217], v[78:81]
	v_mfma_f32_16x16x32_bf16 v[74:77], v[142:145], v[214:217], v[74:77]
	v_mfma_f32_16x16x32_bf16 v[70:73], v[138:141], v[218:221], v[70:73]
	v_mfma_f32_16x16x32_bf16 v[66:69], v[142:145], v[218:221], v[66:69]
	v_mfma_f32_16x16x32_bf16 v[130:133], v[150:153], v[182:185], v[94:97]
	v_mfma_f32_16x16x32_bf16 v[134:137], v[146:149], v[182:185], v[90:93]
	v_mfma_f32_16x16x32_bf16 v[86:89], v[150:153], v[210:213], v[86:89]
	v_mfma_f32_16x16x32_bf16 v[82:85], v[146:149], v[210:213], v[82:85]
	v_mfma_f32_16x16x32_bf16 v[78:81], v[150:153], v[222:225], v[78:81]
	v_mfma_f32_16x16x32_bf16 v[74:77], v[146:149], v[222:225], v[74:77]
	v_mfma_f32_16x16x32_bf16 v[70:73], v[150:153], v[226:229], v[70:73]
	v_mfma_f32_16x16x32_bf16 v[66:69], v[146:149], v[226:229], v[66:69]
	s_setprio 0
	s_barrier
	v_cndmask_b32_e64 v90, 0, 1, s[4:5]
	v_cmp_ne_u32_e64 s[6:7], 1, v90
	s_andn2_b64 vcc, exec, s[4:5]
	s_cbranch_vccnz .LBB0_371
	v_mov_b32_e32 v90, v0
	s_nop 0
	v_lshlrev_b32_e32 v91, 4, v90
	v_bitop3_b32 v91, v91, s3, v90 bitop3:0x48
	v_lshlrev_b32_e32 v90, 8, v90
	v_lshl_or_b32 v91, s55, 19, v91
	v_and_b32_e32 v90, 0xfffff800, v90
	v_add_u32_e32 v197, v91, v90
	v_add_u32_e32 v198, 0x40000, v197
	v_add_u32_e32 v199, 0x20000, v197
	v_add_u32_e32 v200, 0x60000, v197
.LBB0_371:
	s_ashr_i32 s31, s30, 31
	s_lshl_b64 s[36:37], s[30:31], 19
	s_add_u32 s36, s1, s36
	s_addc_u32 s37, s2, s37
	s_and_b64 s[4:5], s[4:5], exec
	ds_read_b128 v[90:93], v207 offset:16384
	ds_read_b128 v[94:97], v207 offset:18432
	ds_read_b128 v[178:181], v208 offset:16384
	ds_read_b128 v[182:185], v208 offset:18432
	ds_read_b128 v[210:213], v207 offset:20480
	ds_read_b128 v[214:217], v207 offset:22528
	ds_read_b128 v[218:221], v208 offset:20480
	ds_read_b128 v[222:225], v208 offset:22528
	s_cselect_b32 s5, s37, s35
	s_cselect_b32 s4, s36, s34
	s_mov_b32 m0, s39
	s_nop 0
	global_load_lds_dwordx4 v195, s[4:5] offset:0
	s_add_u32 s34, s4, 0x40000
	s_mov_b32 m0, s40
	s_nop 0
	global_load_lds_dwordx4 v196, s[4:5] offset:0
	s_addc_u32 s35, s5, 0
	s_mov_b32 m0, s41
	s_nop 0
	global_load_lds_dwordx4 v195, s[34:35] offset:0
	s_nop 0
	s_mov_b32 m0, s42
	s_nop 0
	global_load_lds_dwordx4 v196, s[34:35] offset:0
	s_nop 0
	s_mov_b32 m0, s38
	s_nop 0
	global_load_lds_dwordx4 v197, s[8:9] offset:0
	s_nop 0
	s_mov_b32 m0, s43
	s_nop 0
	global_load_lds_dwordx4 v199, s[8:9] offset:0
	s_waitcnt vmcnt(8)
	s_waitcnt lgkmcnt(0)
	s_barrier
	s_setprio 1
	s_waitcnt lgkmcnt(7)
	v_mfma_f32_16x16x32_bf16 v[62:65], v[154:157], v[90:93], v[62:65]
	s_waitcnt lgkmcnt(6)
	v_mfma_f32_16x16x32_bf16 v[54:57], v[154:157], v[94:97], v[54:57]
	s_waitcnt lgkmcnt(3)
	v_mfma_f32_16x16x32_bf16 v[42:45], v[158:161], v[210:213], v[42:45]
	s_waitcnt lgkmcnt(2)
	v_mfma_f32_16x16x32_bf16 v[38:41], v[154:157], v[214:217], v[38:41]
	v_mfma_f32_16x16x32_bf16 v[62:65], v[166:169], v[178:181], v[62:65]
	v_mfma_f32_16x16x32_bf16 v[58:61], v[158:161], v[90:93], v[58:61]
	v_mfma_f32_16x16x32_bf16 v[54:57], v[166:169], v[182:185], v[54:57]
	v_mfma_f32_16x16x32_bf16 v[50:53], v[158:161], v[94:97], v[50:53]
	v_mfma_f32_16x16x32_bf16 v[46:49], v[154:157], v[210:213], v[46:49]
	s_waitcnt lgkmcnt(1)
	v_mfma_f32_16x16x32_bf16 v[42:45], v[162:165], v[218:221], v[42:45]
	s_waitcnt lgkmcnt(0)
	v_mfma_f32_16x16x32_bf16 v[38:41], v[166:169], v[222:225], v[38:41]
	v_mfma_f32_16x16x32_bf16 v[34:37], v[158:161], v[214:217], v[34:37]
	v_mfma_f32_16x16x32_bf16 v[58:61], v[162:165], v[178:181], v[58:61]
	v_mfma_f32_16x16x32_bf16 v[50:53], v[162:165], v[182:185], v[50:53]
	v_mfma_f32_16x16x32_bf16 v[226:229], v[166:169], v[218:221], v[46:49]
	v_mfma_f32_16x16x32_bf16 v[34:37], v[162:165], v[222:225], v[34:37]
	s_setprio 0
	s_setprio 1
	v_mfma_f32_16x16x32_bf16 v[22:25], v[138:141], v[94:97], v[22:25]
	v_mfma_f32_16x16x32_bf16 v[18:21], v[142:145], v[94:97], v[18:21]
	v_mfma_f32_16x16x32_bf16 v[6:9], v[138:141], v[214:217], v[6:9]
	v_mfma_f32_16x16x32_bf16 v[2:5], v[142:145], v[214:217], v[2:5]
	v_mfma_f32_16x16x32_bf16 v[30:33], v[138:141], v[90:93], v[30:33]
	v_mfma_f32_16x16x32_bf16 v[26:29], v[142:145], v[90:93], v[26:29]
	v_mfma_f32_16x16x32_bf16 v[22:25], v[150:153], v[182:185], v[22:25]
	v_mfma_f32_16x16x32_bf16 v[18:21], v[146:149], v[182:185], v[18:21]
	v_mfma_f32_16x16x32_bf16 v[14:17], v[138:141], v[210:213], v[14:17]
	v_mfma_f32_16x16x32_bf16 v[10:13], v[142:145], v[210:213], v[10:13]
	v_mfma_f32_16x16x32_bf16 v[6:9], v[150:153], v[222:225], v[6:9]
	v_mfma_f32_16x16x32_bf16 v[2:5], v[146:149], v[222:225], v[2:5]
	v_mfma_f32_16x16x32_bf16 v[166:169], v[150:153], v[178:181], v[30:33]
	v_mfma_f32_16x16x32_bf16 v[178:181], v[146:149], v[178:181], v[26:29]
	v_mfma_f32_16x16x32_bf16 v[182:185], v[150:153], v[218:221], v[14:17]
	v_mfma_f32_16x16x32_bf16 v[210:213], v[146:149], v[218:221], v[10:13]
	s_setprio 0
	s_barrier
	s_nop 0
	ds_read_b128 v[10:13], v174
	ds_read_b128 v[146:149], v174 offset:2048
	ds_read_b128 v[14:17], v175
	ds_read_b128 v[214:217], v175 offset:2048
	ds_read_b128 v[218:221], v176
	ds_read_b128 v[222:225], v176 offset:2048
	ds_read_b128 v[230:233], v177
	ds_read_b128 v[174:177], v177 offset:2048
	ds_read_b128 v[26:29], v207 offset:32768
	ds_read_b128 v[30:33], v207 offset:34816
	ds_read_b128 v[46:49], v208 offset:32768
	ds_read_b128 v[234:237], v208 offset:34816
	ds_read_b128 v[238:241], v207 offset:36864
	ds_read_b128 v[242:245], v207 offset:38912
	ds_read_b128 v[246:249], v208 offset:36864
	ds_read_b128 v[250:253], v208 offset:38912
	s_mov_b32 m0, s44
	s_nop 0
	global_load_lds_dwordx4 v198, s[8:9] offset:0
	s_nop 0
	s_mov_b32 m0, s45
	s_nop 0
	global_load_lds_dwordx4 v200, s[8:9] offset:0
	s_waitcnt vmcnt(8)
	s_waitcnt lgkmcnt(0)
	s_barrier
	s_setprio 1
	s_waitcnt lgkmcnt(7)
	v_mfma_f32_16x16x32_bf16 v[90:93], v[10:13], v[26:29], v[126:129]
	s_waitcnt lgkmcnt(5)
	v_mfma_f32_16x16x32_bf16 v[150:153], v[14:17], v[46:49], v[90:93]
	v_mfma_f32_16x16x32_bf16 v[90:93], v[146:149], v[26:29], v[122:125]
	v_mfma_f32_16x16x32_bf16 v[154:157], v[214:217], v[46:49], v[90:93]
	v_mfma_f32_16x16x32_bf16 v[90:93], v[10:13], v[30:33], v[118:121]
	s_waitcnt lgkmcnt(4)
	v_mfma_f32_16x16x32_bf16 v[142:145], v[14:17], v[234:237], v[90:93]
	v_mfma_f32_16x16x32_bf16 v[90:93], v[146:149], v[30:33], v[114:117]
	v_mfma_f32_16x16x32_bf16 v[138:141], v[214:217], v[234:237], v[90:93]
	s_waitcnt lgkmcnt(3)
	v_mfma_f32_16x16x32_bf16 v[90:93], v[10:13], v[238:241], v[110:113]
	s_waitcnt lgkmcnt(1)
	v_mfma_f32_16x16x32_bf16 v[118:121], v[14:17], v[246:249], v[90:93]
	v_mfma_f32_16x16x32_bf16 v[90:93], v[146:149], v[238:241], v[106:109]
	v_mfma_f32_16x16x32_bf16 v[114:117], v[214:217], v[246:249], v[90:93]
	v_mfma_f32_16x16x32_bf16 v[90:93], v[10:13], v[242:245], v[102:105]
	s_waitcnt lgkmcnt(0)
	v_mfma_f32_16x16x32_bf16 v[94:97], v[14:17], v[250:253], v[90:93]
	v_mfma_f32_16x16x32_bf16 v[90:93], v[146:149], v[242:245], v[98:101]
	v_mfma_f32_16x16x32_bf16 v[90:93], v[214:217], v[250:253], v[90:93]
	s_setprio 0
	s_setprio 1
	v_mfma_f32_16x16x32_bf16 v[98:101], v[218:221], v[26:29], v[130:133]
	v_mfma_f32_16x16x32_bf16 v[26:29], v[222:225], v[26:29], v[134:137]
	v_mfma_f32_16x16x32_bf16 v[158:161], v[174:177], v[46:49], v[26:29]
	v_mfma_f32_16x16x32_bf16 v[26:29], v[218:221], v[30:33], v[86:89]
	v_mfma_f32_16x16x32_bf16 v[130:133], v[230:233], v[234:237], v[26:29]
	v_mfma_f32_16x16x32_bf16 v[26:29], v[222:225], v[30:33], v[82:85]
	v_mfma_f32_16x16x32_bf16 v[126:129], v[174:177], v[234:237], v[26:29]
	v_mfma_f32_16x16x32_bf16 v[26:29], v[218:221], v[238:241], v[78:81]
	v_mfma_f32_16x16x32_bf16 v[106:109], v[230:233], v[246:249], v[26:29]
	v_mfma_f32_16x16x32_bf16 v[26:29], v[222:225], v[238:241], v[74:77]
	v_mfma_f32_16x16x32_bf16 v[102:105], v[174:177], v[246:249], v[26:29]
	v_mfma_f32_16x16x32_bf16 v[26:29], v[218:221], v[242:245], v[70:73]
	v_mfma_f32_16x16x32_bf16 v[78:81], v[230:233], v[250:253], v[26:29]
	v_mfma_f32_16x16x32_bf16 v[26:29], v[222:225], v[242:245], v[66:69]
	v_mfma_f32_16x16x32_bf16 v[162:165], v[230:233], v[46:49], v[98:101]
	v_mfma_f32_16x16x32_bf16 v[70:73], v[174:177], v[250:253], v[26:29]
	s_setprio 0
	s_barrier
	ds_read_b128 v[82:85], v207 offset:49152
	ds_read_b128 v[98:101], v207 offset:51200
	ds_read_b128 v[110:113], v208 offset:49152
	ds_read_b128 v[122:125], v208 offset:51200
	ds_read_b128 v[134:137], v207 offset:53248
	ds_read_b128 v[234:237], v207 offset:55296
	ds_read_b128 v[238:241], v208 offset:53248
	ds_read_b128 v[242:245], v208 offset:55296
	s_add_u32 s34, s4, 0x80
	s_addc_u32 s35, s5, 0
	s_mov_b32 m0, s46
	s_nop 0
	global_load_lds_dwordx4 v195, s[34:35] offset:0
	s_add_u32 s4, s4, 0x40080
	s_mov_b32 m0, s47
	s_nop 0
	global_load_lds_dwordx4 v196, s[34:35] offset:0
	s_addc_u32 s5, s5, 0
	s_mov_b32 m0, s50
	s_nop 0
	global_load_lds_dwordx4 v195, s[4:5] offset:0
	s_nop 0
	s_mov_b32 m0, s51
	s_nop 0
	global_load_lds_dwordx4 v196, s[4:5] offset:0
	s_mov_b32 m0, s48
	s_nop 0
	global_load_lds_dwordx4 v197, s[18:19] offset:0
	s_nop 0
	s_mov_b32 m0, s49
	s_nop 0
	global_load_lds_dwordx4 v199, s[18:19] offset:0
	s_waitcnt vmcnt(8)
	s_waitcnt lgkmcnt(0)
	s_barrier
	s_setprio 1
	s_waitcnt lgkmcnt(7)
	v_mfma_f32_16x16x32_bf16 v[26:29], v[10:13], v[82:85], v[62:65]
	s_waitcnt lgkmcnt(5)
	v_mfma_f32_16x16x32_bf16 v[86:89], v[14:17], v[110:113], v[26:29]
	v_mfma_f32_16x16x32_bf16 v[26:29], v[146:149], v[82:85], v[58:61]
	v_mfma_f32_16x16x32_bf16 v[74:77], v[214:217], v[110:113], v[26:29]
	v_mfma_f32_16x16x32_bf16 v[26:29], v[10:13], v[98:101], v[54:57]
	s_waitcnt lgkmcnt(4)
	v_mfma_f32_16x16x32_bf16 v[54:57], v[14:17], v[122:125], v[26:29]
	v_mfma_f32_16x16x32_bf16 v[26:29], v[146:149], v[98:101], v[50:53]
	v_mfma_f32_16x16x32_bf16 v[46:49], v[214:217], v[122:125], v[26:29]
	s_waitcnt lgkmcnt(3)
	v_mfma_f32_16x16x32_bf16 v[26:29], v[10:13], v[134:137], v[226:229]
	s_waitcnt lgkmcnt(2)
	v_mfma_f32_16x16x32_bf16 v[10:13], v[10:13], v[234:237], v[38:41]
	s_waitcnt lgkmcnt(1)
	v_mfma_f32_16x16x32_bf16 v[30:33], v[14:17], v[238:241], v[26:29]
	v_mfma_f32_16x16x32_bf16 v[26:29], v[146:149], v[134:137], v[42:45]
	s_waitcnt lgkmcnt(0)
	v_mfma_f32_16x16x32_bf16 v[14:17], v[14:17], v[242:245], v[10:13]
	v_mfma_f32_16x16x32_bf16 v[10:13], v[146:149], v[234:237], v[34:37]
	v_mfma_f32_16x16x32_bf16 v[26:29], v[214:217], v[238:241], v[26:29]
	v_mfma_f32_16x16x32_bf16 v[10:13], v[214:217], v[242:245], v[10:13]
	s_setprio 0
	s_setprio 1
	v_mfma_f32_16x16x32_bf16 v[18:21], v[222:225], v[98:101], v[18:21]
	v_mfma_f32_16x16x32_bf16 v[34:37], v[218:221], v[82:85], v[166:169]
	v_mfma_f32_16x16x32_bf16 v[22:25], v[218:221], v[98:101], v[22:25]
	v_mfma_f32_16x16x32_bf16 v[38:41], v[174:177], v[122:125], v[18:21]
	v_mfma_f32_16x16x32_bf16 v[18:21], v[218:221], v[134:137], v[182:185]
	v_mfma_f32_16x16x32_bf16 v[66:69], v[230:233], v[110:113], v[34:37]
	v_mfma_f32_16x16x32_bf16 v[34:37], v[222:225], v[82:85], v[178:181]
	v_mfma_f32_16x16x32_bf16 v[42:45], v[230:233], v[122:125], v[22:25]
	v_mfma_f32_16x16x32_bf16 v[22:25], v[230:233], v[238:241], v[18:21]
	v_mfma_f32_16x16x32_bf16 v[18:21], v[222:225], v[134:137], v[210:213]
	v_mfma_f32_16x16x32_bf16 v[6:9], v[218:221], v[234:237], v[6:9]
	v_mfma_f32_16x16x32_bf16 v[2:5], v[222:225], v[234:237], v[2:5]
	v_mfma_f32_16x16x32_bf16 v[62:65], v[174:177], v[110:113], v[34:37]
	v_mfma_f32_16x16x32_bf16 v[18:21], v[174:177], v[238:241], v[18:21]
	v_mfma_f32_16x16x32_bf16 v[6:9], v[230:233], v[242:245], v[6:9]
	v_mfma_f32_16x16x32_bf16 v[2:5], v[174:177], v[242:245], v[2:5]
	s_setprio 0
	s_barrier
	s_andn2_b64 vcc, exec, s[22:23]
	s_cbranch_vccnz .LBB0_373
	s_barrier

.LBB0_429:
	s_mov_b32 m0, s0
	s_nop 0
	global_load_lds_dwordx4 v2, s[4:5] offset:0
	s_addk_i32 s0, 0x2000
	s_add_i32 s1, s1, 8
	s_add_u32 s4, s4, 0x2000
	s_addc_u32 s5, s5, 0
	s_cmpk_gt_i32 s1, 0x78
	s_cbranch_scc0 .LBB0_429

.LBB0_550:
	s_or_b64 exec, exec, s[12:13]
	s_add_u32 s12, s10, 0x15c00000
	v_and_b32_e32 v2, 0x7fffff00, v6
	s_addc_u32 s13, s11, 0
	s_add_i32 s16, 0, 0x20480
	v_lshlrev_b32_e32 v2, 1, v2
	v_lshlrev_b32_e32 v1, 1, v1
	v_cmp_lt_i32_e32 vcc, -1, v7
	v_add3_u32 v1, s16, v2, v1
	s_add_i32 s33, 0, 0x20000
	s_waitcnt vmcnt(16)
	v_cndmask_b32_e32 v2, 0, v31, vcc
	v_cmp_lt_i32_e32 vcc, -1, v9
	ds_write_b16 v1, v2 offset:1024
	s_waitcnt vmcnt(0)
	ds_write_b16 v1, v5
	v_cndmask_b32_e32 v2, 0, v30, vcc
	v_cmp_lt_i32_e32 vcc, -1, v8
	ds_write_b16 v1, v2 offset:2048
	s_nop 0
	v_cndmask_b32_e32 v2, 0, v29, vcc
	v_cmp_lt_i32_e32 vcc, -1, v11
	ds_write_b16 v1, v2 offset:3072
	s_nop 0
	v_cndmask_b32_e32 v2, 0, v28, vcc
	v_cmp_lt_i32_e32 vcc, -1, v10
	ds_write_b16 v1, v2 offset:4096
	s_nop 0
	v_cndmask_b32_e32 v2, 0, v27, vcc
	v_cmp_lt_i32_e32 vcc, -1, v13
	ds_write_b16 v1, v2 offset:5120
	s_nop 0
	v_cndmask_b32_e32 v2, 0, v26, vcc
	v_cmp_lt_i32_e32 vcc, -1, v12
	ds_write_b16 v1, v2 offset:6144
	s_nop 0
	v_cndmask_b32_e32 v2, 0, v25, vcc
	v_cmp_lt_i32_e32 vcc, -1, v15
	ds_write_b16 v1, v2 offset:7168
	s_nop 0
	v_cndmask_b32_e32 v2, 0, v24, vcc
	v_cmp_lt_i32_e32 vcc, -1, v14
	ds_write_b16 v1, v2 offset:8192
	s_nop 0
	v_cndmask_b32_e32 v2, 0, v39, vcc
	v_cmp_lt_i32_e32 vcc, -1, v17
	ds_write_b16 v1, v2 offset:9216
	s_nop 0
	v_cndmask_b32_e32 v2, 0, v38, vcc
	v_cmp_lt_i32_e32 vcc, -1, v16
	ds_write_b16 v1, v2 offset:10240
	s_nop 0
	v_cndmask_b32_e32 v2, 0, v37, vcc
	v_cmp_lt_i32_e32 vcc, -1, v19
	ds_write_b16 v1, v2 offset:11264
	s_nop 0
	v_cndmask_b32_e32 v2, 0, v36, vcc
	v_cmp_lt_i32_e32 vcc, -1, v18
	ds_write_b16 v1, v2 offset:12288
	s_nop 0
	v_cndmask_b32_e32 v2, 0, v35, vcc
	v_cmp_lt_i32_e32 vcc, -1, v21
	ds_write_b16 v1, v2 offset:13312
	s_nop 0
	v_cndmask_b32_e32 v2, 0, v34, vcc
	v_cmp_lt_i32_e32 vcc, -1, v20
	ds_write_b16 v1, v2 offset:14336
	s_nop 0
	v_cndmask_b32_e32 v2, 0, v33, vcc
	v_cmp_lt_i32_e32 vcc, -1, v23
	ds_write_b16 v1, v2 offset:15360
	s_nop 0
	v_cndmask_b32_e32 v2, 0, v32, vcc
	v_cmp_lt_i32_e32 vcc, -1, v22
	ds_write_b16 v1, v2 offset:16384
	s_nop 0
	v_cndmask_b32_e32 v2, 0, v4, vcc
	ds_write_b16 v1, v2 offset:17408
	v_mov_b32_e32 v4, v0
	v_mov_b32_e32 v1, s33
	s_waitcnt lgkmcnt(0)
	s_barrier
	ds_read_b128 v[6:9], v1
	v_readfirstlane_b32 s4, v4
	s_ashr_i32 s5, s4, 6
	s_waitcnt lgkmcnt(0)
	v_readfirstlane_b32 s14, v6
	v_readfirstlane_b32 s37, v7
	v_readfirstlane_b32 s38, v8
	s_cmp_eq_u32 s14, 0
	v_readfirstlane_b32 s40, v9
	s_cbranch_scc1 .LBB0_572
	v_mov_b32_e32 v1, v0
	s_load_dwordx2 s[14:15], s[6:7], 0x80
	v_and_b32_e32 v3, 63, v4
	v_lshlrev_b32_e32 v6, 4, v1
	v_add_u32_e32 v5, 0x2000, v6
	v_ashrrev_i32_e32 v2, 3, v1
	v_ashrrev_i32_e32 v5, 7, v5
	v_lshl_add_u32 v2, v2, 1, s16
	v_lshl_add_u32 v5, v5, 1, s16
	ds_read_u16 v9, v2
	ds_read_u16 v8, v2 offset:256
	ds_read_u16 v7, v5
	ds_read_u16 v5, v5 offset:256
	s_cmp_lt_u32 s4, 64
	s_cselect_b64 s[16:17], -1, 0
	s_cmp_gt_u32 s4, 63
	v_lshlrev_b32_e32 v2, 4, v3
	v_lshlrev_b32_e32 v3, 7, v3
	s_cbranch_scc1 .LBB0_553
	s_ashr_i32 s41, s40, 31
	s_lshl_b64 s[18:19], s[40:41], 13
	s_waitcnt lgkmcnt(0)
	s_add_u32 s20, s14, s18
	s_addc_u32 s21, s15, s19
	s_lshl_b32 s18, s40, 10
	s_lshl_b32 s19, s38, 7
	s_sub_i32 s18, s19, s18
	s_ashr_i32 s19, s18, 31
	s_lshl_b64 s[18:19], s[18:19], 2
	s_add_u32 s18, s20, s18
	v_and_b32_e32 v10, 0x1000, v3
	s_movk_i32 s20, 0x1f0
	s_addc_u32 s19, s21, s19
	v_and_or_b32 v10, v2, s20, v10
	s_add_i32 s20, 0, 0x24cc0
	s_mov_b32 m0, s20
	s_nop 0
	global_load_lds_dwordx4 v10, s[18:19] offset:0
.LBB0_553:
	v_lshrrev_b32_e32 v6, 8, v6
	v_xor_b32_e32 v1, v6, v1
	v_lshlrev_b32_e32 v1, 4, v1
	v_and_b32_e32 v1, 0x70, v1
	s_waitcnt lgkmcnt(0)
	v_and_b32_e32 v6, 0xffff, v9
	v_lshl_or_b32 v171, v6, 10, v1
	v_and_b32_e32 v6, 0xffff, v8
	v_and_b32_e32 v5, 0xffff, v5
	v_lshl_or_b32 v172, v6, 10, v1
	v_and_b32_e32 v6, 0xffff, v7
	v_lshl_or_b32 v175, v5, 10, v1
	v_lshrrev_b32_e32 v5, 4, v4
	v_lshl_or_b32 v174, v6, 10, v1
	v_xor_b32_e32 v1, v5, v4
	v_lshlrev_b32_e32 v1, 4, v1
	s_lshl_b32 s18, s5, 10
	s_ashr_i32 s22, s4, 8
	v_and_b32_e32 v6, 0x70, v1
	v_ashrrev_i32_e32 v1, 3, v4
	s_add_i32 s29, s18, 0
	v_lshlrev_b32_e32 v7, 1, v1
	v_lshrrev_b32_e32 v8, 2, v1
	s_add_u32 s31, s10, 0x5c00000
	v_and_b32_e32 v7, 24, v7
	v_and_b32_e32 v8, 4, v8
	v_and_b32_e32 v1, 0x3fffe3, v1
	v_mov_b32_e32 v170, 0x2000
	s_addc_u32 s41, s11, 0
	v_or3_b32 v1, v1, v8, v7
	v_lshl_add_u32 v7, v4, 4, v170
	s_add_u32 s18, s10, 0xdc00000
	v_ashrrev_i32_e32 v7, 7, v7
	s_addc_u32 s19, s11, 0
	s_ashr_i32 s39, s38, 31
	v_lshlrev_b32_e32 v8, 1, v7
	v_lshrrev_b32_e32 v9, 2, v7
	s_lshl_b64 s[20:21], s[38:39], 18
	v_and_b32_e32 v8, 24, v8
	v_and_b32_e32 v9, 4, v9
	v_and_b32_e32 v7, 0x3fffe3, v7
	s_add_u32 s44, s31, s20
	v_lshl_or_b32 v1, v1, 10, v6
	v_or3_b32 v7, v7, v9, v8
	s_addc_u32 s45, s41, s21
	s_add_i32 s48, s29, 0x10000
	s_mov_b32 m0, s48
	s_nop 0
	global_load_lds_dwordx4 v1, s[44:45] offset:0
	v_lshl_or_b32 v173, v7, 10, v6
	s_add_i32 s49, s29, 0x12000
	s_mov_b32 m0, s49
	s_nop 0
	global_load_lds_dwordx4 v173, s[44:45] offset:0
	s_add_u32 s20, s44, 0x20000
	s_addc_u32 s21, s45, 0
	s_add_i32 s50, s29, 0x14000
	s_mov_b32 m0, s50
	s_nop 0
	global_load_lds_dwordx4 v1, s[20:21] offset:0
	s_add_i32 s51, s29, 0x16000
	s_mov_b32 m0, s51
	s_nop 0
	global_load_lds_dwordx4 v173, s[20:21] offset:0
	s_mov_b32 m0, s29
	s_nop 0
	global_load_lds_dwordx4 v171, s[18:19] offset:0
	s_add_i32 s52, s29, 0x2000
	s_mov_b32 m0, s52
	s_nop 0
	global_load_lds_dwordx4 v174, s[18:19] offset:0
	s_add_i32 s53, s29, 0x4000
	s_mov_b32 m0, s53
	s_nop 0
	global_load_lds_dwordx4 v172, s[18:19] offset:0
	s_add_i32 s54, s29, 0x6000
	s_mov_b32 m0, s54
	s_nop 0
	global_load_lds_dwordx4 v175, s[18:19] offset:0
	s_cmp_eq_u32 s22, 1
	s_mov_b32 s67, 0
	s_cselect_b64 s[20:21], -1, 0
	s_cmp_lg_u32 s22, 1
	s_cbranch_scc1 .LBB0_555
	s_barrier
.LBB0_555:
	v_and_b32_e32 v6, 15, v4
	s_lshl_b32 s5, s5, 5
	v_lshlrev_b32_e32 v7, 7, v6
	s_and_b32 s5, s5, 0x60
	v_lshl_or_b32 v7, s22, 13, v7
	s_add_u32 s22, s44, 0x80
	v_or_b32_e32 v6, s5, v6
	s_waitcnt vmcnt(2)
	s_barrier
	s_addc_u32 s23, s45, 0
	s_add_i32 s55, s29, 0x18000
	s_mov_b32 m0, s55
	s_nop 0
	global_load_lds_dwordx4 v1, s[22:23] offset:0
	s_add_i32 s56, s29, 0x1a000
	s_mov_b32 m0, s56
	s_nop 0
	global_load_lds_dwordx4 v173, s[22:23] offset:0
	s_add_u32 s22, s18, 0x80
	s_addc_u32 s23, s19, 0
	s_add_i32 s57, s29, 0x8000
	s_mov_b32 m0, s57
	s_nop 0
	global_load_lds_dwordx4 v171, s[22:23] offset:0
	s_add_i32 s58, s29, 0xa000
	s_mov_b32 m0, s58
	s_nop 0
	global_load_lds_dwordx4 v174, s[22:23] offset:0
	s_add_u32 s24, s44, 0x20080
	s_addc_u32 s25, s45, 0
	s_add_i32 s59, s29, 0x1c000
	s_mov_b32 m0, s59
	s_nop 0
	global_load_lds_dwordx4 v1, s[24:25] offset:0
	s_add_i32 s60, s29, 0x1e000
	s_add_i32 s61, s29, 0xc000
	v_bfe_u32 v8, v4, 4, 2
	v_bfe_u32 v4, v4, 1, 3
	s_mov_b32 m0, s60
	s_nop 0
	global_load_lds_dwordx4 v173, s[24:25] offset:0
	s_add_u32 s24, s18, 0x380
	v_bitop3_b32 v5, v5, v4, 3 bitop3:0x6c
	v_bitop3_b32 v4, v8, v4, 4 bitop3:0x36
	s_addc_u32 s25, s19, 0
	v_lshlrev_b32_e32 v5, 4, v5
	v_lshlrev_b32_e32 v4, 4, v4
	v_lshlrev_b32_e32 v6, 7, v6
	s_cmpk_lt_u32 s4, 0x100
	v_and_b32_e32 v3, 0x1000, v3
	s_movk_i32 s4, 0x1f0
	v_or_b32_e32 v176, v6, v5
	v_or_b32_e32 v177, v6, v4
	s_waitcnt vmcnt(6)
	s_cselect_b64 s[26:27], -1, 0
	v_and_or_b32 v178, v2, s4, v3
	s_add_i32 s4, 0, 0x10000
	v_or_b32_e32 v9, v5, v7
	v_or_b32_e32 v7, v4, v7
	v_add_u32_e32 v179, s4, v176
	v_add_u32_e32 v180, s4, v177
	s_add_i32 s4, 0, 0x14000
	s_add_i32 s62, s29, 0xe000
	v_add_u32_e32 v181, s4, v176
	v_add_u32_e32 v182, s4, v177
	v_add_u32_e32 v183, 0, v9
	v_add_u32_e32 v184, 0, v7
	v_mov_b32_e32 v185, 0x7f7f7f7f
	s_movk_i32 s63, 0xffc0
	v_mov_b32_e32 v163, 0
	s_mov_b32 s28, 0x3a000000
	s_mov_b32 s30, 0x39000000
	s_mov_b32 s64, 0xc0c00000
	v_mov_b32_e32 v186, 0x41000000
	s_barrier
	s_branch .LBB0_558

.LBB0_561:
	.p2align 3
	s_nop 0
	ds_read_b128 v[18:21], v179
	ds_read_b128 v[26:29], v179 offset:2048
	ds_read_b128 v[22:25], v180
	ds_read_b128 v[30:33], v180 offset:2048
	ds_read_b128 v[2:5], v181
	ds_read_b128 v[10:13], v181 offset:2048
	ds_read_b128 v[6:9], v182
	ds_read_b128 v[14:17], v182 offset:2048
	ds_read_b128 v[194:197], v183
	ds_read_b128 v[202:205], v183 offset:2048
	ds_read_b128 v[198:201], v184
	ds_read_b128 v[206:209], v184 offset:2048
	ds_read_b128 v[210:213], v183 offset:4096
	ds_read_b128 v[218:221], v183 offset:6144
	ds_read_b128 v[214:217], v184 offset:4096
	ds_read_b128 v[222:225], v184 offset:6144
	s_add_u32 s39, s18, s4
	s_addc_u32 s68, s19, s5
	s_add_u32 s42, s39, 0x80
	s_addc_u32 s43, s68, 0
	s_mov_b32 m0, s61
	s_nop 0
	global_load_lds_dwordx4 v172, s[42:43] offset:0
	s_nop 0
	s_mov_b32 m0, s62
	s_nop 0
	global_load_lds_dwordx4 v175, s[42:43] offset:0
	s_waitcnt vmcnt(8)
	s_waitcnt lgkmcnt(0)
	s_barrier
	s_setprio 1
	s_waitcnt lgkmcnt(5)
	v_mfma_f32_16x16x128_f8f6f4 v[158:161], v[18:25], v[194:201], v[158:161]
	v_mfma_f32_16x16x128_f8f6f4 v[150:153], v[26:33], v[194:201], v[150:153]
	s_waitcnt lgkmcnt(4)
	v_mfma_f32_16x16x128_f8f6f4 v[142:145], v[18:25], v[202:209], v[142:145]
	v_mfma_f32_16x16x128_f8f6f4 v[134:137], v[26:33], v[202:209], v[134:137]
	s_waitcnt lgkmcnt(1)
	v_mfma_f32_16x16x128_f8f6f4 v[126:129], v[18:25], v[210:217], v[126:129]
	v_mfma_f32_16x16x128_f8f6f4 v[118:121], v[26:33], v[210:217], v[118:121]
	s_waitcnt lgkmcnt(0)
	v_mfma_f32_16x16x128_f8f6f4 v[110:113], v[18:25], v[218:225], v[110:113]
	v_mfma_f32_16x16x128_f8f6f4 v[102:105], v[26:33], v[218:225], v[102:105]
	s_setprio 0
	s_setprio 1
	v_mfma_f32_16x16x128_f8f6f4 v[154:157], v[2:9], v[194:201], v[154:157]
	v_mfma_f32_16x16x128_f8f6f4 v[146:149], v[10:17], v[194:201], v[146:149]
	v_mfma_f32_16x16x128_f8f6f4 v[138:141], v[2:9], v[202:209], v[138:141]
	v_mfma_f32_16x16x128_f8f6f4 v[130:133], v[10:17], v[202:209], v[130:133]
	v_mfma_f32_16x16x128_f8f6f4 v[122:125], v[2:9], v[210:217], v[122:125]
	v_mfma_f32_16x16x128_f8f6f4 v[114:117], v[10:17], v[210:217], v[114:117]
	v_mfma_f32_16x16x128_f8f6f4 v[106:109], v[2:9], v[218:225], v[106:109]
	v_mfma_f32_16x16x128_f8f6f4 v[98:101], v[10:17], v[218:225], v[98:101]
	s_setprio 0
	s_barrier
	s_add_u32 s69, s44, s4
	s_addc_u32 s70, s45, s5
	ds_read_b128 v[194:197], v183 offset:16384
	ds_read_b128 v[202:205], v183 offset:18432
	ds_read_b128 v[198:201], v184 offset:16384
	ds_read_b128 v[206:209], v184 offset:18432
	ds_read_b128 v[210:213], v183 offset:20480
	ds_read_b128 v[218:221], v183 offset:22528
	ds_read_b128 v[214:217], v184 offset:20480
	ds_read_b128 v[222:225], v184 offset:22528
	s_add_u32 s42, s69, 0x100
	s_addc_u32 s43, s70, 0
	s_mov_b32 m0, s48
	s_nop 0
	global_load_lds_dwordx4 v1, s[42:43] offset:0
	s_nop 0
	s_mov_b32 m0, s49
	s_nop 0
	global_load_lds_dwordx4 v173, s[42:43] offset:0
	s_add_u32 s42, s69, 0x20100
	s_addc_u32 s43, s70, 0
	s_mov_b32 m0, s50
	s_nop 0
	global_load_lds_dwordx4 v1, s[42:43] offset:0
	s_nop 0
	s_mov_b32 m0, s51
	s_nop 0
	global_load_lds_dwordx4 v173, s[42:43] offset:0
	s_add_u32 s42, s39, 0x100
	s_addc_u32 s43, s68, 0
	s_mov_b32 m0, s29
	s_nop 0
	global_load_lds_dwordx4 v171, s[42:43] offset:0
	s_nop 0
	s_mov_b32 m0, s52
	s_nop 0
	global_load_lds_dwordx4 v174, s[42:43] offset:0
	s_waitcnt vmcnt(8)
	s_waitcnt lgkmcnt(0)
	s_barrier
	s_setprio 1
	s_waitcnt lgkmcnt(5)
	v_mfma_f32_16x16x128_f8f6f4 v[94:97], v[18:25], v[194:201], v[94:97]
	v_mfma_f32_16x16x128_f8f6f4 v[86:89], v[26:33], v[194:201], v[86:89]
	s_waitcnt lgkmcnt(4)
	v_mfma_f32_16x16x128_f8f6f4 v[78:81], v[18:25], v[202:209], v[78:81]
	v_mfma_f32_16x16x128_f8f6f4 v[70:73], v[26:33], v[202:209], v[70:73]
	s_waitcnt lgkmcnt(1)
	v_mfma_f32_16x16x128_f8f6f4 v[62:65], v[18:25], v[210:217], v[62:65]
	v_mfma_f32_16x16x128_f8f6f4 v[54:57], v[26:33], v[210:217], v[54:57]
	s_waitcnt lgkmcnt(0)
	v_mfma_f32_16x16x128_f8f6f4 v[46:49], v[18:25], v[218:225], v[46:49]
	v_mfma_f32_16x16x128_f8f6f4 v[38:41], v[26:33], v[218:225], v[38:41]
	s_setprio 0
	s_setprio 1
	v_mfma_f32_16x16x128_f8f6f4 v[90:93], v[2:9], v[194:201], v[90:93]
	v_mfma_f32_16x16x128_f8f6f4 v[82:85], v[10:17], v[194:201], v[82:85]
	v_mfma_f32_16x16x128_f8f6f4 v[74:77], v[2:9], v[202:209], v[74:77]
	v_mfma_f32_16x16x128_f8f6f4 v[66:69], v[10:17], v[202:209], v[66:69]
	v_mfma_f32_16x16x128_f8f6f4 v[58:61], v[2:9], v[210:217], v[58:61]
	v_mfma_f32_16x16x128_f8f6f4 v[50:53], v[10:17], v[210:217], v[50:53]
	v_mfma_f32_16x16x128_f8f6f4 v[42:45], v[2:9], v[218:225], v[42:45]
	v_mfma_f32_16x16x128_f8f6f4 v[34:37], v[10:17], v[218:225], v[34:37]
	s_setprio 0
	s_barrier
	s_add_i32 s71, 0, 0x18000
	v_add_u32_e32 v162, s71, v176
	v_add_u32_e32 v187, s71, v177
	s_add_i32 s71, 0, 0x1c000
	v_add_u32_e32 v194, s71, v176
	ds_read_b128 v[2:5], v162
	ds_read_b128 v[10:13], v162 offset:2048
	ds_read_b128 v[6:9], v187
	ds_read_b128 v[14:17], v187 offset:2048
	v_add_u32_e32 v195, s71, v177
	ds_read_b128 v[18:21], v194
	ds_read_b128 v[26:29], v194 offset:2048
	ds_read_b128 v[22:25], v195
	ds_read_b128 v[30:33], v195 offset:2048
	ds_read_b128 v[196:199], v183 offset:32768
	ds_read_b128 v[204:207], v183 offset:34816
	ds_read_b128 v[200:203], v184 offset:32768
	ds_read_b128 v[208:211], v184 offset:34816
	ds_read_b128 v[212:215], v183 offset:36864
	ds_read_b128 v[220:223], v183 offset:38912
	ds_read_b128 v[216:219], v184 offset:36864
	ds_read_b128 v[224:227], v184 offset:38912
	s_mov_b32 m0, s53
	s_nop 0
	global_load_lds_dwordx4 v172, s[42:43] offset:0
	s_nop 0
	s_mov_b32 m0, s54
	s_nop 0
	global_load_lds_dwordx4 v175, s[42:43] offset:0
	s_waitcnt vmcnt(8)
	s_waitcnt lgkmcnt(0)
	s_barrier
	s_setprio 1
	s_waitcnt lgkmcnt(5)
	v_mfma_f32_16x16x128_f8f6f4 v[158:161], v[2:9], v[196:203], v[158:161]
	v_mfma_f32_16x16x128_f8f6f4 v[150:153], v[10:17], v[196:203], v[150:153]
	s_waitcnt lgkmcnt(4)
	v_mfma_f32_16x16x128_f8f6f4 v[142:145], v[2:9], v[204:211], v[142:145]
	v_mfma_f32_16x16x128_f8f6f4 v[134:137], v[10:17], v[204:211], v[134:137]
	s_waitcnt lgkmcnt(1)
	v_mfma_f32_16x16x128_f8f6f4 v[126:129], v[2:9], v[212:219], v[126:129]
	v_mfma_f32_16x16x128_f8f6f4 v[118:121], v[10:17], v[212:219], v[118:121]
	s_waitcnt lgkmcnt(0)
	v_mfma_f32_16x16x128_f8f6f4 v[110:113], v[2:9], v[220:227], v[110:113]
	v_mfma_f32_16x16x128_f8f6f4 v[102:105], v[10:17], v[220:227], v[102:105]
	s_setprio 0
	s_setprio 1
	v_mfma_f32_16x16x128_f8f6f4 v[154:157], v[18:25], v[196:203], v[154:157]
	v_mfma_f32_16x16x128_f8f6f4 v[146:149], v[26:33], v[196:203], v[146:149]
	v_mfma_f32_16x16x128_f8f6f4 v[138:141], v[18:25], v[204:211], v[138:141]
	v_mfma_f32_16x16x128_f8f6f4 v[130:133], v[26:33], v[204:211], v[130:133]
	v_mfma_f32_16x16x128_f8f6f4 v[122:125], v[18:25], v[212:219], v[122:125]
	v_mfma_f32_16x16x128_f8f6f4 v[114:117], v[26:33], v[212:219], v[114:117]
	v_mfma_f32_16x16x128_f8f6f4 v[106:109], v[18:25], v[220:227], v[106:109]
	v_mfma_f32_16x16x128_f8f6f4 v[98:101], v[26:33], v[220:227], v[98:101]
	s_setprio 0
	s_barrier
	ds_read_b128 v[196:199], v183 offset:49152
	ds_read_b128 v[204:207], v183 offset:51200
	ds_read_b128 v[200:203], v184 offset:49152
	ds_read_b128 v[208:211], v184 offset:51200
	ds_read_b128 v[212:215], v183 offset:53248
	ds_read_b128 v[220:223], v183 offset:55296
	ds_read_b128 v[216:219], v184 offset:53248
	ds_read_b128 v[224:227], v184 offset:55296
	s_add_u32 s42, s69, 0x180
	s_addc_u32 s43, s70, 0
	s_mov_b32 m0, s55
	s_nop 0
	global_load_lds_dwordx4 v1, s[42:43] offset:0
	s_nop 0
	s_mov_b32 m0, s56
	s_nop 0
	global_load_lds_dwordx4 v173, s[42:43] offset:0
	s_add_u32 s42, s69, 0x20180
	s_addc_u32 s43, s70, 0
	s_mov_b32 m0, s59
	s_nop 0
	global_load_lds_dwordx4 v1, s[42:43] offset:0
	s_nop 0
	s_mov_b32 m0, s60
	s_nop 0
	global_load_lds_dwordx4 v173, s[42:43] offset:0
	s_add_u32 s42, s39, 0x180
	s_addc_u32 s43, s68, 0
	s_mov_b32 m0, s57
	s_nop 0
	global_load_lds_dwordx4 v171, s[42:43] offset:0
	s_nop 0
	s_mov_b32 m0, s58
	s_nop 0
	global_load_lds_dwordx4 v174, s[42:43] offset:0
	s_waitcnt vmcnt(8)
	s_waitcnt lgkmcnt(0)
	s_barrier
	s_setprio 1
	s_waitcnt lgkmcnt(5)
	v_mfma_f32_16x16x128_f8f6f4 v[94:97], v[2:9], v[196:203], v[94:97]
	v_mfma_f32_16x16x128_f8f6f4 v[86:89], v[10:17], v[196:203], v[86:89]
	s_waitcnt lgkmcnt(4)
	v_mfma_f32_16x16x128_f8f6f4 v[78:81], v[2:9], v[204:211], v[78:81]
	v_mfma_f32_16x16x128_f8f6f4 v[70:73], v[10:17], v[204:211], v[70:73]
	s_waitcnt lgkmcnt(1)
	v_mfma_f32_16x16x128_f8f6f4 v[62:65], v[2:9], v[212:219], v[62:65]
	v_mfma_f32_16x16x128_f8f6f4 v[54:57], v[10:17], v[212:219], v[54:57]
	s_waitcnt lgkmcnt(0)
	v_mfma_f32_16x16x128_f8f6f4 v[46:49], v[2:9], v[220:227], v[46:49]
	v_mfma_f32_16x16x128_f8f6f4 v[38:41], v[10:17], v[220:227], v[38:41]
	s_setprio 0
	s_setprio 1
	v_mfma_f32_16x16x128_f8f6f4 v[90:93], v[18:25], v[196:203], v[90:93]
	v_mfma_f32_16x16x128_f8f6f4 v[82:85], v[26:33], v[196:203], v[82:85]
	v_mfma_f32_16x16x128_f8f6f4 v[74:77], v[18:25], v[204:211], v[74:77]
	v_mfma_f32_16x16x128_f8f6f4 v[66:69], v[26:33], v[204:211], v[66:69]
	v_mfma_f32_16x16x128_f8f6f4 v[58:61], v[18:25], v[212:219], v[58:61]
	v_mfma_f32_16x16x128_f8f6f4 v[50:53], v[26:33], v[212:219], v[50:53]
	v_mfma_f32_16x16x128_f8f6f4 v[42:45], v[18:25], v[220:227], v[42:45]
	v_mfma_f32_16x16x128_f8f6f4 v[34:37], v[26:33], v[220:227], v[34:37]
	s_setprio 0
	s_barrier
	s_add_i32 s35, s35, 2
	s_add_u32 s4, s4, 0x100
	s_addc_u32 s5, s5, 0
	s_cmp_lt_u32 s35, 4
	s_cbranch_scc1 .LBB0_561
	ds_read_b128 v[18:21], v179
	ds_read_b128 v[26:29], v179 offset:2048
	ds_read_b128 v[22:25], v180
	ds_read_b128 v[30:33], v180 offset:2048
	ds_read_b128 v[2:5], v181
	ds_read_b128 v[10:13], v181 offset:2048
	ds_read_b128 v[6:9], v182
	ds_read_b128 v[14:17], v182 offset:2048
	ds_read_b128 v[196:199], v183
	ds_read_b128 v[204:207], v183 offset:2048
	ds_read_b128 v[200:203], v184
	ds_read_b128 v[208:211], v184 offset:2048
	ds_read_b128 v[212:215], v183 offset:4096
	ds_read_b128 v[220:223], v183 offset:6144
	ds_read_b128 v[216:219], v184 offset:4096
	ds_read_b128 v[224:227], v184 offset:6144
	s_mov_b32 m0, s61
	s_nop 0
	global_load_lds_dwordx4 v172, s[24:25] offset:0
	s_nop 0
	s_mov_b32 m0, s62
	s_nop 0
	global_load_lds_dwordx4 v175, s[24:25] offset:0
	s_waitcnt vmcnt(8)
	s_waitcnt lgkmcnt(0)
	s_barrier
	s_setprio 1
	s_waitcnt lgkmcnt(5)
	v_mfma_f32_16x16x128_f8f6f4 v[158:161], v[18:25], v[196:203], v[158:161]
	v_mfma_f32_16x16x128_f8f6f4 v[150:153], v[26:33], v[196:203], v[150:153]
	s_waitcnt lgkmcnt(4)
	v_mfma_f32_16x16x128_f8f6f4 v[142:145], v[18:25], v[204:211], v[142:145]
	v_mfma_f32_16x16x128_f8f6f4 v[134:137], v[26:33], v[204:211], v[134:137]
	s_waitcnt lgkmcnt(1)
	v_mfma_f32_16x16x128_f8f6f4 v[126:129], v[18:25], v[212:219], v[126:129]
	v_mfma_f32_16x16x128_f8f6f4 v[118:121], v[26:33], v[212:219], v[118:121]
	s_waitcnt lgkmcnt(0)
	v_mfma_f32_16x16x128_f8f6f4 v[110:113], v[18:25], v[220:227], v[110:113]
	v_mfma_f32_16x16x128_f8f6f4 v[102:105], v[26:33], v[220:227], v[102:105]
	s_setprio 0
	s_setprio 1
	v_mfma_f32_16x16x128_f8f6f4 v[154:157], v[2:9], v[196:203], v[154:157]
	v_mfma_f32_16x16x128_f8f6f4 v[146:149], v[10:17], v[196:203], v[146:149]
	v_mfma_f32_16x16x128_f8f6f4 v[138:141], v[2:9], v[204:211], v[138:141]
	v_mfma_f32_16x16x128_f8f6f4 v[130:133], v[10:17], v[204:211], v[130:133]
	v_mfma_f32_16x16x128_f8f6f4 v[122:125], v[2:9], v[212:219], v[122:125]
	v_mfma_f32_16x16x128_f8f6f4 v[114:117], v[10:17], v[212:219], v[114:117]
	v_mfma_f32_16x16x128_f8f6f4 v[106:109], v[2:9], v[220:227], v[106:109]
	v_mfma_f32_16x16x128_f8f6f4 v[98:101], v[10:17], v[220:227], v[98:101]
	s_setprio 0
	s_barrier
	v_cndmask_b32_e64 v196, 0, 1, s[46:47]
	v_cmp_ne_u32_e64 s[4:5], 1, v196
	s_andn2_b64 vcc, exec, s[46:47]
	s_cbranch_vccnz .LBB0_564
	v_mov_b32_e32 v171, v0
	s_lshl_b32 s35, s66, 9
	s_add_i32 s35, s35, 0
	v_lshrrev_b32_e32 v172, 4, v171
	v_xor_b32_e32 v172, v172, v171
	s_add_i32 s35, s35, 0x20480
	v_ashrrev_i32_e32 v174, 3, v171
	v_lshl_add_u32 v171, v171, 4, v170
	v_lshl_add_u32 v174, v174, 1, s35
	v_ashrrev_i32_e32 v171, 7, v171
	v_lshl_add_u32 v171, v171, 1, s35
	ds_read_u16 v175, v174
	ds_read_u16 v174, v174 offset:256
	ds_read_u16 v196, v171
	ds_read_u16 v197, v171 offset:256
	v_lshlrev_b32_e32 v172, 4, v172
	v_and_b32_e32 v198, 0x70, v172
	s_waitcnt lgkmcnt(3)
	v_lshl_or_b32 v171, v175, 10, v198
	s_waitcnt lgkmcnt(2)
	v_lshl_or_b32 v172, v174, 10, v198
	s_waitcnt lgkmcnt(1)
	v_lshl_or_b32 v174, v196, 10, v198
	s_waitcnt lgkmcnt(0)
	v_lshl_or_b32 v175, v197, 10, v198
.LBB0_564:
	s_ashr_i32 s35, s34, 31
	s_lshl_b64 s[42:43], s[34:35], 18
	s_add_u32 s42, s31, s42
	s_addc_u32 s43, s41, s43
	s_and_b64 s[46:47], s[46:47], exec
	ds_read_b128 v[196:199], v183 offset:16384
	ds_read_b128 v[204:207], v183 offset:18432
	ds_read_b128 v[200:203], v184 offset:16384
	ds_read_b128 v[208:211], v184 offset:18432
	ds_read_b128 v[212:215], v183 offset:20480
	ds_read_b128 v[220:223], v183 offset:22528
	ds_read_b128 v[216:219], v184 offset:20480
	ds_read_b128 v[224:227], v184 offset:22528
	s_cselect_b32 s45, s43, s45
	s_cselect_b32 s44, s42, s44
	s_mov_b32 m0, s48
	s_nop 0
	global_load_lds_dwordx4 v1, s[44:45] offset:0
	s_add_u32 s46, s44, 0x20000
	s_mov_b32 m0, s49
	s_nop 0
	global_load_lds_dwordx4 v173, s[44:45] offset:0
	s_addc_u32 s47, s45, 0
	s_mov_b32 m0, s50
	s_nop 0
	global_load_lds_dwordx4 v1, s[46:47] offset:0
	s_nop 0
	s_mov_b32 m0, s51
	s_nop 0
	global_load_lds_dwordx4 v173, s[46:47] offset:0
	s_nop 0
	s_mov_b32 m0, s29
	s_nop 0
	global_load_lds_dwordx4 v171, s[18:19] offset:0
	s_nop 0
	s_mov_b32 m0, s52
	s_nop 0
	global_load_lds_dwordx4 v174, s[18:19] offset:0
	s_waitcnt vmcnt(8)
	s_waitcnt lgkmcnt(0)
	s_barrier
	s_setprio 1
	s_waitcnt lgkmcnt(5)
	v_mfma_f32_16x16x128_f8f6f4 v[94:97], v[18:25], v[196:203], v[94:97]
	v_mfma_f32_16x16x128_f8f6f4 v[86:89], v[26:33], v[196:203], v[86:89]
	s_waitcnt lgkmcnt(4)
	v_mfma_f32_16x16x128_f8f6f4 v[78:81], v[18:25], v[204:211], v[78:81]
	v_mfma_f32_16x16x128_f8f6f4 v[70:73], v[26:33], v[204:211], v[70:73]
	s_waitcnt lgkmcnt(1)
	v_mfma_f32_16x16x128_f8f6f4 v[62:65], v[18:25], v[212:219], v[62:65]
	v_mfma_f32_16x16x128_f8f6f4 v[54:57], v[26:33], v[212:219], v[54:57]
	s_waitcnt lgkmcnt(0)
	v_mfma_f32_16x16x128_f8f6f4 v[46:49], v[18:25], v[220:227], v[46:49]
	v_mfma_f32_16x16x128_f8f6f4 v[38:41], v[26:33], v[220:227], v[38:41]
	s_setprio 0
	s_setprio 1
	v_mfma_f32_16x16x128_f8f6f4 v[90:93], v[2:9], v[196:203], v[90:93]
	v_mfma_f32_16x16x128_f8f6f4 v[82:85], v[10:17], v[196:203], v[82:85]
	v_mfma_f32_16x16x128_f8f6f4 v[74:77], v[2:9], v[204:211], v[74:77]
	v_mfma_f32_16x16x128_f8f6f4 v[66:69], v[10:17], v[204:211], v[66:69]
	v_mfma_f32_16x16x128_f8f6f4 v[58:61], v[2:9], v[212:219], v[58:61]
	v_mfma_f32_16x16x128_f8f6f4 v[50:53], v[10:17], v[212:219], v[50:53]
	v_mfma_f32_16x16x128_f8f6f4 v[42:45], v[2:9], v[220:227], v[42:45]
	v_mfma_f32_16x16x128_f8f6f4 v[34:37], v[10:17], v[220:227], v[34:37]
	s_setprio 0
	s_barrier
	ds_read_b128 v[2:5], v162
	ds_read_b128 v[10:13], v162 offset:2048
	ds_read_b128 v[6:9], v187
	ds_read_b128 v[14:17], v187 offset:2048
	ds_read_b128 v[18:21], v194
	ds_read_b128 v[26:29], v194 offset:2048
	ds_read_b128 v[22:25], v195
	ds_read_b128 v[30:33], v195 offset:2048
	ds_read_b128 v[194:197], v183 offset:32768
	ds_read_b128 v[202:205], v183 offset:34816
	ds_read_b128 v[198:201], v184 offset:32768
	ds_read_b128 v[206:209], v184 offset:34816
	ds_read_b128 v[210:213], v183 offset:36864
	ds_read_b128 v[218:221], v183 offset:38912
	ds_read_b128 v[214:217], v184 offset:36864
	ds_read_b128 v[222:225], v184 offset:38912
	s_mov_b32 m0, s53
	s_nop 0
	global_load_lds_dwordx4 v172, s[18:19] offset:0
	s_nop 0
	s_mov_b32 m0, s54
	s_nop 0
	global_load_lds_dwordx4 v175, s[18:19] offset:0
	s_waitcnt vmcnt(8)
	s_waitcnt lgkmcnt(0)
	s_barrier
	s_setprio 1
	s_waitcnt lgkmcnt(5)
	v_mfma_f32_16x16x128_f8f6f4 v[158:161], v[2:9], v[194:201], v[158:161]
	v_mfma_f32_16x16x128_f8f6f4 v[150:153], v[10:17], v[194:201], v[150:153]
	s_waitcnt lgkmcnt(4)
	v_mfma_f32_16x16x128_f8f6f4 v[142:145], v[2:9], v[202:209], v[142:145]
	v_mfma_f32_16x16x128_f8f6f4 v[134:137], v[10:17], v[202:209], v[134:137]
	s_waitcnt lgkmcnt(1)
	v_mfma_f32_16x16x128_f8f6f4 v[126:129], v[2:9], v[210:217], v[126:129]
	v_mfma_f32_16x16x128_f8f6f4 v[118:121], v[10:17], v[210:217], v[118:121]
	s_waitcnt lgkmcnt(0)
	v_mfma_f32_16x16x128_f8f6f4 v[110:113], v[2:9], v[218:225], v[110:113]
	v_mfma_f32_16x16x128_f8f6f4 v[102:105], v[10:17], v[218:225], v[102:105]
	s_setprio 0
	s_setprio 1
	v_mfma_f32_16x16x128_f8f6f4 v[154:157], v[18:25], v[194:201], v[154:157]
	v_mfma_f32_16x16x128_f8f6f4 v[146:149], v[26:33], v[194:201], v[146:149]
	v_mfma_f32_16x16x128_f8f6f4 v[138:141], v[18:25], v[202:209], v[138:141]
	v_mfma_f32_16x16x128_f8f6f4 v[130:133], v[26:33], v[202:209], v[130:133]
	v_mfma_f32_16x16x128_f8f6f4 v[122:125], v[18:25], v[210:217], v[122:125]
	v_mfma_f32_16x16x128_f8f6f4 v[114:117], v[26:33], v[210:217], v[114:117]
	v_mfma_f32_16x16x128_f8f6f4 v[106:109], v[18:25], v[218:225], v[106:109]
	v_mfma_f32_16x16x128_f8f6f4 v[98:101], v[26:33], v[218:225], v[98:101]
	s_setprio 0
	s_barrier
	ds_read_b128 v[194:197], v183 offset:49152
	ds_read_b128 v[202:205], v183 offset:51200
	ds_read_b128 v[198:201], v184 offset:49152
	ds_read_b128 v[206:209], v184 offset:51200
	ds_read_b128 v[210:213], v183 offset:53248
	ds_read_b128 v[218:221], v183 offset:55296
	ds_read_b128 v[214:217], v184 offset:53248
	ds_read_b128 v[222:225], v184 offset:55296
	s_add_u32 s46, s44, 0x80
	s_addc_u32 s47, s45, 0
	s_mov_b32 m0, s55
	s_nop 0
	global_load_lds_dwordx4 v1, s[46:47] offset:0
	s_add_u32 s44, s44, 0x20080
	s_mov_b32 m0, s56
	s_nop 0
	global_load_lds_dwordx4 v173, s[46:47] offset:0
	s_addc_u32 s45, s45, 0
	s_mov_b32 m0, s59
	s_nop 0
	global_load_lds_dwordx4 v1, s[44:45] offset:0
	s_nop 0
	s_mov_b32 m0, s60
	s_nop 0
	global_load_lds_dwordx4 v173, s[44:45] offset:0
	s_nop 0
	s_mov_b32 m0, s57
	s_nop 0
	global_load_lds_dwordx4 v171, s[22:23] offset:0
	s_nop 0
	s_mov_b32 m0, s58
	s_nop 0
	global_load_lds_dwordx4 v174, s[22:23] offset:0
	s_waitcnt vmcnt(8)
	s_waitcnt lgkmcnt(0)
	s_barrier
	s_setprio 1
	s_waitcnt lgkmcnt(5)
	v_mfma_f32_16x16x128_f8f6f4 v[94:97], v[2:9], v[194:201], v[94:97]
	v_mfma_f32_16x16x128_f8f6f4 v[86:89], v[10:17], v[194:201], v[86:89]
	s_waitcnt lgkmcnt(4)
	v_mfma_f32_16x16x128_f8f6f4 v[78:81], v[2:9], v[202:209], v[78:81]
	v_mfma_f32_16x16x128_f8f6f4 v[70:73], v[10:17], v[202:209], v[70:73]
	s_waitcnt lgkmcnt(1)
	v_mfma_f32_16x16x128_f8f6f4 v[62:65], v[2:9], v[210:217], v[62:65]
	v_mfma_f32_16x16x128_f8f6f4 v[54:57], v[10:17], v[210:217], v[54:57]
	s_waitcnt lgkmcnt(0)
	v_mfma_f32_16x16x128_f8f6f4 v[46:49], v[2:9], v[218:225], v[46:49]
	v_mfma_f32_16x16x128_f8f6f4 v[38:41], v[10:17], v[218:225], v[38:41]
	s_setprio 0
	s_setprio 1
	v_mfma_f32_16x16x128_f8f6f4 v[90:93], v[18:25], v[194:201], v[90:93]
	v_mfma_f32_16x16x128_f8f6f4 v[82:85], v[26:33], v[194:201], v[82:85]
	v_mfma_f32_16x16x128_f8f6f4 v[74:77], v[18:25], v[202:209], v[74:77]
	v_mfma_f32_16x16x128_f8f6f4 v[66:69], v[26:33], v[202:209], v[66:69]
	v_mfma_f32_16x16x128_f8f6f4 v[58:61], v[18:25], v[210:217], v[58:61]
	v_mfma_f32_16x16x128_f8f6f4 v[50:53], v[26:33], v[210:217], v[50:53]
	v_mfma_f32_16x16x128_f8f6f4 v[42:45], v[18:25], v[218:225], v[42:45]
	v_mfma_f32_16x16x128_f8f6f4 v[34:37], v[26:33], v[218:225], v[34:37]
	s_setprio 0
	s_barrier
	s_nop 15
	s_nop 15
	s_andn2_b64 vcc, exec, s[26:27]
	s_cbranch_vccnz .LBB0_566
	s_barrier
.LBB0_566:
	s_lshl_b32 s35, s67, 10
	v_mov_b32_e32 v25, v0
	s_and_b32 s35, s35, 0x400
	s_add_i32 s35, s35, 0
	v_lshrrev_b32_e32 v26, 1, v25
	v_and_b32_e32 v162, 0x60, v26
	v_lshlrev_b32_e32 v3, 1, v25
	s_add_i32 s35, s35, 0x24cc0
	v_lshlrev_b32_e32 v2, 2, v162
	v_and_b32_e32 v3, 0x60, v3
	v_add3_u32 v14, s35, v2, v3
	ds_read_b128 v[2:5], v14
	ds_read_b128 v[6:9], v14 offset:512
	ds_read_b128 v[10:13], v14 offset:16
	v_ashrrev_i32_e32 v24, 2, v25
	s_lshl_b32 s35, s40, 10
	s_lshl_b32 s38, s38, 7
	s_waitcnt lgkmcnt(2)
	v_pk_mul_f32 v[16:17], v[4:5], 4.0 op_sel_hi:[1,0]
	v_pk_mul_f32 v[18:19], v[2:3], 4.0 op_sel_hi:[1,0]
	ds_read_b128 v[2:5], v14 offset:528
	s_waitcnt lgkmcnt(2)
	v_pk_add_f32 v[20:21], v[8:9], 1.0 op_sel_hi:[1,0]
	s_waitcnt lgkmcnt(1)
	v_pk_mul_f32 v[8:9], v[12:13], 4.0 op_sel_hi:[1,0]
	v_pk_add_f32 v[22:23], v[6:7], 1.0 op_sel_hi:[1,0]
	v_and_b32_e32 v6, 16, v26
	s_waitcnt lgkmcnt(0)
	v_pk_add_f32 v[14:15], v[2:3], 1.0 op_sel_hi:[1,0]
	v_and_b32_e32 v2, 15, v25
	v_pk_add_f32 v[12:13], v[4:5], 1.0 op_sel_hi:[1,0]
	v_and_or_b32 v2, v24, s63, v2
	v_pk_fma_f32 v[4:5], v[158:159], s[28:29], v[18:19] op_sel_hi:[1,0,1]
	v_lshl_add_u32 v24, s37, 8, v2
	v_pk_fma_f32 v[2:3], v[160:161], s[28:29], v[16:17] op_sel_hi:[1,0,1]
	v_min_f32_e32 v4, 0x41e00000, v4
	v_min_f32_e32 v5, 0x41e00000, v5
	v_min_f32_e32 v30, 0x41e00000, v2
	v_min_f32_e32 v31, 0x41e00000, v3
	v_mul_f32_e32 v2, 0xbf1d265f, v4
	v_mul_f32_e32 v3, 0xbf1d265f, v5
	v_exp_f32_e32 v2, v2
	v_exp_f32_e32 v3, v3
	v_mul_f32_e32 v32, 0xbf1d265f, v30
	v_mul_f32_e32 v33, 0xbf1d265f, v31
	v_exp_f32_e32 v32, v32
	v_exp_f32_e32 v33, v33
	v_pk_add_f32 v[2:3], v[2:3], 1.0 op_sel_hi:[1,0]
	v_pk_fma_f32 v[28:29], v[154:155], s[30:31], v[22:23] op_sel_hi:[1,0,1]
	v_rcp_f32_e32 v2, v2
	v_rcp_f32_e32 v3, v3
	v_med3_f32 v28, v28, s64, v186
	v_med3_f32 v29, v29, s64, v186
	v_pk_add_f32 v[32:33], v[32:33], 1.0 op_sel_hi:[1,0]
	v_pk_mul_f32 v[4:5], v[4:5], v[28:29]
	v_rcp_f32_e32 v32, v32
	v_rcp_f32_e32 v33, v33
	v_pk_mul_f32 v[4:5], v[4:5], v[2:3]
	v_mov_b32_e32 v2, v163
	v_pk_fma_f32 v[26:27], v[156:157], s[30:31], v[20:21] op_sel_hi:[1,0,1]
	v_cvt_pk_fp8_f32 v2, v4, v5
	v_med3_f32 v26, v26, s64, v186
	v_med3_f32 v27, v27, s64, v186
	v_pk_mul_f32 v[4:5], v[30:31], v[26:27]
	v_pk_mul_f32 v[10:11], v[10:11], 4.0 op_sel_hi:[1,0]
	v_pk_mul_f32 v[4:5], v[4:5], v[32:33]
	v_pk_fma_f32 v[26:27], v[150:151], s[28:29], v[10:11] op_sel_hi:[1,0,1]
	v_cvt_pk_fp8_f32 v2, v4, v5 op_sel:[0,0,1]
	v_pk_fma_f32 v[4:5], v[152:153], s[28:29], v[8:9] op_sel_hi:[1,0,1]
	v_min_f32_e32 v26, 0x41e00000, v26
	v_min_f32_e32 v4, 0x41e00000, v4
	v_min_f32_e32 v27, 0x41e00000, v27
	v_min_f32_e32 v5, 0x41e00000, v5
	v_mul_f32_e32 v3, 0xbf1d265f, v26
	v_mul_f32_e32 v33, 0xbf1d265f, v4
	v_pk_fma_f32 v[30:31], v[146:147], s[30:31], v[14:15] op_sel_hi:[1,0,1]
	v_exp_f32_e32 v32, v3
	v_mul_f32_e32 v3, 0xbf1d265f, v27
	v_exp_f32_e32 v146, v33
	v_mul_f32_e32 v33, 0xbf1d265f, v5
	v_exp_f32_e32 v147, v33
	v_exp_f32_e32 v33, v3
	v_med3_f32 v30, v30, s64, v186
	v_med3_f32 v31, v31, s64, v186
	v_pk_add_f32 v[146:147], v[146:147], 1.0 op_sel_hi:[1,0]
	v_pk_add_f32 v[32:33], v[32:33], 1.0 op_sel_hi:[1,0]
	v_pk_mul_f32 v[26:27], v[26:27], v[30:31]
	v_rcp_f32_e32 v32, v32
	v_rcp_f32_e32 v33, v33
	v_rcp_f32_e32 v146, v146
	v_rcp_f32_e32 v147, v147
	v_mov_b32_e32 v3, v163
	v_pk_mul_f32 v[26:27], v[26:27], v[32:33]
	v_pk_fma_f32 v[28:29], v[148:149], s[30:31], v[12:13] op_sel_hi:[1,0,1]
	v_cvt_pk_fp8_f32 v3, v26, v27
	v_med3_f32 v28, v28, s64, v186
	v_med3_f32 v29, v29, s64, v186
	v_pk_mul_f32 v[4:5], v[4:5], v[28:29]
	v_pk_fma_f32 v[26:27], v[142:143], s[28:29], v[18:19] op_sel_hi:[1,0,1]
	v_pk_mul_f32 v[4:5], v[4:5], v[146:147]
	v_min_f32_e32 v26, 0x41e00000, v26
	v_cvt_pk_fp8_f32 v3, v4, v5 op_sel:[0,0,1]
	v_pk_fma_f32 v[4:5], v[144:145], s[28:29], v[16:17] op_sel_hi:[1,0,1]
	v_min_f32_e32 v27, 0x41e00000, v27
	v_min_f32_e32 v32, 0x41e00000, v4
	v_min_f32_e32 v33, 0x41e00000, v5
	v_mul_f32_e32 v4, 0xbf1d265f, v26
	v_mul_f32_e32 v5, 0xbf1d265f, v27
	v_exp_f32_e32 v4, v4
	v_exp_f32_e32 v5, v5
	v_pk_fma_f32 v[30:31], v[138:139], s[30:31], v[22:23] op_sel_hi:[1,0,1]
	v_mul_f32_e32 v138, 0xbf1d265f, v32
	v_mul_f32_e32 v139, 0xbf1d265f, v33
	v_exp_f32_e32 v138, v138
	v_exp_f32_e32 v139, v139
	v_pk_add_f32 v[4:5], v[4:5], 1.0 op_sel_hi:[1,0]
	v_med3_f32 v30, v30, s64, v186
	v_rcp_f32_e32 v4, v4
	v_rcp_f32_e32 v5, v5
	v_med3_f32 v31, v31, s64, v186
	v_pk_add_f32 v[138:139], v[138:139], 1.0 op_sel_hi:[1,0]
	v_pk_mul_f32 v[26:27], v[26:27], v[30:31]
	v_rcp_f32_e32 v138, v138
	v_rcp_f32_e32 v139, v139
	v_pk_mul_f32 v[26:27], v[26:27], v[4:5]
	v_mov_b32_e32 v4, v163
	v_pk_fma_f32 v[28:29], v[140:141], s[30:31], v[20:21] op_sel_hi:[1,0,1]
	v_cvt_pk_fp8_f32 v4, v26, v27
	v_med3_f32 v28, v28, s64, v186
	v_med3_f32 v29, v29, s64, v186
	v_pk_mul_f32 v[26:27], v[32:33], v[28:29]
	v_pk_fma_f32 v[28:29], v[134:135], s[28:29], v[10:11] op_sel_hi:[1,0,1]
	v_pk_mul_f32 v[26:27], v[26:27], v[138:139]
	v_min_f32_e32 v28, 0x41e00000, v28
	v_cvt_pk_fp8_f32 v4, v26, v27 op_sel:[0,0,1]
	v_pk_fma_f32 v[26:27], v[136:137], s[28:29], v[8:9] op_sel_hi:[1,0,1]
	v_pk_fma_f32 v[32:33], v[130:131], s[30:31], v[14:15] op_sel_hi:[1,0,1]
	v_min_f32_e32 v26, 0x41e00000, v26
	v_min_f32_e32 v29, 0x41e00000, v29
	v_min_f32_e32 v27, 0x41e00000, v27
	v_mul_f32_e32 v5, 0xbf1d265f, v28
	v_mul_f32_e32 v131, 0xbf1d265f, v26
	v_pk_fma_f32 v[30:31], v[132:133], s[30:31], v[12:13] op_sel_hi:[1,0,1]
	v_exp_f32_e32 v130, v5
	v_mul_f32_e32 v5, 0xbf1d265f, v29
	v_exp_f32_e32 v132, v131
	v_mul_f32_e32 v131, 0xbf1d265f, v27
	v_exp_f32_e32 v133, v131
	v_exp_f32_e32 v131, v5
	v_med3_f32 v32, v32, s64, v186
	v_med3_f32 v33, v33, s64, v186
	v_pk_add_f32 v[132:133], v[132:133], 1.0 op_sel_hi:[1,0]
	v_pk_add_f32 v[130:131], v[130:131], 1.0 op_sel_hi:[1,0]
	v_pk_mul_f32 v[28:29], v[28:29], v[32:33]
	v_rcp_f32_e32 v130, v130
	v_rcp_f32_e32 v131, v131
	v_rcp_f32_e32 v132, v132
	v_rcp_f32_e32 v133, v133
	v_mov_b32_e32 v5, v163
	v_pk_mul_f32 v[28:29], v[28:29], v[130:131]
	v_med3_f32 v30, v30, s64, v186
	v_cvt_pk_fp8_f32 v5, v28, v29
	v_pk_fma_f32 v[28:29], v[126:127], s[28:29], v[18:19] op_sel_hi:[1,0,1]
	v_med3_f32 v31, v31, s64, v186
	v_min_f32_e32 v28, 0x41e00000, v28
	v_min_f32_e32 v29, 0x41e00000, v29
	v_pk_mul_f32 v[26:27], v[26:27], v[30:31]
	v_pk_fma_f32 v[32:33], v[122:123], s[30:31], v[22:23] op_sel_hi:[1,0,1]
	v_mul_f32_e32 v122, 0xbf1d265f, v28
	v_mul_f32_e32 v123, 0xbf1d265f, v29
	v_pk_mul_f32 v[26:27], v[26:27], v[132:133]
	v_exp_f32_e32 v122, v122
	v_exp_f32_e32 v123, v123
	v_cvt_pk_fp8_f32 v5, v26, v27 op_sel:[0,0,1]
	v_pk_fma_f32 v[26:27], v[128:129], s[28:29], v[16:17] op_sel_hi:[1,0,1]
	v_pk_fma_f32 v[30:31], v[124:125], s[30:31], v[20:21] op_sel_hi:[1,0,1]
	v_min_f32_e32 v26, 0x41e00000, v26
	v_min_f32_e32 v27, 0x41e00000, v27
	v_mul_f32_e32 v124, 0xbf1d265f, v26
	v_mul_f32_e32 v125, 0xbf1d265f, v27
	v_exp_f32_e32 v124, v124
	v_exp_f32_e32 v125, v125
	v_pk_add_f32 v[122:123], v[122:123], 1.0 op_sel_hi:[1,0]
	v_med3_f32 v32, v32, s64, v186
	v_rcp_f32_e32 v122, v122
	v_rcp_f32_e32 v123, v123
	v_med3_f32 v33, v33, s64, v186
	v_pk_add_f32 v[124:125], v[124:125], 1.0 op_sel_hi:[1,0]
	v_pk_mul_f32 v[28:29], v[28:29], v[32:33]
	v_rcp_f32_e32 v124, v124
	v_rcp_f32_e32 v125, v125
	v_pk_mul_f32 v[32:33], v[28:29], v[122:123]
	v_mov_b32_e32 v28, v163
	v_cvt_pk_fp8_f32 v28, v32, v33
	v_med3_f32 v30, v30, s64, v186
	v_med3_f32 v31, v31, s64, v186
	v_pk_mul_f32 v[26:27], v[26:27], v[30:31]
	v_pk_fma_f32 v[30:31], v[118:119], s[28:29], v[10:11] op_sel_hi:[1,0,1]
	v_pk_mul_f32 v[26:27], v[26:27], v[124:125]
	v_min_f32_e32 v30, 0x41e00000, v30
	v_cvt_pk_fp8_f32 v28, v26, v27 op_sel:[0,0,1]
	v_pk_fma_f32 v[26:27], v[120:121], s[28:29], v[8:9] op_sel_hi:[1,0,1]
	v_pk_fma_f32 v[32:33], v[116:117], s[30:31], v[12:13] op_sel_hi:[1,0,1]
	v_min_f32_e32 v26, 0x41e00000, v26
	v_min_f32_e32 v31, 0x41e00000, v31
	v_min_f32_e32 v27, 0x41e00000, v27
	v_mul_f32_e32 v29, 0xbf1d265f, v30
	v_mul_f32_e32 v117, 0xbf1d265f, v26
	v_exp_f32_e32 v116, v29
	v_mul_f32_e32 v29, 0xbf1d265f, v31
	v_exp_f32_e32 v118, v117
	v_mul_f32_e32 v117, 0xbf1d265f, v27
	v_exp_f32_e32 v119, v117
	v_exp_f32_e32 v117, v29
	v_pk_fma_f32 v[114:115], v[114:115], s[30:31], v[14:15] op_sel_hi:[1,0,1]
	v_mov_b32_e32 v29, v163
	v_med3_f32 v114, v114, s64, v186
	v_pk_add_f32 v[116:117], v[116:117], 1.0 op_sel_hi:[1,0]
	v_med3_f32 v115, v115, s64, v186
	v_rcp_f32_e32 v116, v116
	v_rcp_f32_e32 v117, v117
	v_pk_add_f32 v[118:119], v[118:119], 1.0 op_sel_hi:[1,0]
	v_pk_mul_f32 v[30:31], v[30:31], v[114:115]
	v_rcp_f32_e32 v118, v118
	v_rcp_f32_e32 v119, v119
	v_pk_mul_f32 v[30:31], v[30:31], v[116:117]
	v_med3_f32 v32, v32, s64, v186
	v_cvt_pk_fp8_f32 v29, v30, v31
	v_pk_fma_f32 v[30:31], v[110:111], s[28:29], v[18:19] op_sel_hi:[1,0,1]
	v_med3_f32 v33, v33, s64, v186
	v_min_f32_e32 v30, 0x41e00000, v30
	v_min_f32_e32 v31, 0x41e00000, v31
	v_pk_mul_f32 v[26:27], v[26:27], v[32:33]
	v_pk_fma_f32 v[32:33], v[108:109], s[30:31], v[20:21] op_sel_hi:[1,0,1]
	v_mul_f32_e32 v108, 0xbf1d265f, v30
	v_mul_f32_e32 v109, 0xbf1d265f, v31
	v_pk_mul_f32 v[26:27], v[26:27], v[118:119]
	v_exp_f32_e32 v108, v108
	v_exp_f32_e32 v109, v109
	v_cvt_pk_fp8_f32 v29, v26, v27 op_sel:[0,0,1]
	v_pk_fma_f32 v[26:27], v[112:113], s[28:29], v[16:17] op_sel_hi:[1,0,1]
	v_pk_fma_f32 v[106:107], v[106:107], s[30:31], v[22:23] op_sel_hi:[1,0,1]
	v_min_f32_e32 v26, 0x41e00000, v26
	v_min_f32_e32 v27, 0x41e00000, v27
	v_mul_f32_e32 v110, 0xbf1d265f, v26
	v_mul_f32_e32 v111, 0xbf1d265f, v27
	v_exp_f32_e32 v110, v110
	v_exp_f32_e32 v111, v111
	v_pk_add_f32 v[108:109], v[108:109], 1.0 op_sel_hi:[1,0]
	v_med3_f32 v106, v106, s64, v186
	v_rcp_f32_e32 v108, v108
	v_rcp_f32_e32 v109, v109
	v_med3_f32 v107, v107, s64, v186
	v_pk_add_f32 v[110:111], v[110:111], 1.0 op_sel_hi:[1,0]
	v_pk_mul_f32 v[30:31], v[30:31], v[106:107]
	v_rcp_f32_e32 v110, v110
	v_rcp_f32_e32 v111, v111
	v_pk_mul_f32 v[106:107], v[30:31], v[108:109]
	v_mov_b32_e32 v30, v163
	v_cvt_pk_fp8_f32 v30, v106, v107
	v_med3_f32 v32, v32, s64, v186
	v_med3_f32 v33, v33, s64, v186
	v_pk_mul_f32 v[26:27], v[26:27], v[32:33]
	v_pk_fma_f32 v[32:33], v[102:103], s[28:29], v[10:11] op_sel_hi:[1,0,1]
	v_pk_mul_f32 v[26:27], v[26:27], v[110:111]
	v_min_f32_e32 v32, 0x41e00000, v32
	v_cvt_pk_fp8_f32 v30, v26, v27 op_sel:[0,0,1]
	v_pk_fma_f32 v[26:27], v[104:105], s[28:29], v[8:9] op_sel_hi:[1,0,1]
	v_min_f32_e32 v33, 0x41e00000, v33
	v_min_f32_e32 v26, 0x41e00000, v26
	v_min_f32_e32 v27, 0x41e00000, v27
	v_mul_f32_e32 v31, 0xbf1d265f, v32
	v_mul_f32_e32 v103, 0xbf1d265f, v26
	v_exp_f32_e32 v102, v31
	v_mul_f32_e32 v31, 0xbf1d265f, v33
	v_exp_f32_e32 v104, v103
	v_mul_f32_e32 v103, 0xbf1d265f, v27
	v_exp_f32_e32 v105, v103
	v_exp_f32_e32 v103, v31
	v_pk_fma_f32 v[98:99], v[98:99], s[30:31], v[14:15] op_sel_hi:[1,0,1]
	v_mov_b32_e32 v31, v163
	v_med3_f32 v98, v98, s64, v186
	v_pk_add_f32 v[102:103], v[102:103], 1.0 op_sel_hi:[1,0]
	v_med3_f32 v99, v99, s64, v186
	v_rcp_f32_e32 v102, v102
	v_rcp_f32_e32 v103, v103
	v_pk_add_f32 v[104:105], v[104:105], 1.0 op_sel_hi:[1,0]
	v_pk_mul_f32 v[32:33], v[32:33], v[98:99]
	v_rcp_f32_e32 v104, v104
	v_rcp_f32_e32 v105, v105
	v_pk_mul_f32 v[32:33], v[32:33], v[102:103]
	v_pk_fma_f32 v[100:101], v[100:101], s[30:31], v[12:13] op_sel_hi:[1,0,1]
	v_cvt_pk_fp8_f32 v31, v32, v33
	v_med3_f32 v100, v100, s64, v186
	v_med3_f32 v101, v101, s64, v186
	v_pk_mul_f32 v[26:27], v[26:27], v[100:101]
	v_and_b32_e32 v25, 16, v25
	v_pk_mul_f32 v[26:27], v[26:27], v[104:105]
	s_sub_i32 s38, s38, s35
	v_cvt_pk_fp8_f32 v31, v26, v27 op_sel:[0,0,1]
	v_or_b32_e32 v26, v24, v25
	v_ashrrev_i32_e32 v27, 31, v26
	v_lshlrev_b64 v[26:27], 10, v[26:27]
	s_ashr_i32 s39, s38, 31
	v_lshl_add_u64 v[26:27], s[12:13], 0, v[26:27]
	v_lshl_add_u64 v[26:27], v[26:27], 0, s[38:39]
	v_mov_b32_e32 v7, v163
	v_lshl_add_u64 v[26:27], v[26:27], 0, v[162:163]
	v_permlane16_swap_b32_e32 v2, v4
	v_permlane16_swap_b32_e32 v3, v5
	v_lshl_add_u64 v[26:27], v[26:27], 0, v[6:7]
	global_store_dwordx4 v[26:27], v[2:5], off
	v_or_b32_e32 v26, 32, v25
	v_permlane16_swap_b32_e32 v28, v30
	v_or_b32_e32 v2, v24, v26
	v_ashrrev_i32_e32 v3, 31, v2
	v_lshlrev_b64 v[2:3], 10, v[2:3]
	v_lshl_add_u64 v[2:3], s[12:13], 0, v[2:3]
	v_lshl_add_u64 v[2:3], v[2:3], 0, s[38:39]
	v_lshl_add_u64 v[2:3], v[2:3], 0, v[162:163]
	v_permlane16_swap_b32_e32 v29, v31
	v_lshl_add_u64 v[2:3], v[2:3], 0, v[6:7]
	v_pk_fma_f32 v[4:5], v[94:95], s[28:29], v[18:19] op_sel_hi:[1,0,1]
	global_store_dwordx4 v[2:3], v[28:31], off
	v_pk_fma_f32 v[2:3], v[96:97], s[28:29], v[16:17] op_sel_hi:[1,0,1]
	v_min_f32_e32 v4, 0x41e00000, v4
	v_min_f32_e32 v5, 0x41e00000, v5
	v_min_f32_e32 v32, 0x41e00000, v2
	v_min_f32_e32 v33, 0x41e00000, v3
	v_mul_f32_e32 v2, 0xbf1d265f, v4
	v_mul_f32_e32 v3, 0xbf1d265f, v5
	v_exp_f32_e32 v2, v2
	v_exp_f32_e32 v3, v3
	v_mul_f32_e32 v27, 0xbf1d265f, v32
	v_pk_fma_f32 v[30:31], v[90:91], s[30:31], v[22:23] op_sel_hi:[1,0,1]
	v_exp_f32_e32 v90, v27
	v_mul_f32_e32 v27, 0xbf1d265f, v33
	v_exp_f32_e32 v91, v27
	v_pk_add_f32 v[2:3], v[2:3], 1.0 op_sel_hi:[1,0]
	v_med3_f32 v30, v30, s64, v186
	v_rcp_f32_e32 v2, v2
	v_rcp_f32_e32 v3, v3
	v_med3_f32 v31, v31, s64, v186
	v_pk_fma_f32 v[28:29], v[92:93], s[30:31], v[20:21] op_sel_hi:[1,0,1]
	v_pk_add_f32 v[90:91], v[90:91], 1.0 op_sel_hi:[1,0]
	v_pk_mul_f32 v[4:5], v[4:5], v[30:31]
	v_med3_f32 v28, v28, s64, v186
	v_rcp_f32_e32 v90, v90
	v_rcp_f32_e32 v91, v91
	v_pk_mul_f32 v[4:5], v[4:5], v[2:3]
	v_mov_b32_e32 v2, v163
	v_med3_f32 v29, v29, s64, v186
	v_cvt_pk_fp8_f32 v2, v4, v5
	v_pk_mul_f32 v[4:5], v[32:33], v[28:29]
	v_pk_fma_f32 v[28:29], v[86:87], s[28:29], v[10:11] op_sel_hi:[1,0,1]
	v_pk_mul_f32 v[4:5], v[4:5], v[90:91]
	v_min_f32_e32 v28, 0x41e00000, v28
	v_min_f32_e32 v29, 0x41e00000, v29
	v_mul_f32_e32 v3, 0xbf1d265f, v28
	v_pk_fma_f32 v[32:33], v[82:83], s[30:31], v[14:15] op_sel_hi:[1,0,1]
	v_exp_f32_e32 v82, v3
	v_mul_f32_e32 v3, 0xbf1d265f, v29
	v_cvt_pk_fp8_f32 v2, v4, v5 op_sel:[0,0,1]
	v_pk_fma_f32 v[4:5], v[88:89], s[28:29], v[8:9] op_sel_hi:[1,0,1]
	v_exp_f32_e32 v83, v3
	v_min_f32_e32 v4, 0x41e00000, v4
	v_min_f32_e32 v5, 0x41e00000, v5
	v_mul_f32_e32 v27, 0xbf1d265f, v4
	v_pk_fma_f32 v[30:31], v[84:85], s[30:31], v[12:13] op_sel_hi:[1,0,1]
	v_exp_f32_e32 v84, v27
	v_mul_f32_e32 v27, 0xbf1d265f, v5
	v_exp_f32_e32 v85, v27
	v_pk_add_f32 v[82:83], v[82:83], 1.0 op_sel_hi:[1,0]
	v_med3_f32 v32, v32, s64, v186
	v_rcp_f32_e32 v82, v82
	v_rcp_f32_e32 v83, v83
	v_med3_f32 v33, v33, s64, v186
	v_pk_add_f32 v[84:85], v[84:85], 1.0 op_sel_hi:[1,0]
	v_pk_mul_f32 v[28:29], v[28:29], v[32:33]
	v_rcp_f32_e32 v84, v84
	v_rcp_f32_e32 v85, v85
	v_pk_mul_f32 v[28:29], v[28:29], v[82:83]
	v_mov_b32_e32 v3, v163
	v_cvt_pk_fp8_f32 v3, v28, v29
	v_med3_f32 v30, v30, s64, v186
	v_med3_f32 v31, v31, s64, v186
	v_pk_mul_f32 v[4:5], v[4:5], v[30:31]
	v_pk_fma_f32 v[28:29], v[78:79], s[28:29], v[18:19] op_sel_hi:[1,0,1]
	v_pk_mul_f32 v[4:5], v[4:5], v[84:85]
	v_min_f32_e32 v28, 0x41e00000, v28
	v_cvt_pk_fp8_f32 v3, v4, v5 op_sel:[0,0,1]
	v_pk_fma_f32 v[4:5], v[80:81], s[28:29], v[16:17] op_sel_hi:[1,0,1]
	v_min_f32_e32 v29, 0x41e00000, v29
	v_pk_fma_f32 v[32:33], v[74:75], s[30:31], v[22:23] op_sel_hi:[1,0,1]
	v_min_f32_e32 v74, 0x41e00000, v4
	v_min_f32_e32 v75, 0x41e00000, v5
	v_mul_f32_e32 v4, 0xbf1d265f, v28
	v_mul_f32_e32 v5, 0xbf1d265f, v29
	v_exp_f32_e32 v4, v4
	v_exp_f32_e32 v5, v5
	v_mul_f32_e32 v27, 0xbf1d265f, v74
	v_pk_fma_f32 v[30:31], v[76:77], s[30:31], v[20:21] op_sel_hi:[1,0,1]
	v_exp_f32_e32 v76, v27
	v_mul_f32_e32 v27, 0xbf1d265f, v75
	v_exp_f32_e32 v77, v27
	v_pk_add_f32 v[4:5], v[4:5], 1.0 op_sel_hi:[1,0]
	v_med3_f32 v32, v32, s64, v186
	v_rcp_f32_e32 v4, v4
	v_rcp_f32_e32 v5, v5
	v_med3_f32 v33, v33, s64, v186
	v_pk_add_f32 v[76:77], v[76:77], 1.0 op_sel_hi:[1,0]
	v_pk_mul_f32 v[28:29], v[28:29], v[32:33]
	v_med3_f32 v30, v30, s64, v186
	v_rcp_f32_e32 v76, v76
	v_rcp_f32_e32 v77, v77
	v_pk_mul_f32 v[28:29], v[28:29], v[4:5]
	v_mov_b32_e32 v4, v163
	v_med3_f32 v31, v31, s64, v186
	v_cvt_pk_fp8_f32 v4, v28, v29
	v_pk_mul_f32 v[28:29], v[74:75], v[30:31]
	v_pk_fma_f32 v[30:31], v[70:71], s[28:29], v[10:11] op_sel_hi:[1,0,1]
	v_pk_mul_f32 v[28:29], v[28:29], v[76:77]
	v_min_f32_e32 v30, 0x41e00000, v30
	v_min_f32_e32 v31, 0x41e00000, v31
	v_mul_f32_e32 v5, 0xbf1d265f, v30
	v_pk_fma_f32 v[32:33], v[68:69], s[30:31], v[12:13] op_sel_hi:[1,0,1]
	v_exp_f32_e32 v68, v5
	v_mul_f32_e32 v5, 0xbf1d265f, v31
	v_cvt_pk_fp8_f32 v4, v28, v29 op_sel:[0,0,1]
	v_pk_fma_f32 v[28:29], v[72:73], s[28:29], v[8:9] op_sel_hi:[1,0,1]
	v_exp_f32_e32 v69, v5
	v_min_f32_e32 v28, 0x41e00000, v28
	v_min_f32_e32 v29, 0x41e00000, v29
	v_mul_f32_e32 v27, 0xbf1d265f, v28
	v_exp_f32_e32 v70, v27
	v_mul_f32_e32 v27, 0xbf1d265f, v29
	v_exp_f32_e32 v71, v27
	v_pk_add_f32 v[68:69], v[68:69], 1.0 op_sel_hi:[1,0]
	v_pk_fma_f32 v[66:67], v[66:67], s[30:31], v[14:15] op_sel_hi:[1,0,1]
	v_rcp_f32_e32 v68, v68
	v_rcp_f32_e32 v69, v69
	v_med3_f32 v66, v66, s64, v186
	v_med3_f32 v67, v67, s64, v186
	v_pk_add_f32 v[70:71], v[70:71], 1.0 op_sel_hi:[1,0]
	v_pk_mul_f32 v[30:31], v[30:31], v[66:67]
	v_rcp_f32_e32 v70, v70
	v_rcp_f32_e32 v71, v71
	v_pk_mul_f32 v[30:31], v[30:31], v[68:69]
	v_mov_b32_e32 v5, v163
	v_cvt_pk_fp8_f32 v5, v30, v31
	v_med3_f32 v32, v32, s64, v186
	v_med3_f32 v33, v33, s64, v186
	v_pk_mul_f32 v[28:29], v[28:29], v[32:33]
	v_pk_fma_f32 v[30:31], v[62:63], s[28:29], v[18:19] op_sel_hi:[1,0,1]
	v_pk_mul_f32 v[28:29], v[28:29], v[70:71]
	v_pk_fma_f32 v[32:33], v[60:61], s[30:31], v[20:21] op_sel_hi:[1,0,1]
	v_cvt_pk_fp8_f32 v5, v28, v29 op_sel:[0,0,1]
	v_pk_fma_f32 v[28:29], v[64:65], s[28:29], v[16:17] op_sel_hi:[1,0,1]
	v_min_f32_e32 v30, 0x41e00000, v30
	v_min_f32_e32 v60, 0x41e00000, v28
	v_min_f32_e32 v31, 0x41e00000, v31
	v_min_f32_e32 v61, 0x41e00000, v29
	v_mul_f32_e32 v27, 0xbf1d265f, v30
	v_mul_f32_e32 v29, 0xbf1d265f, v60
	v_exp_f32_e32 v28, v27
	v_mul_f32_e32 v27, 0xbf1d265f, v31
	v_exp_f32_e32 v62, v29
	v_mul_f32_e32 v29, 0xbf1d265f, v61
	v_exp_f32_e32 v63, v29
	v_exp_f32_e32 v29, v27
	v_pk_fma_f32 v[58:59], v[58:59], s[30:31], v[22:23] op_sel_hi:[1,0,1]
	v_med3_f32 v32, v32, s64, v186
	v_med3_f32 v58, v58, s64, v186
	v_pk_add_f32 v[28:29], v[28:29], 1.0 op_sel_hi:[1,0]
	v_med3_f32 v59, v59, s64, v186
	v_rcp_f32_e32 v28, v28
	v_rcp_f32_e32 v29, v29
	v_pk_add_f32 v[62:63], v[62:63], 1.0 op_sel_hi:[1,0]
	v_pk_mul_f32 v[30:31], v[30:31], v[58:59]
	v_rcp_f32_e32 v62, v62
	v_rcp_f32_e32 v63, v63
	v_pk_mul_f32 v[30:31], v[30:31], v[28:29]
	v_mov_b32_e32 v28, v163
	v_med3_f32 v33, v33, s64, v186
	v_cvt_pk_fp8_f32 v28, v30, v31
	v_pk_mul_f32 v[30:31], v[60:61], v[32:33]
	v_pk_fma_f32 v[32:33], v[54:55], s[28:29], v[10:11] op_sel_hi:[1,0,1]
	v_pk_mul_f32 v[30:31], v[30:31], v[62:63]
	v_min_f32_e32 v32, 0x41e00000, v32
	v_min_f32_e32 v33, 0x41e00000, v33
	v_mul_f32_e32 v27, 0xbf1d265f, v32
	v_exp_f32_e32 v54, v27
	v_mul_f32_e32 v27, 0xbf1d265f, v33
	v_cvt_pk_fp8_f32 v28, v30, v31 op_sel:[0,0,1]
	v_pk_fma_f32 v[30:31], v[56:57], s[28:29], v[8:9] op_sel_hi:[1,0,1]
	v_exp_f32_e32 v55, v27
	v_min_f32_e32 v30, 0x41e00000, v30
	v_min_f32_e32 v31, 0x41e00000, v31
	v_mul_f32_e32 v29, 0xbf1d265f, v30
	v_exp_f32_e32 v56, v29
	v_mul_f32_e32 v29, 0xbf1d265f, v31
	v_exp_f32_e32 v57, v29
	v_pk_add_f32 v[54:55], v[54:55], 1.0 op_sel_hi:[1,0]
	v_pk_fma_f32 v[50:51], v[50:51], s[30:31], v[14:15] op_sel_hi:[1,0,1]
	v_rcp_f32_e32 v54, v54
	v_rcp_f32_e32 v55, v55
	v_med3_f32 v50, v50, s64, v186
	v_med3_f32 v51, v51, s64, v186
	v_pk_add_f32 v[56:57], v[56:57], 1.0 op_sel_hi:[1,0]
	v_pk_mul_f32 v[32:33], v[32:33], v[50:51]
	v_rcp_f32_e32 v56, v56
	v_rcp_f32_e32 v57, v57
	v_pk_mul_f32 v[32:33], v[32:33], v[54:55]
	v_mov_b32_e32 v29, v163
	v_pk_fma_f32 v[52:53], v[52:53], s[30:31], v[12:13] op_sel_hi:[1,0,1]
	v_cvt_pk_fp8_f32 v29, v32, v33
	v_med3_f32 v52, v52, s64, v186
	v_med3_f32 v53, v53, s64, v186
	v_pk_mul_f32 v[30:31], v[30:31], v[52:53]
	v_pk_fma_f32 v[16:17], v[48:49], s[28:29], v[16:17] op_sel_hi:[1,0,1]
	v_pk_fma_f32 v[18:19], v[46:47], s[28:29], v[18:19] op_sel_hi:[1,0,1]
	v_pk_mul_f32 v[30:31], v[30:31], v[56:57]
	v_min_f32_e32 v18, 0x41e00000, v18
	v_min_f32_e32 v16, 0x41e00000, v16
	v_cvt_pk_fp8_f32 v29, v30, v31 op_sel:[0,0,1]
	v_min_f32_e32 v19, 0x41e00000, v19
	v_min_f32_e32 v17, 0x41e00000, v17
	v_mul_f32_e32 v27, 0xbf1d265f, v18
	v_mul_f32_e32 v31, 0xbf1d265f, v16
	v_exp_f32_e32 v30, v27
	v_mul_f32_e32 v27, 0xbf1d265f, v19
	v_exp_f32_e32 v32, v31
	v_mul_f32_e32 v31, 0xbf1d265f, v17
	v_exp_f32_e32 v33, v31
	v_exp_f32_e32 v31, v27
	v_pk_fma_f32 v[22:23], v[42:43], s[30:31], v[22:23] op_sel_hi:[1,0,1]
	v_pk_fma_f32 v[20:21], v[44:45], s[30:31], v[20:21] op_sel_hi:[1,0,1]
	v_med3_f32 v22, v22, s64, v186
	v_pk_add_f32 v[30:31], v[30:31], 1.0 op_sel_hi:[1,0]
	v_med3_f32 v23, v23, s64, v186
	v_rcp_f32_e32 v30, v30
	v_rcp_f32_e32 v31, v31
	v_pk_add_f32 v[32:33], v[32:33], 1.0 op_sel_hi:[1,0]
	v_pk_mul_f32 v[18:19], v[18:19], v[22:23]
	v_rcp_f32_e32 v32, v32
	v_rcp_f32_e32 v33, v33
	v_pk_mul_f32 v[18:19], v[18:19], v[30:31]
	v_mov_b32_e32 v30, v163
	v_cvt_pk_fp8_f32 v30, v18, v19
	v_med3_f32 v20, v20, s64, v186
	v_med3_f32 v21, v21, s64, v186
	v_pk_mul_f32 v[16:17], v[16:17], v[20:21]
	v_pk_fma_f32 v[10:11], v[38:39], s[28:29], v[10:11] op_sel_hi:[1,0,1]
	v_pk_mul_f32 v[16:17], v[16:17], v[32:33]
	v_min_f32_e32 v10, 0x41e00000, v10
	v_min_f32_e32 v11, 0x41e00000, v11
	v_cvt_pk_fp8_f32 v30, v16, v17 op_sel:[0,0,1]
	v_mul_f32_e32 v16, 0xbf1d265f, v10
	v_mul_f32_e32 v17, 0xbf1d265f, v11
	v_exp_f32_e32 v16, v16
	v_exp_f32_e32 v17, v17
	v_pk_fma_f32 v[8:9], v[40:41], s[28:29], v[8:9] op_sel_hi:[1,0,1]
	v_pk_fma_f32 v[14:15], v[34:35], s[30:31], v[14:15] op_sel_hi:[1,0,1]
	v_min_f32_e32 v8, 0x41e00000, v8
	v_min_f32_e32 v9, 0x41e00000, v9
	v_mul_f32_e32 v18, 0xbf1d265f, v8
	v_mul_f32_e32 v19, 0xbf1d265f, v9
	v_exp_f32_e32 v18, v18
	v_exp_f32_e32 v19, v19
	v_pk_add_f32 v[16:17], v[16:17], 1.0 op_sel_hi:[1,0]
	v_med3_f32 v14, v14, s64, v186
	v_rcp_f32_e32 v16, v16
	v_rcp_f32_e32 v17, v17
	v_med3_f32 v15, v15, s64, v186
	v_pk_add_f32 v[18:19], v[18:19], 1.0 op_sel_hi:[1,0]
	v_pk_mul_f32 v[10:11], v[10:11], v[14:15]
	v_rcp_f32_e32 v18, v18
	v_rcp_f32_e32 v19, v19
	v_pk_mul_f32 v[10:11], v[10:11], v[16:17]
	v_mov_b32_e32 v31, v163
	v_pk_fma_f32 v[12:13], v[36:37], s[30:31], v[12:13] op_sel_hi:[1,0,1]
	v_cvt_pk_fp8_f32 v31, v10, v11
	v_med3_f32 v12, v12, s64, v186
	v_med3_f32 v13, v13, s64, v186
	v_pk_mul_f32 v[8:9], v[8:9], v[12:13]
	v_add_u32_e32 v10, 0x80, v24
	v_pk_mul_f32 v[8:9], v[8:9], v[18:19]
	v_permlane16_swap_b32_e32 v2, v4
	v_cvt_pk_fp8_f32 v31, v8, v9 op_sel:[0,0,1]
	v_or_b32_e32 v8, v10, v25
	v_ashrrev_i32_e32 v9, 31, v8
	v_lshlrev_b64 v[8:9], 10, v[8:9]
	v_lshl_add_u64 v[8:9], s[12:13], 0, v[8:9]
	v_lshl_add_u64 v[8:9], v[8:9], 0, s[38:39]
	v_lshl_add_u64 v[8:9], v[8:9], 0, v[162:163]
	v_permlane16_swap_b32_e32 v3, v5
	v_lshl_add_u64 v[8:9], v[8:9], 0, v[6:7]
	global_store_dwordx4 v[8:9], v[2:5], off
	v_permlane16_swap_b32_e32 v28, v30
	s_nop 0
	v_or_b32_e32 v2, v10, v26
	v_ashrrev_i32_e32 v3, 31, v2
	v_lshlrev_b64 v[2:3], 10, v[2:3]
	v_lshl_add_u64 v[2:3], s[12:13], 0, v[2:3]
	v_lshl_add_u64 v[2:3], v[2:3], 0, s[38:39]
	v_lshl_add_u64 v[2:3], v[2:3], 0, v[162:163]
	v_permlane16_swap_b32_e32 v29, v31
	v_lshl_add_u64 v[2:3], v[2:3], 0, v[6:7]
	s_and_b64 vcc, exec, s[4:5]
	s_mov_b64 s[4:5], -1
	global_store_dwordx4 v[2:3], v[28:31], off
	s_cbranch_vccnz .LBB0_557
	s_andn2_b64 vcc, exec, s[16:17]
	s_cbranch_vccnz .LBB0_569
	s_lshl_b32 s4, s66, 10
	s_and_b32 s4, s4, 0x400
	s_add_i32 s4, s4, 0
	s_ashr_i32 s37, s36, 31
	s_add_i32 s35, s4, 0x24cc0
	s_lshl_b64 s[4:5], s[36:37], 13
	s_add_u32 s37, s14, s4
	s_addc_u32 s38, s15, s5
	s_lshl_b32 s4, s36, 10
	s_lshl_b32 s5, s34, 7
	s_sub_i32 s4, s5, s4
	s_ashr_i32 s5, s4, 31
	s_lshl_b64 s[4:5], s[4:5], 2
	s_add_u32 s4, s37, s4
	s_addc_u32 s5, s38, s5
	s_mov_b32 m0, s35
	s_nop 0
	global_load_lds_dwordx4 v178, s[4:5] offset:0

.LBB0_639:
	s_or_b64 exec, exec, s[14:15]
	s_add_u32 s14, s10, 0x26400000
	s_addc_u32 s15, s11, 0
	s_add_i32 s3, 0, 0x20000
	v_mov_b32_e32 v2, v0
	v_mov_b32_e32 v1, s3
	s_waitcnt lgkmcnt(0)
	s_barrier
	s_barrier
	ds_read_b128 v[4:7], v1
	v_readfirstlane_b32 s4, v2
	s_ashr_i32 s5, s4, 6
	s_waitcnt lgkmcnt(0)
	v_readfirstlane_b32 s0, v4
	v_readfirstlane_b32 s37, v5
	v_readfirstlane_b32 s38, v6
	s_cmp_eq_u32 s0, 0
	v_readfirstlane_b32 s40, v7
	s_cbranch_scc1 .LBB0_661
	s_load_dwordx2 s[16:17], s[6:7], 0x90
	v_and_b32_e32 v1, 63, v2
	s_cmp_lt_u32 s4, 64
	v_mov_b32_e32 v3, v0
	s_cselect_b64 s[18:19], -1, 0
	s_cmp_gt_u32 s4, 63
	v_lshlrev_b32_e32 v1, 4, v1
	s_cbranch_scc1 .LBB0_642
	s_ashr_i32 s41, s40, 31
	s_lshl_b64 s[0:1], s[40:41], 12
	s_waitcnt lgkmcnt(0)
	s_add_u32 s20, s16, s0
	s_addc_u32 s21, s17, s1
	s_lshl_b32 s0, s40, 10
	s_lshl_b32 s1, s38, 8
	s_sub_i32 s0, s1, s0
	s_ashr_i32 s1, s0, 31
	s_lshl_b64 s[0:1], s[0:1], 2
	s_add_u32 s0, s20, s0
	s_addc_u32 s1, s21, s1
	s_add_i32 s20, 0, 0x24cc0
	s_mov_b32 m0, s20
	s_nop 0
	global_load_lds_dwordx4 v1, s[0:1] offset:0
.LBB0_642:
	v_lshlrev_b32_e32 v4, 4, v3
	s_movk_i32 s0, 0x70
	v_bitop3_b32 v4, v4, s0, v3 bitop3:0x48
	v_lshlrev_b32_e32 v3, 7, v3
	v_lshl_or_b32 v4, s37, 18, v4
	v_and_b32_e32 v3, 0xfffffc00, v3
	v_add_u32_e32 v162, v4, v3
	v_lshrrev_b32_e32 v3, 4, v2
	v_ashrrev_i32_e32 v5, 3, v2
	v_xor_b32_e32 v4, v3, v2
	v_lshlrev_b32_e32 v6, 1, v5
	v_lshrrev_b32_e32 v7, 2, v5
	v_lshlrev_b32_e32 v4, 4, v4
	v_and_b32_e32 v6, 24, v6
	v_and_b32_e32 v7, 4, v7
	v_and_b32_e32 v5, 0x3fffe3, v5
	v_and_b32_e32 v4, 0x70, v4
	v_or3_b32 v5, v5, v7, v6
	s_lshl_b32 s1, s5, 10
	s_ashr_i32 s22, s4, 8
	v_lshl_or_b32 v172, v5, 10, v4
	v_mov_b32_e32 v5, 0x2000
	s_add_i32 s1, s1, 0
	v_lshl_add_u32 v5, v2, 4, v5
	s_add_u32 s29, s10, 0x1c00000
	v_ashrrev_i32_e32 v5, 7, v5
	s_addc_u32 s31, s11, 0
	s_ashr_i32 s39, s38, 31
	v_lshlrev_b32_e32 v6, 1, v5
	v_lshrrev_b32_e32 v7, 2, v5
	s_lshl_b64 s[20:21], s[38:39], 18
	v_and_b32_e32 v6, 24, v6
	v_and_b32_e32 v7, 4, v7
	v_and_b32_e32 v5, 0x3fffe3, v5
	s_add_u32 s42, s29, s20
	v_or3_b32 v5, v5, v7, v6
	s_addc_u32 s43, s31, s21
	s_add_i32 s33, s1, 0x10000
	s_mov_b32 m0, s33
	s_nop 0
	global_load_lds_dwordx4 v172, s[42:43] offset:0
	v_lshl_or_b32 v173, v5, 10, v4
	s_add_i32 s39, s1, 0x12000
	s_mov_b32 m0, s39
	s_nop 0
	global_load_lds_dwordx4 v173, s[42:43] offset:0
	s_add_u32 s20, s42, 0x20000
	s_addc_u32 s21, s43, 0
	s_add_i32 s41, s1, 0x14000
	s_mov_b32 m0, s41
	s_nop 0
	global_load_lds_dwordx4 v172, s[20:21] offset:0
	s_add_i32 s48, s1, 0x16000
	s_mov_b32 m0, s48
	s_nop 0
	global_load_lds_dwordx4 v173, s[20:21] offset:0
	s_mov_b32 m0, s1
	s_nop 0
	global_load_lds_dwordx4 v162, s[12:13] offset:0
	v_add_u32_e32 v170, 0x10000, v162
	s_add_i32 s49, s1, 0x2000
	s_mov_b32 m0, s49
	s_nop 0
	global_load_lds_dwordx4 v170, s[12:13] offset:0
	v_add_u32_e32 v163, 0x20000, v162
	s_add_i32 s50, s1, 0x4000
	s_mov_b32 m0, s50
	s_nop 0
	global_load_lds_dwordx4 v163, s[12:13] offset:0
	v_add_u32_e32 v171, 0x30000, v162
	s_add_i32 s51, s1, 0x6000
	s_mov_b32 m0, s51
	s_nop 0
	global_load_lds_dwordx4 v171, s[12:13] offset:0
	s_cmp_eq_u32 s22, 1
	s_mov_b32 s63, 0
	s_cselect_b64 s[20:21], -1, 0
	s_cmp_lg_u32 s22, 1
	s_cbranch_scc1 .LBB0_644
	s_barrier
.LBB0_644:
	v_and_b32_e32 v4, 15, v2
	s_lshl_b32 s5, s5, 5
	v_lshlrev_b32_e32 v5, 7, v4
	s_and_b32 s5, s5, 0x60
	v_lshl_or_b32 v5, s22, 13, v5
	s_add_u32 s22, s42, 0x80
	v_or_b32_e32 v4, s5, v4
	s_waitcnt vmcnt(2)
	s_barrier
	s_addc_u32 s23, s43, 0
	s_add_i32 s52, s1, 0x18000
	s_mov_b32 m0, s52
	s_nop 0
	global_load_lds_dwordx4 v172, s[22:23] offset:0
	s_add_i32 s53, s1, 0x1a000
	s_mov_b32 m0, s53
	s_nop 0
	global_load_lds_dwordx4 v173, s[22:23] offset:0
	s_add_u32 s22, s12, 0x80
	s_addc_u32 s23, s13, 0
	s_add_i32 s54, s1, 0x8000
	s_mov_b32 m0, s54
	s_nop 0
	global_load_lds_dwordx4 v162, s[22:23] offset:0
	s_add_i32 s55, s1, 0xa000
	s_mov_b32 m0, s55
	s_nop 0
	global_load_lds_dwordx4 v170, s[22:23] offset:0
	s_add_u32 s24, s42, 0x20080
	s_addc_u32 s25, s43, 0
	s_add_i32 s56, s1, 0x1c000
	s_mov_b32 m0, s56
	s_nop 0
	global_load_lds_dwordx4 v172, s[24:25] offset:0
	s_add_i32 s57, s1, 0x1e000
	s_add_i32 s58, s1, 0xc000
	v_bfe_u32 v6, v2, 4, 2
	v_bfe_u32 v2, v2, 1, 3
	s_mov_b32 m0, s57
	s_nop 0
	global_load_lds_dwordx4 v173, s[24:25] offset:0
	s_add_u32 s24, s12, 0x380
	v_bitop3_b32 v3, v3, v2, 3 bitop3:0x6c
	v_bitop3_b32 v2, v6, v2, 4 bitop3:0x36
	s_addc_u32 s25, s13, 0
	v_lshlrev_b32_e32 v3, 4, v3
	v_lshlrev_b32_e32 v2, 4, v2
	v_lshlrev_b32_e32 v4, 7, v4
	s_cmpk_lt_u32 s4, 0x100
	v_or_b32_e32 v174, v4, v3
	v_or_b32_e32 v175, v4, v2
	s_waitcnt vmcnt(6)
	s_cselect_b64 s[26:27], -1, 0
	s_add_i32 s4, 0, 0x10000
	v_or_b32_e32 v7, v3, v5
	v_or_b32_e32 v5, v2, v5
	v_add_u32_e32 v176, s4, v174
	v_add_u32_e32 v177, s4, v175
	s_add_i32 s4, 0, 0x14000
	s_add_i32 s59, s1, 0xe000
	v_add_u32_e32 v178, s4, v174
	v_add_u32_e32 v179, s4, v175
	v_add_u32_e32 v180, 0, v7
	v_add_u32_e32 v181, 0, v5
	v_mov_b32_e32 v182, 0x7f7f7f7f
	s_mov_b32 s28, 0x42000000
	s_movk_i32 s60, 0xffc0
	s_mov_b32 s30, 0x3c800000
	s_barrier
	s_branch .LBB0_647

.LBB0_650:
	.p2align 3
	s_nop 0
	ds_read_b128 v[18:21], v176
	ds_read_b128 v[26:29], v176 offset:2048
	ds_read_b128 v[22:25], v177
	ds_read_b128 v[30:33], v177 offset:2048
	ds_read_b128 v[2:5], v178
	ds_read_b128 v[10:13], v178 offset:2048
	ds_read_b128 v[6:9], v179
	ds_read_b128 v[14:17], v179 offset:2048
	ds_read_b128 v[194:197], v180
	ds_read_b128 v[202:205], v180 offset:2048
	ds_read_b128 v[198:201], v181
	ds_read_b128 v[206:209], v181 offset:2048
	ds_read_b128 v[210:213], v180 offset:4096
	ds_read_b128 v[218:221], v180 offset:6144
	ds_read_b128 v[214:217], v181 offset:4096
	ds_read_b128 v[222:225], v181 offset:6144
	s_add_u32 s64, s12, s4
	s_addc_u32 s65, s13, s5
	s_add_u32 s46, s64, 0x80
	s_addc_u32 s47, s65, 0
	s_mov_b32 m0, s58
	s_nop 0
	global_load_lds_dwordx4 v163, s[46:47] offset:0
	s_nop 0
	s_mov_b32 m0, s59
	s_nop 0
	global_load_lds_dwordx4 v171, s[46:47] offset:0
	s_waitcnt vmcnt(8)
	s_waitcnt lgkmcnt(0)
	s_barrier
	s_setprio 1
	s_waitcnt lgkmcnt(0)
	v_mfma_f32_16x16x128_f8f6f4 v[158:161], v[18:25], v[194:201], v[158:161]
	v_mfma_f32_16x16x128_f8f6f4 v[154:157], v[26:33], v[194:201], v[154:157]
	v_mfma_f32_16x16x128_f8f6f4 v[142:145], v[18:25], v[202:209], v[142:145]
	v_mfma_f32_16x16x128_f8f6f4 v[138:141], v[26:33], v[202:209], v[138:141]
	v_mfma_f32_16x16x128_f8f6f4 v[126:129], v[18:25], v[210:217], v[126:129]
	v_mfma_f32_16x16x128_f8f6f4 v[122:125], v[26:33], v[210:217], v[122:125]
	v_mfma_f32_16x16x128_f8f6f4 v[110:113], v[18:25], v[218:225], v[110:113]
	v_mfma_f32_16x16x128_f8f6f4 v[106:109], v[26:33], v[218:225], v[106:109]
	s_setprio 0
	s_setprio 1
	v_mfma_f32_16x16x128_f8f6f4 v[150:153], v[2:9], v[194:201], v[150:153]
	v_mfma_f32_16x16x128_f8f6f4 v[146:149], v[10:17], v[194:201], v[146:149]
	v_mfma_f32_16x16x128_f8f6f4 v[134:137], v[2:9], v[202:209], v[134:137]
	v_mfma_f32_16x16x128_f8f6f4 v[130:133], v[10:17], v[202:209], v[130:133]
	v_mfma_f32_16x16x128_f8f6f4 v[118:121], v[2:9], v[210:217], v[118:121]
	v_mfma_f32_16x16x128_f8f6f4 v[114:117], v[10:17], v[210:217], v[114:117]
	v_mfma_f32_16x16x128_f8f6f4 v[102:105], v[2:9], v[218:225], v[102:105]
	v_mfma_f32_16x16x128_f8f6f4 v[98:101], v[10:17], v[218:225], v[98:101]
	s_setprio 0
	s_barrier
	s_add_u32 s66, s42, s4
	s_addc_u32 s67, s43, s5
	ds_read_b128 v[194:197], v180 offset:16384
	ds_read_b128 v[202:205], v180 offset:18432
	ds_read_b128 v[198:201], v181 offset:16384
	ds_read_b128 v[206:209], v181 offset:18432
	ds_read_b128 v[210:213], v180 offset:20480
	ds_read_b128 v[218:221], v180 offset:22528
	ds_read_b128 v[214:217], v181 offset:20480
	ds_read_b128 v[222:225], v181 offset:22528
	s_add_u32 s46, s66, 0x100
	s_addc_u32 s47, s67, 0
	s_mov_b32 m0, s33
	s_nop 0
	global_load_lds_dwordx4 v172, s[46:47] offset:0
	s_nop 0
	s_mov_b32 m0, s39
	s_nop 0
	global_load_lds_dwordx4 v173, s[46:47] offset:0
	s_add_u32 s46, s66, 0x20100
	s_addc_u32 s47, s67, 0
	s_mov_b32 m0, s41
	s_nop 0
	global_load_lds_dwordx4 v172, s[46:47] offset:0
	s_nop 0
	s_mov_b32 m0, s48
	s_nop 0
	global_load_lds_dwordx4 v173, s[46:47] offset:0
	s_add_u32 s46, s64, 0x100
	s_addc_u32 s47, s65, 0
	s_mov_b32 m0, s1
	s_nop 0
	global_load_lds_dwordx4 v162, s[46:47] offset:0
	s_nop 0
	s_mov_b32 m0, s49
	s_nop 0
	global_load_lds_dwordx4 v170, s[46:47] offset:0
	s_waitcnt vmcnt(8)
	s_waitcnt lgkmcnt(0)
	s_barrier
	s_setprio 1
	s_waitcnt lgkmcnt(5)
	v_mfma_f32_16x16x128_f8f6f4 v[94:97], v[18:25], v[194:201], v[94:97]
	v_mfma_f32_16x16x128_f8f6f4 v[90:93], v[26:33], v[194:201], v[90:93]
	s_waitcnt lgkmcnt(4)
	v_mfma_f32_16x16x128_f8f6f4 v[78:81], v[18:25], v[202:209], v[78:81]
	v_mfma_f32_16x16x128_f8f6f4 v[74:77], v[26:33], v[202:209], v[74:77]
	s_waitcnt lgkmcnt(1)
	v_mfma_f32_16x16x128_f8f6f4 v[62:65], v[18:25], v[210:217], v[62:65]
	v_mfma_f32_16x16x128_f8f6f4 v[58:61], v[26:33], v[210:217], v[58:61]
	s_waitcnt lgkmcnt(0)
	v_mfma_f32_16x16x128_f8f6f4 v[46:49], v[18:25], v[218:225], v[46:49]
	v_mfma_f32_16x16x128_f8f6f4 v[42:45], v[26:33], v[218:225], v[42:45]
	s_setprio 0
	s_setprio 1
	v_mfma_f32_16x16x128_f8f6f4 v[86:89], v[2:9], v[194:201], v[86:89]
	v_mfma_f32_16x16x128_f8f6f4 v[82:85], v[10:17], v[194:201], v[82:85]
	v_mfma_f32_16x16x128_f8f6f4 v[70:73], v[2:9], v[202:209], v[70:73]
	v_mfma_f32_16x16x128_f8f6f4 v[66:69], v[10:17], v[202:209], v[66:69]
	v_mfma_f32_16x16x128_f8f6f4 v[54:57], v[2:9], v[210:217], v[54:57]
	v_mfma_f32_16x16x128_f8f6f4 v[50:53], v[10:17], v[210:217], v[50:53]
	v_mfma_f32_16x16x128_f8f6f4 v[38:41], v[2:9], v[218:225], v[38:41]
	v_mfma_f32_16x16x128_f8f6f4 v[34:37], v[10:17], v[218:225], v[34:37]
	s_setprio 0
	s_barrier
	s_add_i32 s68, 0, 0x18000
	v_add_u32_e32 v183, s68, v174
	v_add_u32_e32 v184, s68, v175
	s_add_i32 s68, 0, 0x1c000
	v_add_u32_e32 v185, s68, v174
	ds_read_b128 v[2:5], v183
	ds_read_b128 v[10:13], v183 offset:2048
	ds_read_b128 v[6:9], v184
	ds_read_b128 v[14:17], v184 offset:2048
	v_add_u32_e32 v186, s68, v175
	ds_read_b128 v[18:21], v185
	ds_read_b128 v[26:29], v185 offset:2048
	ds_read_b128 v[22:25], v186
	ds_read_b128 v[30:33], v186 offset:2048
	ds_read_b128 v[194:197], v180 offset:32768
	ds_read_b128 v[202:205], v180 offset:34816
	ds_read_b128 v[198:201], v181 offset:32768
	ds_read_b128 v[206:209], v181 offset:34816
	ds_read_b128 v[210:213], v180 offset:36864
	ds_read_b128 v[218:221], v180 offset:38912
	ds_read_b128 v[214:217], v181 offset:36864
	ds_read_b128 v[222:225], v181 offset:38912
	s_mov_b32 m0, s50
	s_nop 0
	global_load_lds_dwordx4 v163, s[46:47] offset:0
	s_nop 0
	s_mov_b32 m0, s51
	s_nop 0
	global_load_lds_dwordx4 v171, s[46:47] offset:0
	s_waitcnt vmcnt(8)
	s_waitcnt lgkmcnt(0)
	s_barrier
	s_setprio 1
	s_waitcnt lgkmcnt(5)
	v_mfma_f32_16x16x128_f8f6f4 v[158:161], v[2:9], v[194:201], v[158:161]
	v_mfma_f32_16x16x128_f8f6f4 v[154:157], v[10:17], v[194:201], v[154:157]
	s_waitcnt lgkmcnt(4)
	v_mfma_f32_16x16x128_f8f6f4 v[142:145], v[2:9], v[202:209], v[142:145]
	v_mfma_f32_16x16x128_f8f6f4 v[138:141], v[10:17], v[202:209], v[138:141]
	s_waitcnt lgkmcnt(1)
	v_mfma_f32_16x16x128_f8f6f4 v[126:129], v[2:9], v[210:217], v[126:129]
	v_mfma_f32_16x16x128_f8f6f4 v[122:125], v[10:17], v[210:217], v[122:125]
	s_waitcnt lgkmcnt(0)
	v_mfma_f32_16x16x128_f8f6f4 v[110:113], v[2:9], v[218:225], v[110:113]
	v_mfma_f32_16x16x128_f8f6f4 v[106:109], v[10:17], v[218:225], v[106:109]
	s_setprio 0
	s_setprio 1
	v_mfma_f32_16x16x128_f8f6f4 v[150:153], v[18:25], v[194:201], v[150:153]
	v_mfma_f32_16x16x128_f8f6f4 v[146:149], v[26:33], v[194:201], v[146:149]
	v_mfma_f32_16x16x128_f8f6f4 v[134:137], v[18:25], v[202:209], v[134:137]
	v_mfma_f32_16x16x128_f8f6f4 v[130:133], v[26:33], v[202:209], v[130:133]
	v_mfma_f32_16x16x128_f8f6f4 v[118:121], v[18:25], v[210:217], v[118:121]
	v_mfma_f32_16x16x128_f8f6f4 v[114:117], v[26:33], v[210:217], v[114:117]
	v_mfma_f32_16x16x128_f8f6f4 v[102:105], v[18:25], v[218:225], v[102:105]
	v_mfma_f32_16x16x128_f8f6f4 v[98:101], v[26:33], v[218:225], v[98:101]
	s_setprio 0
	s_barrier
	ds_read_b128 v[194:197], v180 offset:49152
	ds_read_b128 v[202:205], v180 offset:51200
	ds_read_b128 v[198:201], v181 offset:49152
	ds_read_b128 v[206:209], v181 offset:51200
	ds_read_b128 v[210:213], v180 offset:53248
	ds_read_b128 v[218:221], v180 offset:55296
	ds_read_b128 v[214:217], v181 offset:53248
	ds_read_b128 v[222:225], v181 offset:55296
	s_add_u32 s46, s66, 0x180
	s_addc_u32 s47, s67, 0
	s_mov_b32 m0, s52
	s_nop 0
	global_load_lds_dwordx4 v172, s[46:47] offset:0
	s_nop 0
	s_mov_b32 m0, s53
	s_nop 0
	global_load_lds_dwordx4 v173, s[46:47] offset:0
	s_add_u32 s46, s66, 0x20180
	s_addc_u32 s47, s67, 0
	s_mov_b32 m0, s56
	s_nop 0
	global_load_lds_dwordx4 v172, s[46:47] offset:0
	s_nop 0
	s_mov_b32 m0, s57
	s_nop 0
	global_load_lds_dwordx4 v173, s[46:47] offset:0
	s_add_u32 s46, s64, 0x180
	s_addc_u32 s47, s65, 0
	s_mov_b32 m0, s54
	s_nop 0
	global_load_lds_dwordx4 v162, s[46:47] offset:0
	s_nop 0
	s_mov_b32 m0, s55
	s_nop 0
	global_load_lds_dwordx4 v170, s[46:47] offset:0
	s_waitcnt vmcnt(8)
	s_waitcnt lgkmcnt(0)
	s_barrier
	s_setprio 1
	s_waitcnt lgkmcnt(5)
	v_mfma_f32_16x16x128_f8f6f4 v[94:97], v[2:9], v[194:201], v[94:97]
	v_mfma_f32_16x16x128_f8f6f4 v[90:93], v[10:17], v[194:201], v[90:93]
	s_waitcnt lgkmcnt(4)
	v_mfma_f32_16x16x128_f8f6f4 v[78:81], v[2:9], v[202:209], v[78:81]
	v_mfma_f32_16x16x128_f8f6f4 v[74:77], v[10:17], v[202:209], v[74:77]
	s_waitcnt lgkmcnt(1)
	v_mfma_f32_16x16x128_f8f6f4 v[62:65], v[2:9], v[210:217], v[62:65]
	v_mfma_f32_16x16x128_f8f6f4 v[58:61], v[10:17], v[210:217], v[58:61]
	s_waitcnt lgkmcnt(0)
	v_mfma_f32_16x16x128_f8f6f4 v[46:49], v[2:9], v[218:225], v[46:49]
	v_mfma_f32_16x16x128_f8f6f4 v[42:45], v[10:17], v[218:225], v[42:45]
	s_setprio 0
	s_setprio 1
	v_mfma_f32_16x16x128_f8f6f4 v[86:89], v[18:25], v[194:201], v[86:89]
	v_mfma_f32_16x16x128_f8f6f4 v[82:85], v[26:33], v[194:201], v[82:85]
	v_mfma_f32_16x16x128_f8f6f4 v[70:73], v[18:25], v[202:209], v[70:73]
	v_mfma_f32_16x16x128_f8f6f4 v[66:69], v[26:33], v[202:209], v[66:69]
	v_mfma_f32_16x16x128_f8f6f4 v[54:57], v[18:25], v[210:217], v[54:57]
	v_mfma_f32_16x16x128_f8f6f4 v[50:53], v[26:33], v[210:217], v[50:53]
	v_mfma_f32_16x16x128_f8f6f4 v[38:41], v[18:25], v[218:225], v[38:41]
	v_mfma_f32_16x16x128_f8f6f4 v[34:37], v[26:33], v[218:225], v[34:37]
	s_setprio 0
	s_barrier
	s_add_i32 s35, s35, 2
	s_add_u32 s4, s4, 0x100
	s_addc_u32 s5, s5, 0
	s_cmp_lt_u32 s35, 4
	s_cbranch_scc1 .LBB0_650
	ds_read_b128 v[18:21], v176
	ds_read_b128 v[26:29], v176 offset:2048
	ds_read_b128 v[22:25], v177
	ds_read_b128 v[30:33], v177 offset:2048
	ds_read_b128 v[2:5], v178
	ds_read_b128 v[10:13], v178 offset:2048
	ds_read_b128 v[6:9], v179
	ds_read_b128 v[14:17], v179 offset:2048
	ds_read_b128 v[194:197], v180
	ds_read_b128 v[202:205], v180 offset:2048
	ds_read_b128 v[198:201], v181
	ds_read_b128 v[206:209], v181 offset:2048
	ds_read_b128 v[210:213], v180 offset:4096
	ds_read_b128 v[218:221], v180 offset:6144
	ds_read_b128 v[214:217], v181 offset:4096
	ds_read_b128 v[222:225], v181 offset:6144
	s_mov_b32 m0, s58
	s_nop 0
	global_load_lds_dwordx4 v163, s[24:25] offset:0
	s_nop 0
	s_mov_b32 m0, s59
	s_nop 0
	global_load_lds_dwordx4 v171, s[24:25] offset:0
	s_waitcnt vmcnt(8)
	s_waitcnt lgkmcnt(0)
	s_barrier
	s_setprio 1
	s_waitcnt lgkmcnt(5)
	v_mfma_f32_16x16x128_f8f6f4 v[158:161], v[18:25], v[194:201], v[158:161]
	v_mfma_f32_16x16x128_f8f6f4 v[154:157], v[26:33], v[194:201], v[154:157]
	s_waitcnt lgkmcnt(4)
	v_mfma_f32_16x16x128_f8f6f4 v[142:145], v[18:25], v[202:209], v[142:145]
	v_mfma_f32_16x16x128_f8f6f4 v[138:141], v[26:33], v[202:209], v[138:141]
	s_waitcnt lgkmcnt(1)
	v_mfma_f32_16x16x128_f8f6f4 v[126:129], v[18:25], v[210:217], v[126:129]
	v_mfma_f32_16x16x128_f8f6f4 v[122:125], v[26:33], v[210:217], v[122:125]
	s_waitcnt lgkmcnt(0)
	v_mfma_f32_16x16x128_f8f6f4 v[110:113], v[18:25], v[218:225], v[110:113]
	v_mfma_f32_16x16x128_f8f6f4 v[106:109], v[26:33], v[218:225], v[106:109]
	s_setprio 0
	s_setprio 1
	v_mfma_f32_16x16x128_f8f6f4 v[150:153], v[2:9], v[194:201], v[150:153]
	v_mfma_f32_16x16x128_f8f6f4 v[146:149], v[10:17], v[194:201], v[146:149]
	v_mfma_f32_16x16x128_f8f6f4 v[134:137], v[2:9], v[202:209], v[134:137]
	v_mfma_f32_16x16x128_f8f6f4 v[130:133], v[10:17], v[202:209], v[130:133]
	v_mfma_f32_16x16x128_f8f6f4 v[118:121], v[2:9], v[210:217], v[118:121]
	v_mfma_f32_16x16x128_f8f6f4 v[114:117], v[10:17], v[210:217], v[114:117]
	v_mfma_f32_16x16x128_f8f6f4 v[102:105], v[2:9], v[218:225], v[102:105]
	v_mfma_f32_16x16x128_f8f6f4 v[98:101], v[10:17], v[218:225], v[98:101]
	s_setprio 0
	s_barrier
	v_cndmask_b32_e64 v187, 0, 1, s[44:45]
	v_cmp_ne_u32_e64 s[4:5], 1, v187
	s_andn2_b64 vcc, exec, s[44:45]
	s_cbranch_vccnz .LBB0_653
	v_mov_b32_e32 v162, v0
	s_nop 0
	v_lshlrev_b32_e32 v163, 4, v162
	v_bitop3_b32 v163, v163, s0, v162 bitop3:0x48
	v_lshlrev_b32_e32 v162, 7, v162
	v_lshl_or_b32 v163, s61, 18, v163
	v_and_b32_e32 v162, 0xfffffc00, v162
	v_add_u32_e32 v162, v163, v162
	v_add_u32_e32 v163, 0x20000, v162
	v_add_u32_e32 v170, 0x10000, v162
	v_add_u32_e32 v171, 0x30000, v162
.LBB0_653:
	s_ashr_i32 s35, s34, 31
	s_lshl_b64 s[46:47], s[34:35], 18
	s_add_u32 s46, s29, s46
	s_addc_u32 s47, s31, s47
	s_and_b64 s[44:45], s[44:45], exec
	ds_read_b128 v[194:197], v180 offset:16384
	ds_read_b128 v[202:205], v180 offset:18432
	ds_read_b128 v[198:201], v181 offset:16384
	ds_read_b128 v[206:209], v181 offset:18432
	ds_read_b128 v[210:213], v180 offset:20480
	ds_read_b128 v[218:221], v180 offset:22528
	ds_read_b128 v[214:217], v181 offset:20480
	ds_read_b128 v[222:225], v181 offset:22528
	s_cselect_b32 s43, s47, s43
	s_cselect_b32 s42, s46, s42
	s_mov_b32 m0, s33
	s_nop 0
	global_load_lds_dwordx4 v172, s[42:43] offset:0
	s_add_u32 s44, s42, 0x20000
	s_mov_b32 m0, s39
	s_nop 0
	global_load_lds_dwordx4 v173, s[42:43] offset:0
	s_addc_u32 s45, s43, 0
	s_mov_b32 m0, s41
	s_nop 0
	global_load_lds_dwordx4 v172, s[44:45] offset:0
	s_nop 0
	s_mov_b32 m0, s48
	s_nop 0
	global_load_lds_dwordx4 v173, s[44:45] offset:0
	s_nop 0
	s_mov_b32 m0, s1
	s_nop 0
	global_load_lds_dwordx4 v162, s[12:13] offset:0
	s_nop 0
	s_mov_b32 m0, s49
	s_nop 0
	global_load_lds_dwordx4 v170, s[12:13] offset:0
	s_waitcnt vmcnt(8)
	s_waitcnt lgkmcnt(0)
	s_barrier
	s_setprio 1
	s_waitcnt lgkmcnt(5)
	v_mfma_f32_16x16x128_f8f6f4 v[94:97], v[18:25], v[194:201], v[94:97]
	v_mfma_f32_16x16x128_f8f6f4 v[90:93], v[26:33], v[194:201], v[90:93]
	s_waitcnt lgkmcnt(4)
	v_mfma_f32_16x16x128_f8f6f4 v[78:81], v[18:25], v[202:209], v[78:81]
	v_mfma_f32_16x16x128_f8f6f4 v[74:77], v[26:33], v[202:209], v[74:77]
	s_waitcnt lgkmcnt(1)
	v_mfma_f32_16x16x128_f8f6f4 v[62:65], v[18:25], v[210:217], v[62:65]
	v_mfma_f32_16x16x128_f8f6f4 v[58:61], v[26:33], v[210:217], v[58:61]
	s_waitcnt lgkmcnt(0)
	v_mfma_f32_16x16x128_f8f6f4 v[46:49], v[18:25], v[218:225], v[46:49]
	v_mfma_f32_16x16x128_f8f6f4 v[42:45], v[26:33], v[218:225], v[42:45]
	s_setprio 0
	s_setprio 1
	v_mfma_f32_16x16x128_f8f6f4 v[86:89], v[2:9], v[194:201], v[86:89]
	v_mfma_f32_16x16x128_f8f6f4 v[82:85], v[10:17], v[194:201], v[82:85]
	v_mfma_f32_16x16x128_f8f6f4 v[70:73], v[2:9], v[202:209], v[70:73]
	v_mfma_f32_16x16x128_f8f6f4 v[66:69], v[10:17], v[202:209], v[66:69]
	v_mfma_f32_16x16x128_f8f6f4 v[54:57], v[2:9], v[210:217], v[54:57]
	v_mfma_f32_16x16x128_f8f6f4 v[50:53], v[10:17], v[210:217], v[50:53]
	v_mfma_f32_16x16x128_f8f6f4 v[38:41], v[2:9], v[218:225], v[38:41]
	v_mfma_f32_16x16x128_f8f6f4 v[34:37], v[10:17], v[218:225], v[34:37]
	s_setprio 0
	s_barrier
	ds_read_b128 v[2:5], v183
	ds_read_b128 v[10:13], v183 offset:2048
	ds_read_b128 v[6:9], v184
	ds_read_b128 v[14:17], v184 offset:2048
	ds_read_b128 v[18:21], v185
	ds_read_b128 v[26:29], v185 offset:2048
	ds_read_b128 v[22:25], v186
	ds_read_b128 v[30:33], v186 offset:2048
	ds_read_b128 v[194:197], v180 offset:32768
	ds_read_b128 v[202:205], v180 offset:34816
	ds_read_b128 v[198:201], v181 offset:32768
	ds_read_b128 v[206:209], v181 offset:34816
	ds_read_b128 v[210:213], v180 offset:36864
	ds_read_b128 v[218:221], v180 offset:38912
	ds_read_b128 v[214:217], v181 offset:36864
	ds_read_b128 v[222:225], v181 offset:38912
	s_mov_b32 m0, s50
	s_nop 0
	global_load_lds_dwordx4 v163, s[12:13] offset:0
	s_nop 0
	s_mov_b32 m0, s51
	s_nop 0
	global_load_lds_dwordx4 v171, s[12:13] offset:0
	s_waitcnt vmcnt(8)
	s_waitcnt lgkmcnt(0)
	s_barrier
	s_setprio 1
	s_waitcnt lgkmcnt(5)
	v_mfma_f32_16x16x128_f8f6f4 v[158:161], v[2:9], v[194:201], v[158:161]
	v_mfma_f32_16x16x128_f8f6f4 v[154:157], v[10:17], v[194:201], v[154:157]
	s_waitcnt lgkmcnt(4)
	v_mfma_f32_16x16x128_f8f6f4 v[142:145], v[2:9], v[202:209], v[142:145]
	v_mfma_f32_16x16x128_f8f6f4 v[138:141], v[10:17], v[202:209], v[138:141]
	s_waitcnt lgkmcnt(1)
	v_mfma_f32_16x16x128_f8f6f4 v[126:129], v[2:9], v[210:217], v[126:129]
	v_mfma_f32_16x16x128_f8f6f4 v[122:125], v[10:17], v[210:217], v[122:125]
	s_waitcnt lgkmcnt(0)
	v_mfma_f32_16x16x128_f8f6f4 v[110:113], v[2:9], v[218:225], v[110:113]
	v_mfma_f32_16x16x128_f8f6f4 v[106:109], v[10:17], v[218:225], v[106:109]
	s_setprio 0
	s_setprio 1
	v_mfma_f32_16x16x128_f8f6f4 v[150:153], v[18:25], v[194:201], v[150:153]
	v_mfma_f32_16x16x128_f8f6f4 v[146:149], v[26:33], v[194:201], v[146:149]
	v_mfma_f32_16x16x128_f8f6f4 v[134:137], v[18:25], v[202:209], v[134:137]
	v_mfma_f32_16x16x128_f8f6f4 v[130:133], v[26:33], v[202:209], v[130:133]
	v_mfma_f32_16x16x128_f8f6f4 v[118:121], v[18:25], v[210:217], v[118:121]
	v_mfma_f32_16x16x128_f8f6f4 v[114:117], v[26:33], v[210:217], v[114:117]
	v_mfma_f32_16x16x128_f8f6f4 v[102:105], v[18:25], v[218:225], v[102:105]
	v_mfma_f32_16x16x128_f8f6f4 v[98:101], v[26:33], v[218:225], v[98:101]
	s_setprio 0
	s_barrier
	ds_read_b128 v[194:197], v180 offset:49152
	ds_read_b128 v[202:205], v180 offset:51200
	ds_read_b128 v[198:201], v181 offset:49152
	ds_read_b128 v[206:209], v181 offset:51200
	ds_read_b128 v[210:213], v180 offset:53248
	ds_read_b128 v[218:221], v180 offset:55296
	ds_read_b128 v[214:217], v181 offset:53248
	ds_read_b128 v[222:225], v181 offset:55296
	s_add_u32 s44, s42, 0x80
	s_addc_u32 s45, s43, 0
	s_mov_b32 m0, s52
	s_nop 0
	global_load_lds_dwordx4 v172, s[44:45] offset:0
	s_add_u32 s42, s42, 0x20080
	s_mov_b32 m0, s53
	s_nop 0
	global_load_lds_dwordx4 v173, s[44:45] offset:0
	s_addc_u32 s43, s43, 0
	s_mov_b32 m0, s56
	s_nop 0
	global_load_lds_dwordx4 v172, s[42:43] offset:0
	s_nop 0
	s_mov_b32 m0, s57
	s_nop 0
	global_load_lds_dwordx4 v173, s[42:43] offset:0
	s_nop 0
	s_mov_b32 m0, s54
	s_nop 0
	global_load_lds_dwordx4 v162, s[22:23] offset:0
	s_nop 0
	s_mov_b32 m0, s55
	s_nop 0
	global_load_lds_dwordx4 v170, s[22:23] offset:0
	s_waitcnt vmcnt(8)
	s_waitcnt lgkmcnt(0)
	s_barrier
	s_setprio 1
	s_waitcnt lgkmcnt(5)
	v_mfma_f32_16x16x128_f8f6f4 v[94:97], v[2:9], v[194:201], v[94:97]
	v_mfma_f32_16x16x128_f8f6f4 v[90:93], v[10:17], v[194:201], v[90:93]
	s_waitcnt lgkmcnt(4)
	v_mfma_f32_16x16x128_f8f6f4 v[78:81], v[2:9], v[202:209], v[78:81]
	v_mfma_f32_16x16x128_f8f6f4 v[74:77], v[10:17], v[202:209], v[74:77]
	s_waitcnt lgkmcnt(1)
	v_mfma_f32_16x16x128_f8f6f4 v[62:65], v[2:9], v[210:217], v[62:65]
	v_mfma_f32_16x16x128_f8f6f4 v[58:61], v[10:17], v[210:217], v[58:61]
	s_waitcnt lgkmcnt(0)
	v_mfma_f32_16x16x128_f8f6f4 v[46:49], v[2:9], v[218:225], v[46:49]
	v_mfma_f32_16x16x128_f8f6f4 v[42:45], v[10:17], v[218:225], v[42:45]
	s_setprio 0
	s_setprio 1
	v_mfma_f32_16x16x128_f8f6f4 v[86:89], v[18:25], v[194:201], v[86:89]
	v_mfma_f32_16x16x128_f8f6f4 v[82:85], v[26:33], v[194:201], v[82:85]
	v_mfma_f32_16x16x128_f8f6f4 v[70:73], v[18:25], v[202:209], v[70:73]
	v_mfma_f32_16x16x128_f8f6f4 v[66:69], v[26:33], v[202:209], v[66:69]
	v_mfma_f32_16x16x128_f8f6f4 v[54:57], v[18:25], v[210:217], v[54:57]
	v_mfma_f32_16x16x128_f8f6f4 v[50:53], v[26:33], v[210:217], v[50:53]
	v_mfma_f32_16x16x128_f8f6f4 v[38:41], v[18:25], v[218:225], v[38:41]
	v_mfma_f32_16x16x128_f8f6f4 v[34:37], v[26:33], v[218:225], v[34:37]
	s_setprio 0
	s_barrier
	s_nop 15
	s_nop 15
	s_andn2_b64 vcc, exec, s[26:27]
	s_cbranch_vccnz .LBB0_655
	s_barrier
.LBB0_655:
	s_lshl_b32 s35, s63, 10
	s_and_b32 s35, s35, 0x400
	v_mov_b32_e32 v28, v0
	s_add_i32 s35, s35, 0
	s_add_i32 s35, s35, 0x24cc0
	v_and_b32_e32 v29, 0xc0, v28
	v_and_b32_e32 v30, 48, v28
	v_lshlrev_b32_e32 v2, 2, v29
	v_lshlrev_b32_e32 v3, 2, v30
	v_add3_u32 v6, s35, v2, v3
	ds_read_b128 v[2:5], v6
	ds_read_b128 v[10:13], v6 offset:16
	ds_read_b128 v[20:23], v6 offset:32
	ds_read_b128 v[24:27], v6 offset:48
	s_lshl_b32 s40, s40, 10
	s_lshl_b32 s38, s38, 8
	s_waitcnt lgkmcnt(2)
	v_pk_mul_f32 v[18:19], v[10:11], s[28:29] op_sel_hi:[1,0]
	v_pk_mul_f32 v[16:17], v[2:3], s[28:29] op_sel_hi:[1,0]
	v_pk_mul_f32 v[8:9], v[4:5], s[28:29] op_sel_hi:[1,0]
	v_pk_mul_f32 v[14:15], v[12:13], s[28:29] op_sel_hi:[1,0]
	s_waitcnt lgkmcnt(1)
	v_pk_mul_f32 v[4:5], v[22:23], s[28:29] op_sel_hi:[1,0]
	s_waitcnt lgkmcnt(0)
	v_pk_mul_f32 v[6:7], v[26:27], s[28:29] op_sel_hi:[1,0]
	v_pk_mul_f32 v[12:13], v[24:25], s[28:29] op_sel_hi:[1,0]
	v_pk_fma_f32 v[24:25], v[158:159], s[30:31], v[16:17] op_sel_hi:[1,0,1]
	v_pk_fma_f32 v[26:27], v[154:155], s[30:31], v[18:19] op_sel_hi:[1,0,1]
	v_mov_b32_e32 v22, 0
	v_mov_b32_e32 v23, 0
	v_cvt_pk_fp8_f32 v22, v24, v25
	v_cvt_pk_fp8_f32 v23, v26, v27
	s_sub_i32 s38, s38, s40
	v_pk_mul_f32 v[10:11], v[20:21], s[28:29] op_sel_hi:[1,0]
	v_pk_fma_f32 v[24:25], v[160:161], s[30:31], v[8:9] op_sel_hi:[1,0,1]
	v_pk_fma_f32 v[26:27], v[156:157], s[30:31], v[14:15] op_sel_hi:[1,0,1]
	v_ashrrev_i32_e32 v31, 2, v28
	v_and_b32_e32 v3, 15, v28
	v_or3_b32 v2, v29, s38, v30
	v_cvt_pk_fp8_f32 v22, v24, v25 op_sel:[0,0,1]
	v_cvt_pk_fp8_f32 v23, v26, v27 op_sel:[0,0,1]
	v_pk_fma_f32 v[26:27], v[150:151], s[30:31], v[10:11] op_sel_hi:[1,0,1]
	v_pk_fma_f32 v[28:29], v[146:147], s[30:31], v[12:13] op_sel_hi:[1,0,1]
	v_mov_b32_e32 v24, 0
	v_mov_b32_e32 v25, 0
	v_cvt_pk_fp8_f32 v24, v26, v27
	v_cvt_pk_fp8_f32 v25, v28, v29
	v_and_or_b32 v20, v31, s60, v3
	v_lshl_add_u32 v20, s37, 8, v20
	v_pk_fma_f32 v[26:27], v[152:153], s[30:31], v[4:5] op_sel_hi:[1,0,1]
	v_pk_fma_f32 v[28:29], v[148:149], s[30:31], v[6:7] op_sel_hi:[1,0,1]
	v_ashrrev_i32_e32 v21, 31, v20
	v_cvt_pk_fp8_f32 v24, v26, v27 op_sel:[0,0,1]
	v_cvt_pk_fp8_f32 v25, v28, v29 op_sel:[0,0,1]
	v_lshlrev_b64 v[26:27], 10, v[20:21]
	v_ashrrev_i32_e32 v3, 31, v2
	v_lshl_add_u64 v[26:27], s[14:15], 0, v[26:27]
	v_lshl_add_u64 v[26:27], v[26:27], 0, v[2:3]
	global_store_dwordx4 v[26:27], v[22:25], off
	v_pk_fma_f32 v[28:29], v[138:139], s[30:31], v[18:19] op_sel_hi:[1,0,1]
	v_pk_fma_f32 v[30:31], v[130:131], s[30:31], v[12:13] op_sel_hi:[1,0,1]
	v_pk_fma_f32 v[24:25], v[142:143], s[30:31], v[16:17] op_sel_hi:[1,0,1]
	v_mov_b32_e32 v22, 0
	v_mov_b32_e32 v23, 0
	v_cvt_pk_fp8_f32 v22, v24, v25
	v_cvt_pk_fp8_f32 v23, v28, v29
	v_pk_fma_f32 v[24:25], v[144:145], s[30:31], v[8:9] op_sel_hi:[1,0,1]
	v_pk_fma_f32 v[28:29], v[140:141], s[30:31], v[14:15] op_sel_hi:[1,0,1]
	v_cvt_pk_fp8_f32 v22, v24, v25 op_sel:[0,0,1]
	v_cvt_pk_fp8_f32 v23, v28, v29 op_sel:[0,0,1]
	v_pk_fma_f32 v[28:29], v[134:135], s[30:31], v[10:11] op_sel_hi:[1,0,1]
	v_mov_b32_e32 v24, 0
	v_mov_b32_e32 v25, 0
	v_cvt_pk_fp8_f32 v24, v28, v29
	v_cvt_pk_fp8_f32 v25, v30, v31
	v_or_b32_e32 v26, 16, v20
	v_pk_fma_f32 v[28:29], v[136:137], s[30:31], v[4:5] op_sel_hi:[1,0,1]
	v_pk_fma_f32 v[30:31], v[132:133], s[30:31], v[6:7] op_sel_hi:[1,0,1]
	v_ashrrev_i32_e32 v27, 31, v26
	v_cvt_pk_fp8_f32 v24, v28, v29 op_sel:[0,0,1]
	v_cvt_pk_fp8_f32 v25, v30, v31 op_sel:[0,0,1]
	v_lshlrev_b64 v[26:27], 10, v[26:27]
	v_lshl_add_u64 v[26:27], s[14:15], 0, v[26:27]
	v_lshl_add_u64 v[26:27], v[26:27], 0, v[2:3]
	global_store_dwordx4 v[26:27], v[22:25], off
	v_pk_fma_f32 v[28:29], v[122:123], s[30:31], v[18:19] op_sel_hi:[1,0,1]
	v_pk_fma_f32 v[30:31], v[114:115], s[30:31], v[12:13] op_sel_hi:[1,0,1]
	v_pk_fma_f32 v[24:25], v[126:127], s[30:31], v[16:17] op_sel_hi:[1,0,1]
	v_mov_b32_e32 v22, 0
	v_mov_b32_e32 v23, 0
	v_cvt_pk_fp8_f32 v22, v24, v25
	v_cvt_pk_fp8_f32 v23, v28, v29
	v_pk_fma_f32 v[24:25], v[128:129], s[30:31], v[8:9] op_sel_hi:[1,0,1]
	v_pk_fma_f32 v[28:29], v[124:125], s[30:31], v[14:15] op_sel_hi:[1,0,1]
	v_cvt_pk_fp8_f32 v22, v24, v25 op_sel:[0,0,1]
	v_cvt_pk_fp8_f32 v23, v28, v29 op_sel:[0,0,1]
	v_pk_fma_f32 v[28:29], v[118:119], s[30:31], v[10:11] op_sel_hi:[1,0,1]
	v_mov_b32_e32 v24, 0
	v_mov_b32_e32 v25, 0
	v_cvt_pk_fp8_f32 v24, v28, v29
	v_cvt_pk_fp8_f32 v25, v30, v31
	v_or_b32_e32 v26, 32, v20
	v_pk_fma_f32 v[28:29], v[120:121], s[30:31], v[4:5] op_sel_hi:[1,0,1]
	v_pk_fma_f32 v[30:31], v[116:117], s[30:31], v[6:7] op_sel_hi:[1,0,1]
	v_ashrrev_i32_e32 v27, 31, v26
	v_cvt_pk_fp8_f32 v24, v28, v29 op_sel:[0,0,1]
	v_cvt_pk_fp8_f32 v25, v30, v31 op_sel:[0,0,1]
	v_lshlrev_b64 v[26:27], 10, v[26:27]
	v_lshl_add_u64 v[26:27], s[14:15], 0, v[26:27]
	v_lshl_add_u64 v[26:27], v[26:27], 0, v[2:3]
	global_store_dwordx4 v[26:27], v[22:25], off
	v_pk_fma_f32 v[28:29], v[106:107], s[30:31], v[18:19] op_sel_hi:[1,0,1]
	v_pk_fma_f32 v[30:31], v[98:99], s[30:31], v[12:13] op_sel_hi:[1,0,1]
	v_pk_fma_f32 v[24:25], v[110:111], s[30:31], v[16:17] op_sel_hi:[1,0,1]
	v_mov_b32_e32 v22, 0
	v_mov_b32_e32 v23, 0
	v_cvt_pk_fp8_f32 v22, v24, v25
	v_cvt_pk_fp8_f32 v23, v28, v29
	v_pk_fma_f32 v[24:25], v[112:113], s[30:31], v[8:9] op_sel_hi:[1,0,1]
	v_pk_fma_f32 v[28:29], v[108:109], s[30:31], v[14:15] op_sel_hi:[1,0,1]
	v_cvt_pk_fp8_f32 v22, v24, v25 op_sel:[0,0,1]
	v_cvt_pk_fp8_f32 v23, v28, v29 op_sel:[0,0,1]
	v_pk_fma_f32 v[28:29], v[102:103], s[30:31], v[10:11] op_sel_hi:[1,0,1]
	v_mov_b32_e32 v24, 0
	v_mov_b32_e32 v25, 0
	v_cvt_pk_fp8_f32 v24, v28, v29
	v_cvt_pk_fp8_f32 v25, v30, v31
	v_or_b32_e32 v26, 48, v20
	v_pk_fma_f32 v[28:29], v[104:105], s[30:31], v[4:5] op_sel_hi:[1,0,1]
	v_pk_fma_f32 v[30:31], v[100:101], s[30:31], v[6:7] op_sel_hi:[1,0,1]
	v_ashrrev_i32_e32 v27, 31, v26
	v_cvt_pk_fp8_f32 v24, v28, v29 op_sel:[0,0,1]
	v_cvt_pk_fp8_f32 v25, v30, v31 op_sel:[0,0,1]
	v_lshlrev_b64 v[26:27], 10, v[26:27]
	v_lshl_add_u64 v[26:27], s[14:15], 0, v[26:27]
	v_lshl_add_u64 v[26:27], v[26:27], 0, v[2:3]
	global_store_dwordx4 v[26:27], v[22:25], off
	v_pk_fma_f32 v[28:29], v[90:91], s[30:31], v[18:19] op_sel_hi:[1,0,1]
	v_pk_fma_f32 v[30:31], v[82:83], s[30:31], v[12:13] op_sel_hi:[1,0,1]
	v_pk_fma_f32 v[24:25], v[94:95], s[30:31], v[16:17] op_sel_hi:[1,0,1]
	v_mov_b32_e32 v22, 0
	v_mov_b32_e32 v23, 0
	v_cvt_pk_fp8_f32 v22, v24, v25
	v_cvt_pk_fp8_f32 v23, v28, v29
	v_pk_fma_f32 v[24:25], v[96:97], s[30:31], v[8:9] op_sel_hi:[1,0,1]
	v_pk_fma_f32 v[28:29], v[92:93], s[30:31], v[14:15] op_sel_hi:[1,0,1]
	v_cvt_pk_fp8_f32 v22, v24, v25 op_sel:[0,0,1]
	v_cvt_pk_fp8_f32 v23, v28, v29 op_sel:[0,0,1]
	v_pk_fma_f32 v[28:29], v[86:87], s[30:31], v[10:11] op_sel_hi:[1,0,1]
	v_mov_b32_e32 v24, 0
	v_mov_b32_e32 v25, 0
	v_cvt_pk_fp8_f32 v24, v28, v29
	v_cvt_pk_fp8_f32 v25, v30, v31
	v_add_u32_e32 v26, 0x80, v20
	v_pk_fma_f32 v[28:29], v[88:89], s[30:31], v[4:5] op_sel_hi:[1,0,1]
	v_pk_fma_f32 v[30:31], v[84:85], s[30:31], v[6:7] op_sel_hi:[1,0,1]
	v_ashrrev_i32_e32 v27, 31, v26
	v_cvt_pk_fp8_f32 v24, v28, v29 op_sel:[0,0,1]
	v_cvt_pk_fp8_f32 v25, v30, v31 op_sel:[0,0,1]
	v_lshlrev_b64 v[26:27], 10, v[26:27]
	v_lshl_add_u64 v[26:27], s[14:15], 0, v[26:27]
	v_lshl_add_u64 v[26:27], v[26:27], 0, v[2:3]
	global_store_dwordx4 v[26:27], v[22:25], off
	v_pk_fma_f32 v[28:29], v[74:75], s[30:31], v[18:19] op_sel_hi:[1,0,1]
	v_pk_fma_f32 v[30:31], v[66:67], s[30:31], v[12:13] op_sel_hi:[1,0,1]
	v_pk_fma_f32 v[24:25], v[78:79], s[30:31], v[16:17] op_sel_hi:[1,0,1]
	v_mov_b32_e32 v22, 0
	v_mov_b32_e32 v23, 0
	v_cvt_pk_fp8_f32 v22, v24, v25
	v_cvt_pk_fp8_f32 v23, v28, v29
	v_pk_fma_f32 v[24:25], v[80:81], s[30:31], v[8:9] op_sel_hi:[1,0,1]
	v_pk_fma_f32 v[28:29], v[76:77], s[30:31], v[14:15] op_sel_hi:[1,0,1]
	v_cvt_pk_fp8_f32 v22, v24, v25 op_sel:[0,0,1]
	v_cvt_pk_fp8_f32 v23, v28, v29 op_sel:[0,0,1]
	v_pk_fma_f32 v[28:29], v[70:71], s[30:31], v[10:11] op_sel_hi:[1,0,1]
	v_mov_b32_e32 v24, 0
	v_mov_b32_e32 v25, 0
	v_cvt_pk_fp8_f32 v24, v28, v29
	v_cvt_pk_fp8_f32 v25, v30, v31
	v_add_u32_e32 v26, 0x90, v20
	v_pk_fma_f32 v[28:29], v[72:73], s[30:31], v[4:5] op_sel_hi:[1,0,1]
	v_pk_fma_f32 v[30:31], v[68:69], s[30:31], v[6:7] op_sel_hi:[1,0,1]
	v_ashrrev_i32_e32 v27, 31, v26
	v_cvt_pk_fp8_f32 v24, v28, v29 op_sel:[0,0,1]
	v_cvt_pk_fp8_f32 v25, v30, v31 op_sel:[0,0,1]
	v_lshlrev_b64 v[26:27], 10, v[26:27]
	v_lshl_add_u64 v[26:27], s[14:15], 0, v[26:27]
	v_lshl_add_u64 v[26:27], v[26:27], 0, v[2:3]
	global_store_dwordx4 v[26:27], v[22:25], off
	v_pk_fma_f32 v[28:29], v[58:59], s[30:31], v[18:19] op_sel_hi:[1,0,1]
	v_pk_fma_f32 v[30:31], v[50:51], s[30:31], v[12:13] op_sel_hi:[1,0,1]
	v_pk_fma_f32 v[24:25], v[62:63], s[30:31], v[16:17] op_sel_hi:[1,0,1]
	v_mov_b32_e32 v22, 0
	v_mov_b32_e32 v23, 0
	v_cvt_pk_fp8_f32 v22, v24, v25
	v_cvt_pk_fp8_f32 v23, v28, v29
	v_pk_fma_f32 v[24:25], v[64:65], s[30:31], v[8:9] op_sel_hi:[1,0,1]
	v_pk_fma_f32 v[28:29], v[60:61], s[30:31], v[14:15] op_sel_hi:[1,0,1]
	v_cvt_pk_fp8_f32 v22, v24, v25 op_sel:[0,0,1]
	v_cvt_pk_fp8_f32 v23, v28, v29 op_sel:[0,0,1]
	v_pk_fma_f32 v[28:29], v[54:55], s[30:31], v[10:11] op_sel_hi:[1,0,1]
	v_mov_b32_e32 v24, 0
	v_mov_b32_e32 v25, 0
	v_cvt_pk_fp8_f32 v24, v28, v29
	v_cvt_pk_fp8_f32 v25, v30, v31
	v_add_u32_e32 v26, 0xa0, v20
	v_pk_fma_f32 v[28:29], v[56:57], s[30:31], v[4:5] op_sel_hi:[1,0,1]
	v_pk_fma_f32 v[30:31], v[52:53], s[30:31], v[6:7] op_sel_hi:[1,0,1]
	v_ashrrev_i32_e32 v27, 31, v26
	v_cvt_pk_fp8_f32 v24, v28, v29 op_sel:[0,0,1]
	v_cvt_pk_fp8_f32 v25, v30, v31 op_sel:[0,0,1]
	v_lshlrev_b64 v[26:27], 10, v[26:27]
	v_lshl_add_u64 v[26:27], s[14:15], 0, v[26:27]
	v_lshl_add_u64 v[26:27], v[26:27], 0, v[2:3]
	global_store_dwordx4 v[26:27], v[22:25], off
	v_pk_fma_f32 v[18:19], v[42:43], s[30:31], v[18:19] op_sel_hi:[1,0,1]
	v_pk_fma_f32 v[8:9], v[48:49], s[30:31], v[8:9] op_sel_hi:[1,0,1]
	v_pk_fma_f32 v[22:23], v[46:47], s[30:31], v[16:17] op_sel_hi:[1,0,1]
	v_mov_b32_e32 v16, 0
	v_cvt_pk_fp8_f32 v16, v22, v23
	v_mov_b32_e32 v17, 0
	v_cvt_pk_fp8_f32 v17, v18, v19
	v_mov_b32_e32 v18, 0
	v_cvt_pk_fp8_f32 v16, v8, v9 op_sel:[0,0,1]
	v_pk_fma_f32 v[8:9], v[38:39], s[30:31], v[10:11] op_sel_hi:[1,0,1]
	v_pk_fma_f32 v[10:11], v[34:35], s[30:31], v[12:13] op_sel_hi:[1,0,1]
	v_mov_b32_e32 v19, 0
	v_cvt_pk_fp8_f32 v18, v8, v9
	v_cvt_pk_fp8_f32 v19, v10, v11
	v_add_u32_e32 v20, 0xb0, v20
	v_pk_fma_f32 v[14:15], v[44:45], s[30:31], v[14:15] op_sel_hi:[1,0,1]
	v_pk_fma_f32 v[4:5], v[40:41], s[30:31], v[4:5] op_sel_hi:[1,0,1]
	v_pk_fma_f32 v[6:7], v[36:37], s[30:31], v[6:7] op_sel_hi:[1,0,1]
	v_ashrrev_i32_e32 v21, 31, v20
	v_cvt_pk_fp8_f32 v17, v14, v15 op_sel:[0,0,1]
	v_cvt_pk_fp8_f32 v18, v4, v5 op_sel:[0,0,1]
	v_cvt_pk_fp8_f32 v19, v6, v7 op_sel:[0,0,1]
	v_lshlrev_b64 v[4:5], 10, v[20:21]
	v_lshl_add_u64 v[4:5], s[14:15], 0, v[4:5]
	v_lshl_add_u64 v[2:3], v[4:5], 0, v[2:3]
	s_and_b64 vcc, exec, s[4:5]
	s_mov_b64 s[4:5], -1
	global_store_dwordx4 v[2:3], v[16:19], off
	s_cbranch_vccnz .LBB0_646
	s_andn2_b64 vcc, exec, s[18:19]
	s_cbranch_vccnz .LBB0_658
	s_lshl_b32 s4, s62, 10
	s_and_b32 s4, s4, 0x400
	s_add_i32 s4, s4, 0
	s_ashr_i32 s37, s36, 31
	s_add_i32 s35, s4, 0x24cc0
	s_lshl_b64 s[4:5], s[36:37], 12
	s_add_u32 s37, s16, s4
	s_addc_u32 s38, s17, s5
	s_lshl_b32 s4, s36, 10
	s_lshl_b32 s5, s34, 8
	s_sub_i32 s4, s5, s4
	s_ashr_i32 s5, s4, 31
	s_lshl_b64 s[4:5], s[4:5], 2
	s_add_u32 s4, s37, s4
	s_addc_u32 s5, s38, s5
	s_mov_b32 m0, s35
	s_nop 0
	global_load_lds_dwordx4 v1, s[4:5] offset:0
